# v15 + instruction selection: all 2613 packed f32 ops (v_pk_add/mul/fma_f32) of the Hyena FFT phase split into scalar v_add/v_mul/v_fma_f32 (packed f32 measured slower than two scalar ops on gfx950)
# baseline (speedup 1.0000x reference)
; FFT_HD cf2 mk2(float x, float y) { return (cf2){x, y}; }
; FFT_HD void fft_sincos(float frac, float& s, float& c) { s = __builtin_amdgcn_sinf(frac); c = __builtin_amdgcn_cosf(frac); }
; FFT_HD cf2 cmul(cf2 a, cf2 b) { return mk2(a.x * b.x - a.y * b.y, a.x * b.y + a.y * b.x); }
; FFT_HD cf2 cadd(cf2 a, cf2 b) { return mk2(a.x + b.x, a.y + b.y); }
; FFT_HD cf2 csub(cf2 a, cf2 b) { return mk2(a.x - b.x, a.y - b.y); }
; template <bool INV> FFT_HD void dft4(cf2& a, cf2& b, cf2& c, cf2& d) {
;     const cf2 s0 = cadd(a, c), s1 = csub(a, c), s2 = cadd(b, d), s3 = csub(b, d);
;     a = cadd(s0, s2); c = csub(s0, s2);
;     const cf2 r = INV ? mk2(-s3.y, s3.x) : mk2(s3.y, -s3.x);
;     b = cadd(s1, r); d = csub(s1, r);
; }
; template <bool INV> FFT_HD void dft16(cf2 (&x)[16]) {
;     const float C1 = 0.9238795325112867f, S1 = 0.3826834323650898f, H = 0.7071067811865476f;
; #pragma unroll
;     for (int b = 0; b < 4; ++b) dft4<INV>(x[b], x[4 + b], x[8 + b], x[12 + b]);
;     const float s = INV ? -1.f : 1.f;
;     x[4 + 1] = cmul(x[4 + 1], mk2(C1, -s * S1)); x[8 + 1] = cmul(x[8 + 1], mk2(H, -s * H));   x[12 + 1] = cmul(x[12 + 1], mk2(S1, -s * C1));
;     x[4 + 2] = cmul(x[4 + 2], mk2(H, -s * H));   x[8 + 2] = cmul(x[8 + 2], mk2(0.f, -s));     x[12 + 2] = cmul(x[12 + 2], mk2(-H, -s * H));
;     x[4 + 3] = cmul(x[4 + 3], mk2(S1, -s * C1)); x[8 + 3] = cmul(x[8 + 3], mk2(-H, -s * H));  x[12 + 3] = cmul(x[12 + 3], mk2(-C1, s * S1));
; #pragma unroll
;     for (int c = 0; c < 4; ++c) dft4<INV>(x[4 * c], x[4 * c + 1], x[4 * c + 2], x[4 * c + 3]);
; #pragma unroll
;     for (int c = 0; c < 4; ++c)
; #pragma unroll
;         for (int d = c + 1; d < 4; ++d) { const cf2 t = x[4 * c + d]; x[4 * c + d] = x[4 * d + c]; x[4 * d + c] = t; }
; }
; FFT_HD void fft_gen_tw(float frac, cf2 (&tw)[16]) {
;     float sn, cs; fft_sincos(frac, sn, cs);
;     tw[1] = mk2(cs, -sn);
;     tw[2] = cmul(tw[1], tw[1]); tw[3] = cmul(tw[2], tw[1]); tw[4] = cmul(tw[2], tw[2]); tw[5] = cmul(tw[4], tw[1]); tw[6] = cmul(tw[4], tw[2]); tw[7] = cmul(tw[4], tw[3]);
;     tw[8] = cmul(tw[4], tw[4]);
; #pragma unroll
;     for (int j = 9; j < 16; ++j) tw[j] = cmul(tw[8], tw[j - 8]);
; }
.LBB0_566:
	v_add_u32_e32 v4, s1, v57
	v_and_b32_e32 v5, 0x3ff, v4
	v_lshlrev_b32_e32 v4, 4, v4
	v_and_or_b32 v4, v4, s81, v5
	v_cvt_f32_u32_e32 v5, v5
	v_ashrrev_i32_e32 v6, 5, v4
	v_lshlrev_b32_e32 v6, 3, v6
	v_lshlrev_b32_e32 v4, 3, v4
	v_and_b32_e32 v6, 0xfffff0f0, v6
	v_mul_f32_e32 v7, 0x38800000, v5
	v_add3_u32 v65, 0, v6, v4
	v_sin_f32_e32 v5, v7
	v_cos_f32_e32 v4, v7
	v_add_u32_e32 v67, 0x10800, v65
	ds_read_b64 v[6:7], v65
	ds_read_b64 v[42:43], v65 offset:8448
	ds_read_b64 v[44:45], v65 offset:16896
	ds_read_b64 v[46:47], v65 offset:25344
	ds_read_b64 v[48:49], v65 offset:33792
	ds_read_b64 v[50:51], v65 offset:42240
	ds_read_b64 v[52:53], v65 offset:50688
	ds_read_b64 v[54:55], v65 offset:59136
	v_add_u32_e32 v168, 0x12900, v65
	v_add_u32_e32 v169, 0x14a00, v65
	v_add_u32_e32 v170, 0x16b00, v65
	v_add_u32_e32 v171, 0x18c00, v65
	v_add_u32_e32 v172, 0x1ad00, v65
	v_add_u32_e32 v173, 0x1ce00, v65
	v_add_u32_e32 v174, 0x1ef00, v65
	ds_read_b64 v[68:69], v67
	ds_read_b64 v[70:71], v168
	ds_read_b64 v[72:73], v169
	ds_read_b64 v[74:75], v170
	ds_read_b64 v[76:77], v171
	ds_read_b64 v[78:79], v172
	ds_read_b64 v[80:81], v173
	ds_read_b64 v[82:83], v174
	v_mul_f32 v84, v4, v4
	v_mul_f32 v85, v5, v5
	v_mul_f32_e64 v86, v4, -v5
	v_mov_b32_e32 v87, v84
	v_mov_b32_e32 v84, v86
	s_waitcnt lgkmcnt(10)
	v_pk_mov_b32 v[90:91], v[42:43], v[50:51] op_sel:[1,0]
	v_mov_b32_e32 v92, v42
	v_mov_b32_e32 v93, v51
	s_waitcnt lgkmcnt(9)
	v_pk_mov_b32 v[94:95], v[44:45], v[52:53] op_sel:[1,0]
	v_mov_b32_e32 v96, v44
	v_mov_b32_e32 v97, v53
	s_waitcnt lgkmcnt(8)
	v_pk_mov_b32 v[98:99], v[46:47], v[54:55] op_sel:[1,0]
	v_mov_b32_e32 v100, v46
	v_mov_b32_e32 v101, v55
	v_add_f32 v102, v86, v84
	v_add_f32 v103, v87, v85
	v_add_f32_e64 v84, v86, -v84
	v_add_f32_e64 v85, v87, -v85
	s_waitcnt lgkmcnt(2)
	v_pk_mov_b32 v[86:87], v[70:71], v[78:79] op_sel:[1,0]
	v_mov_b32_e32 v104, v70
	v_mov_b32_e32 v105, v79
	s_waitcnt lgkmcnt(1)
	v_pk_mov_b32 v[106:107], v[72:73], v[80:81] op_sel:[1,0]
	v_mov_b32_e32 v108, v72
	v_mov_b32_e32 v109, v81
	s_waitcnt lgkmcnt(0)
	v_pk_mov_b32 v[110:111], v[74:75], v[82:83] op_sel:[1,0]
	v_mov_b32_e32 v112, v74
	v_mov_b32_e32 v113, v83
	v_add_f32 v114, v6, v68
	v_add_f32 v115, v7, v69
	v_add_f32 v116, v48, v76
	v_add_f32 v117, v49, v77
	v_add_f32 v42, v42, v70
	v_add_f32 v43, v43, v71
	v_add_f32 v50, v50, v78
	v_add_f32 v51, v51, v79
	v_add_f32 v44, v44, v72
	v_add_f32 v45, v45, v73
	v_add_f32 v52, v52, v80
	v_add_f32 v53, v53, v81
	v_add_f32 v46, v46, v74
	v_add_f32 v47, v47, v75
	v_add_f32 v54, v54, v82
	v_add_f32 v55, v55, v83
	v_add_f32_e64 v48, v48, -v76
	v_add_f32_e64 v49, v49, -v77
	v_mov_b32_e32 v88, v5
	v_mov_b32_e32 v89, v4
	v_add_f32_e64 v6, v6, -v68
	v_add_f32_e64 v7, v7, -v69
	v_mov_b32_e32 v68, v102
	v_mov_b32_e32 v69, v85
	v_add_f32_e64 v72, v90, -v86
	v_add_f32_e64 v73, v91, -v87
	v_add_f32_e64 v74, v92, -v104
	v_add_f32_e64 v75, v93, -v105
	v_add_f32_e64 v76, v94, -v106
	v_add_f32_e64 v77, v95, -v107
	v_add_f32_e64 v78, v96, -v108
	v_add_f32_e64 v79, v97, -v109
	v_add_f32_e64 v80, v98, -v110
	v_add_f32_e64 v81, v99, -v111
	v_add_f32_e64 v82, v100, -v112
	v_add_f32_e64 v83, v101, -v113
	v_add_f32 v86, v114, v116
	v_add_f32 v87, v115, v117
	v_add_f32 v90, v42, v50
	v_add_f32 v91, v43, v51
	v_add_f32 v92, v44, v52
	v_add_f32 v93, v45, v53
	v_add_f32 v94, v46, v54
	v_add_f32 v95, v47, v55
	v_pk_mov_b32 v[96:97], v[48:49], v[48:49] op_sel:[1,0]
	v_add_f32_e64 v44, v44, -v52
	v_add_f32_e64 v45, v45, -v53
	v_mov_b32_e32 v52, v46
	v_mov_b32_e32 v53, v43
	v_mov_b32_e32 v104, v54
	v_mov_b32_e32 v105, v51
	v_mov_b32_e32 v106, v42
	v_mov_b32_e32 v107, v46
	v_mov_b32_e32 v108, v50
	v_mov_b32_e32 v109, v54
	v_mov_b32_e32 v110, v43
	v_mov_b32_e32 v111, v47
	v_mov_b32_e32 v112, v51
	v_mov_b32_e32 v113, v55
	v_pk_mov_b32 v[42:43], v[46:47], v[42:43] op_sel:[1,0]
	v_pk_mov_b32 v[46:47], v[54:55], v[50:51] op_sel:[1,0]
	s_mov_b32 s50, s27
	s_mov_b32 s51, s26
	s_mov_b32 s52, s25
	s_mov_b32 s53, s24
	v_add_f32 v98, v6, v49
	v_add_f32 v99, v7, v48
	v_add_f32_e64 v253, v6, -v49
	v_add_f32_e64 v49, v7, -v48
	v_mov_b32_e32 v48, v253
	v_add_f32_e64 v100, v114, -v116
	v_add_f32_e64 v101, v115, -v117
	v_mul_f32 v50, v88, v68
	v_mul_f32 v51, v89, v69
	v_mul_f32 v54, v4, v68
	v_mul_f32 v55, v5, v69
	v_mul_f32 v114, v68, v68
	v_mul_f32 v115, v69, v69
	v_mul_f32 v116, v85, v68
	v_mul_f32 v117, v84, v69
	v_add_f32_e32 v7, v78, v79
	v_sub_f32_e32 v97, v76, v77
	v_mov_b32_e32 v152, v82
	v_mov_b32_e32 v153, v80
	v_mov_b32_e32 v154, v83
	v_mov_b32_e32 v155, v81
	v_add_f32 v156, v86, v92
	v_add_f32 v157, v87, v93
	v_add_f32 v162, v74, v75
	v_add_f32 v163, v74, v75
	v_add_f32_e64 v164, v72, -v73
	v_add_f32_e64 v165, v72, -v73
	v_add_f32 v253, v82, v83
	v_add_f32 v83, v82, v83
	v_mov_b32_e32 v82, v253
	v_add_f32_e64 v52, v52, -v104
	v_add_f32_e64 v53, v53, -v105
	v_add_f32_e64 v104, v106, -v108
	v_add_f32_e64 v105, v107, -v109
	v_add_f32_e64 v106, v110, -v112
	v_add_f32_e64 v107, v111, -v113
	v_add_f32_e64 v42, v42, -v46
	v_add_f32_e64 v43, v43, -v47
	v_fma_f32 v46, v44, 0, v45
	v_fma_f32 v47, v45, 0, v44
	v_fma_f32 v253, v44, 0, -v45
	v_fma_f32 v45, v45, 0, -v44
	v_mov_b32_e32 v44, v253
	v_mov_b32_e32 v108, v74
	v_mov_b32_e32 v109, v78
	v_mov_b32_e32 v78, v75
	v_mov_b32_e32 v74, v72
	v_mov_b32_e32 v75, v76
	v_mov_b32_e32 v76, v73
	v_add_f32_e64 v72, v86, -v92
	v_add_f32_e64 v73, v87, -v93
	v_add_f32_e64 v86, v90, -v94
	v_add_f32_e64 v87, v91, -v95
	s_mov_b32 s58, s26
	s_mov_b32 s59, s24
	v_add_f32 v158, v90, v94
	v_add_f32 v159, v91, v95
	v_add_f32_e64 v253, v80, -v81
	v_add_f32_e64 v81, v80, -v81
	v_mov_b32_e32 v80, v253
; FFT_HD cf2 mk2(float x, float y) { return (cf2){x, y}; }
; FFT_HD cf2 cmul(cf2 a, cf2 b) { return mk2(a.x * b.x - a.y * b.y, a.x * b.y + a.y * b.x); }
; FFT_HD cf2 cadd(cf2 a, cf2 b) { return mk2(a.x + b.x, a.y + b.y); }
; FFT_HD cf2 csub(cf2 a, cf2 b) { return mk2(a.x - b.x, a.y - b.y); }
; template <bool INV> FFT_HD void dft4(cf2& a, cf2& b, cf2& c, cf2& d) {
;     const cf2 s0 = cadd(a, c), s1 = csub(a, c), s2 = cadd(b, d), s3 = csub(b, d);
;     a = cadd(s0, s2); c = csub(s0, s2);
;     const cf2 r = INV ? mk2(-s3.y, s3.x) : mk2(s3.y, -s3.x);
;     b = cadd(s1, r); d = csub(s1, r);
; }
; template <bool INV> FFT_HD void dft16(cf2 (&x)[16]) {
;     const float C1 = 0.9238795325112867f, S1 = 0.3826834323650898f, H = 0.7071067811865476f;
; #pragma unroll
;     for (int b = 0; b < 4; ++b) dft4<INV>(x[b], x[4 + b], x[8 + b], x[12 + b]);
;     const float s = INV ? -1.f : 1.f;
;     x[4 + 1] = cmul(x[4 + 1], mk2(C1, -s * S1)); x[8 + 1] = cmul(x[8 + 1], mk2(H, -s * H));   x[12 + 1] = cmul(x[12 + 1], mk2(S1, -s * C1));
;     x[4 + 2] = cmul(x[4 + 2], mk2(H, -s * H));   x[8 + 2] = cmul(x[8 + 2], mk2(0.f, -s));     x[12 + 2] = cmul(x[12 + 2], mk2(-H, -s * H));
;     x[4 + 3] = cmul(x[4 + 3], mk2(S1, -s * C1)); x[8 + 3] = cmul(x[8 + 3], mk2(-H, -s * H));  x[12 + 3] = cmul(x[12 + 3], mk2(-C1, s * S1));
; #pragma unroll
;     for (int c = 0; c < 4; ++c) dft4<INV>(x[4 * c], x[4 * c + 1], x[4 * c + 2], x[4 * c + 3]);
; #pragma unroll
;     for (int c = 0; c < 4; ++c)
; #pragma unroll
;         for (int d = c + 1; d < 4; ++d) { const cf2 t = x[4 * c + d]; x[4 * c + d] = x[4 * d + c]; x[4 * d + c] = t; }
; }
	v_pk_mov_b32 v[90:91], v[114:115], v[116:117] op_sel:[1,0]
	v_mov_b32_e32 v115, v116
	v_mov_b32_e32 v92, v54
	v_mov_b32_e32 v93, v51
	v_pk_mov_b32 v[50:51], v[54:55], v[50:51] op_sel:[1,0]
	v_mul_f32_e32 v7, 0x3f3504f3, v7
	v_add_f32_e64 v54, v152, -v154
	v_add_f32_e64 v55, v153, -v155
	v_add_f32 v94, v152, v154
	v_add_f32 v95, v153, v155
	v_mul_f32_e64 v112, v162, s26
	v_mul_f32_e64 v113, v163, s27
	v_mul_f32_e64 v82, v82, s50
	v_mul_f32_e64 v83, v83, s51
	v_mov_b32_e32 v47, v45
	v_mul_f32_e64 v44, v106, s52
	v_mul_f32_e64 v45, v107, s53
	v_mul_f32_e64 v42, v42, s24
	v_mul_f32_e64 v43, v43, s25
	v_add_f32_e64 v78, v108, -v78
	v_add_f32_e64 v79, v109, -v79
	v_add_f32 v74, v74, v76
	v_add_f32 v75, v75, v77
	v_add_f32 v76, v72, v87
	v_add_f32 v77, v73, v86
	v_add_f32_e64 v72, v72, -v87
	v_add_f32_e64 v73, v73, -v86
	s_mov_b32 s56, s27
	s_mov_b32 s57, s24
	s_mov_b32 s28, s25
	v_add_f32 v110, v156, v158
	v_add_f32 v111, v157, v159
	v_add_f32_e64 v86, v156, -v158
	v_add_f32_e64 v87, v157, -v159
	v_add_f32_e64 v106, v90, -v114
	v_add_f32_e64 v107, v91, -v115
	v_add_f32 v90, v90, v114
	v_add_f32 v91, v91, v115
	v_add_f32_e64 v108, v92, -v50
	v_add_f32_e64 v109, v93, -v51
	v_add_f32 v50, v92, v50
	v_add_f32 v51, v93, v51
	v_mov_b32_e32 v55, v95
	v_mul_f32_e32 v60, 0x3ec3ef15, v95
	v_mul_f32_e32 v158, 0x3ec3ef15, v54
	v_mul_f32_e32 v159, 0x3f6c835e, v95
	v_fma_f32 v92, v164, s50, v112
	v_fma_f32 v93, v165, s51, v113
	v_fma_f32 v94, v164, s50, -v112
	v_fma_f32 v95, v165, s51, -v113
	v_fma_f32 v114, v97, s25, -v7
	v_fma_f32 v116, v80, s26, v82
	v_fma_f32 v117, v81, s27, v83
	v_fma_f32 v80, v80, s26, -v82
	v_fma_f32 v81, v81, s27, -v83
	v_fma_f32 v42, v52, s24, -v42
	v_fma_f32 v43, v53, s25, -v43
	v_fma_f32 v44, v104, s52, v44
	v_fma_f32 v45, v105, s53, v45
	v_pk_mov_b32 v[82:83], v[78:79], v[74:75] op_sel:[1,0]
	v_mul_f32_e64 v104, v74, s58
	v_mul_f32_e64 v105, v75, s59
	v_pk_mov_b32 v[74:75], v[74:75], v[78:79] op_sel:[1,0]
	v_pk_mov_b32 v[154:155], v[72:73], v[76:77] op_sel:[1,0]
	s_mov_b32 s54, s24
	s_mov_b32 s55, s27
	v_mov_b32_e32 v56, v5
	v_pk_mov_b32 v[70:71], v[84:85], v[102:103] op_sel:[1,0]
	v_mov_b32_e32 v160, v98
	v_mov_b32_e32 v161, v49
	v_fmamk_f32 v112, v97, 0x3f3504f3, v7
	v_add_f32 v52, v100, v46
	v_add_f32 v53, v101, v47
	v_mov_b32_e32 v152, v76
	v_mov_b32_e32 v153, v73
	v_add_f32_e64 v46, v100, -v46
	v_add_f32_e64 v47, v101, -v47
	v_mov_b32_e32 v100, v106
	v_mov_b32_e32 v101, v91
	v_fma_f32 v54, v54, s30, -v60
	v_fma_f32 v55, v55, s31, -v60
	v_mov_b32_e32 v94, v92
	v_mov_b32_e32 v115, v114
	v_mov_b32_e32 v113, v114
	v_mov_b32_e32 v80, v116
	v_pk_mov_b32 v[48:49], v[48:49], v[92:93] op_sel:[1,0]
	v_add_f32 v92, v44, v42
	v_add_f32 v93, v45, v43
	v_mul_f32_e64 v74, v74, s28
	v_mul_f32_e64 v75, v75, s29
	v_fma_f32 v78, v78, s56, v104
	v_fma_f32 v79, v79, s57, v105
	v_mov_b32_e32 v7, v158
	v_mov_b32_e32 v97, v159
	v_pk_mov_b32 v[104:105], v[90:91], v[106:107] op_sel:[1,0]
	v_mul_f32 v154, v91, v154
	v_mul_f32 v155, v91, v155
	v_pk_mov_b32 v[158:159], v[42:43], v[44:45] op_sel:[1,0]
	v_pk_mov_b32 v[42:43], v[44:45], v[42:43] op_sel:[1,0]
	v_pk_mov_b32 v[156:157], v[50:51], v[108:109] op_sel:[1,0]
	v_mul_f32 v44, v70, v100
	v_mul_f32 v45, v71, v101
	v_mul_f32 v70, v68, v100
	v_mul_f32 v71, v69, v101
	v_mul_f32 v164, v100, v100
	v_mul_f32 v165, v101, v101
	v_mul_f32 v253, v100, v91
	v_mul_f32 v91, v101, v90
	v_mov_b32_e32 v90, v253
	v_add_f32 v160, v160, v112
	v_add_f32 v161, v161, v113
	v_add_f32 v166, v94, v80
	v_add_f32 v167, v95, v81
	v_pk_mov_b32 v[114:115], v[114:115], v[116:117] op_sel:[1,0]
	v_mov_b32_e32 v94, v98
	v_mov_b32_e32 v113, v81
	v_add_f32 v80, v52, v92
	v_add_f32 v81, v53, v93
	v_fma_f32 v74, v82, s54, v74
	v_fma_f32 v75, v83, s55, v75
	v_add_f32_e64 v6, v6, -v96
	v_add_f32_e64 v7, v7, -v97
	v_mov_b32_e32 v98, v54
	v_fma_f32 v82, v106, v76, -v154
	v_fma_f32 v83, v107, v77, -v155
	v_fma_f32 v96, v106, v152, v154
	v_fma_f32 v97, v106, v153, v155
	v_mul_f32 v104, v56, v104
	v_mul_f32 v105, v56, v105
	v_add_f32_e64 v42, v158, -v42
	v_add_f32_e64 v43, v159, -v43
	ds_write_b64 v65, v[110:111]
	v_mov_b32_e32 v110, v108
	v_mov_b32_e32 v111, v51
	v_mul_f32 v156, v100, v156
	v_mul_f32 v157, v101, v157
	v_add_f32_e64 v52, v52, -v92
	v_add_f32_e64 v53, v53, -v93
	v_mov_b32_e32 v91, v164
	v_mov_b32_e32 v164, v90
	v_add_f32_e64 v48, v48, -v114
	v_add_f32_e64 v49, v49, -v115
	v_add_f32_e64 v92, v94, -v112
	v_add_f32_e64 v93, v95, -v113
	v_add_f32 v94, v160, v166
	v_add_f32 v95, v161, v167
	v_mul_f32 v103, v102, v80
	v_mul_f32 v102, v102, v81
	v_add_f32 v106, v74, v6
	v_add_f32 v107, v75, v7
	v_add_f32 v112, v78, v98
	v_add_f32 v113, v79, v99
	v_mov_b32_e32 v83, v97
	v_fma_f32 v96, v4, v100, v104
	v_fma_f32 v97, v4, v101, v105
	v_fma_f32 v104, v4, v100, -v104
	v_fma_f32 v105, v4, v101, -v105
	v_add_f32 v114, v46, v42
	v_add_f32 v115, v47, v43
	v_add_f32_e64 v42, v46, -v42
	v_add_f32_e64 v43, v47, -v43
	v_add_f32 v46, v70, v71
	v_add_f32 v47, v70, v71
	v_pk_mov_b32 v[70:71], v[74:75], v[78:79] op_sel:[1,0]
	v_pk_mov_b32 v[54:55], v[6:7], v[54:55] op_sel:[1,0]
	v_mov_b32_e32 v7, v99
	v_mov_b32_e32 v75, v79
	v_mul_f32 v162, v100, v110
	v_mul_f32 v163, v101, v111
	v_add_f32_e64 v98, v156, -v157
	v_add_f32_e64 v99, v156, -v157
	v_add_f32_e64 v116, v160, -v166
	v_add_f32_e64 v117, v161, -v167
	v_add_f32 v152, v90, v164
	v_add_f32 v153, v91, v165
	v_add_f32_e64 v90, v90, -v164
	v_add_f32_e64 v91, v91, -v165
	v_mul_f32 v154, v56, v94
	v_mul_f32 v155, v56, v95
	v_fma_f32 v156, v85, v80, -v102
	v_fma_f32 v157, v85, v81, -v103
	v_fma_f32 v80, v85, v80, v102
	v_fma_f32 v81, v85, v81, v103
	v_add_f32 v84, v112, v106
	v_add_f32 v85, v113, v107
; FFT_HD cf2 mk2(float x, float y) { return (cf2){x, y}; }
; FFT_HD cf2 cmul(cf2 a, cf2 b) { return mk2(a.x * b.x - a.y * b.y, a.x * b.y + a.y * b.x); }
; template <bool INV> FFT_HD void dft16(cf2 (&x)[16]) {
;     const float C1 = 0.9238795325112867f, S1 = 0.3826834323650898f, H = 0.7071067811865476f;
; #pragma unroll
;     for (int b = 0; b < 4; ++b) dft4<INV>(x[b], x[4 + b], x[8 + b], x[12 + b]);
;     const float s = INV ? -1.f : 1.f;
;     x[4 + 1] = cmul(x[4 + 1], mk2(C1, -s * S1)); x[8 + 1] = cmul(x[8 + 1], mk2(H, -s * H));   x[12 + 1] = cmul(x[12 + 1], mk2(S1, -s * C1));
;     x[4 + 2] = cmul(x[4 + 2], mk2(H, -s * H));   x[8 + 2] = cmul(x[8 + 2], mk2(0.f, -s));     x[12 + 2] = cmul(x[12 + 2], mk2(-H, -s * H));
;     x[4 + 3] = cmul(x[4 + 3], mk2(S1, -s * C1)); x[8 + 3] = cmul(x[8 + 3], mk2(-H, -s * H));  x[12 + 3] = cmul(x[12 + 3], mk2(-C1, s * S1));
; #pragma unroll
;     for (int c = 0; c < 4; ++c) dft4<INV>(x[4 * c], x[4 * c + 1], x[4 * c + 2], x[4 * c + 3]);
; #pragma unroll
;     for (int c = 0; c < 4; ++c)
; #pragma unroll
;         for (int d = c + 1; d < 4; ++d) { const cf2 t = x[4 * c + d]; x[4 * c + d] = x[4 * d + c]; x[4 * d + c] = t; }
; }
; template <bool INV, int lS, class ZP> FFT_HD void fft_r16_pass(ZP z, int tid) {
;     ...
;             if (!INV) {
; #pragma unroll
;                 for (int j = 1; j < 16; ++j) x[j] = cmul(x[j], tw[j]);
;             }
; #pragma unroll
;             for (int j = 0; j < 16; ++j) z[pb + j * STEP] = x[j];
;         }
	v_mov_b32_e32 v102, v96
	v_mov_b32_e32 v103, v105
	v_pk_mov_b32 v[104:105], v[104:105], v[96:97] op_sel:[1,0]
	v_add_f32_e64 v160, v48, -v49
	v_add_f32_e64 v161, v48, -v49
	v_pk_mov_b32 v[164:165], v[42:43], v[114:115] op_sel:[1,0]
	v_add_f32_e64 v54, v70, -v54
	v_add_f32_e64 v55, v71, -v55
	v_add_f32_e64 v6, v6, -v74
	v_add_f32_e64 v7, v7, -v75
	v_mov_b32_e32 v70, v106
	v_mov_b32_e32 v71, v113
	v_mov_b32_e32 v113, v107
	v_add_f32_e64 v253, v44, -v45
	v_add_f32_e64 v45, v44, -v45
	v_mov_b32_e32 v44, v253
	v_add_f32 v78, v162, v163
	v_add_f32 v79, v162, v163
	v_add_f32 v158, v92, v93
	v_add_f32 v159, v92, v93
	v_mov_b32_e32 v162, v114
	v_mov_b32_e32 v163, v43
	v_add_f32_e64 v74, v92, -v93
	v_add_f32_e64 v75, v92, -v93
	ds_write_b64 v65, v[82:83] offset:33792
	v_mov_b32_e32 v82, v152
	v_mov_b32_e32 v83, v91
	v_pk_mov_b32 v[92:93], v[90:91], v[152:153] op_sel:[1,0]
	v_fma_f32 v106, v4, v94, v155
	v_fma_f32 v107, v5, v95, v154
	v_fma_f32 v94, v4, v94, -v155
	v_fma_f32 v95, v4, v95, -v154
	v_mov_b32_e32 v157, v81
	v_mul_f32 v80, v108, v85
	v_mul_f32 v81, v108, v84
	v_mul_f32 v104, v104, v160
	v_mul_f32 v105, v105, v161
	v_mul_f32 v108, v46, v164
	v_mul_f32 v109, v47, v165
	v_add_f32 v154, v6, v54
	v_add_f32 v155, v7, v55
	v_add_f32_e64 v6, v6, -v54
	v_add_f32_e64 v7, v7, -v55
	v_mul_f32 v54, v152, v86
	v_mul_f32 v55, v152, v87
	v_add_f32_e64 v70, v70, -v112
	v_add_f32_e64 v71, v71, -v113
	v_mul_f32 v112, v100, v152
	v_mul_f32 v113, v101, v152
	v_mul_f32 v153, v152, v103
	v_mul_f32 v152, v152, v102
	v_mul_f32 v4, v4, v82
	v_mul_f32 v5, v5, v83
	v_mul_f32 v160, v68, v82
	v_mul_f32 v161, v69, v83
	v_mul_f32 v68, v68, v92
	v_mul_f32 v69, v69, v93
	v_mul_f32 v164, v110, v82
	v_mul_f32 v165, v111, v83
	v_mul_f32 v92, v110, v92
	v_mul_f32 v93, v111, v93
	v_mov_b32_e32 v107, v95
	v_fma_f32 v94, v51, v84, -v80
	v_fma_f32 v95, v51, v85, -v81
	v_fma_f32 v50, v51, v84, v80
	v_fma_f32 v51, v51, v85, v81
	v_fma_f32 v80, v96, v158, -v104
	v_fma_f32 v81, v97, v159, -v105
	v_fma_f32 v84, v102, v158, v104
	v_fma_f32 v85, v103, v159, v105
	v_fma_f32 v96, v44, v114, -v108
	v_fma_f32 v97, v45, v115, -v109
	v_fma_f32 v104, v44, v162, v108
	v_fma_f32 v105, v45, v163, v109
	v_pk_mov_b32 v[110:111], v[6:7], v[154:155] op_sel:[1,0]
	v_fma_f32 v158, v91, v86, -v55
	v_fma_f32 v159, v91, v87, -v54
	v_fma_f32 v253, v91, v86, v55
	v_fma_f32 v55, v91, v87, v54
	v_mov_b32_e32 v54, v253
	v_fma_f32 v86, v100, v91, -v113
	v_fma_f32 v87, v101, v91, -v112
	v_fma_f32 v100, v100, v91, v113
	v_fma_f32 v101, v101, v91, v112
	v_fma_f32 v112, v91, v102, -v153
	v_fma_f32 v113, v91, v103, -v152
	v_fma_f32 v90, v91, v102, v153
	v_fma_f32 v91, v91, v103, v152
	v_mul_f32 v44, v82, v44
	v_mul_f32 v45, v83, v45
	v_mul_f32 v102, v82, v98
	v_mul_f32 v103, v83, v99
	v_add_f32 v253, v48, v49
	v_add_f32 v49, v48, v49
	v_mov_b32_e32 v48, v253
	v_mul_f32 v88, v88, v82
	v_mul_f32 v89, v89, v83
	v_mov_b32_e32 v108, v154
	v_mov_b32_e32 v109, v7
	v_mov_b32_e32 v95, v51
	v_mov_b32_e32 v97, v105
	v_mul_f32 v50, v78, v110
	v_mul_f32 v51, v79, v111
	v_add_f32_e64 v253, v4, -v5
	v_add_f32_e64 v5, v4, -v5
	v_mov_b32_e32 v4, v253
	v_mov_b32_e32 v105, v101
	v_pk_mov_b32 v[100:101], v[100:101], v[86:87] op_sel:[1,0]
	v_mov_b32_e32 v111, v91
	v_pk_mov_b32 v[90:91], v[90:91], v[112:113] op_sel:[1,0]
	v_fma_f32 v152, -v82, v46, v45
	v_fma_f32 v153, -v83, v47, v44
	v_fma_f32 v253, v82, v46, v45
	v_fma_f32 v45, v83, v47, v44
	v_mov_b32_e32 v44, v253
	v_fma_f32 v46, -v82, v78, v103
	v_fma_f32 v47, -v83, v79, v102
	v_fma_f32 v78, v82, v78, v103
	v_fma_f32 v79, v83, v79, v102
	v_mov_b32_e32 v81, v85
	v_mov_b32_e32 v159, v55
	v_add_f32 v54, v89, v88
	v_add_f32 v55, v89, v88
	v_add_f32 v253, v68, v69
	v_add_f32 v69, v68, v69
	v_mov_b32_e32 v68, v253
	v_add_f32 v88, v92, v93
	v_add_f32 v89, v92, v93
	v_mov_b32_e32 v104, v86
	v_mov_b32_e32 v110, v112
	v_fma_f32 v82, v98, v154, -v50
	v_fma_f32 v83, v99, v155, -v51
	v_fma_f32 v50, v98, v108, v50
	v_fma_f32 v51, v99, v109, v51
	v_mul_f32 v4, v4, v117
	v_mul_f32 v5, v5, v116
	v_mul_f32 v76, v100, v77
	v_mul_f32 v77, v101, v77
	v_mul_f32 v48, v90, v48
	v_mul_f32 v49, v91, v49
	v_mov_b32_e32 v91, v45
	v_pk_mov_b32 v[44:45], v[44:45], v[152:153] op_sel:[1,0]
	v_mov_b32_e32 v99, v79
	v_pk_mov_b32 v[78:79], v[78:79], v[46:47] op_sel:[1,0]
	ds_write_b64 v65, v[156:157] offset:16896
	v_add_f32_e64 v84, v161, -v160
	v_add_f32_e64 v85, v161, -v160
	v_add_f32_e64 v92, v165, -v164
	v_add_f32_e64 v93, v165, -v164
	ds_write_b64 v65, v[106:107] offset:8448
	v_mul_f32 v68, v68, v53
	v_mul_f32 v69, v69, v52
	v_mul_f32 v88, v88, v71
	v_mul_f32 v89, v89, v70
	v_mov_b32_e32 v90, v152
	v_mov_b32_e32 v98, v46
	ds_write_b64 v65, v[94:95] offset:25344
	ds_write_b64 v65, v[80:81] offset:42240
	ds_write_b64 v65, v[96:97] offset:50688
	ds_write_b64 v67, v[158:159]
	v_mov_b32_e32 v83, v51
	v_fma_f32 v50, v54, v116, -v4
	v_fma_f32 v51, v55, v117, -v5
	v_fma_f32 v4, v54, v116, v4
	v_fma_f32 v5, v55, v117, v5
	v_fma_f32 v80, v86, v72, -v76
	v_fma_f32 v81, v87, v73, -v77
	v_fma_f32 v73, v105, v72, v77
	v_fma_f32 v72, v104, v72, v76
	v_fma_f32 v76, v112, v74, -v48
	v_fma_f32 v77, v113, v75, -v49
	v_fma_f32 v48, v110, v74, v48
	v_fma_f32 v49, v111, v75, v49
	v_mul_f32 v44, v44, v115
	v_mul_f32 v45, v45, v115
	v_mul_f32 v74, v78, v155
	v_mul_f32 v75, v79, v155
	s_movk_i32 s1, 0x200
	s_and_b64 vcc, exec, s[44:45]
	s_mov_b64 s[44:45], 0
	v_fma_f32 v54, v84, v52, -v68
	v_fma_f32 v55, v85, v53, -v69
	v_fma_f32 v52, v84, v52, v68
	v_fma_f32 v53, v85, v53, v69
	v_fma_f32 v68, v92, v70, -v88
	v_fma_f32 v69, v93, v71, -v89
	v_fma_f32 v70, v92, v70, v88
	v_fma_f32 v71, v93, v71, v89
	v_mov_b32_e32 v51, v5
	v_fma_f32 v4, v152, v42, -v44
	v_fma_f32 v5, v153, v43, -v45
	v_fma_f32 v43, v91, v42, v45
	v_fma_f32 v42, v90, v42, v44
	v_fma_f32 v44, v46, v6, -v74
	v_fma_f32 v45, v47, v7, -v75
	v_fma_f32 v7, v99, v6, v75
	v_fma_f32 v6, v98, v6, v74
	v_mov_b32_e32 v55, v53
	v_mov_b32_e32 v69, v71
	v_mov_b32_e32 v81, v73
	v_mov_b32_e32 v77, v49
	ds_write_b64 v65, v[82:83] offset:59136
	v_mov_b32_e32 v5, v43
	v_mov_b32_e32 v45, v7
	ds_write_b64 v168, v[50:51]
	ds_write_b64 v169, v[54:55]
	ds_write_b64 v170, v[68:69]
	ds_write_b64 v171, v[80:81]
	ds_write_b64 v172, v[76:77]
	ds_write_b64 v173, v[4:5]
	ds_write_b64 v174, v[44:45]
	s_cbranch_vccnz .LBB0_566
; __device__ __forceinline__ unsigned cvt_pk_bf16(float lo, float hi) { unsigned r; asm volatile("v_cvt_pk_bf16_f32 %0, %1, %2" : "=v"(r) : "v"(lo), "v"(hi)); return r; }
; template <int BANK, int WAITN> __device__ __forceinline__ void bg_finish1(BgState& b) {
;     if (WAITN == 32) asm volatile("s_waitcnt vmcnt(32)" ::: "memory"); else asm volatile("s_waitcnt vmcnt(0)" ::: "memory");
;     asm volatile("" : BG_TIE16(BANK * 32) :: "memory");
;     asm volatile("" : BG_TIE16(BANK * 32 + 16) :: "memory");
;     bf16_t* dst = b.dst[BANK];
;     if (dst != nullptr) {
; #pragma unroll
;         for (int c = 0; c < 4; ++c) { u32x4 w;
;             w.x = cvt_pk_bf16(b.r[(BANK * 8 + 0) * 4 + c], b.r[(BANK * 8 + 1) * 4 + c]); w.y = cvt_pk_bf16(b.r[(BANK * 8 + 2) * 4 + c], b.r[(BANK * 8 + 3) * 4 + c]);
;             w.z = cvt_pk_bf16(b.r[(BANK * 8 + 4) * 4 + c], b.r[(BANK * 8 + 5) * 4 + c]); w.w = cvt_pk_bf16(b.r[(BANK * 8 + 6) * 4 + c], b.r[(BANK * 8 + 7) * 4 + c]);
;             bf16_t* dp = dst + (c & 1) * 512 + (c >> 1) * b.o2[BANK];
;             asm volatile("global_store_dwordx4 %0, %1, off\n\ts_nop 1" :: "v"(dp), "v"(w) : "memory"); }
;     }
; }
	s_waitcnt lgkmcnt(0)
	s_barrier
	s_waitcnt vmcnt(32)
	v_cmp_ne_u64_e32 vcc, 0, v[2:3]
	s_and_saveexec_b64 s[44:45], vcc
	s_cbranch_execz .LBB0_569
	v_cvt_pk_bf16_f32 v4, v32, v36
	v_cvt_pk_bf16_f32 v5, v33, v38
	v_cvt_pk_bf16_f32 v6, v37, v40
	v_cvt_pk_bf16_f32 v7, v39, v41
	s_lshl_b32 s12, s48, 1
	global_store_dwordx4 v[2:3], v[4:7], off nt
	s_nop 1
	v_cvt_pk_bf16_f32 v4, v24, v26
	v_cvt_pk_bf16_f32 v5, v25, v28
	v_cvt_pk_bf16_f32 v6, v27, v30
	v_cvt_pk_bf16_f32 v7, v29, v31
	v_lshl_add_u64 v[24:25], v[2:3], 0, s[22:23]
	global_store_dwordx4 v[24:25], v[4:7], off nt
	s_nop 1
	v_cvt_pk_bf16_f32 v4, v16, v18
	v_cvt_pk_bf16_f32 v5, v17, v20
	v_cvt_pk_bf16_f32 v6, v19, v22
	v_cvt_pk_bf16_f32 v7, v21, v23
	v_lshl_add_u64 v[2:3], v[2:3], 0, s[12:13]
	global_store_dwordx4 v[2:3], v[4:7], off nt
	s_nop 1
	v_cvt_pk_bf16_f32 v2, v8, v10
	v_cvt_pk_bf16_f32 v3, v9, v12
	v_cvt_pk_bf16_f32 v4, v11, v14
	v_cvt_pk_bf16_f32 v5, v13, v15
	v_lshl_add_u64 v[6:7], v[24:25], 0, s[12:13]
	global_store_dwordx4 v[6:7], v[2:5], off nt
	s_nop 1

; __device__ __forceinline__ KP kparams() { KP q = (KP)__builtin_amdgcn_kernarg_segment_ptr(); asm volatile("" : "+s"(q)); return q; }
; FFT_HD cf2 mk2(float x, float y) { return (cf2){x, y}; }
; FFT_HD void fft_sincos(float frac, float& s, float& c) { s = __builtin_amdgcn_sinf(frac); c = __builtin_amdgcn_cosf(frac); }
; FFT_HD cf2 cmul(cf2 a, cf2 b) { return mk2(a.x * b.x - a.y * b.y, a.x * b.y + a.y * b.x); }
; template <int BANK> __device__ __forceinline__ void bg_issue1(BgState& b, int wg, int NW, int lane) {
;     KP kp = kparams();
;     const float* src; int ldS; bf16_t* dst; int o2;
;     bg_decode(b.st, wg, NW, lane, kp, src, ldS, dst, o2);
;     b.dst[BANK] = dst; b.o2[BANK] = o2;
;     asm volatile("s_nop 6" ::: "memory");
; #pragma unroll
;     for (int i = 0; i < 8; ++i) { const float* p = src + (size_t)i * ldS;
;         asm volatile("global_load_dword %0, %4, off\n\tglobal_load_dword %1, %4, off offset:256\n\tglobal_load_dword %2, %4, off offset:512\n\tglobal_load_dword %3, %4, off offset:768"
;                      : "=&v"(b.r[(BANK * 8 + i) * 4 + 0]), "=&v"(b.r[(BANK * 8 + i) * 4 + 1]), "=&v"(b.r[(BANK * 8 + i) * 4 + 2]), "=&v"(b.r[(BANK * 8 + i) * 4 + 3]) : "v"(p) : "memory"); }
;     b.st += 1;
; }
; FFT_HD void fft_gen_tw(float frac, cf2 (&tw)[16]) {
;     float sn, cs; fft_sincos(frac, sn, cs);
;     tw[1] = mk2(cs, -sn);
;     tw[2] = cmul(tw[1], tw[1]); tw[3] = cmul(tw[2], tw[1]); tw[4] = cmul(tw[2], tw[2]); tw[5] = cmul(tw[4], tw[1]); tw[6] = cmul(tw[4], tw[2]); tw[7] = cmul(tw[4], tw[3]);
;     tw[8] = cmul(tw[4], tw[4]);
; #pragma unroll
;     for (int j = 9; j < 16; ++j) tw[j] = cmul(tw[8], tw[j - 8]);
; }
.LBB0_579:
	s_nop 6
	s_lshl_b32 s12, s48, 2
	global_load_dword v176, v[2:3], off nt
	global_load_dword v168, v[2:3], off offset:256 nt
	global_load_dword v160, v[2:3], off offset:512 nt
	global_load_dword v152, v[2:3], off offset:768 nt
	v_lshl_add_u64 v[2:3], v[2:3], 0, s[12:13]
	v_and_b32_e32 v14, 63, v57
	global_load_dword v178, v[2:3], off nt
	global_load_dword v170, v[2:3], off offset:256 nt
	global_load_dword v162, v[2:3], off offset:512 nt
	global_load_dword v154, v[2:3], off offset:768 nt
	v_lshl_add_u64 v[2:3], v[2:3], 0, s[12:13]
	v_cvt_f32_ubyte0_e32 v4, v14
	global_load_dword v177, v[2:3], off nt
	global_load_dword v169, v[2:3], off offset:256 nt
	global_load_dword v161, v[2:3], off offset:512 nt
	global_load_dword v153, v[2:3], off offset:768 nt
	v_lshl_add_u64 v[2:3], v[2:3], 0, s[12:13]
	v_mul_f32_e32 v4, 0x3a800000, v4
	global_load_dword v180, v[2:3], off nt
	global_load_dword v172, v[2:3], off offset:256 nt
	global_load_dword v164, v[2:3], off offset:512 nt
	global_load_dword v156, v[2:3], off offset:768 nt
	v_lshl_add_u64 v[2:3], v[2:3], 0, s[12:13]
	v_sin_f32_e32 v39, v4
	v_cos_f32_e32 v38, v4
	global_load_dword v179, v[2:3], off nt
	global_load_dword v171, v[2:3], off offset:256 nt
	global_load_dword v163, v[2:3], off offset:512 nt
	global_load_dword v155, v[2:3], off offset:768 nt
	v_lshl_add_u64 v[2:3], v[2:3], 0, s[12:13]
	global_load_dword v181, v[2:3], off nt
	global_load_dword v173, v[2:3], off offset:256 nt
	global_load_dword v165, v[2:3], off offset:512 nt
	global_load_dword v157, v[2:3], off offset:768 nt
	v_lshl_add_u64 v[2:3], v[2:3], 0, s[12:13]
	global_load_dword v182, v[2:3], off nt
	global_load_dword v174, v[2:3], off offset:256 nt
	global_load_dword v166, v[2:3], off offset:512 nt
	global_load_dword v158, v[2:3], off offset:768 nt
	v_lshl_add_u64 v[2:3], v[2:3], 0, s[12:13]
	global_load_dword v183, v[2:3], off nt
	global_load_dword v175, v[2:3], off offset:256 nt
	global_load_dword v167, v[2:3], off offset:512 nt
	global_load_dword v159, v[2:3], off offset:768 nt
	v_mul_f32 v2, v38, v38
	v_mul_f32 v3, v39, v39
	v_mul_f32_e64 v4, v38, -v39
	v_mov_b32_e32 v5, v2
	v_mov_b32_e32 v2, v4
	v_add_f32 v202, v4, v2
	v_add_f32 v203, v5, v3
	v_add_f32_e64 v204, v4, -v2
	v_add_f32_e64 v205, v5, -v3
	v_mov_b32_e32 v46, v202
	v_mov_b32_e32 v47, v205
	v_mul_f32 v8, v46, v46
	v_mul_f32 v9, v47, v47
	v_mul_f32 v10, v205, v46
	v_mul_f32 v11, v204, v47
	v_mov_b32_e32 v2, v39
	v_mov_b32_e32 v3, v38
	v_pk_mov_b32 v[12:13], v[8:9], v[10:11] op_sel:[1,0]
	v_mov_b32_e32 v9, v10
	v_mul_f32 v4, v2, v46
	v_mul_f32 v5, v3, v47
	v_mul_f32 v6, v38, v46
	v_mul_f32 v7, v39, v47
	v_add_f32_e64 v48, v12, -v8
	v_add_f32_e64 v49, v13, -v9
	v_add_f32 v68, v12, v8
	v_add_f32 v69, v13, v9
	v_mov_b32_e32 v50, v48
	v_mov_b32_e32 v51, v69
	v_mov_b32_e32 v8, v6
	v_mov_b32_e32 v9, v5
	v_pk_mov_b32 v[4:5], v[6:7], v[4:5] op_sel:[1,0]
	v_mul_f32 v6, v50, v69
	v_mul_f32 v7, v51, v68
	v_add_f32_e64 v72, v8, -v4
	v_add_f32_e64 v73, v9, -v5
	v_add_f32 v70, v8, v4
	v_add_f32 v71, v9, v5
	v_mul_f32 v4, v50, v50
	v_mul_f32 v5, v51, v51
	v_lshlrev_b32_e32 v184, 4, v57
	v_mov_b32_e32 v7, v4
	v_mov_b32_e32 v4, v6
	v_add_f32 v76, v6, v4
	v_add_f32 v77, v7, v5
	v_add_f32_e64 v74, v6, -v4
	v_add_f32_e64 v75, v7, -v5
	v_mov_b32_e32 v54, v76
	v_mov_b32_e32 v55, v75
	v_mul_f32 v86, v2, v54
	v_mul_f32 v87, v3, v55
	v_and_b32_e32 v2, 0xfffffc00, v184
	v_lshlrev_b32_e32 v4, 3, v2
	v_lshlrev_b32_e32 v5, 3, v14
	v_add_u32_e32 v3, 0x2000, v2
	v_add3_u32 v4, 0, v4, v5
	v_ashrrev_i32_e32 v2, 2, v2
	v_add_u32_e32 v238, v4, v2
	v_add_u32_e32 v239, 0x800, v238
	v_add_u32_e32 v240, 0x1000, v238
	v_add_u32_e32 v241, 0x1800, v238
	ds_read2_b64 v[98:101], v238 offset1:66
	ds_read2_b64 v[102:105], v238 offset0:132 offset1:198
	ds_read2_b64 v[106:109], v239 offset0:8 offset1:74
	ds_read2_b64 v[110:113], v239 offset0:140 offset1:206
	ds_read2_b64 v[114:117], v240 offset0:16 offset1:82
	ds_read2_b64 v[186:189], v240 offset0:148 offset1:214
	ds_read2_b64 v[190:193], v241 offset0:24 offset1:90
	ds_read2_b64 v[198:201], v241 offset0:156 offset1:222
	s_mov_b32 s48, s27
	s_waitcnt lgkmcnt(5)
	v_pk_mov_b32 v[206:207], v[100:101], v[108:109] op_sel:[1,0]
	s_waitcnt lgkmcnt(3)
	v_mov_b32_e32 v210, v116
	s_waitcnt lgkmcnt(1)
	v_pk_mov_b32 v[208:209], v[116:117], v[192:193] op_sel:[1,0]
	v_mov_b32_e32 v211, v193
	v_add_f32_e64 v206, v206, -v208
	v_add_f32_e64 v207, v207, -v209
	v_mov_b32_e32 v208, v100
	v_mov_b32_e32 v209, v109
	v_add_f32_e64 v208, v208, -v210
	v_add_f32_e64 v209, v209, -v211
	v_pk_mov_b32 v[210:211], v[102:103], v[110:111] op_sel:[1,0]
	s_waitcnt lgkmcnt(0)
; FFT_HD cf2 mk2(float x, float y) { return (cf2){x, y}; }
; FFT_HD void fft_sincos(float frac, float& s, float& c) { s = __builtin_amdgcn_sinf(frac); c = __builtin_amdgcn_cosf(frac); }
; FFT_HD cf2 cmul(cf2 a, cf2 b) { return mk2(a.x * b.x - a.y * b.y, a.x * b.y + a.y * b.x); }
; FFT_HD cf2 cadd(cf2 a, cf2 b) { return mk2(a.x + b.x, a.y + b.y); }
; FFT_HD cf2 csub(cf2 a, cf2 b) { return mk2(a.x - b.x, a.y - b.y); }
; template <bool INV> FFT_HD void dft4(cf2& a, cf2& b, cf2& c, cf2& d) {
;     const cf2 s0 = cadd(a, c), s1 = csub(a, c), s2 = cadd(b, d), s3 = csub(b, d);
;     a = cadd(s0, s2); c = csub(s0, s2);
;     const cf2 r = INV ? mk2(-s3.y, s3.x) : mk2(s3.y, -s3.x);
;     b = cadd(s1, r); d = csub(s1, r);
; }
; template <bool INV> FFT_HD void dft16(cf2 (&x)[16]) {
;     const float C1 = 0.9238795325112867f, S1 = 0.3826834323650898f, H = 0.7071067811865476f;
; #pragma unroll
;     for (int b = 0; b < 4; ++b) dft4<INV>(x[b], x[4 + b], x[8 + b], x[12 + b]);
;     const float s = INV ? -1.f : 1.f;
;     x[4 + 1] = cmul(x[4 + 1], mk2(C1, -s * S1)); x[8 + 1] = cmul(x[8 + 1], mk2(H, -s * H));   x[12 + 1] = cmul(x[12 + 1], mk2(S1, -s * C1));
;     x[4 + 2] = cmul(x[4 + 2], mk2(H, -s * H));   x[8 + 2] = cmul(x[8 + 2], mk2(0.f, -s));     x[12 + 2] = cmul(x[12 + 2], mk2(-H, -s * H));
;     x[4 + 3] = cmul(x[4 + 3], mk2(S1, -s * C1)); x[8 + 3] = cmul(x[8 + 3], mk2(-H, -s * H));  x[12 + 3] = cmul(x[12 + 3], mk2(-C1, s * S1));
; #pragma unroll
;     for (int c = 0; c < 4; ++c) dft4<INV>(x[4 * c], x[4 * c + 1], x[4 * c + 2], x[4 * c + 3]);
; #pragma unroll
;     for (int c = 0; c < 4; ++c)
; #pragma unroll
;         for (int d = c + 1; d < 4; ++d) { const cf2 t = x[4 * c + d]; x[4 * c + d] = x[4 * d + c]; x[4 * d + c] = t; }
; }
; FFT_HD void fft_gen_tw(float frac, cf2 (&tw)[16]) {
;     float sn, cs; fft_sincos(frac, sn, cs);
;     tw[1] = mk2(cs, -sn);
;     tw[2] = cmul(tw[1], tw[1]); tw[3] = cmul(tw[2], tw[1]); tw[4] = cmul(tw[2], tw[2]); tw[5] = cmul(tw[4], tw[1]); tw[6] = cmul(tw[4], tw[2]); tw[7] = cmul(tw[4], tw[3]);
;     tw[8] = cmul(tw[4], tw[4]);
; #pragma unroll
;     for (int j = 9; j < 16; ++j) tw[j] = cmul(tw[8], tw[j - 8]);
; }
	v_pk_mov_b32 v[212:213], v[186:187], v[198:199] op_sel:[1,0]
	v_mov_b32_e32 v214, v186
	v_add_f32_e64 v210, v210, -v212
	v_add_f32_e64 v211, v211, -v213
	v_mov_b32_e32 v212, v102
	v_mov_b32_e32 v213, v111
	v_mov_b32_e32 v215, v199
	v_add_f32_e64 v212, v212, -v214
	v_add_f32_e64 v213, v213, -v215
	v_pk_mov_b32 v[214:215], v[104:105], v[112:113] op_sel:[1,0]
	v_pk_mov_b32 v[216:217], v[188:189], v[200:201] op_sel:[1,0]
	v_mov_b32_e32 v218, v188
	v_add_f32_e64 v214, v214, -v216
	v_add_f32_e64 v215, v215, -v217
	v_mov_b32_e32 v216, v104
	v_mov_b32_e32 v217, v113
	v_mov_b32_e32 v219, v201
	v_add_f32_e64 v216, v216, -v218
	v_add_f32_e64 v217, v217, -v219
	v_mov_b32_e32 v219, v214
	v_mov_b32_e32 v218, v216
	v_mov_b32_e32 v220, v217
	v_mov_b32_e32 v221, v215
	v_add_f32_e32 v56, v212, v213
	v_add_f32_e64 v222, v218, -v220
	v_add_f32_e64 v223, v219, -v221
	v_add_f32 v218, v218, v220
	v_add_f32 v219, v219, v221
	v_mul_f32_e32 v235, 0x3f3504f3, v56
	v_mov_b32_e32 v223, v219
	v_mul_f32_e32 v56, 0x3ec3ef15, v219
	v_add_f32 v228, v208, v209
	v_add_f32 v229, v208, v209
	s_mov_b32 s49, s26
	v_add_f32 v253, v216, v217
	v_add_f32 v217, v216, v217
	v_mov_b32_e32 v216, v253
	v_sub_f32_e32 v234, v210, v211
	v_fma_f32 v220, v222, s30, -v56
	v_fma_f32 v221, v223, s31, -v56
	v_mul_f32_e32 v242, 0x3ec3ef15, v222
	v_mul_f32_e32 v243, 0x3f6c835e, v219
	v_add_f32 v218, v98, v114
	v_add_f32 v219, v99, v115
	v_add_f32 v222, v106, v190
	v_add_f32 v223, v107, v191
	v_add_f32_e64 v98, v98, -v114
	v_add_f32_e64 v99, v99, -v115
	v_add_f32_e64 v106, v106, -v190
	v_add_f32_e64 v107, v107, -v191
	v_mul_f32_e64 v228, v228, s26
	v_mul_f32_e64 v229, v229, s27
	v_add_f32_e64 v230, v206, -v207
	v_add_f32_e64 v231, v206, -v207
	v_mul_f32_e64 v216, v216, s48
	v_mul_f32_e64 v217, v217, s49
	v_add_f32_e64 v253, v214, -v215
	v_add_f32_e64 v215, v214, -v215
	v_mov_b32_e32 v214, v253
	v_pk_mov_b32 v[114:115], v[106:107], v[106:107] op_sel:[1,0]
	v_add_f32 v190, v98, v107
	v_add_f32 v191, v99, v106
	v_add_f32_e64 v253, v98, -v107
	v_add_f32_e64 v107, v99, -v106
	v_mov_b32_e32 v106, v253
	v_fma_f32 v232, v230, s48, v228
	v_fma_f32 v233, v231, s49, v229
	v_fma_f32 v228, v230, s48, -v228
	v_fma_f32 v229, v231, s49, -v229
	v_fmamk_f32 v230, v234, 0x3f3504f3, v235
	v_fma_f32 v234, v234, s25, -v235
	v_fma_f32 v236, v214, s26, v216
	v_fma_f32 v237, v215, s27, v217
	v_fma_f32 v214, v214, s26, -v216
	v_fma_f32 v215, v215, s27, -v217
	v_mov_b32_e32 v226, v190
	v_mov_b32_e32 v227, v107
	v_mov_b32_e32 v228, v232
	v_mov_b32_e32 v235, v234
	v_mov_b32_e32 v231, v234
	v_mov_b32_e32 v214, v236
	v_add_f32 v216, v226, v230
	v_add_f32 v217, v227, v231
	v_add_f32 v226, v228, v214
	v_add_f32 v227, v229, v215
	v_pk_mov_b32 v[106:107], v[106:107], v[232:233] op_sel:[1,0]
	v_pk_mov_b32 v[232:233], v[234:235], v[236:237] op_sel:[1,0]
	v_mov_b32_e32 v228, v190
	v_add_f32_e64 v232, v106, -v232
	v_add_f32_e64 v233, v107, -v233
	v_mov_b32_e32 v231, v215
	v_add_f32 v106, v216, v226
	v_add_f32 v107, v217, v227
	v_mov_b32_e32 v56, v39
	v_add_f32_e64 v214, v228, -v230
	v_add_f32_e64 v215, v229, -v231
	v_mul_f32 v228, v56, v106
	v_mul_f32 v229, v56, v107
	v_add_f32 v100, v100, v116
	v_add_f32 v101, v101, v117
	v_add_f32 v108, v108, v192
	v_add_f32 v109, v109, v193
	v_add_f32 v102, v102, v186
	v_add_f32 v103, v103, v187
	v_add_f32 v186, v110, v198
	v_add_f32 v187, v111, v199
	v_add_f32 v104, v104, v188
	v_add_f32 v105, v105, v189
	v_add_f32 v112, v112, v200
	v_add_f32 v113, v113, v201
	v_fma_f32 v230, v38, v106, v229
	v_fma_f32 v231, v39, v107, v228
	v_fma_f32 v106, v38, v106, -v229
	v_fma_f32 v107, v38, v107, -v228
	v_add_f32 v224, v218, v222
	v_add_f32 v225, v219, v223
	v_add_f32 v192, v102, v186
	v_add_f32 v193, v103, v187
	v_mov_b32_e32 v231, v107
	v_add_f32_e64 v106, v218, -v222
	v_add_f32_e64 v107, v219, -v223
	v_add_f32_e64 v102, v102, -v186
	v_add_f32_e64 v103, v103, -v187
	v_mov_b32_e32 v186, v104
	v_mov_b32_e32 v187, v101
	v_mov_b32_e32 v218, v112
	v_mov_b32_e32 v219, v109
	v_add_f32_e64 v186, v186, -v218
	v_add_f32_e64 v187, v187, -v219
	v_mov_b32_e32 v218, v100
	v_mov_b32_e32 v219, v104
	v_mov_b32_e32 v222, v108
	v_mov_b32_e32 v223, v112
	v_add_f32 v116, v100, v108
	v_add_f32 v117, v101, v109
	v_add_f32 v188, v104, v112
	v_add_f32 v189, v105, v113
	v_add_f32_e64 v218, v218, -v222
	v_add_f32_e64 v219, v219, -v223
	v_mov_b32_e32 v222, v101
	v_mov_b32_e32 v223, v105
	v_mov_b32_e32 v228, v109
	v_mov_b32_e32 v229, v113
	v_pk_mov_b32 v[100:101], v[104:105], v[100:101] op_sel:[1,0]
	v_pk_mov_b32 v[104:105], v[112:113], v[108:109] op_sel:[1,0]
	v_add_f32_e64 v222, v222, -v228
	v_add_f32_e64 v223, v223, -v229
	v_add_f32_e64 v100, v100, -v104
	v_add_f32_e64 v101, v101, -v105
	v_fma_f32 v104, v102, 0, v103
	v_fma_f32 v105, v103, 0, v102
	v_fma_f32 v253, v102, 0, -v103
	v_fma_f32 v103, v103, 0, -v102
	v_mov_b32_e32 v102, v253
	s_mov_b32 s50, s25
	s_mov_b32 s51, s24
	v_mov_b32_e32 v105, v103
	v_mul_f32_e64 v102, v222, s50
	v_mul_f32_e64 v103, v223, s51
	v_mul_f32_e64 v100, v100, s24
	v_mul_f32_e64 v101, v101, s25
	v_fma_f32 v102, v218, s50, v102
	v_fma_f32 v103, v219, s51, v103
	v_fma_f32 v100, v186, s24, -v100
	v_fma_f32 v101, v187, s25, -v101
	v_add_f32 v108, v106, v104
	v_add_f32 v109, v107, v105
	v_add_f32 v186, v102, v100
	v_add_f32 v187, v103, v101
	v_pk_mov_b32 v[44:45], v[204:205], v[202:203] op_sel:[1,0]
	v_add_f32 v112, v108, v186
	v_add_f32 v113, v109, v187
	s_mov_b32 s56, s26
	v_mul_f32 v203, v202, v112
	v_mul_f32 v202, v202, v113
	v_fma_f32 v218, v205, v112, -v202
	v_fma_f32 v219, v205, v113, -v203
	v_fma_f32 v112, v205, v112, v202
	v_fma_f32 v113, v205, v113, v203
	v_mov_b32_e32 v202, v206
	v_mov_b32_e32 v219, v113
; FFT_HD cf2 mk2(float x, float y) { return (cf2){x, y}; }
; FFT_HD void fft_sincos(float frac, float& s, float& c) { s = __builtin_amdgcn_sinf(frac); c = __builtin_amdgcn_cosf(frac); }
; FFT_HD cf2 cmul(cf2 a, cf2 b) { return mk2(a.x * b.x - a.y * b.y, a.x * b.y + a.y * b.x); }
; template <bool INV> FFT_HD void dft16(cf2 (&x)[16]) {
;     const float C1 = 0.9238795325112867f, S1 = 0.3826834323650898f, H = 0.7071067811865476f;
; #pragma unroll
;     for (int b = 0; b < 4; ++b) dft4<INV>(x[b], x[4 + b], x[8 + b], x[12 + b]);
;     const float s = INV ? -1.f : 1.f;
;     x[4 + 1] = cmul(x[4 + 1], mk2(C1, -s * S1)); x[8 + 1] = cmul(x[8 + 1], mk2(H, -s * H));   x[12 + 1] = cmul(x[12 + 1], mk2(S1, -s * C1));
;     x[4 + 2] = cmul(x[4 + 2], mk2(H, -s * H));   x[8 + 2] = cmul(x[8 + 2], mk2(0.f, -s));     x[12 + 2] = cmul(x[12 + 2], mk2(-H, -s * H));
;     x[4 + 3] = cmul(x[4 + 3], mk2(S1, -s * C1)); x[8 + 3] = cmul(x[8 + 3], mk2(-H, -s * H));  x[12 + 3] = cmul(x[12 + 3], mk2(-C1, s * S1));
; #pragma unroll
;     for (int c = 0; c < 4; ++c) dft4<INV>(x[4 * c], x[4 * c + 1], x[4 * c + 2], x[4 * c + 3]);
; #pragma unroll
;     for (int c = 0; c < 4; ++c)
; #pragma unroll
;         for (int d = c + 1; d < 4; ++d) { const cf2 t = x[4 * c + d]; x[4 * c + d] = x[4 * d + c]; x[4 * d + c] = t; }
; }
; FFT_HD void fft_gen_tw(float frac, cf2 (&tw)[16]) {
;     float sn, cs; fft_sincos(frac, sn, cs);
;     tw[1] = mk2(cs, -sn);
;     tw[2] = cmul(tw[1], tw[1]); tw[3] = cmul(tw[2], tw[1]); tw[4] = cmul(tw[2], tw[2]); tw[5] = cmul(tw[4], tw[1]); tw[6] = cmul(tw[4], tw[2]); tw[7] = cmul(tw[4], tw[3]);
;     tw[8] = cmul(tw[4], tw[4]);
; #pragma unroll
;     for (int j = 9; j < 16; ++j) tw[j] = cmul(tw[8], tw[j - 8]);
; }
	v_mov_b32_e32 v112, v208
	v_mov_b32_e32 v113, v212
	v_mov_b32_e32 v212, v209
	v_mov_b32_e32 v203, v210
	v_mov_b32_e32 v210, v207
	v_add_f32_e64 v112, v112, -v212
	v_add_f32_e64 v113, v113, -v213
	v_add_f32 v202, v202, v210
	v_add_f32 v203, v203, v211
	s_mov_b32 s57, s24
	v_pk_mov_b32 v[204:205], v[112:113], v[202:203] op_sel:[1,0]
	v_mul_f32_e64 v206, v202, s56
	v_mul_f32_e64 v207, v203, s57
	v_pk_mov_b32 v[202:203], v[202:203], v[112:113] op_sel:[1,0]
	s_mov_b32 s28, s25
	s_mov_b32 s52, s27
	s_mov_b32 s53, s24
	s_mov_b32 s54, s24
	s_mov_b32 s55, s27
	v_mul_f32_e64 v202, v202, s28
	v_mul_f32_e64 v203, v203, s29
	v_mov_b32_e32 v99, v242
	v_mov_b32_e32 v115, v243
	v_fma_f32 v202, v204, s54, v202
	v_fma_f32 v203, v205, s55, v203
	v_fma_f32 v204, v112, s52, v206
	v_fma_f32 v205, v113, s53, v207
	v_add_f32_e64 v98, v98, -v114
	v_add_f32_e64 v99, v99, -v115
	v_mov_b32_e32 v190, v220
	v_add_f32 v206, v202, v98
	v_add_f32 v207, v203, v99
	v_add_f32 v208, v204, v190
	v_add_f32 v209, v205, v191
	v_mov_b32_e32 v42, v72
	v_add_f32 v112, v208, v206
	v_add_f32 v113, v209, v207
	v_pk_mov_b32 v[40:41], v[70:71], v[72:73] op_sel:[1,0]
	v_mul_f32 v73, v72, v112
	v_mul_f32 v72, v72, v113
	v_mov_b32_e32 v43, v71
	v_fma_f32 v210, v71, v112, -v72
	v_fma_f32 v211, v71, v113, -v73
	v_fma_f32 v70, v71, v112, v72
	v_fma_f32 v71, v71, v113, v73
	v_add_f32_e64 v72, v116, -v188
	v_add_f32_e64 v73, v117, -v189
	v_mov_b32_e32 v211, v71
	v_add_f32_e64 v70, v224, -v192
	v_add_f32_e64 v71, v225, -v193
	v_add_f32 v198, v224, v192
	v_add_f32 v199, v225, v193
	v_add_f32 v200, v116, v188
	v_add_f32 v201, v117, v189
	v_add_f32 v188, v70, v73
	v_add_f32 v189, v71, v72
	v_add_f32_e64 v192, v70, -v73
	v_add_f32_e64 v193, v71, -v72
	v_mov_b32_e32 v70, v188
	v_pk_mov_b32 v[72:73], v[192:193], v[188:189] op_sel:[1,0]
	v_mov_b32_e32 v71, v193
	v_pk_mov_b32 v[112:113], v[68:69], v[48:49] op_sel:[1,0]
	v_mul_f32 v68, v69, v72
	v_mul_f32 v69, v69, v73
	v_add_f32_e64 v116, v232, -v233
	v_add_f32_e64 v117, v232, -v233
	v_fma_f32 v212, v48, v188, -v68
	v_fma_f32 v213, v49, v189, -v69
	v_fma_f32 v68, v48, v70, v68
	v_fma_f32 v69, v48, v71, v69
	v_mul_f32 v70, v56, v112
	v_mul_f32 v71, v56, v113
	v_mov_b32_e32 v213, v69
	v_fma_f32 v68, v38, v50, v70
	v_fma_f32 v69, v38, v51, v71
	v_fma_f32 v72, v38, v50, -v70
	v_fma_f32 v73, v38, v51, -v71
	v_mov_b32_e32 v71, v73
	v_pk_mov_b32 v[72:73], v[72:73], v[68:69] op_sel:[1,0]
	v_add_f32_e64 v104, v106, -v104
	v_add_f32_e64 v105, v107, -v105
	v_pk_mov_b32 v[106:107], v[100:101], v[102:103] op_sel:[1,0]
	v_pk_mov_b32 v[100:101], v[102:103], v[100:101] op_sel:[1,0]
	v_mov_b32_e32 v70, v68
	v_add_f32 v114, v214, v215
	v_add_f32 v115, v214, v215
	v_mul_f32 v116, v72, v116
	v_mul_f32 v117, v73, v117
	v_add_f32_e64 v100, v106, -v100
	v_add_f32_e64 v101, v107, -v101
	v_mul_f32 v96, v46, v50
	v_mul_f32 v97, v47, v51
	v_fma_f32 v222, v68, v114, -v116
	v_fma_f32 v223, v69, v115, -v117
	v_fma_f32 v114, v70, v114, v116
	v_fma_f32 v115, v71, v115, v117
	v_add_f32 v102, v104, v100
	v_add_f32 v103, v105, v101
	v_add_f32_e64 v100, v104, -v100
	v_add_f32_e64 v101, v105, -v101
	v_mul_f32 v94, v44, v50
	v_mul_f32 v95, v45, v51
	v_mov_b32_e32 v223, v115
	v_add_f32 v114, v96, v97
	v_add_f32 v115, v96, v97
	v_pk_mov_b32 v[96:97], v[100:101], v[102:103] op_sel:[1,0]
	v_mov_b32_e32 v104, v102
	v_mov_b32_e32 v105, v101
	v_mul_f32 v96, v114, v96
	v_mul_f32 v97, v115, v97
	v_add_f32_e64 v116, v94, -v95
	v_add_f32_e64 v117, v94, -v95
	v_fma_f32 v224, v116, v102, -v96
	v_fma_f32 v225, v117, v103, -v97
	v_fma_f32 v94, v116, v104, v96
	v_fma_f32 v95, v117, v105, v97
	v_pk_mov_b32 v[96:97], v[98:99], v[220:221] op_sel:[1,0]
	v_mov_b32_e32 v225, v95
	v_pk_mov_b32 v[94:95], v[202:203], v[204:205] op_sel:[1,0]
	v_mov_b32_e32 v99, v191
	v_mov_b32_e32 v203, v205
	v_add_f32_e64 v94, v94, -v96
	v_add_f32_e64 v95, v95, -v97
	v_add_f32_e64 v96, v98, -v202
	v_add_f32_e64 v97, v99, -v203
	v_mul_f32 v92, v50, v42
	v_mul_f32 v93, v51, v43
	v_add_f32 v190, v96, v94
	v_add_f32 v191, v97, v95
	v_add_f32_e64 v202, v96, -v94
	v_add_f32_e64 v203, v97, -v95
	v_mul_f32 v84, v50, v40
	v_mul_f32 v85, v51, v41
	v_add_f32 v104, v92, v93
	v_add_f32 v105, v92, v93
	v_pk_mov_b32 v[92:93], v[202:203], v[190:191] op_sel:[1,0]
	v_mov_b32_e32 v94, v190
	v_mov_b32_e32 v95, v203
	v_mul_f32 v92, v104, v92
	v_mul_f32 v93, v105, v93
	v_add_f32_e64 v106, v84, -v85
	v_add_f32_e64 v107, v84, -v85
	v_fma_f32 v204, v106, v190, -v92
	v_fma_f32 v205, v107, v191, -v93
	v_fma_f32 v84, v106, v94, v92
	v_fma_f32 v85, v107, v95, v93
	v_mul_f32 v90, v38, v54
	v_mul_f32 v91, v39, v55
	v_mov_b32_e32 v205, v85
	v_add_f32_e64 v84, v198, -v200
	v_add_f32_e64 v85, v199, -v201
	v_add_f32 v110, v198, v200
	v_add_f32 v111, v199, v201
	v_mul_f32 v92, v76, v84
	v_mul_f32 v93, v76, v85
	v_fma_f32 v198, v75, v84, -v93
	v_fma_f32 v199, v75, v85, -v92
	v_fma_f32 v84, v75, v84, v93
	v_fma_f32 v85, v75, v85, v92
	v_add_f32_e64 v92, v216, -v226
	v_add_f32_e64 v93, v217, -v227
	v_mov_b32_e32 v199, v85
	v_add_f32_e64 v84, v90, -v91
	v_add_f32_e64 v85, v90, -v91
	v_pk_mov_b32 v[52:53], v[74:75], v[76:77] op_sel:[1,0]
	v_mul_f32 v90, v84, v92
	v_mul_f32 v91, v85, v93
	v_add_f32 v253, v87, v86
	v_add_f32 v87, v87, v86
	v_mov_b32_e32 v86, v253
	v_mul_f32 v88, v46, v52
	v_mul_f32 v89, v47, v53
	v_fma_f32 v200, v86, v92, -v91
	v_fma_f32 v201, v87, v93, -v90
	v_fma_f32 v253, v86, v92, v91
	v_fma_f32 v91, v87, v93, v90
	v_mov_b32_e32 v90, v253
	v_mul_f32 v82, v46, v54
	v_mul_f32 v83, v47, v55
	v_mov_b32_e32 v201, v91
	v_add_f32_e64 v90, v108, -v186
	v_add_f32_e64 v91, v109, -v187
	v_add_f32 v186, v88, v89
	v_add_f32 v187, v88, v89
	v_mul_f32 v88, v186, v90
; FFT_HD cf2 cmul(cf2 a, cf2 b) { return mk2(a.x * b.x - a.y * b.y, a.x * b.y + a.y * b.x); }
; FFT_HD cf2 cmulc(cf2 a, cf2 b) { return mk2(a.x * b.x + a.y * b.y, a.y * b.x - a.x * b.y); }
; template <bool INV, int lS, class ZP> FFT_HD void fft_r16_pass(ZP z, int tid) {
;     ...
;         for (int j = 0; j < 16; ++j) x[j] = z[pb0 + j * STEP];
; #pragma unroll
;         for (int j = 0; j < 16; ++j) y[j] = z[pb1 + j * STEP];
;         if (INV) {
; #pragma unroll
;             for (int j = 1; j < 16; ++j) x[j] = cmulc(x[j], tw[j]);
;         }
;         dft16<INV>(x);
;         if (!INV) {
; #pragma unroll
;             for (int j = 1; j < 16; ++j) x[j] = cmul(x[j], tw[j]);
;         }
; #pragma unroll
;         for (int j = 0; j < 16; ++j) z[pb0 + j * STEP] = x[j];
;         if (INV) {
; #pragma unroll
;             for (int j = 1; j < 16; ++j) y[j] = cmulc(y[j], tw[j]);
;         }
;         dft16<INV>(y);
;         if (!INV) {
; #pragma unroll
;             for (int j = 1; j < 16; ++j) y[j] = cmul(y[j], tw[j]);
;         }
; #pragma unroll
;         for (int j = 0; j < 16; ++j) z[pb1 + j * STEP] = y[j];
	v_mul_f32 v89, v187, v91
	v_add_f32_e64 v216, v83, -v82
	v_add_f32_e64 v217, v83, -v82
	v_mul_f32 v80, v42, v52
	v_mul_f32 v81, v43, v53
	v_fma_f32 v220, v216, v90, -v89
	v_fma_f32 v221, v217, v91, -v88
	v_fma_f32 v82, v216, v90, v89
	v_fma_f32 v83, v217, v91, v88
	v_mul_f32 v78, v42, v54
	v_mul_f32 v79, v43, v55
	v_mov_b32_e32 v221, v83
	v_mov_b32_e32 v82, v206
	v_mov_b32_e32 v83, v209
	v_mov_b32_e32 v209, v207
	v_add_f32_e64 v82, v82, -v208
	v_add_f32_e64 v83, v83, -v209
	v_add_f32 v253, v80, v81
	v_add_f32 v81, v80, v81
	v_mov_b32_e32 v80, v253
	v_mul_f32 v88, v80, v82
	v_mul_f32 v89, v81, v83
	v_add_f32_e64 v253, v79, -v78
	v_add_f32_e64 v79, v79, -v78
	v_mov_b32_e32 v78, v253
	v_add_f32 v96, v232, v233
	v_add_f32 v97, v232, v233
	v_fma_f32 v206, v78, v82, -v89
	v_fma_f32 v207, v79, v83, -v88
	v_fma_f32 v82, v78, v82, v89
	v_fma_f32 v83, v79, v83, v88
	v_mul_f32 v88, v50, v76
	v_mul_f32 v89, v51, v76
	v_mov_b32_e32 v207, v83
	v_fma_f32 v82, v50, v75, -v89
	v_fma_f32 v83, v51, v75, -v88
	v_fma_f32 v90, v50, v75, v89
	v_fma_f32 v91, v51, v75, v88
	v_mov_b32_e32 v88, v82
	v_mov_b32_e32 v89, v91
	v_pk_mov_b32 v[90:91], v[90:91], v[82:83] op_sel:[1,0]
	v_add_f32_e64 v94, v214, -v215
	v_add_f32_e64 v95, v214, -v215
	v_mul_f32 v92, v90, v189
	v_mul_f32 v93, v91, v189
	v_ashrrev_i32_e32 v2, 2, v3
	v_fma_f32 v188, v82, v192, -v92
	v_fma_f32 v189, v83, v193, -v93
	v_fma_f32 v92, v88, v192, v92
	v_fma_f32 v93, v89, v192, v93
	v_add3_u32 v60, v4, v2, s71
	v_mov_b32_e32 v189, v93
	v_mul_f32 v92, v76, v70
	v_mul_f32 v93, v76, v71
	v_fma_f32 v76, v75, v70, -v93
	v_fma_f32 v77, v75, v71, -v92
	v_fma_f32 v253, v75, v70, v93
	v_fma_f32 v93, v75, v71, v92
	v_mov_b32_e32 v92, v253
	v_mov_b32_e32 v74, v76
	v_mov_b32_e32 v75, v93
	v_pk_mov_b32 v[92:93], v[92:93], v[76:77] op_sel:[1,0]
	v_add_u32_e32 v65, 0x800, v60
	v_mul_f32 v96, v92, v96
	v_mul_f32 v97, v93, v97
	v_add_u32_e32 v67, 0x1000, v60
	v_fma_f32 v192, v76, v94, -v96
	v_fma_f32 v193, v77, v95, -v97
	v_fma_f32 v94, v74, v94, v96
	v_fma_f32 v95, v75, v95, v97
	v_mul_f32 v96, v54, v116
	v_mul_f32 v97, v55, v117
	v_mov_b32_e32 v193, v95
	v_fma_f32 v94, -v54, v114, v97
	v_fma_f32 v95, -v55, v115, v96
	v_fma_f32 v98, v54, v114, v97
	v_fma_f32 v99, v55, v115, v96
	v_mov_b32_e32 v96, v94
	v_mov_b32_e32 v97, v99
	v_pk_mov_b32 v[98:99], v[98:99], v[94:95] op_sel:[1,0]
	v_add_u32_e32 v185, 0x1800, v60
	v_mul_f32 v102, v98, v103
	v_mul_f32 v103, v99, v103
	ds_read2_b64 v[2:5], v60 offset1:66
	ds_read2_b64 v[18:21], v60 offset0:132 offset1:198
	v_fma_f32 v208, v94, v100, -v102
	v_fma_f32 v209, v95, v101, -v103
	v_fma_f32 v101, v97, v100, v103
	v_fma_f32 v100, v96, v100, v102
	v_mul_f32 v102, v54, v106
	v_mul_f32 v103, v55, v107
	ds_read2_b64 v[6:9], v65 offset0:8 offset1:74
	ds_read2_b64 v[22:25], v65 offset0:140 offset1:206
	ds_read2_b64 v[10:13], v67 offset0:16 offset1:82
	ds_read2_b64 v[26:29], v67 offset0:148 offset1:214
	ds_read2_b64 v[14:17], v185 offset0:24 offset1:90
	ds_read2_b64 v[30:33], v185 offset0:156 offset1:222
	v_mov_b32_e32 v209, v101
	v_fma_f32 v100, -v54, v104, v103
	v_fma_f32 v101, -v55, v105, v102
	v_fma_f32 v108, v54, v104, v103
	v_fma_f32 v109, v55, v105, v102
	v_mov_b32_e32 v102, v100
	v_mov_b32_e32 v103, v109
	v_pk_mov_b32 v[108:109], v[108:109], v[100:101] op_sel:[1,0]
	v_cmp_ne_u64_e32 vcc, 0, v[34:35]
	v_mul_f32 v190, v108, v191
	v_mul_f32 v191, v109, v191
	s_nop 0
	v_fma_f32 v214, v100, v202, -v190
	v_fma_f32 v215, v101, v203, -v191
	v_fma_f32 v190, v102, v202, v190
	v_fma_f32 v191, v103, v202, v191
	s_waitcnt lgkmcnt(1)
	v_add_f32 v202, v6, v14
	v_add_f32 v203, v7, v15
	v_mov_b32_e32 v215, v191
	ds_write2_b64 v238, v[110:111], v[230:231] offset1:66
	ds_write2_b64 v238, v[218:219], v[210:211] offset0:132 offset1:198
	ds_write2_b64 v239, v[212:213], v[222:223] offset0:8 offset1:74
	ds_write2_b64 v239, v[224:225], v[204:205] offset0:140 offset1:206
	ds_write2_b64 v240, v[198:199], v[200:201] offset0:16 offset1:82
	ds_write2_b64 v240, v[220:221], v[206:207] offset0:148 offset1:214
	ds_write2_b64 v241, v[188:189], v[192:193] offset0:24 offset1:90
	ds_write2_b64 v241, v[208:209], v[214:215] offset0:156 offset1:222
	v_pk_mov_b32 v[110:111], v[4:5], v[8:9] op_sel:[1,0]
	v_pk_mov_b32 v[188:189], v[12:13], v[16:17] op_sel:[1,0]
	v_mov_b32_e32 v190, v12
	v_add_f32_e64 v110, v110, -v188
	v_add_f32_e64 v111, v111, -v189
	v_mov_b32_e32 v188, v4
	v_mov_b32_e32 v189, v9
	v_mov_b32_e32 v191, v17
	v_add_f32_e64 v188, v188, -v190
	v_add_f32_e64 v189, v189, -v191
	v_pk_mov_b32 v[190:191], v[18:19], v[22:23] op_sel:[1,0]
	s_waitcnt lgkmcnt(8)
; FFT_HD cf2 mk2(float x, float y) { return (cf2){x, y}; }
; FFT_HD cf2 cmul(cf2 a, cf2 b) { return mk2(a.x * b.x - a.y * b.y, a.x * b.y + a.y * b.x); }
; FFT_HD cf2 cmulc(cf2 a, cf2 b) { return mk2(a.x * b.x + a.y * b.y, a.y * b.x - a.x * b.y); }
; FFT_HD cf2 cadd(cf2 a, cf2 b) { return mk2(a.x + b.x, a.y + b.y); }
; FFT_HD cf2 csub(cf2 a, cf2 b) { return mk2(a.x - b.x, a.y - b.y); }
; template <bool INV> FFT_HD void dft4(cf2& a, cf2& b, cf2& c, cf2& d) {
;     const cf2 s0 = cadd(a, c), s1 = csub(a, c), s2 = cadd(b, d), s3 = csub(b, d);
;     a = cadd(s0, s2); c = csub(s0, s2);
;     const cf2 r = INV ? mk2(-s3.y, s3.x) : mk2(s3.y, -s3.x);
;     b = cadd(s1, r); d = csub(s1, r);
; }
; template <bool INV> FFT_HD void dft16(cf2 (&x)[16]) {
;     const float C1 = 0.9238795325112867f, S1 = 0.3826834323650898f, H = 0.7071067811865476f;
; #pragma unroll
;     for (int b = 0; b < 4; ++b) dft4<INV>(x[b], x[4 + b], x[8 + b], x[12 + b]);
;     const float s = INV ? -1.f : 1.f;
;     x[4 + 1] = cmul(x[4 + 1], mk2(C1, -s * S1)); x[8 + 1] = cmul(x[8 + 1], mk2(H, -s * H));   x[12 + 1] = cmul(x[12 + 1], mk2(S1, -s * C1));
;     x[4 + 2] = cmul(x[4 + 2], mk2(H, -s * H));   x[8 + 2] = cmul(x[8 + 2], mk2(0.f, -s));     x[12 + 2] = cmul(x[12 + 2], mk2(-H, -s * H));
;     x[4 + 3] = cmul(x[4 + 3], mk2(S1, -s * C1)); x[8 + 3] = cmul(x[8 + 3], mk2(-H, -s * H));  x[12 + 3] = cmul(x[12 + 3], mk2(-C1, s * S1));
; #pragma unroll
;     for (int c = 0; c < 4; ++c) dft4<INV>(x[4 * c], x[4 * c + 1], x[4 * c + 2], x[4 * c + 3]);
; #pragma unroll
;     for (int c = 0; c < 4; ++c)
; #pragma unroll
;         for (int d = c + 1; d < 4; ++d) { const cf2 t = x[4 * c + d]; x[4 * c + d] = x[4 * d + c]; x[4 * d + c] = t; }
; }
; template <bool INV, int lS, class ZP> FFT_HD void fft_r16_pass(ZP z, int tid) {
;     ...
;         if (INV) {
; #pragma unroll
;             for (int j = 1; j < 16; ++j) y[j] = cmulc(y[j], tw[j]);
;         }
;         dft16<INV>(y);
	v_pk_mov_b32 v[192:193], v[26:27], v[30:31] op_sel:[1,0]
	v_pk_mov_b32 v[206:207], v[20:21], v[4:5] op_sel:[1,0]
	v_pk_mov_b32 v[208:209], v[28:29], v[12:13] op_sel:[1,0]
	v_add_f32_e64 v190, v190, -v192
	v_add_f32_e64 v191, v191, -v193
	v_mov_b32_e32 v192, v18
	v_mov_b32_e32 v193, v23
	v_mov_b32_e32 v198, v26
	v_mov_b32_e32 v199, v31
	v_add_f32 v206, v206, v208
	v_add_f32 v207, v207, v209
	v_mov_b32_e32 v208, v4
	v_mov_b32_e32 v209, v20
	v_mov_b32_e32 v210, v12
	v_mov_b32_e32 v211, v28
	v_add_f32_e64 v192, v192, -v198
	v_add_f32_e64 v193, v193, -v199
	v_add_f32 v208, v208, v210
	v_add_f32 v209, v209, v211
	v_pk_mov_b32 v[210:211], v[24:25], v[8:9] op_sel:[1,0]
	v_pk_mov_b32 v[212:213], v[32:33], v[16:17] op_sel:[1,0]
	v_add_f32_e32 v39, v192, v193
	v_sub_f32_e32 v218, v190, v191
	v_sub_f32_e32 v219, v192, v193
	v_add_f32_e32 v200, v190, v191
	v_pk_mov_b32 v[190:191], v[20:21], v[24:25] op_sel:[1,0]
	v_pk_mov_b32 v[192:193], v[28:29], v[32:33] op_sel:[1,0]
	v_add_f32 v210, v210, v212
	v_add_f32 v211, v211, v213
	v_mov_b32_e32 v212, v8
	v_mov_b32_e32 v213, v24
	v_mov_b32_e32 v214, v16
	v_mov_b32_e32 v215, v32
	v_mov_b32_e32 v4, v20
	v_mov_b32_e32 v12, v28
	v_mov_b32_e32 v8, v24
	v_mov_b32_e32 v16, v32
	v_add_f32_e64 v190, v190, -v192
	v_add_f32_e64 v191, v191, -v193
	v_mov_b32_e32 v192, v20
	v_mov_b32_e32 v198, v28
	v_add_f32 v212, v212, v214
	v_add_f32 v213, v213, v215
	v_add_f32 v214, v4, v12
	v_add_f32 v215, v5, v13
	v_mov_b32_e32 v20, v5
	v_mov_b32_e32 v28, v13
	v_add_f32 v12, v8, v16
	v_add_f32 v13, v9, v17
	v_mov_b32_e32 v24, v9
	v_mov_b32_e32 v32, v17
	v_add_f32 v16, v18, v26
	v_add_f32 v17, v19, v27
	v_add_f32 v18, v22, v30
	v_add_f32 v19, v23, v31
	v_add_f32 v4, v20, v28
	v_add_f32 v5, v21, v29
	v_add_f32 v8, v24, v32
	v_add_f32 v9, v25, v33
	v_add_f32_e64 v20, v16, -v18
	v_add_f32_e64 v21, v17, -v19
	v_mov_b32_e32 v193, v25
	v_add_f32_e64 v24, v4, -v8
	v_add_f32_e64 v25, v5, -v9
	v_add_f32_e64 v26, v206, -v210
	v_add_f32_e64 v27, v207, -v211
	v_fma_f32 v28, v20, 0, v21
	v_fma_f32 v29, v21, 0, v20
	v_fma_f32 v253, v20, 0, -v21
	v_fma_f32 v21, v21, 0, -v20
	v_mov_b32_e32 v20, v253
	v_mov_b32_e32 v199, v33
	v_add_f32_e64 v12, v214, -v12
	v_add_f32_e64 v13, v215, -v13
	v_mov_b32_e32 v29, v21
	v_mul_f32_e64 v20, v24, s50
	v_mul_f32_e64 v21, v25, s51
	v_mul_f32_e64 v24, v26, s24
	v_mul_f32_e64 v25, v27, s25
	v_add_f32_e64 v192, v192, -v198
	v_add_f32_e64 v193, v193, -v199
	v_mul_f32_e32 v199, 0xbf3504f3, v200
	v_add_f32 v200, v2, v10
	v_add_f32 v201, v3, v11
	v_add_f32_e64 v22, v208, -v212
	v_add_f32_e64 v23, v209, -v213
	v_fma_f32 v12, v12, s24, -v24
	v_fma_f32 v13, v13, s25, -v25
	v_mov_b32_e32 v24, v208
	v_mov_b32_e32 v25, v4
	v_mov_b32_e32 v26, v212
	v_mov_b32_e32 v27, v8
	v_mov_b32_e32 v4, v209
	v_mov_b32_e32 v8, v213
	v_fma_f32 v20, v22, s50, v20
	v_fma_f32 v21, v23, s51, v21
	v_add_f32 v22, v200, v202
	v_add_f32 v23, v201, v203
	v_add_f32 v24, v24, v26
	v_add_f32 v25, v25, v27
	v_add_f32 v16, v16, v18
	v_add_f32 v17, v17, v19
	v_add_f32 v4, v4, v8
	v_add_f32 v5, v5, v9
	v_add_f32_e64 v204, v200, -v202
	v_add_f32_e64 v205, v201, -v203
	v_add_f32 v8, v22, v16
	v_add_f32 v9, v23, v17
	v_add_f32 v18, v24, v4
	v_add_f32 v19, v25, v5
	v_pk_mov_b32 v[26:27], v[22:23], v[24:25] op_sel:[1,0]
	v_pk_mov_b32 v[30:31], v[16:17], v[4:5] op_sel:[1,0]
	v_mov_b32_e32 v23, v25
	v_mov_b32_e32 v17, v5
	v_add_f32_e64 v4, v22, -v16
	v_add_f32_e64 v5, v23, -v17
	v_add_f32 v16, v8, v18
	v_add_f32 v17, v9, v19
	v_add_f32_e64 v8, v8, -v18
	v_add_f32_e64 v9, v9, -v19
	v_add_f32 v18, v204, v28
	v_add_f32 v19, v205, v29
	v_add_f32 v22, v20, v12
	v_add_f32 v23, v21, v13
	v_add_f32_e64 v26, v26, -v30
	v_add_f32_e64 v27, v27, -v31
	v_add_f32 v24, v18, v22
	v_add_f32 v25, v19, v23
	v_add_f32_e64 v18, v18, -v22
	v_add_f32_e64 v19, v19, -v23
	v_mul_f32 v22, v46, v25
	v_mul_f32 v23, v47, v25
	v_add_f32_e64 v2, v2, -v10
	v_add_f32_e64 v3, v3, -v11
	v_fma_f32 v30, v44, v24, -v22
	v_fma_f32 v31, v45, v25, -v23
	v_fma_f32 v22, v44, v24, v22
	v_fma_f32 v23, v45, v24, v23
	v_add_f32_e64 v24, v26, -v27
	v_add_f32_e64 v25, v26, -v27
	v_mov_b32_e32 v31, v23
	v_add_f32 v22, v4, v5
	v_add_f32 v23, v4, v5
	v_mul_f32 v24, v112, v24
	v_mul_f32 v25, v113, v25
	v_add_f32_e64 v10, v188, -v189
	v_add_f32_e64 v11, v188, -v189
	v_fma_f32 v32, v48, v22, -v24
	v_fma_f32 v33, v49, v23, -v25
	v_fma_f32 v22, v50, v22, v24
	v_fma_f32 v23, v51, v23, v25
	v_pk_mov_b32 v[24:25], v[12:13], v[20:21] op_sel:[1,0]
	v_pk_mov_b32 v[12:13], v[20:21], v[12:13] op_sel:[1,0]
	v_mov_b32_e32 v33, v23
	v_add_f32_e64 v22, v204, -v28
	v_add_f32_e64 v23, v205, -v29
	v_add_f32_e64 v12, v24, -v12
	v_add_f32_e64 v13, v25, -v13
	v_add_f32_e64 v6, v6, -v14
	v_add_f32_e64 v7, v7, -v15
	v_add_f32 v20, v22, v12
	v_add_f32 v21, v23, v13
	v_add_f32_e64 v12, v22, -v12
	v_add_f32_e64 v13, v23, -v13
	v_mov_b32_e32 v22, v20
	v_pk_mov_b32 v[24:25], v[12:13], v[20:21] op_sel:[1,0]
	v_mov_b32_e32 v23, v13
	v_mul_f32 v24, v114, v24
	v_mul_f32 v25, v115, v25
	v_mul_f32_e64 v10, v10, s48
	v_mul_f32_e64 v11, v11, s49
	v_fma_f32 v28, v116, v20, -v24
	v_fma_f32 v29, v117, v21, -v25
	v_fma_f32 v22, v116, v22, v24
	v_fma_f32 v23, v117, v23, v25
	v_add_f32 v14, v110, v111
	v_add_f32 v15, v110, v111
	v_mov_b32_e32 v29, v23
	v_mul_f32 v22, v54, v9
	v_mul_f32 v23, v55, v9
	v_mul_f32_e32 v198, 0xbf3504f3, v219
	v_fma_f32 v24, v52, v8, -v22
	v_fma_f32 v25, v53, v9, -v23
	v_fma_f32 v9, v53, v8, v23
	v_fma_f32 v8, v52, v8, v22
	v_sub_f32_e32 v198, v198, v199
	v_mov_b32_e32 v25, v9
	v_mul_f32 v8, v186, v18
	v_mul_f32 v9, v187, v19
	v_fmac_f32_e32 v199, 0xbf3504f3, v219
	v_fma_f32 v22, v216, v18, -v9
	v_fma_f32 v23, v217, v19, -v8
; __device__ __forceinline__ unsigned cvt_pk_bf16(float lo, float hi) { unsigned r; asm volatile("v_cvt_pk_bf16_f32 %0, %1, %2" : "=v"(r) : "v"(lo), "v"(hi)); return r; }
; FFT_HD cf2 cmul(cf2 a, cf2 b) { return mk2(a.x * b.x - a.y * b.y, a.x * b.y + a.y * b.x); }
; FFT_HD cf2 cmulc(cf2 a, cf2 b) { return mk2(a.x * b.x + a.y * b.y, a.y * b.x - a.x * b.y); }
; template <int BANK, int WAITN> __device__ __forceinline__ void bg_finish1(BgState& b) {
;     if (WAITN == 32) asm volatile("s_waitcnt vmcnt(32)" ::: "memory"); else asm volatile("s_waitcnt vmcnt(0)" ::: "memory");
;     asm volatile("" : BG_TIE16(BANK * 32) :: "memory");
;     asm volatile("" : BG_TIE16(BANK * 32 + 16) :: "memory");
;     bf16_t* dst = b.dst[BANK];
;     if (dst != nullptr) {
; #pragma unroll
;         for (int c = 0; c < 4; ++c) { u32x4 w;
;             w.x = cvt_pk_bf16(b.r[(BANK * 8 + 0) * 4 + c], b.r[(BANK * 8 + 1) * 4 + c]); w.y = cvt_pk_bf16(b.r[(BANK * 8 + 2) * 4 + c], b.r[(BANK * 8 + 3) * 4 + c]);
;             w.z = cvt_pk_bf16(b.r[(BANK * 8 + 4) * 4 + c], b.r[(BANK * 8 + 5) * 4 + c]); w.w = cvt_pk_bf16(b.r[(BANK * 8 + 6) * 4 + c], b.r[(BANK * 8 + 7) * 4 + c]);
;             bf16_t* dp = dst + (c & 1) * 512 + (c >> 1) * b.o2[BANK];
;             asm volatile("global_store_dwordx4 %0, %1, off\n\ts_nop 1" :: "v"(dp), "v"(w) : "memory"); }
;     }
; }
; template <bool INV, int lS, class ZP> FFT_HD void fft_r16_pass(ZP z, int tid) {
;     ...
;         dft16<INV>(x);
;         if (!INV) {
; #pragma unroll
;             for (int j = 1; j < 16; ++j) x[j] = cmul(x[j], tw[j]);
;         }
; #pragma unroll
;         for (int j = 0; j < 16; ++j) z[pb0 + j * STEP] = x[j];
;         if (INV) {
; #pragma unroll
;             for (int j = 1; j < 16; ++j) y[j] = cmulc(y[j], tw[j]);
;         }
;         dft16<INV>(y);
;         if (!INV) {
; #pragma unroll
;             for (int j = 1; j < 16; ++j) y[j] = cmul(y[j], tw[j]);
;         }
; #pragma unroll
;         for (int j = 0; j < 16; ++j) z[pb1 + j * STEP] = y[j];
	v_fma_f32 v253, v216, v18, v9
	v_fma_f32 v9, v217, v19, v8
	v_mov_b32_e32 v8, v253
	v_fma_f32 v18, v14, s26, v10
	v_fma_f32 v19, v15, s27, v11
	v_fma_f32 v10, v14, s26, -v10
	v_fma_f32 v11, v15, s27, -v11
	v_add_f32 v14, v190, v191
	v_add_f32 v15, v190, v191
	v_mov_b32_e32 v23, v9
	v_add_f32_e64 v8, v2, -v7
	v_add_f32_e64 v9, v3, -v6
	v_add_f32 v2, v2, v7
	v_add_f32 v3, v3, v6
	v_mov_b32_e32 v19, v11
	v_add_f32_e64 v10, v192, -v193
	v_add_f32_e64 v11, v192, -v193
	v_mul_f32_e64 v14, v14, s48
	v_mul_f32_e64 v15, v15, s49
	v_mov_b32_e32 v6, v8
	v_mov_b32_e32 v7, v3
	v_fma_f32 v10, v10, s30, -v14
	v_fma_f32 v11, v11, s31, -v15
	v_add_f32 v14, v6, v198
	v_add_f32 v15, v7, v199
	v_add_f32 v44, v18, v10
	v_add_f32 v45, v19, v11
	v_add_f32_e64 v6, v6, -v198
	v_add_f32_e64 v7, v7, -v199
	v_add_f32 v46, v14, v44
	v_add_f32 v47, v15, v45
	v_add_f32_e64 v10, v18, -v10
	v_add_f32_e64 v11, v19, -v11
	v_mul_f32 v42, v42, v47
	v_mul_f32 v43, v43, v47
	v_add_f32_e64 v14, v14, -v44
	v_add_f32_e64 v15, v15, -v45
	v_fma_f32 v44, v40, v46, -v42
	v_fma_f32 v45, v41, v47, -v43
	v_fma_f32 v40, v40, v46, v42
	v_fma_f32 v41, v41, v46, v43
	v_add_f32 v18, v6, v11
	v_add_f32 v19, v7, v10
	v_add_f32_e64 v6, v6, -v11
	v_add_f32_e64 v7, v7, -v10
	v_mov_b32_e32 v45, v41
	v_pk_mov_b32 v[40:41], v[6:7], v[18:19] op_sel:[1,0]
	v_mov_b32_e32 v10, v18
	v_mov_b32_e32 v11, v7
	v_mul_f32 v40, v104, v40
	v_mul_f32 v41, v105, v41
	v_add_f32 v50, v192, v193
	v_add_f32 v51, v192, v193
	v_fma_f32 v42, v106, v18, -v40
	v_fma_f32 v43, v107, v19, -v41
	v_fma_f32 v10, v106, v10, v40
	v_fma_f32 v11, v107, v11, v41
	v_mul_f32_e32 v39, 0x3f3504f3, v39
	v_mov_b32_e32 v43, v11
	v_add_f32 v10, v188, v189
	v_add_f32 v11, v188, v189
	v_mul_f32_e64 v10, v10, s26
	v_mul_f32_e64 v11, v11, s27
	v_add_f32_e64 v40, v110, -v111
	v_add_f32_e64 v41, v110, -v111
	v_mul_f32_e64 v50, v50, s48
	v_mul_f32_e64 v51, v51, s49
	v_add_f32_e64 v52, v190, -v191
	v_add_f32_e64 v53, v190, -v191
	v_fma_f32 v46, v40, s48, v10
	v_fma_f32 v47, v41, s49, v11
	v_fma_f32 v10, v40, s48, -v10
	v_fma_f32 v11, v41, s49, -v11
	v_fma_f32 v48, v218, s25, -v39
	v_fma_f32 v54, v52, s26, v50
	v_fma_f32 v55, v53, s27, v51
	v_fma_f32 v50, v52, s26, -v50
	v_fma_f32 v51, v53, s27, -v51
	v_mov_b32_e32 v10, v46
	v_fmamk_f32 v40, v218, 0x3f3504f3, v39
	v_mov_b32_e32 v41, v48
	v_mov_b32_e32 v50, v54
	v_mov_b32_e32 v3, v9
	v_mov_b32_e32 v49, v48
	v_add_f32 v52, v10, v50
	v_add_f32 v53, v11, v51
	v_add_f32 v104, v2, v40
	v_add_f32 v105, v3, v41
	v_mov_b32_e32 v3, v11
	v_mov_b32_e32 v41, v51
	v_add_f32_e64 v2, v2, -v40
	v_add_f32_e64 v3, v3, -v41
	v_pk_mov_b32 v[8:9], v[8:9], v[46:47] op_sel:[1,0]
	v_pk_mov_b32 v[10:11], v[48:49], v[54:55] op_sel:[1,0]
	v_add_f32 v40, v104, v52
	v_add_f32 v41, v105, v53
	v_add_f32_e64 v8, v8, -v10
	v_add_f32_e64 v9, v9, -v11
	v_mul_f32 v46, v56, v40
	v_mul_f32 v47, v56, v41
	v_fma_f32 v48, v38, v40, v47
	v_fma_f32 v49, v39, v41, v46
	v_fma_f32 v39, v38, v41, -v46
	v_fma_f32 v38, v38, v40, -v47
	v_add_f32_e64 v40, v8, -v9
	v_add_f32_e64 v41, v8, -v9
	v_mov_b32_e32 v49, v39
	v_add_f32 v38, v2, v3
	v_add_f32 v39, v2, v3
	v_mul_f32 v40, v72, v40
	v_mul_f32 v41, v73, v41
	v_add_f32_e64 v10, v104, -v52
	v_add_f32_e64 v11, v105, -v53
	v_fma_f32 v46, v68, v38, -v40
	v_fma_f32 v47, v69, v39, -v41
	v_fma_f32 v38, v70, v38, v40
	v_fma_f32 v39, v71, v39, v41
	v_add_f32_e64 v253, v4, -v5
	v_add_f32_e64 v5, v4, -v5
	v_mov_b32_e32 v4, v253
	v_mov_b32_e32 v47, v39
	v_mul_f32 v38, v84, v10
	v_mul_f32 v39, v85, v11
	v_add_f32_e64 v253, v2, -v3
	v_add_f32_e64 v3, v2, -v3
	v_mov_b32_e32 v2, v253
	v_fma_f32 v40, v86, v10, -v39
	v_fma_f32 v41, v87, v11, -v38
	v_fma_f32 v10, v86, v10, v39
	v_fma_f32 v11, v87, v11, v38
	s_nop 0
	v_mov_b32_e32 v41, v11
	v_mul_f32 v10, v80, v14
	v_mul_f32 v11, v81, v15
	s_nop 0
	v_fma_f32 v38, v78, v14, -v11
	v_fma_f32 v39, v79, v15, -v10
	v_fma_f32 v253, v78, v14, v11
	v_fma_f32 v11, v79, v15, v10
	v_mov_b32_e32 v10, v253
	s_nop 0
	v_mov_b32_e32 v39, v11
	v_add_f32 v10, v26, v27
	v_add_f32 v11, v26, v27
	v_mul_f32 v10, v90, v10
	v_mul_f32 v11, v91, v11
	s_nop 0
	v_fma_f32 v14, v82, v4, -v10
	v_fma_f32 v15, v83, v5, -v11
	v_fma_f32 v4, v88, v4, v10
	v_fma_f32 v5, v89, v5, v11
	s_nop 0
	v_mov_b32_e32 v15, v5
	v_add_f32 v4, v8, v9
	v_add_f32 v5, v8, v9
	v_mul_f32 v4, v92, v4
	v_mul_f32 v5, v93, v5
	s_nop 0
	v_fma_f32 v8, v76, v2, -v4
	v_fma_f32 v9, v77, v3, -v5
	v_fma_f32 v2, v74, v2, v4
	v_fma_f32 v3, v75, v3, v5
	s_nop 0
	v_mov_b32_e32 v9, v3
	v_mul_f32 v2, v98, v21
	v_mul_f32 v3, v99, v21
	s_nop 0
	v_fma_f32 v4, v94, v12, -v2
	v_fma_f32 v5, v95, v13, -v3
	v_fma_f32 v2, v96, v12, v2
	v_fma_f32 v3, v97, v12, v3
	s_nop 0
	v_mov_b32_e32 v5, v3
	v_mul_f32 v2, v108, v19
	v_mul_f32 v3, v109, v19
	s_nop 0
	v_fma_f32 v10, v100, v6, -v2
	v_fma_f32 v11, v101, v7, -v3
	v_fma_f32 v2, v102, v6, v2
	v_fma_f32 v3, v103, v6, v3
	s_nop 0
	v_mov_b32_e32 v11, v3
	ds_write2_b64 v60, v[16:17], v[48:49] offset1:66
	ds_write2_b64 v60, v[30:31], v[44:45] offset0:132 offset1:198
	ds_write2_b64 v65, v[32:33], v[46:47] offset0:8 offset1:74
	ds_write2_b64 v65, v[28:29], v[42:43] offset0:140 offset1:206
	ds_write2_b64 v67, v[24:25], v[40:41] offset0:16 offset1:82
	ds_write2_b64 v67, v[22:23], v[38:39] offset0:148 offset1:214
	ds_write2_b64 v185, v[14:15], v[8:9] offset0:24 offset1:90
	ds_write2_b64 v185, v[4:5], v[10:11] offset0:156 offset1:222
	s_waitcnt lgkmcnt(0)
	s_barrier
	s_waitcnt vmcnt(32)
	s_and_saveexec_b64 s[48:49], vcc
	s_cbranch_execz .LBB0_581
	v_cvt_pk_bf16_f32 v2, v144, v146
	v_cvt_pk_bf16_f32 v3, v145, v148
	v_cvt_pk_bf16_f32 v4, v147, v150
	v_cvt_pk_bf16_f32 v5, v149, v151
	v_lshl_add_u64 v[6:7], v[34:35], 0, s[22:23]
	global_store_dwordx4 v[34:35], v[2:5], off nt
	s_nop 1
	v_cvt_pk_bf16_f32 v2, v136, v138
	v_cvt_pk_bf16_f32 v3, v137, v140
	v_cvt_pk_bf16_f32 v4, v139, v142
	v_cvt_pk_bf16_f32 v5, v141, v143
	s_lshl_b32 s12, s42, 1
	global_store_dwordx4 v[6:7], v[2:5], off nt
	s_nop 1
	v_cvt_pk_bf16_f32 v2, v128, v130
	v_cvt_pk_bf16_f32 v3, v129, v132
	v_cvt_pk_bf16_f32 v4, v131, v134
	v_cvt_pk_bf16_f32 v5, v133, v135
	v_lshl_add_u64 v[8:9], v[34:35], 0, s[12:13]
	global_store_dwordx4 v[8:9], v[2:5], off nt
	s_nop 1
	v_cvt_pk_bf16_f32 v2, v120, v122
	v_cvt_pk_bf16_f32 v3, v121, v124
	v_cvt_pk_bf16_f32 v4, v123, v126
	v_cvt_pk_bf16_f32 v5, v125, v127
	v_lshl_add_u64 v[6:7], v[6:7], 0, s[12:13]
	global_store_dwordx4 v[6:7], v[2:5], off nt
	s_nop 1

; __device__ __forceinline__ KP kparams() { KP q = (KP)__builtin_amdgcn_kernarg_segment_ptr(); asm volatile("" : "+s"(q)); return q; }
; FFT_HD cf2 mk2(float x, float y) { return (cf2){x, y}; }
; FFT_HD void fft_sincos(float frac, float& s, float& c) { s = __builtin_amdgcn_sinf(frac); c = __builtin_amdgcn_cosf(frac); }
; FFT_HD cf2 cmul(cf2 a, cf2 b) { return mk2(a.x * b.x - a.y * b.y, a.x * b.y + a.y * b.x); }
; template <int BANK> __device__ __forceinline__ void bg_issue1(BgState& b, int wg, int NW, int lane) {
;     KP kp = kparams();
;     const float* src; int ldS; bf16_t* dst; int o2;
;     bg_decode(b.st, wg, NW, lane, kp, src, ldS, dst, o2);
;     b.dst[BANK] = dst; b.o2[BANK] = o2;
;     asm volatile("s_nop 6" ::: "memory");
; #pragma unroll
;     for (int i = 0; i < 8; ++i) { const float* p = src + (size_t)i * ldS;
;         asm volatile("global_load_dword %0, %4, off\n\tglobal_load_dword %1, %4, off offset:256\n\tglobal_load_dword %2, %4, off offset:512\n\tglobal_load_dword %3, %4, off offset:768"
;                      : "=&v"(b.r[(BANK * 8 + i) * 4 + 0]), "=&v"(b.r[(BANK * 8 + i) * 4 + 1]), "=&v"(b.r[(BANK * 8 + i) * 4 + 2]), "=&v"(b.r[(BANK * 8 + i) * 4 + 3]) : "v"(p) : "memory"); }
;     b.st += 1;
; }
; FFT_HD void fft_gen_tw(float frac, cf2 (&tw)[16]) {
;     float sn, cs; fft_sincos(frac, sn, cs);
;     tw[1] = mk2(cs, -sn);
;     tw[2] = cmul(tw[1], tw[1]); tw[3] = cmul(tw[2], tw[1]); tw[4] = cmul(tw[2], tw[2]); tw[5] = cmul(tw[4], tw[1]); tw[6] = cmul(tw[4], tw[2]); tw[7] = cmul(tw[4], tw[3]);
;     tw[8] = cmul(tw[4], tw[4]);
; #pragma unroll
;     for (int j = 9; j < 16; ++j) tw[j] = cmul(tw[8], tw[j - 8]);
; }
; template <bool INV, int lS, class ZP> FFT_HD void fft_r16_pass(ZP z, int tid) {
;     constexpr int S = 1 << lS, STEP = (S >= 64) ? S + S / 32 : S;
;     constexpr float inv = 1.0f / (float)(16 * S);
;     cf2 tw[16];
;     if (lS != 10) {
;         fft_gen_tw((float)(tid & (S - 1)) * inv, tw);
;         const int w0 = tid, w1 = tid + 512;
;         const int pb0 = PADI(((w0 >> lS) << (lS + 4)) + (w0 & (S - 1))), pb1 = PADI(((w1 >> lS) << (lS + 4)) + (w1 & (S - 1)));
;         cf2 x[16], y[16];
; #pragma unroll
;         for (int j = 0; j < 16; ++j) x[j] = z[pb0 + j * STEP];
.LBB0_591:
	s_nop 6
	s_lshl_b32 s12, s48, 2
	global_load_dword v144, v[2:3], off nt
	global_load_dword v136, v[2:3], off offset:256 nt
	global_load_dword v128, v[2:3], off offset:512 nt
	global_load_dword v120, v[2:3], off offset:768 nt
	v_lshl_add_u64 v[2:3], v[2:3], 0, s[12:13]
	v_and_b32_e32 v14, 3, v57
	global_load_dword v146, v[2:3], off nt
	global_load_dword v138, v[2:3], off offset:256 nt
	global_load_dword v130, v[2:3], off offset:512 nt
	global_load_dword v122, v[2:3], off offset:768 nt
	v_lshl_add_u64 v[2:3], v[2:3], 0, s[12:13]
	v_cvt_f32_ubyte0_e32 v4, v14
	global_load_dword v145, v[2:3], off nt
	global_load_dword v137, v[2:3], off offset:256 nt
	global_load_dword v129, v[2:3], off offset:512 nt
	global_load_dword v121, v[2:3], off offset:768 nt
	v_lshl_add_u64 v[2:3], v[2:3], 0, s[12:13]
	v_mul_f32_e32 v4, 0x3c800000, v4
	global_load_dword v148, v[2:3], off nt
	global_load_dword v140, v[2:3], off offset:256 nt
	global_load_dword v132, v[2:3], off offset:512 nt
	global_load_dword v124, v[2:3], off offset:768 nt
	v_lshl_add_u64 v[2:3], v[2:3], 0, s[12:13]
	v_sin_f32_e32 v39, v4
	v_cos_f32_e32 v38, v4
	global_load_dword v147, v[2:3], off nt
	global_load_dword v139, v[2:3], off offset:256 nt
	global_load_dword v131, v[2:3], off offset:512 nt
	global_load_dword v123, v[2:3], off offset:768 nt
	v_lshl_add_u64 v[2:3], v[2:3], 0, s[12:13]
	global_load_dword v149, v[2:3], off nt
	global_load_dword v141, v[2:3], off offset:256 nt
	global_load_dword v133, v[2:3], off offset:512 nt
	global_load_dword v125, v[2:3], off offset:768 nt
	v_lshl_add_u64 v[2:3], v[2:3], 0, s[12:13]
	global_load_dword v150, v[2:3], off nt
	global_load_dword v142, v[2:3], off offset:256 nt
	global_load_dword v134, v[2:3], off offset:512 nt
	global_load_dword v126, v[2:3], off offset:768 nt
	v_lshl_add_u64 v[2:3], v[2:3], 0, s[12:13]
	global_load_dword v151, v[2:3], off nt
	global_load_dword v143, v[2:3], off offset:256 nt
	global_load_dword v135, v[2:3], off offset:512 nt
	global_load_dword v127, v[2:3], off offset:768 nt
	v_mul_f32 v2, v38, v38
	v_mul_f32 v3, v39, v39
	v_mul_f32_e64 v4, v38, -v39
	v_mov_b32_e32 v5, v2
	v_mov_b32_e32 v2, v4
	v_add_f32 v192, v4, v2
	v_add_f32 v193, v5, v3
	v_add_f32_e64 v202, v4, -v2
	v_add_f32_e64 v203, v5, -v3
	v_mov_b32_e32 v46, v192
	v_mov_b32_e32 v47, v203
	v_mul_f32 v8, v46, v46
	v_mul_f32 v9, v47, v47
	v_mul_f32 v10, v203, v46
	v_mul_f32 v11, v202, v47
	v_mov_b32_e32 v2, v39
	v_mov_b32_e32 v3, v38
	v_pk_mov_b32 v[12:13], v[8:9], v[10:11] op_sel:[1,0]
	v_mov_b32_e32 v9, v10
	v_mul_f32 v4, v2, v46
	v_mul_f32 v5, v3, v47
	v_mul_f32 v6, v38, v46
	v_mul_f32 v7, v39, v47
	v_add_f32_e64 v48, v12, -v8
	v_add_f32_e64 v49, v13, -v9
	v_add_f32 v68, v12, v8
	v_add_f32 v69, v13, v9
	v_mov_b32_e32 v50, v48
	v_mov_b32_e32 v51, v69
	v_mov_b32_e32 v8, v6
	v_mov_b32_e32 v9, v5
	v_pk_mov_b32 v[4:5], v[6:7], v[4:5] op_sel:[1,0]
	v_mul_f32 v6, v50, v69
	v_mul_f32 v7, v51, v68
	v_add_f32_e64 v72, v8, -v4
	v_add_f32_e64 v73, v9, -v5
	v_add_f32 v70, v8, v4
	v_add_f32 v71, v9, v5
	v_mul_f32 v4, v50, v50
	v_mul_f32 v5, v51, v51
	s_mov_b32 s48, s27
	v_mov_b32_e32 v7, v4
	v_mov_b32_e32 v4, v6
	v_add_f32 v76, v6, v4
	v_add_f32 v77, v7, v5
	v_add_f32_e64 v74, v6, -v4
	v_add_f32_e64 v75, v7, -v5
	v_mov_b32_e32 v54, v76
	v_mov_b32_e32 v55, v75
	v_mul_f32 v84, v2, v54
	v_mul_f32 v85, v3, v55
	v_and_b32_e32 v2, 0xffffffc0, v184
	v_ashrrev_i32_e32 v3, 5, v184
	v_add_u32_e32 v4, 0x2000, v2
	v_lshlrev_b32_e32 v2, 3, v2
	v_lshlrev_b32_e32 v5, 3, v14
	v_lshlrev_b32_e32 v3, 3, v3
	v_add3_u32 v2, 0, v2, v5
	v_and_b32_e32 v3, -16, v3
	v_add_u32_e32 v65, v2, v3
	ds_read2_b64 v[98:101], v65 offset1:4
	ds_read2_b64 v[102:105], v65 offset0:8 offset1:12
	ds_read2_b64 v[106:109], v65 offset0:16 offset1:20
	ds_read2_b64 v[110:113], v65 offset0:24 offset1:28
	ds_read2_b64 v[114:117], v65 offset0:32 offset1:36
	ds_read2_b64 v[184:187], v65 offset0:40 offset1:44
	ds_read2_b64 v[188:191], v65 offset0:48 offset1:52
	ds_read2_b64 v[198:201], v65 offset0:56 offset1:60
	s_waitcnt lgkmcnt(5)
	v_pk_mov_b32 v[204:205], v[100:101], v[108:109] op_sel:[1,0]
	s_waitcnt lgkmcnt(3)
	v_mov_b32_e32 v208, v116
	s_waitcnt lgkmcnt(2)
	v_mov_b32_e32 v212, v184
	s_waitcnt lgkmcnt(1)
	v_pk_mov_b32 v[206:207], v[116:117], v[190:191] op_sel:[1,0]
	v_mov_b32_e32 v209, v191
	v_add_f32_e64 v204, v204, -v206
	v_add_f32_e64 v205, v205, -v207
	v_mov_b32_e32 v206, v100
	v_mov_b32_e32 v207, v109
	v_add_f32_e64 v206, v206, -v208
	v_add_f32_e64 v207, v207, -v209
	v_pk_mov_b32 v[208:209], v[102:103], v[110:111] op_sel:[1,0]
	s_waitcnt lgkmcnt(0)
; FFT_HD cf2 mk2(float x, float y) { return (cf2){x, y}; }
; FFT_HD cf2 cmul(cf2 a, cf2 b) { return mk2(a.x * b.x - a.y * b.y, a.x * b.y + a.y * b.x); }
; FFT_HD cf2 cadd(cf2 a, cf2 b) { return mk2(a.x + b.x, a.y + b.y); }
; FFT_HD cf2 csub(cf2 a, cf2 b) { return mk2(a.x - b.x, a.y - b.y); }
; template <bool INV> FFT_HD void dft4(cf2& a, cf2& b, cf2& c, cf2& d) {
;     const cf2 s0 = cadd(a, c), s1 = csub(a, c), s2 = cadd(b, d), s3 = csub(b, d);
;     a = cadd(s0, s2); c = csub(s0, s2);
;     const cf2 r = INV ? mk2(-s3.y, s3.x) : mk2(s3.y, -s3.x);
;     b = cadd(s1, r); d = csub(s1, r);
; }
; template <bool INV> FFT_HD void dft16(cf2 (&x)[16]) {
;     const float C1 = 0.9238795325112867f, S1 = 0.3826834323650898f, H = 0.7071067811865476f;
; #pragma unroll
;     for (int b = 0; b < 4; ++b) dft4<INV>(x[b], x[4 + b], x[8 + b], x[12 + b]);
;     const float s = INV ? -1.f : 1.f;
;     x[4 + 1] = cmul(x[4 + 1], mk2(C1, -s * S1)); x[8 + 1] = cmul(x[8 + 1], mk2(H, -s * H));   x[12 + 1] = cmul(x[12 + 1], mk2(S1, -s * C1));
;     x[4 + 2] = cmul(x[4 + 2], mk2(H, -s * H));   x[8 + 2] = cmul(x[8 + 2], mk2(0.f, -s));     x[12 + 2] = cmul(x[12 + 2], mk2(-H, -s * H));
;     x[4 + 3] = cmul(x[4 + 3], mk2(S1, -s * C1)); x[8 + 3] = cmul(x[8 + 3], mk2(-H, -s * H));  x[12 + 3] = cmul(x[12 + 3], mk2(-C1, s * S1));
; #pragma unroll
;     for (int c = 0; c < 4; ++c) dft4<INV>(x[4 * c], x[4 * c + 1], x[4 * c + 2], x[4 * c + 3]);
; #pragma unroll
;     for (int c = 0; c < 4; ++c)
; #pragma unroll
;         for (int d = c + 1; d < 4; ++d) { const cf2 t = x[4 * c + d]; x[4 * c + d] = x[4 * d + c]; x[4 * d + c] = t; }
; }
	v_pk_mov_b32 v[210:211], v[184:185], v[198:199] op_sel:[1,0]
	v_mov_b32_e32 v213, v199
	v_add_f32_e64 v208, v208, -v210
	v_add_f32_e64 v209, v209, -v211
	v_mov_b32_e32 v210, v102
	v_mov_b32_e32 v211, v111
	v_add_f32_e64 v210, v210, -v212
	v_add_f32_e64 v211, v211, -v213
	v_pk_mov_b32 v[212:213], v[104:105], v[112:113] op_sel:[1,0]
	v_pk_mov_b32 v[214:215], v[186:187], v[200:201] op_sel:[1,0]
	v_mov_b32_e32 v216, v186
	v_add_f32_e64 v212, v212, -v214
	v_add_f32_e64 v213, v213, -v215
	v_mov_b32_e32 v214, v104
	v_mov_b32_e32 v215, v113
	v_mov_b32_e32 v217, v201
	v_add_f32_e64 v214, v214, -v216
	v_add_f32_e64 v215, v215, -v217
	v_mov_b32_e32 v217, v212
	v_mov_b32_e32 v216, v214
	v_mov_b32_e32 v218, v215
	v_mov_b32_e32 v219, v213
	v_add_f32_e32 v56, v210, v211
	v_add_f32_e64 v220, v216, -v218
	v_add_f32_e64 v221, v217, -v219
	v_add_f32 v216, v216, v218
	v_add_f32 v217, v217, v219
	v_mul_f32_e32 v232, 0x3f3504f3, v56
	v_mov_b32_e32 v221, v217
	v_mul_f32_e32 v56, 0x3ec3ef15, v217
	v_add_f32 v226, v206, v207
	v_add_f32 v227, v206, v207
	s_mov_b32 s49, s26
	v_add_f32 v253, v214, v215
	v_add_f32 v215, v214, v215
	v_mov_b32_e32 v214, v253
	v_sub_f32_e32 v67, v208, v209
	v_fma_f32 v218, v220, s30, -v56
	v_fma_f32 v219, v221, s31, -v56
	v_mul_f32_e32 v236, 0x3ec3ef15, v220
	v_mul_f32_e32 v237, 0x3f6c835e, v217
	v_add_f32 v216, v98, v114
	v_add_f32 v217, v99, v115
	v_add_f32 v220, v106, v188
	v_add_f32 v221, v107, v189
	v_add_f32_e64 v98, v98, -v114
	v_add_f32_e64 v99, v99, -v115
	v_add_f32_e64 v106, v106, -v188
	v_add_f32_e64 v107, v107, -v189
	v_mul_f32_e64 v226, v226, s26
	v_mul_f32_e64 v227, v227, s27
	v_add_f32_e64 v228, v204, -v205
	v_add_f32_e64 v229, v204, -v205
	v_mul_f32_e64 v214, v214, s48
	v_mul_f32_e64 v215, v215, s49
	v_add_f32_e64 v253, v212, -v213
	v_add_f32_e64 v213, v212, -v213
	v_mov_b32_e32 v212, v253
	v_pk_mov_b32 v[114:115], v[106:107], v[106:107] op_sel:[1,0]
	v_add_f32 v188, v98, v107
	v_add_f32 v189, v99, v106
	v_add_f32_e64 v253, v98, -v107
	v_add_f32_e64 v107, v99, -v106
	v_mov_b32_e32 v106, v253
	v_fma_f32 v230, v228, s48, v226
	v_fma_f32 v231, v229, s49, v227
	v_fma_f32 v226, v228, s48, -v226
	v_fma_f32 v227, v229, s49, -v227
	v_fmamk_f32 v228, v67, 0x3f3504f3, v232
	v_fma_f32 v232, v67, s25, -v232
	v_fma_f32 v234, v212, s26, v214
	v_fma_f32 v235, v213, s27, v215
	v_fma_f32 v212, v212, s26, -v214
	v_fma_f32 v213, v213, s27, -v215
	v_mov_b32_e32 v224, v188
	v_mov_b32_e32 v225, v107
	v_mov_b32_e32 v226, v230
	v_mov_b32_e32 v233, v232
	v_mov_b32_e32 v229, v232
	v_mov_b32_e32 v212, v234
	v_add_f32 v214, v224, v228
	v_add_f32 v215, v225, v229
	v_add_f32 v224, v226, v212
	v_add_f32 v225, v227, v213
	v_pk_mov_b32 v[106:107], v[106:107], v[230:231] op_sel:[1,0]
	v_pk_mov_b32 v[230:231], v[232:233], v[234:235] op_sel:[1,0]
	v_mov_b32_e32 v226, v188
	v_add_f32_e64 v230, v106, -v230
	v_add_f32_e64 v231, v107, -v231
	v_mov_b32_e32 v229, v213
	v_add_f32 v106, v214, v224
	v_add_f32 v107, v215, v225
	v_mov_b32_e32 v56, v39
	v_add_f32_e64 v212, v226, -v228
	v_add_f32_e64 v213, v227, -v229
	v_mul_f32 v226, v56, v106
	v_mul_f32 v227, v56, v107
	v_add_f32 v100, v100, v116
	v_add_f32 v101, v101, v117
	v_add_f32 v108, v108, v190
	v_add_f32 v109, v109, v191
	v_add_f32 v102, v102, v184
	v_add_f32 v103, v103, v185
	v_add_f32 v184, v110, v198
	v_add_f32 v185, v111, v199
	v_add_f32 v104, v104, v186
	v_add_f32 v105, v105, v187
	v_add_f32 v112, v112, v200
	v_add_f32 v113, v113, v201
	v_fma_f32 v228, v38, v106, v227
	v_fma_f32 v229, v39, v107, v226
	v_fma_f32 v106, v38, v106, -v227
	v_fma_f32 v107, v38, v107, -v226
	v_add_f32 v222, v216, v220
	v_add_f32 v223, v217, v221
	v_add_f32 v190, v102, v184
	v_add_f32 v191, v103, v185
	v_mov_b32_e32 v229, v107
	v_add_f32_e64 v106, v216, -v220
	v_add_f32_e64 v107, v217, -v221
	v_add_f32_e64 v102, v102, -v184
	v_add_f32_e64 v103, v103, -v185
	v_mov_b32_e32 v184, v104
	v_mov_b32_e32 v185, v101
	v_mov_b32_e32 v216, v112
	v_mov_b32_e32 v217, v109
	v_add_f32_e64 v184, v184, -v216
	v_add_f32_e64 v185, v185, -v217
	v_mov_b32_e32 v216, v100
	v_mov_b32_e32 v217, v104
	v_mov_b32_e32 v220, v108
	v_mov_b32_e32 v221, v112
	v_add_f32 v116, v100, v108
	v_add_f32 v117, v101, v109
	v_add_f32 v186, v104, v112
	v_add_f32 v187, v105, v113
	v_add_f32_e64 v216, v216, -v220
	v_add_f32_e64 v217, v217, -v221
	v_mov_b32_e32 v220, v101
	v_mov_b32_e32 v221, v105
	v_mov_b32_e32 v226, v109
	v_mov_b32_e32 v227, v113
	v_pk_mov_b32 v[100:101], v[104:105], v[100:101] op_sel:[1,0]
	v_pk_mov_b32 v[104:105], v[112:113], v[108:109] op_sel:[1,0]
	v_add_f32_e64 v220, v220, -v226
	v_add_f32_e64 v221, v221, -v227
	v_add_f32_e64 v100, v100, -v104
	v_add_f32_e64 v101, v101, -v105
	v_fma_f32 v104, v102, 0, v103
	v_fma_f32 v105, v103, 0, v102
	v_fma_f32 v253, v102, 0, -v103
	v_fma_f32 v103, v103, 0, -v102
	v_mov_b32_e32 v102, v253
	s_mov_b32 s50, s25
	s_mov_b32 s51, s24
	v_mov_b32_e32 v105, v103
	v_mul_f32_e64 v102, v220, s50
	v_mul_f32_e64 v103, v221, s51
	v_mul_f32_e64 v100, v100, s24
	v_mul_f32_e64 v101, v101, s25
	v_fma_f32 v102, v216, s50, v102
	v_fma_f32 v103, v217, s51, v103
	v_fma_f32 v100, v184, s24, -v100
	v_fma_f32 v101, v185, s25, -v101
	v_add_f32 v108, v106, v104
	v_add_f32 v109, v107, v105
	v_add_f32 v184, v102, v100
	v_add_f32 v185, v103, v101
	v_pk_mov_b32 v[44:45], v[202:203], v[192:193] op_sel:[1,0]
	v_add_f32 v112, v108, v184
	v_add_f32 v113, v109, v185
	s_mov_b32 s56, s26
	v_mul_f32 v193, v192, v112
	v_mul_f32 v192, v192, v113
	v_fma_f32 v216, v203, v112, -v192
	v_fma_f32 v217, v203, v113, -v193
	v_fma_f32 v112, v203, v112, v192
	v_fma_f32 v113, v203, v113, v193
	v_mov_b32_e32 v192, v204
	v_mov_b32_e32 v217, v113
	v_mov_b32_e32 v112, v206
; template <bool INV> FFT_HD void dft16(cf2 (&x)[16]) {
;     const float C1 = 0.9238795325112867f, S1 = 0.3826834323650898f, H = 0.7071067811865476f;
; #pragma unroll
;     for (int b = 0; b < 4; ++b) dft4<INV>(x[b], x[4 + b], x[8 + b], x[12 + b]);
;     const float s = INV ? -1.f : 1.f;
;     x[4 + 1] = cmul(x[4 + 1], mk2(C1, -s * S1)); x[8 + 1] = cmul(x[8 + 1], mk2(H, -s * H));   x[12 + 1] = cmul(x[12 + 1], mk2(S1, -s * C1));
;     x[4 + 2] = cmul(x[4 + 2], mk2(H, -s * H));   x[8 + 2] = cmul(x[8 + 2], mk2(0.f, -s));     x[12 + 2] = cmul(x[12 + 2], mk2(-H, -s * H));
;     x[4 + 3] = cmul(x[4 + 3], mk2(S1, -s * C1)); x[8 + 3] = cmul(x[8 + 3], mk2(-H, -s * H));  x[12 + 3] = cmul(x[12 + 3], mk2(-C1, s * S1));
; #pragma unroll
;     for (int c = 0; c < 4; ++c) dft4<INV>(x[4 * c], x[4 * c + 1], x[4 * c + 2], x[4 * c + 3]);
; #pragma unroll
;     for (int c = 0; c < 4; ++c)
; #pragma unroll
;         for (int d = c + 1; d < 4; ++d) { const cf2 t = x[4 * c + d]; x[4 * c + d] = x[4 * d + c]; x[4 * d + c] = t; }
; }
; FFT_HD void fft_gen_tw(float frac, cf2 (&tw)[16]) {
;     float sn, cs; fft_sincos(frac, sn, cs);
;     tw[1] = mk2(cs, -sn);
;     tw[2] = cmul(tw[1], tw[1]); tw[3] = cmul(tw[2], tw[1]); tw[4] = cmul(tw[2], tw[2]); tw[5] = cmul(tw[4], tw[1]); tw[6] = cmul(tw[4], tw[2]); tw[7] = cmul(tw[4], tw[3]);
;     tw[8] = cmul(tw[4], tw[4]);
; #pragma unroll
;     for (int j = 9; j < 16; ++j) tw[j] = cmul(tw[8], tw[j - 8]);
; }
; template <bool INV, int lS, class ZP> FFT_HD void fft_r16_pass(ZP z, int tid) {
;     constexpr int S = 1 << lS, STEP = (S >= 64) ? S + S / 32 : S;
;     constexpr float inv = 1.0f / (float)(16 * S);
;     cf2 tw[16];
;     if (lS != 10) {
;         fft_gen_tw((float)(tid & (S - 1)) * inv, tw);
;         const int w0 = tid, w1 = tid + 512;
;         const int pb0 = PADI(((w0 >> lS) << (lS + 4)) + (w0 & (S - 1))), pb1 = PADI(((w1 >> lS) << (lS + 4)) + (w1 & (S - 1)));
;         cf2 x[16], y[16];
; #pragma unroll
;         for (int j = 0; j < 16; ++j) x[j] = z[pb0 + j * STEP];
; #pragma unroll
;         for (int j = 0; j < 16; ++j) y[j] = z[pb1 + j * STEP];
;         if (INV) {
; #pragma unroll
;             for (int j = 1; j < 16; ++j) x[j] = cmulc(x[j], tw[j]);
;         }
;         dft16<INV>(x);
;         if (!INV) {
; #pragma unroll
;             for (int j = 1; j < 16; ++j) x[j] = cmul(x[j], tw[j]);
;         }
	v_mov_b32_e32 v113, v210
	v_mov_b32_e32 v210, v207
	v_mov_b32_e32 v193, v208
	v_mov_b32_e32 v208, v205
	v_add_f32_e64 v112, v112, -v210
	v_add_f32_e64 v113, v113, -v211
	v_add_f32 v192, v192, v208
	v_add_f32 v193, v193, v209
	s_mov_b32 s57, s24
	v_pk_mov_b32 v[202:203], v[112:113], v[192:193] op_sel:[1,0]
	v_mul_f32_e64 v204, v192, s56
	v_mul_f32_e64 v205, v193, s57
	v_pk_mov_b32 v[192:193], v[192:193], v[112:113] op_sel:[1,0]
	s_mov_b32 s28, s25
	s_mov_b32 s52, s27
	s_mov_b32 s53, s24
	s_mov_b32 s54, s24
	s_mov_b32 s55, s27
	v_mul_f32_e64 v192, v192, s28
	v_mul_f32_e64 v193, v193, s29
	v_mov_b32_e32 v99, v236
	v_mov_b32_e32 v115, v237
	v_fma_f32 v192, v202, s54, v192
	v_fma_f32 v193, v203, s55, v193
	v_fma_f32 v202, v112, s52, v204
	v_fma_f32 v203, v113, s53, v205
	v_add_f32_e64 v98, v98, -v114
	v_add_f32_e64 v99, v99, -v115
	v_mov_b32_e32 v188, v218
	v_add_f32 v204, v192, v98
	v_add_f32 v205, v193, v99
	v_add_f32 v206, v202, v188
	v_add_f32 v207, v203, v189
	v_mov_b32_e32 v42, v72
	v_add_f32 v112, v206, v204
	v_add_f32 v113, v207, v205
	v_pk_mov_b32 v[40:41], v[70:71], v[72:73] op_sel:[1,0]
	v_mul_f32 v73, v72, v112
	v_mul_f32 v72, v72, v113
	v_mov_b32_e32 v43, v71
	v_fma_f32 v208, v71, v112, -v72
	v_fma_f32 v209, v71, v113, -v73
	v_fma_f32 v70, v71, v112, v72
	v_fma_f32 v71, v71, v113, v73
	v_add_f32_e64 v72, v116, -v186
	v_add_f32_e64 v73, v117, -v187
	v_mov_b32_e32 v209, v71
	v_add_f32_e64 v70, v222, -v190
	v_add_f32_e64 v71, v223, -v191
	v_add_f32 v198, v222, v190
	v_add_f32 v199, v223, v191
	v_add_f32 v200, v116, v186
	v_add_f32 v201, v117, v187
	v_add_f32 v186, v70, v73
	v_add_f32 v187, v71, v72
	v_add_f32_e64 v190, v70, -v73
	v_add_f32_e64 v191, v71, -v72
	v_mov_b32_e32 v70, v186
	v_pk_mov_b32 v[72:73], v[190:191], v[186:187] op_sel:[1,0]
	v_mov_b32_e32 v71, v191
	v_pk_mov_b32 v[112:113], v[68:69], v[48:49] op_sel:[1,0]
	v_mul_f32 v68, v69, v72
	v_mul_f32 v69, v69, v73
	v_add_f32_e64 v116, v230, -v231
	v_add_f32_e64 v117, v230, -v231
	v_fma_f32 v210, v48, v186, -v68
	v_fma_f32 v211, v49, v187, -v69
	v_fma_f32 v68, v48, v70, v68
	v_fma_f32 v69, v48, v71, v69
	v_mul_f32 v70, v56, v112
	v_mul_f32 v71, v56, v113
	v_mov_b32_e32 v211, v69
	v_fma_f32 v68, v38, v50, v70
	v_fma_f32 v69, v38, v51, v71
	v_fma_f32 v72, v38, v50, -v70
	v_fma_f32 v73, v38, v51, -v71
	v_mov_b32_e32 v71, v73
	v_pk_mov_b32 v[72:73], v[72:73], v[68:69] op_sel:[1,0]
	v_add_f32_e64 v104, v106, -v104
	v_add_f32_e64 v105, v107, -v105
	v_pk_mov_b32 v[106:107], v[100:101], v[102:103] op_sel:[1,0]
	v_pk_mov_b32 v[100:101], v[102:103], v[100:101] op_sel:[1,0]
	v_mov_b32_e32 v70, v68
	v_add_f32 v114, v212, v213
	v_add_f32 v115, v212, v213
	v_mul_f32 v116, v72, v116
	v_mul_f32 v117, v73, v117
	v_add_f32_e64 v100, v106, -v100
	v_add_f32_e64 v101, v107, -v101
	v_mul_f32 v96, v46, v50
	v_mul_f32 v97, v47, v51
	v_fma_f32 v220, v68, v114, -v116
	v_fma_f32 v221, v69, v115, -v117
	v_fma_f32 v114, v70, v114, v116
	v_fma_f32 v115, v71, v115, v117
	v_add_f32 v102, v104, v100
	v_add_f32 v103, v105, v101
	v_add_f32_e64 v100, v104, -v100
	v_add_f32_e64 v101, v105, -v101
	v_mul_f32 v94, v44, v50
	v_mul_f32 v95, v45, v51
	v_mov_b32_e32 v221, v115
	v_add_f32 v114, v96, v97
	v_add_f32 v115, v96, v97
	v_pk_mov_b32 v[96:97], v[100:101], v[102:103] op_sel:[1,0]
	v_mov_b32_e32 v104, v102
	v_mov_b32_e32 v105, v101
	v_mul_f32 v96, v114, v96
	v_mul_f32 v97, v115, v97
	v_add_f32_e64 v116, v94, -v95
	v_add_f32_e64 v117, v94, -v95
	v_fma_f32 v222, v116, v102, -v96
	v_fma_f32 v223, v117, v103, -v97
	v_fma_f32 v94, v116, v104, v96
	v_fma_f32 v95, v117, v105, v97
	v_pk_mov_b32 v[96:97], v[98:99], v[218:219] op_sel:[1,0]
	v_mov_b32_e32 v223, v95
	v_pk_mov_b32 v[94:95], v[192:193], v[202:203] op_sel:[1,0]
	v_mov_b32_e32 v99, v189
	v_mov_b32_e32 v193, v203
	v_add_f32_e64 v94, v94, -v96
	v_add_f32_e64 v95, v95, -v97
	v_add_f32_e64 v96, v98, -v192
	v_add_f32_e64 v97, v99, -v193
	v_mul_f32 v92, v50, v42
	v_mul_f32 v93, v51, v43
	v_add_f32 v188, v96, v94
	v_add_f32 v189, v97, v95
	v_add_f32_e64 v192, v96, -v94
	v_add_f32_e64 v193, v97, -v95
	v_mul_f32 v82, v50, v40
	v_mul_f32 v83, v51, v41
	v_add_f32 v104, v92, v93
	v_add_f32 v105, v92, v93
	v_pk_mov_b32 v[92:93], v[192:193], v[188:189] op_sel:[1,0]
	v_mov_b32_e32 v94, v188
	v_mov_b32_e32 v95, v193
	v_mul_f32 v92, v104, v92
	v_mul_f32 v93, v105, v93
	v_add_f32_e64 v106, v82, -v83
	v_add_f32_e64 v107, v82, -v83
	v_fma_f32 v202, v106, v188, -v92
	v_fma_f32 v203, v107, v189, -v93
	v_fma_f32 v82, v106, v94, v92
	v_fma_f32 v83, v107, v95, v93
	v_mul_f32 v90, v38, v54
	v_mul_f32 v91, v39, v55
	v_mov_b32_e32 v203, v83
	v_add_f32_e64 v82, v198, -v200
	v_add_f32_e64 v83, v199, -v201
	v_add_f32 v110, v198, v200
	v_add_f32 v111, v199, v201
	v_mul_f32 v92, v76, v82
	v_mul_f32 v93, v76, v83
	v_fma_f32 v198, v75, v82, -v93
	v_fma_f32 v199, v75, v83, -v92
	v_fma_f32 v82, v75, v82, v93
	v_fma_f32 v83, v75, v83, v92
	v_add_f32_e64 v92, v214, -v224
	v_add_f32_e64 v93, v215, -v225
	v_mov_b32_e32 v199, v83
	v_add_f32_e64 v82, v90, -v91
	v_add_f32_e64 v83, v90, -v91
	v_pk_mov_b32 v[52:53], v[74:75], v[76:77] op_sel:[1,0]
	v_mul_f32 v90, v82, v92
	v_mul_f32 v91, v83, v93
	v_add_f32 v253, v85, v84
	v_add_f32 v85, v85, v84
	v_mov_b32_e32 v84, v253
	v_mul_f32 v88, v46, v52
	v_mul_f32 v89, v47, v53
	v_fma_f32 v200, v84, v92, -v91
	v_fma_f32 v201, v85, v93, -v90
	v_fma_f32 v253, v84, v92, v91
	v_fma_f32 v91, v85, v93, v90
	v_mov_b32_e32 v90, v253
	v_mul_f32 v86, v46, v54
	v_mul_f32 v87, v47, v55
	v_mov_b32_e32 v201, v91
	v_add_f32_e64 v90, v108, -v184
	v_add_f32_e64 v91, v109, -v185
	v_add_f32 v184, v88, v89
	v_add_f32 v185, v88, v89
	v_mul_f32 v88, v184, v90
	v_mul_f32 v89, v185, v91
; FFT_HD cf2 cmul(cf2 a, cf2 b) { return mk2(a.x * b.x - a.y * b.y, a.x * b.y + a.y * b.x); }
; FFT_HD cf2 cmulc(cf2 a, cf2 b) { return mk2(a.x * b.x + a.y * b.y, a.y * b.x - a.x * b.y); }
; template <bool INV, int lS, class ZP> FFT_HD void fft_r16_pass(ZP z, int tid) {
;     ...
;         for (int j = 0; j < 16; ++j) y[j] = z[pb1 + j * STEP];
;         if (INV) {
; #pragma unroll
;             for (int j = 1; j < 16; ++j) x[j] = cmulc(x[j], tw[j]);
;         }
;         dft16<INV>(x);
;         if (!INV) {
; #pragma unroll
;             for (int j = 1; j < 16; ++j) x[j] = cmul(x[j], tw[j]);
;         }
; #pragma unroll
;         for (int j = 0; j < 16; ++j) z[pb0 + j * STEP] = x[j];
;         if (INV) {
; #pragma unroll
;             for (int j = 1; j < 16; ++j) y[j] = cmulc(y[j], tw[j]);
;         }
;         dft16<INV>(y);
;         if (!INV) {
; #pragma unroll
;             for (int j = 1; j < 16; ++j) y[j] = cmul(y[j], tw[j]);
;         }
; #pragma unroll
;         for (int j = 0; j < 16; ++j) z[pb1 + j * STEP] = y[j];
	v_add_f32_e64 v214, v87, -v86
	v_add_f32_e64 v215, v87, -v86
	v_mul_f32 v80, v42, v52
	v_mul_f32 v81, v43, v53
	v_fma_f32 v218, v214, v90, -v89
	v_fma_f32 v219, v215, v91, -v88
	v_fma_f32 v86, v214, v90, v89
	v_fma_f32 v87, v215, v91, v88
	v_mul_f32 v78, v42, v54
	v_mul_f32 v79, v43, v55
	v_mov_b32_e32 v219, v87
	v_mov_b32_e32 v86, v204
	v_mov_b32_e32 v87, v207
	v_mov_b32_e32 v207, v205
	v_add_f32_e64 v86, v86, -v206
	v_add_f32_e64 v87, v87, -v207
	v_add_f32 v253, v80, v81
	v_add_f32 v81, v80, v81
	v_mov_b32_e32 v80, v253
	v_mul_f32 v88, v80, v86
	v_mul_f32 v89, v81, v87
	v_add_f32_e64 v253, v79, -v78
	v_add_f32_e64 v79, v79, -v78
	v_mov_b32_e32 v78, v253
	v_add_f32 v96, v230, v231
	v_add_f32 v97, v230, v231
	v_fma_f32 v204, v78, v86, -v89
	v_fma_f32 v205, v79, v87, -v88
	v_fma_f32 v86, v78, v86, v89
	v_fma_f32 v87, v79, v87, v88
	v_mul_f32 v88, v50, v76
	v_mul_f32 v89, v51, v76
	v_mov_b32_e32 v205, v87
	v_fma_f32 v86, v50, v75, -v89
	v_fma_f32 v87, v51, v75, -v88
	v_fma_f32 v90, v50, v75, v89
	v_fma_f32 v91, v51, v75, v88
	v_mov_b32_e32 v88, v86
	v_mov_b32_e32 v89, v91
	v_pk_mov_b32 v[90:91], v[90:91], v[86:87] op_sel:[1,0]
	v_add_f32_e64 v94, v212, -v213
	v_add_f32_e64 v95, v212, -v213
	v_mul_f32 v92, v90, v187
	v_mul_f32 v93, v91, v187
	v_ashrrev_i32_e32 v3, 2, v4
	v_fma_f32 v186, v86, v190, -v92
	v_fma_f32 v187, v87, v191, -v93
	v_fma_f32 v92, v88, v190, v92
	v_fma_f32 v93, v89, v190, v93
	v_add3_u32 v60, v2, v3, s71
	v_mov_b32_e32 v187, v93
	v_mul_f32 v92, v76, v70
	v_mul_f32 v93, v76, v71
	v_fma_f32 v76, v75, v70, -v93
	v_fma_f32 v77, v75, v71, -v92
	v_fma_f32 v253, v75, v70, v93
	v_fma_f32 v93, v75, v71, v92
	v_mov_b32_e32 v92, v253
	v_mov_b32_e32 v74, v76
	v_mov_b32_e32 v75, v93
	v_pk_mov_b32 v[92:93], v[92:93], v[76:77] op_sel:[1,0]
	ds_read2_b64 v[2:5], v60 offset1:4
	ds_read2_b64 v[18:21], v60 offset0:8 offset1:12
	ds_read2_b64 v[6:9], v60 offset0:16 offset1:20
	ds_read2_b64 v[22:25], v60 offset0:24 offset1:28
	ds_read2_b64 v[10:13], v60 offset0:32 offset1:36
	ds_read2_b64 v[26:29], v60 offset0:40 offset1:44
	ds_read2_b64 v[14:17], v60 offset0:48 offset1:52
	ds_read2_b64 v[30:33], v60 offset0:56 offset1:60
	v_mul_f32 v96, v92, v96
	v_mul_f32 v97, v93, v97
	v_cmp_ne_u64_e32 vcc, 0, v[36:37]
	v_fma_f32 v190, v76, v94, -v96
	v_fma_f32 v191, v77, v95, -v97
	v_fma_f32 v94, v74, v94, v96
	v_fma_f32 v95, v75, v95, v97
	v_mul_f32 v96, v54, v116
	v_mul_f32 v97, v55, v117
	v_mov_b32_e32 v191, v95
	v_fma_f32 v94, -v54, v114, v97
	v_fma_f32 v95, -v55, v115, v96
	v_fma_f32 v98, v54, v114, v97
	v_fma_f32 v99, v55, v115, v96
	v_mov_b32_e32 v96, v94
	v_mov_b32_e32 v97, v99
	v_pk_mov_b32 v[98:99], v[98:99], v[94:95] op_sel:[1,0]
	s_nop 0
	v_mul_f32 v102, v98, v103
	v_mul_f32 v103, v99, v103
	s_nop 0
	v_fma_f32 v206, v94, v100, -v102
	v_fma_f32 v207, v95, v101, -v103
	v_fma_f32 v101, v97, v100, v103
	v_fma_f32 v100, v96, v100, v102
	v_mul_f32 v102, v54, v106
	v_mul_f32 v103, v55, v107
	v_mov_b32_e32 v207, v101
	v_fma_f32 v100, -v54, v104, v103
	v_fma_f32 v101, -v55, v105, v102
	v_fma_f32 v108, v54, v104, v103
	v_fma_f32 v109, v55, v105, v102
	v_mov_b32_e32 v102, v100
	v_mov_b32_e32 v103, v109
	v_pk_mov_b32 v[108:109], v[108:109], v[100:101] op_sel:[1,0]
	s_nop 0
	v_mul_f32 v188, v108, v189
	v_mul_f32 v189, v109, v189
	s_nop 0
	v_fma_f32 v212, v100, v192, -v188
	v_fma_f32 v213, v101, v193, -v189
	v_fma_f32 v188, v102, v192, v188
	v_fma_f32 v189, v103, v192, v189
	s_waitcnt lgkmcnt(2)
	v_mov_b32_e32 v192, v26
	v_mov_b32_e32 v213, v189
	ds_write2_b64 v65, v[110:111], v[228:229] offset1:4
	ds_write2_b64 v65, v[216:217], v[208:209] offset0:8 offset1:12
	ds_write2_b64 v65, v[210:211], v[220:221] offset0:16 offset1:20
	ds_write2_b64 v65, v[222:223], v[202:203] offset0:24 offset1:28
	ds_write2_b64 v65, v[198:199], v[200:201] offset0:32 offset1:36
	ds_write2_b64 v65, v[218:219], v[204:205] offset0:40 offset1:44
	ds_write2_b64 v65, v[186:187], v[190:191] offset0:48 offset1:52
	ds_write2_b64 v65, v[206:207], v[212:213] offset0:56 offset1:60
	v_pk_mov_b32 v[110:111], v[4:5], v[8:9] op_sel:[1,0]
	s_waitcnt lgkmcnt(9)
	v_pk_mov_b32 v[186:187], v[12:13], v[16:17] op_sel:[1,0]
	v_mov_b32_e32 v188, v12
	v_add_f32_e64 v110, v110, -v186
	v_add_f32_e64 v111, v111, -v187
	v_mov_b32_e32 v186, v4
	v_mov_b32_e32 v187, v9
	v_mov_b32_e32 v189, v17
	v_add_f32_e64 v186, v186, -v188
	v_add_f32_e64 v187, v187, -v189
	v_pk_mov_b32 v[188:189], v[18:19], v[22:23] op_sel:[1,0]
	s_waitcnt lgkmcnt(8)
; FFT_HD cf2 mk2(float x, float y) { return (cf2){x, y}; }
; FFT_HD cf2 cmul(cf2 a, cf2 b) { return mk2(a.x * b.x - a.y * b.y, a.x * b.y + a.y * b.x); }
; FFT_HD cf2 cadd(cf2 a, cf2 b) { return mk2(a.x + b.x, a.y + b.y); }
; FFT_HD cf2 csub(cf2 a, cf2 b) { return mk2(a.x - b.x, a.y - b.y); }
; template <bool INV> FFT_HD void dft4(cf2& a, cf2& b, cf2& c, cf2& d) {
;     const cf2 s0 = cadd(a, c), s1 = csub(a, c), s2 = cadd(b, d), s3 = csub(b, d);
;     a = cadd(s0, s2); c = csub(s0, s2);
;     const cf2 r = INV ? mk2(-s3.y, s3.x) : mk2(s3.y, -s3.x);
;     b = cadd(s1, r); d = csub(s1, r);
; }
; template <bool INV> FFT_HD void dft16(cf2 (&x)[16]) {
;     const float C1 = 0.9238795325112867f, S1 = 0.3826834323650898f, H = 0.7071067811865476f;
; #pragma unroll
;     for (int b = 0; b < 4; ++b) dft4<INV>(x[b], x[4 + b], x[8 + b], x[12 + b]);
;     const float s = INV ? -1.f : 1.f;
;     x[4 + 1] = cmul(x[4 + 1], mk2(C1, -s * S1)); x[8 + 1] = cmul(x[8 + 1], mk2(H, -s * H));   x[12 + 1] = cmul(x[12 + 1], mk2(S1, -s * C1));
;     x[4 + 2] = cmul(x[4 + 2], mk2(H, -s * H));   x[8 + 2] = cmul(x[8 + 2], mk2(0.f, -s));     x[12 + 2] = cmul(x[12 + 2], mk2(-H, -s * H));
;     x[4 + 3] = cmul(x[4 + 3], mk2(S1, -s * C1)); x[8 + 3] = cmul(x[8 + 3], mk2(-H, -s * H));  x[12 + 3] = cmul(x[12 + 3], mk2(-C1, s * S1));
; #pragma unroll
;     for (int c = 0; c < 4; ++c) dft4<INV>(x[4 * c], x[4 * c + 1], x[4 * c + 2], x[4 * c + 3]);
; #pragma unroll
;     for (int c = 0; c < 4; ++c)
; #pragma unroll
;         for (int d = c + 1; d < 4; ++d) { const cf2 t = x[4 * c + d]; x[4 * c + d] = x[4 * d + c]; x[4 * d + c] = t; }
; }
	v_pk_mov_b32 v[190:191], v[26:27], v[30:31] op_sel:[1,0]
	v_pk_mov_b32 v[204:205], v[20:21], v[4:5] op_sel:[1,0]
	v_pk_mov_b32 v[206:207], v[28:29], v[12:13] op_sel:[1,0]
	v_add_f32_e64 v188, v188, -v190
	v_add_f32_e64 v189, v189, -v191
	v_mov_b32_e32 v190, v18
	v_mov_b32_e32 v191, v23
	v_mov_b32_e32 v193, v31
	v_add_f32 v204, v204, v206
	v_add_f32 v205, v205, v207
	v_mov_b32_e32 v206, v4
	v_mov_b32_e32 v207, v20
	v_mov_b32_e32 v208, v12
	v_mov_b32_e32 v209, v28
	v_add_f32_e64 v190, v190, -v192
	v_add_f32_e64 v191, v191, -v193
	v_add_f32 v206, v206, v208
	v_add_f32 v207, v207, v209
	v_pk_mov_b32 v[208:209], v[24:25], v[8:9] op_sel:[1,0]
	v_pk_mov_b32 v[210:211], v[32:33], v[16:17] op_sel:[1,0]
	v_add_f32_e32 v39, v190, v191
	v_sub_f32_e32 v65, v188, v189
	v_sub_f32_e32 v67, v190, v191
	v_add_f32_e32 v198, v188, v189
	v_pk_mov_b32 v[188:189], v[20:21], v[24:25] op_sel:[1,0]
	v_pk_mov_b32 v[190:191], v[28:29], v[32:33] op_sel:[1,0]
	v_add_f32 v208, v208, v210
	v_add_f32 v209, v209, v211
	v_mov_b32_e32 v210, v8
	v_mov_b32_e32 v211, v24
	v_mov_b32_e32 v212, v16
	v_mov_b32_e32 v213, v32
	v_mov_b32_e32 v4, v20
	v_mov_b32_e32 v12, v28
	v_mov_b32_e32 v8, v24
	v_mov_b32_e32 v16, v32
	v_add_f32_e64 v188, v188, -v190
	v_add_f32_e64 v189, v189, -v191
	v_mov_b32_e32 v190, v20
	v_mov_b32_e32 v192, v28
	v_add_f32 v210, v210, v212
	v_add_f32 v211, v211, v213
	v_add_f32 v212, v4, v12
	v_add_f32 v213, v5, v13
	v_mov_b32_e32 v20, v5
	v_mov_b32_e32 v28, v13
	v_add_f32 v12, v8, v16
	v_add_f32 v13, v9, v17
	v_mov_b32_e32 v24, v9
	v_mov_b32_e32 v32, v17
	v_add_f32 v16, v18, v26
	v_add_f32 v17, v19, v27
	v_add_f32 v18, v22, v30
	v_add_f32 v19, v23, v31
	v_add_f32 v4, v20, v28
	v_add_f32 v5, v21, v29
	v_add_f32 v8, v24, v32
	v_add_f32 v9, v25, v33
	v_add_f32_e64 v20, v16, -v18
	v_add_f32_e64 v21, v17, -v19
	v_mov_b32_e32 v191, v25
	v_add_f32_e64 v24, v4, -v8
	v_add_f32_e64 v25, v5, -v9
	v_add_f32_e64 v26, v204, -v208
	v_add_f32_e64 v27, v205, -v209
	v_fma_f32 v28, v20, 0, v21
	v_fma_f32 v29, v21, 0, v20
	v_fma_f32 v253, v20, 0, -v21
	v_fma_f32 v21, v21, 0, -v20
	v_mov_b32_e32 v20, v253
	v_mov_b32_e32 v193, v33
	v_add_f32_e64 v12, v212, -v12
	v_add_f32_e64 v13, v213, -v13
	v_mov_b32_e32 v29, v21
	v_mul_f32_e64 v20, v24, s50
	v_mul_f32_e64 v21, v25, s51
	v_mul_f32_e64 v24, v26, s24
	v_mul_f32_e64 v25, v27, s25
	v_add_f32_e64 v190, v190, -v192
	v_add_f32_e64 v191, v191, -v193
	v_mul_f32_e32 v193, 0xbf3504f3, v198
	v_add_f32 v198, v2, v10
	v_add_f32 v199, v3, v11
	v_add_f32 v200, v6, v14
	v_add_f32 v201, v7, v15
	v_add_f32_e64 v22, v206, -v210
	v_add_f32_e64 v23, v207, -v211
	v_fma_f32 v12, v12, s24, -v24
	v_fma_f32 v13, v13, s25, -v25
	v_mov_b32_e32 v24, v206
	v_mov_b32_e32 v25, v4
	v_mov_b32_e32 v26, v210
	v_mov_b32_e32 v27, v8
	v_mov_b32_e32 v4, v207
	v_mov_b32_e32 v8, v211
	v_fma_f32 v20, v22, s50, v20
	v_fma_f32 v21, v23, s51, v21
	v_add_f32 v22, v198, v200
	v_add_f32 v23, v199, v201
	v_add_f32 v24, v24, v26
	v_add_f32 v25, v25, v27
	v_add_f32 v16, v16, v18
	v_add_f32 v17, v17, v19
	v_add_f32 v4, v4, v8
	v_add_f32 v5, v5, v9
	v_add_f32_e64 v202, v198, -v200
	v_add_f32_e64 v203, v199, -v201
	v_add_f32 v8, v22, v16
	v_add_f32 v9, v23, v17
	v_add_f32 v18, v24, v4
	v_add_f32 v19, v25, v5
	v_pk_mov_b32 v[26:27], v[22:23], v[24:25] op_sel:[1,0]
	v_pk_mov_b32 v[30:31], v[16:17], v[4:5] op_sel:[1,0]
	v_mov_b32_e32 v23, v25
	v_mov_b32_e32 v17, v5
	v_add_f32_e64 v4, v22, -v16
	v_add_f32_e64 v5, v23, -v17
	v_add_f32 v16, v8, v18
	v_add_f32 v17, v9, v19
	v_add_f32_e64 v8, v8, -v18
	v_add_f32_e64 v9, v9, -v19
	v_add_f32 v18, v202, v28
	v_add_f32 v19, v203, v29
	v_add_f32 v22, v20, v12
	v_add_f32 v23, v21, v13
	v_add_f32_e64 v26, v26, -v30
	v_add_f32_e64 v27, v27, -v31
	v_add_f32 v24, v18, v22
	v_add_f32 v25, v19, v23
	v_add_f32_e64 v18, v18, -v22
	v_add_f32_e64 v19, v19, -v23
	v_mul_f32 v22, v46, v25
	v_mul_f32 v23, v47, v25
	v_add_f32_e64 v2, v2, -v10
	v_add_f32_e64 v3, v3, -v11
	v_fma_f32 v30, v44, v24, -v22
	v_fma_f32 v31, v45, v25, -v23
	v_fma_f32 v22, v44, v24, v22
	v_fma_f32 v23, v45, v24, v23
	v_add_f32_e64 v24, v26, -v27
	v_add_f32_e64 v25, v26, -v27
	v_mov_b32_e32 v31, v23
	v_add_f32 v22, v4, v5
	v_add_f32 v23, v4, v5
	v_mul_f32 v24, v112, v24
	v_mul_f32 v25, v113, v25
	v_add_f32_e64 v10, v186, -v187
	v_add_f32_e64 v11, v186, -v187
	v_fma_f32 v32, v48, v22, -v24
	v_fma_f32 v33, v49, v23, -v25
	v_fma_f32 v22, v50, v22, v24
	v_fma_f32 v23, v51, v23, v25
	v_pk_mov_b32 v[24:25], v[12:13], v[20:21] op_sel:[1,0]
	v_pk_mov_b32 v[12:13], v[20:21], v[12:13] op_sel:[1,0]
	v_mov_b32_e32 v33, v23
	v_add_f32_e64 v22, v202, -v28
	v_add_f32_e64 v23, v203, -v29
	v_add_f32_e64 v12, v24, -v12
	v_add_f32_e64 v13, v25, -v13
	v_add_f32_e64 v6, v6, -v14
	v_add_f32_e64 v7, v7, -v15
	v_add_f32 v20, v22, v12
	v_add_f32 v21, v23, v13
	v_add_f32_e64 v12, v22, -v12
	v_add_f32_e64 v13, v23, -v13
	v_mov_b32_e32 v22, v20
	v_pk_mov_b32 v[24:25], v[12:13], v[20:21] op_sel:[1,0]
	v_mov_b32_e32 v23, v13
	v_mul_f32 v24, v114, v24
	v_mul_f32 v25, v115, v25
	v_mul_f32_e64 v10, v10, s48
	v_mul_f32_e64 v11, v11, s49
	v_fma_f32 v28, v116, v20, -v24
	v_fma_f32 v29, v117, v21, -v25
	v_fma_f32 v22, v116, v22, v24
	v_fma_f32 v23, v117, v23, v25
	v_add_f32 v14, v110, v111
	v_add_f32 v15, v110, v111
	v_mov_b32_e32 v29, v23
	v_mul_f32 v22, v54, v9
	v_mul_f32 v23, v55, v9
	v_mul_f32_e32 v192, 0xbf3504f3, v67
	v_fma_f32 v24, v52, v8, -v22
	v_fma_f32 v25, v53, v9, -v23
	v_fma_f32 v9, v53, v8, v23
	v_fma_f32 v8, v52, v8, v22
	v_sub_f32_e32 v192, v192, v193
	v_mov_b32_e32 v25, v9
	v_mul_f32 v8, v184, v18
	v_mul_f32 v9, v185, v19
	v_fmac_f32_e32 v193, 0xbf3504f3, v67
	v_fma_f32 v22, v214, v18, -v9
	v_fma_f32 v23, v215, v19, -v8
; __device__ __forceinline__ unsigned cvt_pk_bf16(float lo, float hi) { unsigned r; asm volatile("v_cvt_pk_bf16_f32 %0, %1, %2" : "=v"(r) : "v"(lo), "v"(hi)); return r; }
; FFT_HD cf2 cmul(cf2 a, cf2 b) { return mk2(a.x * b.x - a.y * b.y, a.x * b.y + a.y * b.x); }
; FFT_HD cf2 cmulc(cf2 a, cf2 b) { return mk2(a.x * b.x + a.y * b.y, a.y * b.x - a.x * b.y); }
; template <int BANK, int WAITN> __device__ __forceinline__ void bg_finish1(BgState& b) {
;     if (WAITN == 32) asm volatile("s_waitcnt vmcnt(32)" ::: "memory"); else asm volatile("s_waitcnt vmcnt(0)" ::: "memory");
;     asm volatile("" : BG_TIE16(BANK * 32) :: "memory");
;     asm volatile("" : BG_TIE16(BANK * 32 + 16) :: "memory");
;     bf16_t* dst = b.dst[BANK];
;     if (dst != nullptr) {
; #pragma unroll
;         for (int c = 0; c < 4; ++c) { u32x4 w;
;             w.x = cvt_pk_bf16(b.r[(BANK * 8 + 0) * 4 + c], b.r[(BANK * 8 + 1) * 4 + c]); w.y = cvt_pk_bf16(b.r[(BANK * 8 + 2) * 4 + c], b.r[(BANK * 8 + 3) * 4 + c]);
;             w.z = cvt_pk_bf16(b.r[(BANK * 8 + 4) * 4 + c], b.r[(BANK * 8 + 5) * 4 + c]); w.w = cvt_pk_bf16(b.r[(BANK * 8 + 6) * 4 + c], b.r[(BANK * 8 + 7) * 4 + c]);
;             bf16_t* dp = dst + (c & 1) * 512 + (c >> 1) * b.o2[BANK];
;             asm volatile("global_store_dwordx4 %0, %1, off\n\ts_nop 1" :: "v"(dp), "v"(w) : "memory"); }
;     }
; }
; template <bool INV, int lS, class ZP> FFT_HD void fft_r16_pass(ZP z, int tid) {
;     ...
;         if (INV) {
; #pragma unroll
;             for (int j = 1; j < 16; ++j) y[j] = cmulc(y[j], tw[j]);
;         }
;         dft16<INV>(y);
;         if (!INV) {
; #pragma unroll
;             for (int j = 1; j < 16; ++j) y[j] = cmul(y[j], tw[j]);
;         }
; #pragma unroll
;         for (int j = 0; j < 16; ++j) z[pb1 + j * STEP] = y[j];
	v_fma_f32 v253, v214, v18, v9
	v_fma_f32 v9, v215, v19, v8
	v_mov_b32_e32 v8, v253
	v_fma_f32 v18, v14, s26, v10
	v_fma_f32 v19, v15, s27, v11
	v_fma_f32 v10, v14, s26, -v10
	v_fma_f32 v11, v15, s27, -v11
	v_add_f32 v14, v188, v189
	v_add_f32 v15, v188, v189
	v_mov_b32_e32 v23, v9
	v_add_f32_e64 v8, v2, -v7
	v_add_f32_e64 v9, v3, -v6
	v_add_f32 v2, v2, v7
	v_add_f32 v3, v3, v6
	v_mov_b32_e32 v19, v11
	v_add_f32_e64 v10, v190, -v191
	v_add_f32_e64 v11, v190, -v191
	v_mul_f32_e64 v14, v14, s48
	v_mul_f32_e64 v15, v15, s49
	v_mov_b32_e32 v6, v8
	v_mov_b32_e32 v7, v3
	v_fma_f32 v10, v10, s30, -v14
	v_fma_f32 v11, v11, s31, -v15
	v_add_f32 v14, v6, v192
	v_add_f32 v15, v7, v193
	v_add_f32 v44, v18, v10
	v_add_f32 v45, v19, v11
	v_add_f32_e64 v6, v6, -v192
	v_add_f32_e64 v7, v7, -v193
	v_add_f32 v46, v14, v44
	v_add_f32 v47, v15, v45
	v_add_f32_e64 v10, v18, -v10
	v_add_f32_e64 v11, v19, -v11
	v_mul_f32 v42, v42, v47
	v_mul_f32 v43, v43, v47
	v_add_f32_e64 v14, v14, -v44
	v_add_f32_e64 v15, v15, -v45
	v_fma_f32 v44, v40, v46, -v42
	v_fma_f32 v45, v41, v47, -v43
	v_fma_f32 v40, v40, v46, v42
	v_fma_f32 v41, v41, v46, v43
	v_add_f32 v18, v6, v11
	v_add_f32 v19, v7, v10
	v_add_f32_e64 v6, v6, -v11
	v_add_f32_e64 v7, v7, -v10
	v_mov_b32_e32 v45, v41
	v_pk_mov_b32 v[40:41], v[6:7], v[18:19] op_sel:[1,0]
	v_mov_b32_e32 v10, v18
	v_mov_b32_e32 v11, v7
	v_mul_f32 v40, v104, v40
	v_mul_f32 v41, v105, v41
	v_add_f32 v50, v190, v191
	v_add_f32 v51, v190, v191
	v_fma_f32 v42, v106, v18, -v40
	v_fma_f32 v43, v107, v19, -v41
	v_fma_f32 v10, v106, v10, v40
	v_fma_f32 v11, v107, v11, v41
	v_mul_f32_e32 v39, 0x3f3504f3, v39
	v_mov_b32_e32 v43, v11
	v_add_f32 v10, v186, v187
	v_add_f32 v11, v186, v187
	v_mul_f32_e64 v10, v10, s26
	v_mul_f32_e64 v11, v11, s27
	v_add_f32_e64 v40, v110, -v111
	v_add_f32_e64 v41, v110, -v111
	v_mul_f32_e64 v50, v50, s48
	v_mul_f32_e64 v51, v51, s49
	v_add_f32_e64 v52, v188, -v189
	v_add_f32_e64 v53, v188, -v189
	v_fma_f32 v46, v40, s48, v10
	v_fma_f32 v47, v41, s49, v11
	v_fma_f32 v10, v40, s48, -v10
	v_fma_f32 v11, v41, s49, -v11
	v_fma_f32 v48, v65, s25, -v39
	v_fma_f32 v54, v52, s26, v50
	v_fma_f32 v55, v53, s27, v51
	v_fma_f32 v50, v52, s26, -v50
	v_fma_f32 v51, v53, s27, -v51
	v_mov_b32_e32 v10, v46
	v_fmamk_f32 v40, v65, 0x3f3504f3, v39
	v_mov_b32_e32 v41, v48
	v_mov_b32_e32 v50, v54
	v_mov_b32_e32 v3, v9
	v_mov_b32_e32 v49, v48
	v_add_f32 v52, v10, v50
	v_add_f32 v53, v11, v51
	v_add_f32 v104, v2, v40
	v_add_f32 v105, v3, v41
	v_mov_b32_e32 v3, v11
	v_mov_b32_e32 v41, v51
	v_add_f32_e64 v2, v2, -v40
	v_add_f32_e64 v3, v3, -v41
	v_pk_mov_b32 v[8:9], v[8:9], v[46:47] op_sel:[1,0]
	v_pk_mov_b32 v[10:11], v[48:49], v[54:55] op_sel:[1,0]
	v_add_f32 v40, v104, v52
	v_add_f32 v41, v105, v53
	v_add_f32_e64 v8, v8, -v10
	v_add_f32_e64 v9, v9, -v11
	v_mul_f32 v46, v56, v40
	v_mul_f32 v47, v56, v41
	v_fma_f32 v48, v38, v40, v47
	v_fma_f32 v49, v39, v41, v46
	v_fma_f32 v39, v38, v41, -v46
	v_fma_f32 v38, v38, v40, -v47
	v_add_f32_e64 v40, v8, -v9
	v_add_f32_e64 v41, v8, -v9
	v_mov_b32_e32 v49, v39
	v_add_f32 v38, v2, v3
	v_add_f32 v39, v2, v3
	v_mul_f32 v40, v72, v40
	v_mul_f32 v41, v73, v41
	v_add_f32_e64 v10, v104, -v52
	v_add_f32_e64 v11, v105, -v53
	v_fma_f32 v46, v68, v38, -v40
	v_fma_f32 v47, v69, v39, -v41
	v_fma_f32 v38, v70, v38, v40
	v_fma_f32 v39, v71, v39, v41
	v_add_f32_e64 v253, v4, -v5
	v_add_f32_e64 v5, v4, -v5
	v_mov_b32_e32 v4, v253
	v_mov_b32_e32 v47, v39
	v_mul_f32 v38, v82, v10
	v_mul_f32 v39, v83, v11
	v_add_f32_e64 v253, v2, -v3
	v_add_f32_e64 v3, v2, -v3
	v_mov_b32_e32 v2, v253
	v_fma_f32 v40, v84, v10, -v39
	v_fma_f32 v41, v85, v11, -v38
	v_fma_f32 v10, v84, v10, v39
	v_fma_f32 v11, v85, v11, v38
	s_nop 0
	v_mov_b32_e32 v41, v11
	v_mul_f32 v10, v80, v14
	v_mul_f32 v11, v81, v15
	s_nop 0
	v_fma_f32 v38, v78, v14, -v11
	v_fma_f32 v39, v79, v15, -v10
	v_fma_f32 v253, v78, v14, v11
	v_fma_f32 v11, v79, v15, v10
	v_mov_b32_e32 v10, v253
	s_nop 0
	v_mov_b32_e32 v39, v11
	v_add_f32 v10, v26, v27
	v_add_f32 v11, v26, v27
	v_mul_f32 v10, v90, v10
	v_mul_f32 v11, v91, v11
	s_nop 0
	v_fma_f32 v14, v86, v4, -v10
	v_fma_f32 v15, v87, v5, -v11
	v_fma_f32 v4, v88, v4, v10
	v_fma_f32 v5, v89, v5, v11
	s_nop 0
	v_mov_b32_e32 v15, v5
	v_add_f32 v4, v8, v9
	v_add_f32 v5, v8, v9
	v_mul_f32 v4, v92, v4
	v_mul_f32 v5, v93, v5
	s_nop 0
	v_fma_f32 v8, v76, v2, -v4
	v_fma_f32 v9, v77, v3, -v5
	v_fma_f32 v2, v74, v2, v4
	v_fma_f32 v3, v75, v3, v5
	s_nop 0
	v_mov_b32_e32 v9, v3
	v_mul_f32 v2, v98, v21
	v_mul_f32 v3, v99, v21
	s_nop 0
	v_fma_f32 v4, v94, v12, -v2
	v_fma_f32 v5, v95, v13, -v3
	v_fma_f32 v2, v96, v12, v2
	v_fma_f32 v3, v97, v12, v3
	s_nop 0
	v_mov_b32_e32 v5, v3
	v_mul_f32 v2, v108, v19
	v_mul_f32 v3, v109, v19
	s_nop 0
	v_fma_f32 v10, v100, v6, -v2
	v_fma_f32 v11, v101, v7, -v3
	v_fma_f32 v2, v102, v6, v2
	v_fma_f32 v3, v103, v6, v3
	s_nop 0
	v_mov_b32_e32 v11, v3
	ds_write2_b64 v60, v[16:17], v[48:49] offset1:4
	ds_write2_b64 v60, v[30:31], v[44:45] offset0:8 offset1:12
	ds_write2_b64 v60, v[32:33], v[46:47] offset0:16 offset1:20
	ds_write2_b64 v60, v[28:29], v[42:43] offset0:24 offset1:28
	ds_write2_b64 v60, v[24:25], v[40:41] offset0:32 offset1:36
	ds_write2_b64 v60, v[22:23], v[38:39] offset0:40 offset1:44
	ds_write2_b64 v60, v[14:15], v[8:9] offset0:48 offset1:52
	ds_write2_b64 v60, v[4:5], v[10:11] offset0:56 offset1:60
	s_waitcnt lgkmcnt(0)
	s_barrier
	s_waitcnt vmcnt(32)
	s_and_saveexec_b64 s[48:49], vcc
	s_cbranch_execz .LBB0_593
	v_cvt_pk_bf16_f32 v2, v176, v178
	v_cvt_pk_bf16_f32 v3, v177, v180
	v_cvt_pk_bf16_f32 v4, v179, v181
	v_cvt_pk_bf16_f32 v5, v182, v183
	v_lshl_add_u64 v[6:7], v[36:37], 0, s[22:23]
	global_store_dwordx4 v[36:37], v[2:5], off nt
	s_nop 1
	v_cvt_pk_bf16_f32 v2, v168, v170
	v_cvt_pk_bf16_f32 v3, v169, v172
	v_cvt_pk_bf16_f32 v4, v171, v173
	v_cvt_pk_bf16_f32 v5, v174, v175
	s_lshl_b32 s12, s44, 1
	global_store_dwordx4 v[6:7], v[2:5], off nt
	s_nop 1
	v_cvt_pk_bf16_f32 v2, v160, v162
	v_cvt_pk_bf16_f32 v3, v161, v164
	v_cvt_pk_bf16_f32 v4, v163, v165
	v_cvt_pk_bf16_f32 v5, v166, v167
	v_lshl_add_u64 v[8:9], v[36:37], 0, s[12:13]
	global_store_dwordx4 v[8:9], v[2:5], off nt
	s_nop 1
	v_cvt_pk_bf16_f32 v2, v152, v154
	v_cvt_pk_bf16_f32 v3, v153, v156
	v_cvt_pk_bf16_f32 v4, v155, v157
	v_cvt_pk_bf16_f32 v5, v158, v159
	v_lshl_add_u64 v[6:7], v[6:7], 0, s[12:13]
	global_store_dwordx4 v[6:7], v[2:5], off nt
	s_nop 1

; FFT_HD cf2 mk2(float x, float y) { return (cf2){x, y}; }
; FFT_HD cf2 cadd(cf2 a, cf2 b) { return mk2(a.x + b.x, a.y + b.y); }
; FFT_HD cf2 csub(cf2 a, cf2 b) { return mk2(a.x - b.x, a.y - b.y); }
; template <bool INV> FFT_HD void dft4(cf2& a, cf2& b, cf2& c, cf2& d) {
;     const cf2 s0 = cadd(a, c), s1 = csub(a, c), s2 = cadd(b, d), s3 = csub(b, d);
;     a = cadd(s0, s2); c = csub(s0, s2);
;     const cf2 r = INV ? mk2(-s3.y, s3.x) : mk2(s3.y, -s3.x);
;     b = cadd(s1, r); d = csub(s1, r);
; }
; template <bool INV, class ZP> FFT_HD void fft_r4_pass(ZP z, int tid, int nthr) {
;     for (int w = tid; w < FN / 4; w += nthr) {
;         const int base = PADI(4 * w);
;         cf2 a = z[base], b = z[base + 1], c = z[base + 2], d = z[base + 3];
;         dft4<INV>(a, b, c, d);
;         z[base] = a; z[base + 1] = b; z[base + 2] = c; z[base + 3] = d;
;     }
; }
.LBB0_605:
	v_and_b32_e32 v5, -16, v57
	v_add_u32_e32 v6, 0x200, v57
	v_add_u32_e32 v5, v4, v5
	v_cmp_lt_i32_e32 vcc, s82, v57
	v_mov_b32_e32 v57, v6
	ds_read_b128 v[6:9], v5
	ds_read_b128 v[10:13], v5 offset:16
	v_add_u32_e32 v4, 0x4000, v4
	s_or_b64 s[50:51], vcc, s[50:51]
	s_waitcnt lgkmcnt(0)
	v_add_f32 v14, v6, v10
	v_add_f32 v15, v7, v11
	v_add_f32 v16, v8, v12
	v_add_f32 v17, v9, v13
	v_add_f32_e64 v18, v6, -v10
	v_add_f32_e64 v19, v7, -v11
	v_add_f32_e64 v8, v8, -v12
	v_add_f32_e64 v9, v9, -v13
	v_add_f32 v6, v14, v16
	v_add_f32 v7, v15, v17
	v_add_f32_e64 v10, v14, -v16
	v_add_f32_e64 v11, v15, -v17
	v_add_f32 v14, v18, v9
	v_add_f32 v15, v19, v8
	v_add_f32_e64 v12, v18, -v9
	v_add_f32_e64 v13, v19, -v8
	v_mov_b32_e32 v8, v14
	v_mov_b32_e32 v9, v13
	v_mov_b32_e32 v13, v15
	ds_write_b128 v5, v[6:9]
	ds_write_b128 v5, v[10:13] offset:16
	s_andn2_b64 exec, exec, s[50:51]
	s_cbranch_execnz .LBB0_605

; __device__ __forceinline__ unsigned cvt_pk_bf16(float lo, float hi) { unsigned r; asm volatile("v_cvt_pk_bf16_f32 %0, %1, %2" : "=v"(r) : "v"(lo), "v"(hi)); return r; }
; FFT_HD int fpos(int k) { return ((k & 15) << 10) + (((k >> 4) & 15) << 6) + (((k >> 8) & 15) << 2) + (k >> 12); }
; __device__ __forceinline__ void hy_fft_phase(LAS unsigned char* lds, int bid, int G, const bf16_t* vgT, bf16_t* zT, const float* a3, const float* wout, const float* skip, float* filt, float4* gspec) {
;     ...
; #pragma unroll 4
;             for (int k = tid; k <= FN / 2; k += NTHR) {
;                 const cf2 zk = z[PADI(fpos(k))], zm = z[PADI(fpos((FN - k) & (FN - 1)))];
;                 u32x2 g; g.x = cvt_pk_bf16(0.5f * (zk.x + zm.x), 0.5f * (zk.y - zm.y)); g.y = cvt_pk_bf16(0.5f * (zk.y + zm.y), -0.5f * (zk.x - zm.x)); GS[k] = g;
;             }
.LBB0_620:
	v_and_b32_e32 v65, 0x3c0, v57
	v_lshrrev_b32_e32 v67, 6, v6
	v_ashrrev_i32_e32 v85, 12, v6
	v_and_b32_e32 v86, 0x3000, v7
	v_lshlrev_b32_e32 v88, 2, v7
	v_lshrrev_b32_e32 v89, 3, v7
	v_and_or_b32 v65, v60, s79, v65
	v_and_b32_e32 v67, 60, v67
	v_lshlrev_b32_e32 v87, 10, v7
	v_and_b32_e32 v88, 0x3c0, v88
	v_and_b32_e32 v89, 0x1e0, v89
	v_lshrrev_b32_e32 v86, 9, v86
	v_add3_u32 v65, v67, v85, v65
	v_and_or_b32 v67, v87, s79, v88
	v_add3_u32 v85, 0, v89, v86
	v_ashrrev_i32_e32 v86, 5, v65
	v_lshlrev_b32_e32 v87, 3, v67
	v_lshrrev_b32_e32 v67, 2, v67
	v_lshlrev_b32_e32 v86, 3, v86
	v_lshlrev_b32_e32 v65, 3, v65
	v_add3_u32 v67, v85, v87, v67
	v_and_b32_e32 v85, -16, v86
	v_add3_u32 v65, 0, v65, v85
	ds_read_b64 v[86:87], v65
	ds_read_b64 v[88:89], v67
	v_add_u32_e32 v90, 0x200, v6
	v_cmp_lt_i32_e32 vcc, s83, v6
	v_mov_b32_e32 v6, v90
	s_mov_b64 s[52:53], 0x1000
	s_waitcnt lgkmcnt(0)
	v_add_f32 v90, v86, v88
	v_add_f32 v91, v87, v89
	v_add_f32_e64 v86, v86, -v88
	v_add_f32_e64 v87, v87, -v89
	v_add_u32_e32 v7, 0xfffffe00, v7
	v_mul_f32_e32 v67, 0.5, v87
	v_mul_f32_e32 v87, -0.5, v86
	v_add_u32_e32 v57, 0x800, v57
	v_add_u32_e32 v60, 0x80000, v60
	s_or_b64 s[50:51], vcc, s[50:51]
	v_mul_f32_e32 v65, 0.5, v90
	v_mul_f32_e32 v85, 0.5, v91
	v_cvt_pk_bf16_f32 v86, v65, v67
	v_cvt_pk_bf16_f32 v87, v85, v87
	global_store_dwordx2 v[8:9], v[86:87], off
	v_lshl_add_u64 v[8:9], v[8:9], 0, s[52:53]
	s_andn2_b64 exec, exec, s[50:51]
	s_cbranch_execnz .LBB0_620

; FFT_HD cf2 mk2(float x, float y) { return (cf2){x, y}; }
; FFT_HD void fft_sincos(float frac, float& s, float& c) { s = __builtin_amdgcn_sinf(frac); c = __builtin_amdgcn_cosf(frac); }
; FFT_HD cf2 cmul(cf2 a, cf2 b) { return mk2(a.x * b.x - a.y * b.y, a.x * b.y + a.y * b.x); }
; FFT_HD cf2 cmulc(cf2 a, cf2 b) { return mk2(a.x * b.x + a.y * b.y, a.y * b.x - a.x * b.y); }
; FFT_HD void fft_gen_tw(float frac, cf2 (&tw)[16]) {
;     float sn, cs; fft_sincos(frac, sn, cs);
;     tw[1] = mk2(cs, -sn);
;     tw[2] = cmul(tw[1], tw[1]); tw[3] = cmul(tw[2], tw[1]); tw[4] = cmul(tw[2], tw[2]); tw[5] = cmul(tw[4], tw[1]); tw[6] = cmul(tw[4], tw[2]); tw[7] = cmul(tw[4], tw[3]);
;     tw[8] = cmul(tw[4], tw[4]);
; #pragma unroll
;     for (int j = 9; j < 16; ++j) tw[j] = cmul(tw[8], tw[j - 8]);
; }
; template <bool INV, int lS, class ZP> FFT_HD void fft_r16_pass(ZP z, int tid) {
;     ...
; #pragma unroll 1
;         for (int it = 0; it < 2; ++it) {
;             const int w = tid + 512 * it;
;             const int blk = w >> lS, p = w & (S - 1), pb = PADI((blk << (lS + 4)) + p);
;             fft_gen_tw((float)p * inv, tw);
;             cf2 x[16];
; #pragma unroll
;             for (int j = 0; j < 16; ++j) x[j] = z[pb + j * STEP];
;             if (INV) {
; #pragma unroll
;                 for (int j = 1; j < 16; ++j) x[j] = cmulc(x[j], tw[j]);
.LBB0_646:
	v_add_u32_e32 v4, s12, v120
	v_and_b32_e32 v5, 0x3ff, v4
	v_lshlrev_b32_e32 v4, 4, v4
	v_and_or_b32 v48, v4, s81, v5
	v_cvt_f32_u32_e32 v4, v5
	v_ashrrev_i32_e32 v49, 5, v48
	s_mov_b32 s50, s27
	s_mov_b32 s51, s26
	v_mul_f32_e32 v4, 0x38800000, v4
	v_sin_f32_e32 v29, v4
	v_cos_f32_e32 v28, v4
	s_mov_b32 s54, s26
	s_mov_b32 s55, s24
	v_mov_b32_e32 v14, v29
	v_mul_f32 v4, v28, v28
	v_mul_f32 v5, v29, v29
	v_mul_f32_e64 v6, v28, -v29
	v_mov_b32_e32 v7, v4
	v_mov_b32_e32 v4, v6
	v_add_f32 v74, v6, v4
	v_add_f32 v75, v7, v5
	v_add_f32_e64 v72, v6, -v4
	v_add_f32_e64 v73, v7, -v5
	v_mov_b32_e32 v12, v74
	v_mov_b32_e32 v13, v73
	v_mul_f32 v6, v12, v12
	v_mul_f32 v7, v13, v13
	v_mul_f32 v16, v73, v12
	v_mul_f32 v17, v72, v13
	v_pk_mov_b32 v[18:19], v[6:7], v[16:17] op_sel:[1,0]
	v_mov_b32_e32 v7, v16
	v_mov_b32_e32 v15, v28
	v_add_f32_e64 v38, v18, -v6
	v_add_f32_e64 v39, v19, -v7
	v_add_f32 v40, v18, v6
	v_add_f32 v41, v19, v7
	v_pk_mov_b32 v[4:5], v[72:73], v[74:75] op_sel:[1,0]
	v_mul_f32 v8, v14, v12
	v_mul_f32 v9, v15, v13
	v_mul_f32 v10, v28, v12
	v_mul_f32 v11, v29, v13
	v_mov_b32_e32 v6, v38
	v_mov_b32_e32 v7, v41
	v_mul_f32 v30, v4, v6
	v_mul_f32 v31, v5, v7
	v_mov_b32_e32 v4, v10
	v_mov_b32_e32 v5, v9
	v_pk_mov_b32 v[8:9], v[10:11], v[8:9] op_sel:[1,0]
	v_mul_f32 v32, v12, v6
	v_mul_f32 v33, v13, v7
	v_add_f32_e64 v44, v4, -v8
	v_add_f32_e64 v45, v5, -v9
	v_add_f32 v42, v4, v8
	v_add_f32 v43, v5, v9
	v_mul_f32 v8, v6, v41
	v_mul_f32 v9, v7, v40
	v_pk_mov_b32 v[4:5], v[42:43], v[44:45] op_sel:[1,0]
	v_mov_b32_e32 v36, v44
	v_mul_f32 v22, v6, v4
	v_mul_f32 v23, v7, v5
	v_mul_f32 v4, v6, v6
	v_mul_f32 v5, v7, v7
	v_mov_b32_e32 v37, v43
	v_mov_b32_e32 v9, v4
	v_mov_b32_e32 v4, v8
	v_add_f32 v10, v8, v4
	v_add_f32 v11, v9, v5
	v_add_f32_e64 v8, v8, -v4
	v_add_f32_e64 v9, v9, -v5
	v_mov_b32_e32 v4, v10
	v_mov_b32_e32 v5, v9
	v_pk_mov_b32 v[46:47], v[8:9], v[10:11] op_sel:[1,0]
	v_mul_f32 v26, v6, v36
	v_mul_f32 v27, v7, v37
	v_mul_f32 v20, v14, v4
	v_mul_f32 v21, v15, v5
	v_mul_f32 v16, v12, v4
	v_mul_f32 v17, v13, v5
	v_mul_f32 v18, v12, v46
	v_mul_f32 v19, v13, v47
	v_mul_f32 v12, v36, v4
	v_mul_f32 v13, v37, v5
	v_mul_f32 v14, v36, v46
	v_mul_f32 v15, v37, v47
	v_lshlrev_b32_e32 v36, 3, v49
	v_and_b32_e32 v36, 0xfffff0f0, v36
	v_lshlrev_b32_e32 v37, 3, v48
	v_add3_u32 v65, 0, v36, v37
	v_add_u32_e32 v67, 0x10800, v65
	v_add_u32_e32 v183, 0x12900, v65
	v_add_u32_e32 v186, 0x18c00, v65
	v_add_u32_e32 v187, 0x1ad00, v65
	ds_read_b64 v[52:53], v65
	ds_read_b64 v[36:37], v65 offset:8448
	ds_read_b64 v[46:47], v65 offset:16896
	ds_read_b64 v[50:51], v65 offset:25344
	ds_read_b64 v[78:79], v65 offset:33792
	ds_read_b64 v[56:57], v65 offset:42240
	ds_read_b64 v[68:69], v65 offset:50688
	ds_read_b64 v[70:71], v65 offset:59136
	ds_read_b64 v[76:77], v67
	ds_read_b64 v[88:89], v183
	ds_read_b64 v[108:109], v186
	ds_read_b64 v[90:91], v187
	v_add_u32_e32 v184, 0x14a00, v65
	v_add_u32_e32 v188, 0x1ce00, v65
	ds_read_b64 v[92:93], v184
	ds_read_b64 v[104:105], v188
	v_add_u32_e32 v185, 0x16b00, v65
	v_add_u32_e32 v189, 0x1ef00, v65
	ds_read_b64 v[94:95], v185
	ds_read_b64 v[110:111], v189
	s_waitcnt lgkmcnt(10)
	v_pk_mov_b32 v[48:49], v[36:37], v[56:57] op_sel:[1,0]
	s_waitcnt lgkmcnt(4)
	v_pk_mov_b32 v[54:55], v[88:89], v[90:91] op_sel:[1,0]
	v_add_f32 v100, v78, v108
	v_add_f32 v101, v79, v109
	v_add_f32_e64 v80, v48, -v54
	v_add_f32_e64 v81, v49, -v55
	v_mov_b32_e32 v48, v36
	v_mov_b32_e32 v49, v57
	v_mov_b32_e32 v54, v88
	v_mov_b32_e32 v55, v91
	v_add_f32_e64 v84, v48, -v54
	v_add_f32_e64 v85, v49, -v55
	v_pk_mov_b32 v[48:49], v[46:47], v[68:69] op_sel:[1,0]
	s_waitcnt lgkmcnt(2)
	v_pk_mov_b32 v[54:55], v[92:93], v[104:105] op_sel:[1,0]
	v_add_f32 v112, v84, v85
	v_add_f32 v113, v84, v85
	v_add_f32_e64 v82, v48, -v54
	v_add_f32_e64 v83, v49, -v55
	v_mov_b32_e32 v48, v46
	v_mov_b32_e32 v49, v69
	v_mov_b32_e32 v54, v92
	v_mov_b32_e32 v55, v105
	v_add_f32_e64 v86, v48, -v54
	v_add_f32_e64 v87, v49, -v55
	v_pk_mov_b32 v[48:49], v[50:51], v[70:71] op_sel:[1,0]
	s_waitcnt lgkmcnt(0)
	v_pk_mov_b32 v[54:55], v[94:95], v[110:111] op_sel:[1,0]
	v_add_f32_e32 v98, v86, v87
	v_add_f32_e64 v96, v48, -v54
	v_add_f32_e64 v97, v49, -v55
	v_mov_b32_e32 v48, v50
	v_mov_b32_e32 v49, v71
	v_mov_b32_e32 v54, v94
	v_mov_b32_e32 v55, v111
	v_add_f32_e64 v106, v48, -v54
	v_add_f32_e64 v107, v49, -v55
	v_mov_b32_e32 v49, v96
	v_mov_b32_e32 v48, v106
	v_mov_b32_e32 v54, v107
	v_mov_b32_e32 v55, v97
	v_mul_f32_e32 v192, 0x3f3504f3, v98
	v_add_f32_e64 v98, v48, -v54
	v_add_f32_e64 v99, v49, -v55
	v_add_f32 v54, v48, v54
	v_add_f32 v55, v49, v55
	v_add_f32 v253, v106, v107
	v_add_f32 v107, v106, v107
	v_mov_b32_e32 v106, v253
	v_mov_b32_e32 v99, v55
	v_mul_f32_e32 v48, 0x3ec3ef15, v55
	v_sub_f32_e32 v60, v82, v83
	v_fma_f32 v49, v99, s31, -v48
	v_fma_f32 v48, v98, s30, -v48
	v_mul_f32_e32 v190, 0x3ec3ef15, v98
	v_add_f32 v98, v52, v76
	v_add_f32 v99, v53, v77
	v_add_f32_e64 v76, v52, -v76
	v_add_f32_e64 v77, v53, -v77
	v_add_f32_e64 v108, v78, -v108
	v_add_f32_e64 v109, v79, -v109
	v_mul_f32_e64 v112, v112, s26
	v_mul_f32_e64 v113, v113, s27
	v_add_f32_e64 v114, v80, -v81
	v_add_f32_e64 v115, v80, -v81
	v_mul_f32_e64 v106, v106, s50
	v_mul_f32_e64 v107, v107, s51
	v_add_f32_e64 v253, v96, -v97
	v_add_f32_e64 v97, v96, -v97
	v_mov_b32_e32 v96, v253
	v_pk_mov_b32 v[78:79], v[108:109], v[108:109] op_sel:[1,0]
	v_add_f32 v52, v76, v109
	v_add_f32 v53, v77, v108
	v_add_f32_e64 v253, v76, -v109
	v_add_f32_e64 v109, v77, -v108
	v_mov_b32_e32 v108, v253
	v_fma_f32 v198, v114, s50, v112
	v_fma_f32 v199, v115, s51, v113
	v_fma_f32 v114, v114, s50, -v112
	v_fma_f32 v115, v115, s51, -v113
; FFT_HD cf2 mk2(float x, float y) { return (cf2){x, y}; }
; FFT_HD cf2 cmul(cf2 a, cf2 b) { return mk2(a.x * b.x - a.y * b.y, a.x * b.y + a.y * b.x); }
; template <bool INV> FFT_HD void dft16(cf2 (&x)[16]) {
;     const float C1 = 0.9238795325112867f, S1 = 0.3826834323650898f, H = 0.7071067811865476f;
; #pragma unroll
;     for (int b = 0; b < 4; ++b) dft4<INV>(x[b], x[4 + b], x[8 + b], x[12 + b]);
;     const float s = INV ? -1.f : 1.f;
;     x[4 + 1] = cmul(x[4 + 1], mk2(C1, -s * S1)); x[8 + 1] = cmul(x[8 + 1], mk2(H, -s * H));   x[12 + 1] = cmul(x[12 + 1], mk2(S1, -s * C1));
;     x[4 + 2] = cmul(x[4 + 2], mk2(H, -s * H));   x[8 + 2] = cmul(x[8 + 2], mk2(0.f, -s));     x[12 + 2] = cmul(x[12 + 2], mk2(-H, -s * H));
;     x[4 + 3] = cmul(x[4 + 3], mk2(S1, -s * C1)); x[8 + 3] = cmul(x[8 + 3], mk2(-H, -s * H));  x[12 + 3] = cmul(x[12 + 3], mk2(-C1, s * S1));
; #pragma unroll
;     for (int c = 0; c < 4; ++c) dft4<INV>(x[4 * c], x[4 * c + 1], x[4 * c + 2], x[4 * c + 3]);
; #pragma unroll
;     for (int c = 0; c < 4; ++c)
; #pragma unroll
;         for (int d = c + 1; d < 4; ++d) { const cf2 t = x[4 * c + d]; x[4 * c + d] = x[4 * d + c]; x[4 * d + c] = t; }
; }
	v_fmamk_f32 v200, v60, 0x3f3504f3, v192
	v_fma_f32 v192, v60, s25, -v192
	v_fma_f32 v202, v96, s26, v106
	v_fma_f32 v203, v97, s27, v107
	v_fma_f32 v96, v96, s26, -v106
	v_fma_f32 v97, v97, s27, -v107
	v_add_f32 v102, v46, v92
	v_add_f32 v103, v47, v93
	v_add_f32 v92, v50, v94
	v_add_f32 v93, v51, v95
	v_add_f32 v94, v70, v110
	v_add_f32 v95, v71, v111
	v_mov_b32_e32 v110, v52
	v_mov_b32_e32 v111, v109
	v_mov_b32_e32 v114, v198
	v_mov_b32_e32 v193, v192
	v_mov_b32_e32 v201, v192
	v_mov_b32_e32 v96, v202
	v_add_f32 v110, v110, v200
	v_add_f32 v111, v111, v201
	v_add_f32 v112, v114, v96
	v_add_f32 v113, v115, v97
	v_pk_mov_b32 v[106:107], v[108:109], v[198:199] op_sel:[1,0]
	v_pk_mov_b32 v[108:109], v[192:193], v[202:203] op_sel:[1,0]
	v_mov_b32_e32 v114, v52
	v_mov_b32_e32 v201, v97
	v_add_f32_e64 v106, v106, -v108
	v_add_f32_e64 v107, v107, -v109
	v_add_f32_e64 v108, v114, -v200
	v_add_f32_e64 v109, v115, -v201
	v_add_f32 v114, v110, v112
	v_add_f32 v115, v111, v113
	v_mov_b32_e32 v60, v29
	v_add_f32 v88, v36, v88
	v_add_f32 v89, v37, v89
	v_add_f32 v90, v56, v90
	v_add_f32 v91, v57, v91
	v_add_f32 v104, v68, v104
	v_add_f32 v105, v69, v105
	v_mul_f32 v192, v60, v114
	v_mul_f32 v193, v60, v115
	v_mul_f32_e32 v191, 0x3f6c835e, v55
	v_add_f32 v54, v98, v100
	v_add_f32 v55, v99, v101
	v_add_f32 v68, v102, v104
	v_add_f32 v69, v103, v105
	v_fma_f32 v96, v28, v114, v193
	v_fma_f32 v97, v29, v115, v192
	v_fma_f32 v114, v28, v114, -v193
	v_fma_f32 v115, v28, v115, -v192
	v_add_f32_e64 v98, v98, -v100
	v_add_f32_e64 v99, v99, -v101
	v_add_f32_e64 v100, v102, -v104
	v_add_f32_e64 v101, v103, -v105
	v_mov_b32_e32 v102, v92
	v_mov_b32_e32 v103, v89
	v_mov_b32_e32 v104, v94
	v_mov_b32_e32 v105, v91
	v_mov_b32_e32 v97, v115
	v_add_f32_e64 v102, v102, -v104
	v_add_f32_e64 v103, v103, -v105
	v_mov_b32_e32 v104, v88
	v_mov_b32_e32 v105, v92
	v_mov_b32_e32 v114, v90
	v_mov_b32_e32 v115, v94
	v_add_f32 v56, v88, v90
	v_add_f32 v57, v89, v91
	v_add_f32_e64 v104, v104, -v114
	v_add_f32_e64 v105, v105, -v115
	v_mov_b32_e32 v114, v89
	v_mov_b32_e32 v115, v93
	v_mov_b32_e32 v192, v91
	v_mov_b32_e32 v193, v95
	v_pk_mov_b32 v[88:89], v[92:93], v[88:89] op_sel:[1,0]
	v_pk_mov_b32 v[90:91], v[94:95], v[90:91] op_sel:[1,0]
	v_add_f32 v70, v92, v94
	v_add_f32 v71, v93, v95
	v_add_f32_e64 v114, v114, -v192
	v_add_f32_e64 v115, v115, -v193
	v_add_f32_e64 v90, v88, -v90
	v_add_f32_e64 v91, v89, -v91
	v_fma_f32 v88, v100, 0, v101
	v_fma_f32 v89, v101, 0, v100
	v_fma_f32 v92, v100, 0, -v101
	v_fma_f32 v93, v101, 0, -v100
	s_mov_b32 s50, s25
	s_mov_b32 s51, s24
	v_mov_b32_e32 v89, v93
	v_mul_f32_e64 v92, v114, s50
	v_mul_f32_e64 v93, v115, s51
	v_mul_f32_e64 v90, v90, s24
	v_mul_f32_e64 v91, v91, s25
	v_fma_f32 v92, v104, s50, v92
	v_fma_f32 v93, v105, s51, v93
	v_fma_f32 v90, v102, s24, -v90
	v_fma_f32 v91, v103, s25, -v91
	v_add_f32 v94, v98, v88
	v_add_f32 v95, v99, v89
	v_add_f32 v100, v92, v90
	v_add_f32 v101, v93, v91
	s_mov_b32 s28, s25
	v_add_f32 v102, v94, v100
	v_add_f32 v103, v95, v101
	s_mov_b32 s50, s27
	v_mul_f32 v104, v74, v103
	v_mul_f32 v105, v74, v102
	v_fma_f32 v74, v73, v102, -v104
	v_fma_f32 v75, v73, v103, -v105
	v_fma_f32 v72, v73, v102, v104
	v_fma_f32 v73, v73, v103, v105
	s_mov_b32 s52, s24
	v_mov_b32_e32 v75, v73
	v_mov_b32_e32 v72, v84
	v_mov_b32_e32 v73, v86
	v_mov_b32_e32 v86, v85
	v_mov_b32_e32 v84, v80
	v_mov_b32_e32 v85, v82
	v_mov_b32_e32 v82, v81
	v_add_f32_e64 v72, v72, -v86
	v_add_f32_e64 v73, v73, -v87
	v_add_f32 v80, v84, v82
	v_add_f32 v81, v85, v83
	s_mov_b32 s53, s27
	v_pk_mov_b32 v[82:83], v[72:73], v[80:81] op_sel:[1,0]
	v_mul_f32_e64 v84, v80, s54
	v_mul_f32_e64 v85, v81, s55
	v_pk_mov_b32 v[80:81], v[80:81], v[72:73] op_sel:[1,0]
	v_mov_b32_e32 v77, v190
	v_mul_f32_e64 v80, v80, s28
	v_mul_f32_e64 v81, v81, s29
	v_mov_b32_e32 v79, v191
	v_fma_f32 v80, v82, s52, v80
	v_fma_f32 v81, v83, s53, v81
	v_fma_f32 v72, v72, s50, v84
	v_fma_f32 v73, v73, s51, v85
	v_add_f32_e64 v76, v76, -v78
	v_add_f32_e64 v77, v77, -v79
	v_mov_b32_e32 v52, v48
	v_add_f32 v78, v80, v76
	v_add_f32 v79, v81, v77
	v_add_f32 v82, v72, v52
	v_add_f32 v83, v73, v53
	v_add_f32 v46, v54, v68
	v_add_f32 v47, v55, v69
	v_add_f32 v84, v82, v78
	v_add_f32 v85, v83, v79
	v_add_f32 v50, v56, v70
	v_add_f32 v51, v57, v71
	v_mul_f32 v45, v44, v84
	v_mul_f32 v44, v44, v85
	v_fma_f32 v86, v43, v84, -v44
	v_fma_f32 v87, v43, v85, -v45
	v_fma_f32 v42, v43, v84, v44
	v_fma_f32 v43, v43, v85, v45
	v_add_f32_e64 v44, v56, -v70
	v_add_f32_e64 v45, v57, -v71
	v_mov_b32_e32 v87, v43
	v_add_f32_e64 v42, v54, -v68
	v_add_f32_e64 v43, v55, -v69
	v_pk_mov_b32 v[56:57], v[40:41], v[38:39] op_sel:[1,0]
	v_add_f32 v54, v42, v45
	v_add_f32 v55, v43, v44
	v_add_f32_e64 v42, v42, -v45
	v_add_f32_e64 v43, v43, -v44
	v_mov_b32_e32 v44, v54
	v_pk_mov_b32 v[68:69], v[42:43], v[54:55] op_sel:[1,0]
	v_mov_b32_e32 v45, v43
	v_mul_f32 v40, v41, v68
	v_mul_f32 v41, v41, v69
	v_mul_f32 v24, v28, v4
	v_mul_f32 v25, v29, v5
	v_fma_f32 v68, v38, v54, -v40
	v_fma_f32 v69, v39, v55, -v41
	v_fma_f32 v39, v38, v45, v41
	v_fma_f32 v38, v38, v44, v40
	v_mov_b32_e32 v69, v39
	v_mul_f32 v38, v60, v56
	v_mul_f32 v39, v60, v57
	v_fma_f32 v40, v28, v6, v38
	v_fma_f32 v41, v28, v7, v39
	v_fma_f32 v29, v28, v7, -v39
	v_fma_f32 v28, v28, v6, -v38
	v_mov_b32_e32 v39, v29
	v_pk_mov_b32 v[28:29], v[28:29], v[40:41] op_sel:[1,0]
	v_add_f32_e64 v56, v106, -v107
	v_add_f32_e64 v57, v106, -v107
	v_mov_b32_e32 v38, v40
	v_add_f32 v44, v108, v109
	v_add_f32 v45, v108, v109
	v_mul_f32 v28, v28, v56
	v_mul_f32 v29, v29, v57
	v_pk_mov_b32 v[56:57], v[92:93], v[90:91] op_sel:[1,0]
	v_fma_f32 v40, v40, v44, -v28
; FFT_HD cf2 mk2(float x, float y) { return (cf2){x, y}; }
; FFT_HD void fft_sincos(float frac, float& s, float& c) { s = __builtin_amdgcn_sinf(frac); c = __builtin_amdgcn_cosf(frac); }
; FFT_HD cf2 cmul(cf2 a, cf2 b) { return mk2(a.x * b.x - a.y * b.y, a.x * b.y + a.y * b.x); }
; template <bool INV> FFT_HD void dft16(cf2 (&x)[16]) {
;     const float C1 = 0.9238795325112867f, S1 = 0.3826834323650898f, H = 0.7071067811865476f;
; #pragma unroll
;     for (int b = 0; b < 4; ++b) dft4<INV>(x[b], x[4 + b], x[8 + b], x[12 + b]);
;     const float s = INV ? -1.f : 1.f;
;     x[4 + 1] = cmul(x[4 + 1], mk2(C1, -s * S1)); x[8 + 1] = cmul(x[8 + 1], mk2(H, -s * H));   x[12 + 1] = cmul(x[12 + 1], mk2(S1, -s * C1));
;     x[4 + 2] = cmul(x[4 + 2], mk2(H, -s * H));   x[8 + 2] = cmul(x[8 + 2], mk2(0.f, -s));     x[12 + 2] = cmul(x[12 + 2], mk2(-H, -s * H));
;     x[4 + 3] = cmul(x[4 + 3], mk2(S1, -s * C1)); x[8 + 3] = cmul(x[8 + 3], mk2(-H, -s * H));  x[12 + 3] = cmul(x[12 + 3], mk2(-C1, s * S1));
; #pragma unroll
;     for (int c = 0; c < 4; ++c) dft4<INV>(x[4 * c], x[4 * c + 1], x[4 * c + 2], x[4 * c + 3]);
; #pragma unroll
;     for (int c = 0; c < 4; ++c)
; #pragma unroll
;         for (int d = c + 1; d < 4; ++d) { const cf2 t = x[4 * c + d]; x[4 * c + d] = x[4 * d + c]; x[4 * d + c] = t; }
; }
; FFT_HD void fft_gen_tw(float frac, cf2 (&tw)[16]) {
;     float sn, cs; fft_sincos(frac, sn, cs);
;     tw[1] = mk2(cs, -sn);
;     tw[2] = cmul(tw[1], tw[1]); tw[3] = cmul(tw[2], tw[1]); tw[4] = cmul(tw[2], tw[2]); tw[5] = cmul(tw[4], tw[1]); tw[6] = cmul(tw[4], tw[2]); tw[7] = cmul(tw[4], tw[3]);
;     tw[8] = cmul(tw[4], tw[4]);
; #pragma unroll
;     for (int j = 9; j < 16; ++j) tw[j] = cmul(tw[8], tw[j - 8]);
; }
; template <bool INV, int lS, class ZP> FFT_HD void fft_r16_pass(ZP z, int tid) {
;     ...
;             dft16<INV>(x);
;             if (!INV) {
; #pragma unroll
;                 for (int j = 1; j < 16; ++j) x[j] = cmul(x[j], tw[j]);
;             }
; #pragma unroll
;             for (int j = 0; j < 16; ++j) z[pb + j * STEP] = x[j];
;         }
	v_fma_f32 v41, v41, v45, -v29
	v_fma_f32 v28, v38, v44, v28
	v_fma_f32 v29, v39, v45, v29
	v_pk_mov_b32 v[44:45], v[90:91], v[92:93] op_sel:[1,0]
	v_mov_b32_e32 v41, v29
	v_add_f32_e64 v28, v98, -v88
	v_add_f32_e64 v29, v99, -v89
	v_add_f32_e64 v44, v44, -v56
	v_add_f32_e64 v45, v45, -v57
	v_add_f32 v253, v32, v33
	v_add_f32 v33, v32, v33
	v_mov_b32_e32 v32, v253
	v_add_f32 v56, v28, v44
	v_add_f32 v57, v29, v45
	v_add_f32_e64 v28, v28, -v44
	v_add_f32_e64 v29, v29, -v45
	v_mov_b32_e32 v44, v56
	v_pk_mov_b32 v[70:71], v[28:29], v[56:57] op_sel:[1,0]
	v_mov_b32_e32 v45, v29
	v_mul_f32 v70, v32, v70
	v_mul_f32 v71, v33, v71
	v_add_f32_e64 v253, v30, -v31
	v_add_f32_e64 v31, v30, -v31
	v_mov_b32_e32 v30, v253
	v_fma_f32 v84, v30, v56, -v70
	v_fma_f32 v85, v31, v57, -v71
	v_fma_f32 v44, v30, v44, v70
	v_fma_f32 v45, v31, v45, v71
	v_pk_mov_b32 v[48:49], v[76:77], v[48:49] op_sel:[1,0]
	v_mov_b32_e32 v85, v45
	v_pk_mov_b32 v[44:45], v[80:81], v[72:73] op_sel:[1,0]
	v_mov_b32_e32 v77, v53
	v_mov_b32_e32 v81, v73
	v_add_f32_e64 v44, v44, -v48
	v_add_f32_e64 v45, v45, -v49
	v_add_f32_e64 v48, v76, -v80
	v_add_f32_e64 v49, v77, -v81
	v_add_f32 v253, v26, v27
	v_add_f32 v27, v26, v27
	v_mov_b32_e32 v26, v253
	v_add_f32 v52, v48, v44
	v_add_f32 v53, v49, v45
	v_add_f32_e64 v44, v48, -v44
	v_add_f32_e64 v45, v49, -v45
	v_mov_b32_e32 v48, v52
	v_pk_mov_b32 v[70:71], v[44:45], v[52:53] op_sel:[1,0]
	v_mov_b32_e32 v49, v45
	v_mul_f32 v70, v26, v70
	v_mul_f32 v71, v27, v71
	v_add_f32_e64 v253, v22, -v23
	v_add_f32_e64 v23, v22, -v23
	v_mov_b32_e32 v22, v253
	v_add_f32 v36, v46, v50
	v_add_f32 v37, v47, v51
	v_fma_f32 v72, v22, v52, -v70
	v_fma_f32 v73, v23, v53, -v71
	v_fma_f32 v48, v22, v48, v70
	v_fma_f32 v49, v23, v49, v71
	v_add_f32_e64 v46, v46, -v50
	v_add_f32_e64 v47, v47, -v51
	v_mov_b32_e32 v73, v49
	v_mul_f32 v48, v10, v46
	v_mul_f32 v49, v10, v47
	v_fma_f32 v50, v9, v46, -v49
	v_fma_f32 v51, v9, v47, -v48
	v_fma_f32 v46, v9, v46, v49
	v_fma_f32 v47, v9, v47, v48
	v_add_f32_e64 v253, v24, -v25
	v_add_f32_e64 v25, v24, -v25
	v_mov_b32_e32 v24, v253
	v_mov_b32_e32 v51, v47
	v_add_f32_e64 v46, v110, -v112
	v_add_f32_e64 v47, v111, -v113
	v_add_f32 v253, v21, v20
	v_add_f32 v21, v21, v20
	v_mov_b32_e32 v20, v253
	v_mul_f32 v24, v24, v47
	v_mul_f32 v25, v25, v46
	v_add_f32 v253, v18, v19
	v_add_f32 v19, v18, v19
	v_mov_b32_e32 v18, v253
	v_fma_f32 v48, v20, v46, -v24
	v_fma_f32 v49, v21, v47, -v25
	v_fma_f32 v20, v20, v46, v24
	v_fma_f32 v21, v21, v47, v25
	v_add_f32_e64 v253, v17, -v16
	v_add_f32_e64 v17, v17, -v16
	v_mov_b32_e32 v16, v253
	v_mov_b32_e32 v49, v21
	v_add_f32_e64 v20, v94, -v100
	v_add_f32_e64 v21, v95, -v101
	v_add_f32 v253, v14, v15
	v_add_f32 v15, v14, v15
	v_mov_b32_e32 v14, v253
	v_mul_f32 v18, v18, v21
	v_mul_f32 v19, v19, v20
	v_add_f32_e64 v253, v13, -v12
	v_add_f32_e64 v13, v13, -v12
	v_mov_b32_e32 v12, v253
	v_fma_f32 v24, v16, v20, -v18
	v_fma_f32 v25, v17, v21, -v19
	v_fma_f32 v16, v16, v20, v18
	v_fma_f32 v17, v17, v21, v19
	s_movk_i32 s12, 0x200
	v_mov_b32_e32 v25, v17
	v_mov_b32_e32 v16, v78
	v_mov_b32_e32 v17, v83
	v_mov_b32_e32 v83, v79
	v_add_f32_e64 v16, v16, -v82
	v_add_f32_e64 v17, v17, -v83
	s_and_b64 vcc, exec, s[46:47]
	v_mul_f32 v14, v14, v17
	v_mul_f32 v15, v15, v16
	s_mov_b64 s[46:47], 0
	v_fma_f32 v18, v12, v16, -v14
	v_fma_f32 v19, v13, v17, -v15
	v_fma_f32 v12, v12, v16, v14
	v_fma_f32 v13, v13, v17, v15
	v_add_f32 v16, v106, v107
	v_add_f32 v17, v106, v107
	v_mov_b32_e32 v19, v13
	v_mul_f32 v12, v6, v10
	v_mul_f32 v13, v7, v10
	s_nop 0
	v_fma_f32 v14, v6, v9, -v13
	v_fma_f32 v15, v7, v9, -v12
	v_fma_f32 v6, v6, v9, v13
	v_fma_f32 v7, v7, v9, v12
	v_mov_b32_e32 v12, v14
	v_mov_b32_e32 v13, v7
	v_pk_mov_b32 v[6:7], v[6:7], v[14:15] op_sel:[1,0]
	s_nop 0
	v_mul_f32 v6, v6, v55
	v_mul_f32 v7, v7, v55
	s_nop 0
	v_fma_f32 v14, v14, v42, -v6
	v_fma_f32 v15, v15, v43, -v7
	v_fma_f32 v6, v12, v42, v6
	v_fma_f32 v7, v13, v42, v7
	v_add_f32_e64 v12, v108, -v109
	v_add_f32_e64 v13, v108, -v109
	v_mov_b32_e32 v15, v7
	v_mul_f32 v6, v10, v38
	v_mul_f32 v7, v10, v39
	v_fma_f32 v10, v9, v38, -v7
	v_fma_f32 v11, v9, v39, -v6
	v_fma_f32 v253, v9, v38, v7
	v_fma_f32 v7, v9, v39, v6
	v_mov_b32_e32 v6, v253
	v_mov_b32_e32 v8, v10
	v_mov_b32_e32 v9, v7
	v_pk_mov_b32 v[6:7], v[6:7], v[10:11] op_sel:[1,0]
	s_nop 0
	v_mul_f32 v6, v6, v16
	v_mul_f32 v7, v7, v17
	s_nop 0
	v_fma_f32 v10, v10, v12, -v6
	v_fma_f32 v11, v11, v13, -v7
	v_fma_f32 v6, v8, v12, v6
	v_fma_f32 v7, v9, v13, v7
	s_nop 0
	v_mov_b32_e32 v11, v7
	v_mul_f32 v6, v4, v30
	v_mul_f32 v7, v5, v31
	s_nop 0
	v_fma_f32 v8, -v4, v32, v7
	v_fma_f32 v9, -v5, v33, v6
	v_fma_f32 v253, v4, v32, v7
	v_fma_f32 v7, v5, v33, v6
	v_mov_b32_e32 v6, v253
	v_mov_b32_e32 v12, v8
	v_mov_b32_e32 v13, v7
	v_pk_mov_b32 v[6:7], v[6:7], v[8:9] op_sel:[1,0]
	s_nop 0
	v_mul_f32 v6, v6, v57
	v_mul_f32 v7, v7, v57
	s_nop 0
	v_fma_f32 v8, v8, v28, -v6
	v_fma_f32 v9, v9, v29, -v7
	v_fma_f32 v6, v12, v28, v6
	v_fma_f32 v7, v13, v28, v7
	s_nop 0
	v_mov_b32_e32 v9, v7
	v_mul_f32 v6, v4, v22
	v_mul_f32 v7, v5, v23
	s_nop 0
	v_fma_f32 v12, -v4, v26, v7
	v_fma_f32 v13, -v5, v27, v6
	v_fma_f32 v4, v4, v26, v7
	v_fma_f32 v5, v5, v27, v6
	v_mov_b32_e32 v6, v12
	v_mov_b32_e32 v7, v5
	v_pk_mov_b32 v[4:5], v[4:5], v[12:13] op_sel:[1,0]
	s_nop 0
	v_mul_f32 v4, v4, v53
	v_mul_f32 v5, v5, v53
	s_nop 0
	v_fma_f32 v12, v12, v44, -v4
	v_fma_f32 v13, v13, v45, -v5
	v_fma_f32 v4, v6, v44, v4
	v_fma_f32 v5, v7, v44, v5
	s_nop 0
	v_mov_b32_e32 v13, v5
	ds_write_b64 v65, v[36:37]
	ds_write_b64 v65, v[96:97] offset:8448
	ds_write_b64 v65, v[74:75] offset:16896
	ds_write_b64 v65, v[86:87] offset:25344
	ds_write_b64 v65, v[68:69] offset:33792
	ds_write_b64 v65, v[40:41] offset:42240
	ds_write_b64 v65, v[84:85] offset:50688
	ds_write_b64 v65, v[72:73] offset:59136
	ds_write_b64 v67, v[50:51]
	ds_write_b64 v183, v[48:49]
	ds_write_b64 v184, v[24:25]
	ds_write_b64 v185, v[18:19]
	ds_write_b64 v186, v[14:15]
	ds_write_b64 v187, v[10:11]
	ds_write_b64 v188, v[8:9]
	ds_write_b64 v189, v[12:13]
	s_cbranch_vccnz .LBB0_646
; __device__ __forceinline__ unsigned cvt_pk_bf16(float lo, float hi) { unsigned r; asm volatile("v_cvt_pk_bf16_f32 %0, %1, %2" : "=v"(r) : "v"(lo), "v"(hi)); return r; }
; template <int BANK, int WAITN> __device__ __forceinline__ void bg_finish1(BgState& b) {
;     if (WAITN == 32) asm volatile("s_waitcnt vmcnt(32)" ::: "memory"); else asm volatile("s_waitcnt vmcnt(0)" ::: "memory");
;     asm volatile("" : BG_TIE16(BANK * 32) :: "memory");
;     asm volatile("" : BG_TIE16(BANK * 32 + 16) :: "memory");
;     bf16_t* dst = b.dst[BANK];
;     if (dst != nullptr) {
; #pragma unroll
;         for (int c = 0; c < 4; ++c) { u32x4 w;
;             w.x = cvt_pk_bf16(b.r[(BANK * 8 + 0) * 4 + c], b.r[(BANK * 8 + 1) * 4 + c]); w.y = cvt_pk_bf16(b.r[(BANK * 8 + 2) * 4 + c], b.r[(BANK * 8 + 3) * 4 + c]);
;             w.z = cvt_pk_bf16(b.r[(BANK * 8 + 4) * 4 + c], b.r[(BANK * 8 + 5) * 4 + c]); w.w = cvt_pk_bf16(b.r[(BANK * 8 + 6) * 4 + c], b.r[(BANK * 8 + 7) * 4 + c]);
;             bf16_t* dp = dst + (c & 1) * 512 + (c >> 1) * b.o2[BANK];
;             asm volatile("global_store_dwordx4 %0, %1, off\n\ts_nop 1" :: "v"(dp), "v"(w) : "memory"); }
;     }
; }
	s_waitcnt lgkmcnt(0)
	s_barrier
	s_waitcnt vmcnt(32)
	v_cmp_ne_u64_e32 vcc, 0, v[2:3]
	s_and_saveexec_b64 s[46:47], vcc
	s_cbranch_execz .LBB0_649
	v_cvt_pk_bf16_f32 v4, v175, v177
	v_cvt_pk_bf16_f32 v5, v176, v179
	v_cvt_pk_bf16_f32 v6, v178, v181
	v_cvt_pk_bf16_f32 v7, v180, v182
	s_lshl_b32 s12, s48, 1
	global_store_dwordx4 v[2:3], v[4:7], off nt
	s_nop 1
	v_cvt_pk_bf16_f32 v4, v167, v169
	v_cvt_pk_bf16_f32 v5, v168, v171
	v_cvt_pk_bf16_f32 v6, v170, v173
	v_cvt_pk_bf16_f32 v7, v172, v174
	v_lshl_add_u64 v[8:9], v[2:3], 0, s[22:23]
	global_store_dwordx4 v[8:9], v[4:7], off nt
	s_nop 1
	v_cvt_pk_bf16_f32 v4, v159, v161
	v_cvt_pk_bf16_f32 v5, v160, v163
	v_cvt_pk_bf16_f32 v6, v162, v165
	v_cvt_pk_bf16_f32 v7, v164, v166
	v_lshl_add_u64 v[2:3], v[2:3], 0, s[12:13]
	global_store_dwordx4 v[2:3], v[4:7], off nt
	s_nop 1
	v_cvt_pk_bf16_f32 v2, v116, v153
	v_cvt_pk_bf16_f32 v3, v117, v155
	v_cvt_pk_bf16_f32 v4, v154, v157
	v_cvt_pk_bf16_f32 v5, v156, v158
	v_lshl_add_u64 v[6:7], v[8:9], 0, s[12:13]
	global_store_dwordx4 v[6:7], v[2:5], off nt
	s_nop 1

; __device__ __forceinline__ KP kparams() { KP q = (KP)__builtin_amdgcn_kernarg_segment_ptr(); asm volatile("" : "+s"(q)); return q; }
; FFT_HD cf2 mk2(float x, float y) { return (cf2){x, y}; }
; FFT_HD void fft_sincos(float frac, float& s, float& c) { s = __builtin_amdgcn_sinf(frac); c = __builtin_amdgcn_cosf(frac); }
; FFT_HD cf2 cmul(cf2 a, cf2 b) { return mk2(a.x * b.x - a.y * b.y, a.x * b.y + a.y * b.x); }
; template <int BANK> __device__ __forceinline__ void bg_issue1(BgState& b, int wg, int NW, int lane) {
;     KP kp = kparams();
;     const float* src; int ldS; bf16_t* dst; int o2;
;     bg_decode(b.st, wg, NW, lane, kp, src, ldS, dst, o2);
;     b.dst[BANK] = dst; b.o2[BANK] = o2;
;     asm volatile("s_nop 6" ::: "memory");
; #pragma unroll
;     for (int i = 0; i < 8; ++i) { const float* p = src + (size_t)i * ldS;
;         asm volatile("global_load_dword %0, %4, off\n\tglobal_load_dword %1, %4, off offset:256\n\tglobal_load_dword %2, %4, off offset:512\n\tglobal_load_dword %3, %4, off offset:768"
;                      : "=&v"(b.r[(BANK * 8 + i) * 4 + 0]), "=&v"(b.r[(BANK * 8 + i) * 4 + 1]), "=&v"(b.r[(BANK * 8 + i) * 4 + 2]), "=&v"(b.r[(BANK * 8 + i) * 4 + 3]) : "v"(p) : "memory"); }
;     b.st += 1;
; }
; FFT_HD void fft_gen_tw(float frac, cf2 (&tw)[16]) {
;     float sn, cs; fft_sincos(frac, sn, cs);
;     tw[1] = mk2(cs, -sn);
;     tw[2] = cmul(tw[1], tw[1]); tw[3] = cmul(tw[2], tw[1]); tw[4] = cmul(tw[2], tw[2]); tw[5] = cmul(tw[4], tw[1]); tw[6] = cmul(tw[4], tw[2]); tw[7] = cmul(tw[4], tw[3]);
;     tw[8] = cmul(tw[4], tw[4]);
; #pragma unroll
;     for (int j = 9; j < 16; ++j) tw[j] = cmul(tw[8], tw[j - 8]);
; }
; template <bool INV, int lS, class ZP> FFT_HD void fft_r16_pass(ZP z, int tid) {
;     constexpr int S = 1 << lS, STEP = (S >= 64) ? S + S / 32 : S;
;     constexpr float inv = 1.0f / (float)(16 * S);
;     cf2 tw[16];
;     if (lS != 10) {
;         fft_gen_tw((float)(tid & (S - 1)) * inv, tw);
;         const int w0 = tid, w1 = tid + 512;
;         const int pb0 = PADI(((w0 >> lS) << (lS + 4)) + (w0 & (S - 1))), pb1 = PADI(((w1 >> lS) << (lS + 4)) + (w1 & (S - 1)));
;         cf2 x[16], y[16];
; #pragma unroll
;         for (int j = 0; j < 16; ++j) x[j] = z[pb0 + j * STEP];
; #pragma unroll
;         for (int j = 0; j < 16; ++j) y[j] = z[pb1 + j * STEP];
.LBB0_659:
	s_nop 6
	s_lshl_b32 s12, s48, 2
	global_load_dword v176, v[2:3], off nt
	global_load_dword v168, v[2:3], off offset:256 nt
	global_load_dword v160, v[2:3], off offset:512 nt
	global_load_dword v57, v[2:3], off offset:768 nt
	v_lshl_add_u64 v[2:3], v[2:3], 0, s[12:13]
	v_and_b32_e32 v14, 63, v120
	global_load_dword v178, v[2:3], off nt
	global_load_dword v170, v[2:3], off offset:256 nt
	global_load_dword v162, v[2:3], off offset:512 nt
	global_load_dword v154, v[2:3], off offset:768 nt
	v_lshl_add_u64 v[2:3], v[2:3], 0, s[12:13]
	v_cvt_f32_ubyte0_e32 v4, v14
	global_load_dword v177, v[2:3], off nt
	global_load_dword v169, v[2:3], off offset:256 nt
	global_load_dword v161, v[2:3], off offset:512 nt
	global_load_dword v153, v[2:3], off offset:768 nt
	v_lshl_add_u64 v[2:3], v[2:3], 0, s[12:13]
	v_mul_f32_e32 v4, 0x3a800000, v4
	global_load_dword v180, v[2:3], off nt
	global_load_dword v172, v[2:3], off offset:256 nt
	global_load_dword v164, v[2:3], off offset:512 nt
	global_load_dword v156, v[2:3], off offset:768 nt
	v_lshl_add_u64 v[2:3], v[2:3], 0, s[12:13]
	v_sin_f32_e32 v39, v4
	v_cos_f32_e32 v38, v4
	global_load_dword v179, v[2:3], off nt
	global_load_dword v171, v[2:3], off offset:256 nt
	global_load_dword v163, v[2:3], off offset:512 nt
	global_load_dword v155, v[2:3], off offset:768 nt
	v_lshl_add_u64 v[2:3], v[2:3], 0, s[12:13]
	global_load_dword v181, v[2:3], off nt
	global_load_dword v173, v[2:3], off offset:256 nt
	global_load_dword v165, v[2:3], off offset:512 nt
	global_load_dword v157, v[2:3], off offset:768 nt
	v_lshl_add_u64 v[2:3], v[2:3], 0, s[12:13]
	global_load_dword v182, v[2:3], off nt
	global_load_dword v174, v[2:3], off offset:256 nt
	global_load_dword v166, v[2:3], off offset:512 nt
	global_load_dword v158, v[2:3], off offset:768 nt
	v_lshl_add_u64 v[2:3], v[2:3], 0, s[12:13]
	global_load_dword v183, v[2:3], off nt
	global_load_dword v175, v[2:3], off offset:256 nt
	global_load_dword v167, v[2:3], off offset:512 nt
	global_load_dword v159, v[2:3], off offset:768 nt
	v_mul_f32 v2, v38, v38
	v_mul_f32 v3, v39, v39
	v_mul_f32_e64 v4, v38, -v39
	v_mov_b32_e32 v5, v2
	v_mov_b32_e32 v2, v4
	v_add_f32 v202, v4, v2
	v_add_f32 v203, v5, v3
	v_add_f32_e64 v204, v4, -v2
	v_add_f32_e64 v205, v5, -v3
	v_mov_b32_e32 v46, v202
	v_mov_b32_e32 v47, v205
	v_mul_f32 v8, v46, v46
	v_mul_f32 v9, v47, v47
	v_mul_f32 v10, v205, v46
	v_mul_f32 v11, v204, v47
	v_mov_b32_e32 v2, v39
	v_mov_b32_e32 v3, v38
	v_pk_mov_b32 v[12:13], v[8:9], v[10:11] op_sel:[1,0]
	v_mov_b32_e32 v9, v10
	v_mul_f32 v4, v2, v46
	v_mul_f32 v5, v3, v47
	v_mul_f32 v6, v38, v46
	v_mul_f32 v7, v39, v47
	v_add_f32_e64 v48, v12, -v8
	v_add_f32_e64 v49, v13, -v9
	v_add_f32 v68, v12, v8
	v_add_f32 v69, v13, v9
	v_mov_b32_e32 v50, v48
	v_mov_b32_e32 v51, v69
	v_mov_b32_e32 v8, v6
	v_mov_b32_e32 v9, v5
	v_pk_mov_b32 v[4:5], v[6:7], v[4:5] op_sel:[1,0]
	v_mul_f32 v6, v50, v69
	v_mul_f32 v7, v51, v68
	v_add_f32_e64 v72, v8, -v4
	v_add_f32_e64 v73, v9, -v5
	v_add_f32 v70, v8, v4
	v_add_f32 v71, v9, v5
	v_mul_f32 v4, v50, v50
	v_mul_f32 v5, v51, v51
	v_lshlrev_b32_e32 v184, 4, v120
	v_mov_b32_e32 v7, v4
	v_mov_b32_e32 v4, v6
	v_add_f32 v76, v6, v4
	v_add_f32 v77, v7, v5
	v_add_f32_e64 v74, v6, -v4
	v_add_f32_e64 v75, v7, -v5
	v_mov_b32_e32 v54, v76
	v_mov_b32_e32 v55, v75
	v_mul_f32 v86, v2, v54
	v_mul_f32 v87, v3, v55
	v_and_b32_e32 v2, 0xfffffc00, v184
	v_lshlrev_b32_e32 v4, 3, v2
	v_lshlrev_b32_e32 v5, 3, v14
	v_add_u32_e32 v3, 0x2000, v2
	v_add3_u32 v4, 0, v4, v5
	v_ashrrev_i32_e32 v2, 2, v2
	v_add_u32_e32 v238, v4, v2
	v_add_u32_e32 v239, 0x800, v238
	v_add_u32_e32 v240, 0x1000, v238
	v_add_u32_e32 v241, 0x1800, v238
	ds_read2_b64 v[98:101], v238 offset1:66
	ds_read2_b64 v[102:105], v238 offset0:132 offset1:198
	ds_read2_b64 v[106:109], v239 offset0:8 offset1:74
	ds_read2_b64 v[110:113], v239 offset0:140 offset1:206
	ds_read2_b64 v[114:117], v240 offset0:16 offset1:82
	ds_read2_b64 v[186:189], v240 offset0:148 offset1:214
	ds_read2_b64 v[190:193], v241 offset0:24 offset1:90
	ds_read2_b64 v[198:201], v241 offset0:156 offset1:222
	s_mov_b32 s48, s27
	s_waitcnt lgkmcnt(5)
	v_pk_mov_b32 v[206:207], v[100:101], v[108:109] op_sel:[1,0]
	s_waitcnt lgkmcnt(3)
	v_mov_b32_e32 v210, v116
	s_waitcnt lgkmcnt(1)
	v_pk_mov_b32 v[208:209], v[116:117], v[192:193] op_sel:[1,0]
	v_mov_b32_e32 v211, v193
	v_add_f32_e64 v206, v206, -v208
	v_add_f32_e64 v207, v207, -v209
	v_mov_b32_e32 v208, v100
	v_mov_b32_e32 v209, v109
	v_add_f32_e64 v208, v208, -v210
	v_add_f32_e64 v209, v209, -v211
	v_pk_mov_b32 v[210:211], v[102:103], v[110:111] op_sel:[1,0]
	s_waitcnt lgkmcnt(0)
; FFT_HD cf2 mk2(float x, float y) { return (cf2){x, y}; }
; FFT_HD cf2 cmul(cf2 a, cf2 b) { return mk2(a.x * b.x - a.y * b.y, a.x * b.y + a.y * b.x); }
; FFT_HD cf2 cadd(cf2 a, cf2 b) { return mk2(a.x + b.x, a.y + b.y); }
; FFT_HD cf2 csub(cf2 a, cf2 b) { return mk2(a.x - b.x, a.y - b.y); }
; template <bool INV> FFT_HD void dft4(cf2& a, cf2& b, cf2& c, cf2& d) {
;     const cf2 s0 = cadd(a, c), s1 = csub(a, c), s2 = cadd(b, d), s3 = csub(b, d);
;     a = cadd(s0, s2); c = csub(s0, s2);
;     const cf2 r = INV ? mk2(-s3.y, s3.x) : mk2(s3.y, -s3.x);
;     b = cadd(s1, r); d = csub(s1, r);
; }
; template <bool INV> FFT_HD void dft16(cf2 (&x)[16]) {
;     const float C1 = 0.9238795325112867f, S1 = 0.3826834323650898f, H = 0.7071067811865476f;
; #pragma unroll
;     for (int b = 0; b < 4; ++b) dft4<INV>(x[b], x[4 + b], x[8 + b], x[12 + b]);
;     const float s = INV ? -1.f : 1.f;
;     x[4 + 1] = cmul(x[4 + 1], mk2(C1, -s * S1)); x[8 + 1] = cmul(x[8 + 1], mk2(H, -s * H));   x[12 + 1] = cmul(x[12 + 1], mk2(S1, -s * C1));
;     x[4 + 2] = cmul(x[4 + 2], mk2(H, -s * H));   x[8 + 2] = cmul(x[8 + 2], mk2(0.f, -s));     x[12 + 2] = cmul(x[12 + 2], mk2(-H, -s * H));
;     x[4 + 3] = cmul(x[4 + 3], mk2(S1, -s * C1)); x[8 + 3] = cmul(x[8 + 3], mk2(-H, -s * H));  x[12 + 3] = cmul(x[12 + 3], mk2(-C1, s * S1));
; #pragma unroll
;     for (int c = 0; c < 4; ++c) dft4<INV>(x[4 * c], x[4 * c + 1], x[4 * c + 2], x[4 * c + 3]);
; #pragma unroll
;     for (int c = 0; c < 4; ++c)
; #pragma unroll
;         for (int d = c + 1; d < 4; ++d) { const cf2 t = x[4 * c + d]; x[4 * c + d] = x[4 * d + c]; x[4 * d + c] = t; }
; }
	v_pk_mov_b32 v[212:213], v[186:187], v[198:199] op_sel:[1,0]
	v_mov_b32_e32 v214, v186
	v_add_f32_e64 v210, v210, -v212
	v_add_f32_e64 v211, v211, -v213
	v_mov_b32_e32 v212, v102
	v_mov_b32_e32 v213, v111
	v_mov_b32_e32 v215, v199
	v_add_f32_e64 v212, v212, -v214
	v_add_f32_e64 v213, v213, -v215
	v_pk_mov_b32 v[214:215], v[104:105], v[112:113] op_sel:[1,0]
	v_pk_mov_b32 v[216:217], v[188:189], v[200:201] op_sel:[1,0]
	v_mov_b32_e32 v218, v188
	v_add_f32_e64 v214, v214, -v216
	v_add_f32_e64 v215, v215, -v217
	v_mov_b32_e32 v216, v104
	v_mov_b32_e32 v217, v113
	v_mov_b32_e32 v219, v201
	v_add_f32_e64 v216, v216, -v218
	v_add_f32_e64 v217, v217, -v219
	v_mov_b32_e32 v219, v214
	v_mov_b32_e32 v218, v216
	v_mov_b32_e32 v220, v217
	v_mov_b32_e32 v221, v215
	v_add_f32_e32 v56, v212, v213
	v_add_f32_e64 v222, v218, -v220
	v_add_f32_e64 v223, v219, -v221
	v_add_f32 v218, v218, v220
	v_add_f32 v219, v219, v221
	v_mul_f32_e32 v235, 0x3f3504f3, v56
	v_mov_b32_e32 v223, v219
	v_mul_f32_e32 v56, 0x3ec3ef15, v219
	v_add_f32 v228, v208, v209
	v_add_f32 v229, v208, v209
	s_mov_b32 s49, s26
	v_add_f32 v253, v216, v217
	v_add_f32 v217, v216, v217
	v_mov_b32_e32 v216, v253
	v_sub_f32_e32 v234, v210, v211
	v_fma_f32 v220, v222, s30, -v56
	v_fma_f32 v221, v223, s31, -v56
	v_mul_f32_e32 v242, 0x3ec3ef15, v222
	v_mul_f32_e32 v243, 0x3f6c835e, v219
	v_add_f32 v218, v98, v114
	v_add_f32 v219, v99, v115
	v_add_f32 v222, v106, v190
	v_add_f32 v223, v107, v191
	v_add_f32_e64 v98, v98, -v114
	v_add_f32_e64 v99, v99, -v115
	v_add_f32_e64 v106, v106, -v190
	v_add_f32_e64 v107, v107, -v191
	v_mul_f32_e64 v228, v228, s26
	v_mul_f32_e64 v229, v229, s27
	v_add_f32_e64 v230, v206, -v207
	v_add_f32_e64 v231, v206, -v207
	v_mul_f32_e64 v216, v216, s48
	v_mul_f32_e64 v217, v217, s49
	v_add_f32_e64 v253, v214, -v215
	v_add_f32_e64 v215, v214, -v215
	v_mov_b32_e32 v214, v253
	v_pk_mov_b32 v[114:115], v[106:107], v[106:107] op_sel:[1,0]
	v_add_f32 v190, v98, v107
	v_add_f32 v191, v99, v106
	v_add_f32_e64 v253, v98, -v107
	v_add_f32_e64 v107, v99, -v106
	v_mov_b32_e32 v106, v253
	v_fma_f32 v232, v230, s48, v228
	v_fma_f32 v233, v231, s49, v229
	v_fma_f32 v228, v230, s48, -v228
	v_fma_f32 v229, v231, s49, -v229
	v_fmamk_f32 v230, v234, 0x3f3504f3, v235
	v_fma_f32 v234, v234, s25, -v235
	v_fma_f32 v236, v214, s26, v216
	v_fma_f32 v237, v215, s27, v217
	v_fma_f32 v214, v214, s26, -v216
	v_fma_f32 v215, v215, s27, -v217
	v_mov_b32_e32 v226, v190
	v_mov_b32_e32 v227, v107
	v_mov_b32_e32 v228, v232
	v_mov_b32_e32 v235, v234
	v_mov_b32_e32 v231, v234
	v_mov_b32_e32 v214, v236
	v_add_f32 v216, v226, v230
	v_add_f32 v217, v227, v231
	v_add_f32 v226, v228, v214
	v_add_f32 v227, v229, v215
	v_pk_mov_b32 v[106:107], v[106:107], v[232:233] op_sel:[1,0]
	v_pk_mov_b32 v[232:233], v[234:235], v[236:237] op_sel:[1,0]
	v_mov_b32_e32 v228, v190
	v_add_f32_e64 v232, v106, -v232
	v_add_f32_e64 v233, v107, -v233
	v_mov_b32_e32 v231, v215
	v_add_f32 v106, v216, v226
	v_add_f32 v107, v217, v227
	v_mov_b32_e32 v56, v39
	v_add_f32_e64 v214, v228, -v230
	v_add_f32_e64 v215, v229, -v231
	v_mul_f32 v228, v56, v106
	v_mul_f32 v229, v56, v107
	v_add_f32 v100, v100, v116
	v_add_f32 v101, v101, v117
	v_add_f32 v108, v108, v192
	v_add_f32 v109, v109, v193
	v_add_f32 v102, v102, v186
	v_add_f32 v103, v103, v187
	v_add_f32 v186, v110, v198
	v_add_f32 v187, v111, v199
	v_add_f32 v104, v104, v188
	v_add_f32 v105, v105, v189
	v_add_f32 v112, v112, v200
	v_add_f32 v113, v113, v201
	v_fma_f32 v230, v38, v106, v229
	v_fma_f32 v231, v39, v107, v228
	v_fma_f32 v106, v38, v106, -v229
	v_fma_f32 v107, v38, v107, -v228
	v_add_f32 v224, v218, v222
	v_add_f32 v225, v219, v223
	v_add_f32 v192, v102, v186
	v_add_f32 v193, v103, v187
	v_mov_b32_e32 v231, v107
	v_add_f32_e64 v106, v218, -v222
	v_add_f32_e64 v107, v219, -v223
	v_add_f32_e64 v102, v102, -v186
	v_add_f32_e64 v103, v103, -v187
	v_mov_b32_e32 v186, v104
	v_mov_b32_e32 v187, v101
	v_mov_b32_e32 v218, v112
	v_mov_b32_e32 v219, v109
	v_add_f32_e64 v186, v186, -v218
	v_add_f32_e64 v187, v187, -v219
	v_mov_b32_e32 v218, v100
	v_mov_b32_e32 v219, v104
	v_mov_b32_e32 v222, v108
	v_mov_b32_e32 v223, v112
	v_add_f32 v116, v100, v108
	v_add_f32 v117, v101, v109
	v_add_f32 v188, v104, v112
	v_add_f32 v189, v105, v113
	v_add_f32_e64 v218, v218, -v222
	v_add_f32_e64 v219, v219, -v223
	v_mov_b32_e32 v222, v101
	v_mov_b32_e32 v223, v105
	v_mov_b32_e32 v228, v109
	v_mov_b32_e32 v229, v113
	v_pk_mov_b32 v[100:101], v[104:105], v[100:101] op_sel:[1,0]
	v_pk_mov_b32 v[104:105], v[112:113], v[108:109] op_sel:[1,0]
	v_add_f32_e64 v222, v222, -v228
	v_add_f32_e64 v223, v223, -v229
	v_add_f32_e64 v100, v100, -v104
	v_add_f32_e64 v101, v101, -v105
	v_fma_f32 v104, v102, 0, v103
	v_fma_f32 v105, v103, 0, v102
	v_fma_f32 v253, v102, 0, -v103
	v_fma_f32 v103, v103, 0, -v102
	v_mov_b32_e32 v102, v253
	s_mov_b32 s50, s25
	s_mov_b32 s51, s24
	v_mov_b32_e32 v105, v103
	v_mul_f32_e64 v102, v222, s50
	v_mul_f32_e64 v103, v223, s51
	v_mul_f32_e64 v100, v100, s24
	v_mul_f32_e64 v101, v101, s25
	v_fma_f32 v102, v218, s50, v102
	v_fma_f32 v103, v219, s51, v103
	v_fma_f32 v100, v186, s24, -v100
	v_fma_f32 v101, v187, s25, -v101
	v_add_f32 v108, v106, v104
	v_add_f32 v109, v107, v105
	v_add_f32 v186, v102, v100
	v_add_f32 v187, v103, v101
	v_pk_mov_b32 v[44:45], v[204:205], v[202:203] op_sel:[1,0]
	v_add_f32 v112, v108, v186
	v_add_f32 v113, v109, v187
	s_mov_b32 s56, s26
	v_mul_f32 v203, v202, v112
	v_mul_f32 v202, v202, v113
	v_fma_f32 v218, v205, v112, -v202
	v_fma_f32 v219, v205, v113, -v203
	v_fma_f32 v112, v205, v112, v202
	v_fma_f32 v113, v205, v113, v203
	v_mov_b32_e32 v202, v206
	v_mov_b32_e32 v219, v113
; FFT_HD cf2 mk2(float x, float y) { return (cf2){x, y}; }
; FFT_HD cf2 cmul(cf2 a, cf2 b) { return mk2(a.x * b.x - a.y * b.y, a.x * b.y + a.y * b.x); }
; template <bool INV> FFT_HD void dft16(cf2 (&x)[16]) {
;     const float C1 = 0.9238795325112867f, S1 = 0.3826834323650898f, H = 0.7071067811865476f;
; #pragma unroll
;     for (int b = 0; b < 4; ++b) dft4<INV>(x[b], x[4 + b], x[8 + b], x[12 + b]);
;     const float s = INV ? -1.f : 1.f;
;     x[4 + 1] = cmul(x[4 + 1], mk2(C1, -s * S1)); x[8 + 1] = cmul(x[8 + 1], mk2(H, -s * H));   x[12 + 1] = cmul(x[12 + 1], mk2(S1, -s * C1));
;     x[4 + 2] = cmul(x[4 + 2], mk2(H, -s * H));   x[8 + 2] = cmul(x[8 + 2], mk2(0.f, -s));     x[12 + 2] = cmul(x[12 + 2], mk2(-H, -s * H));
;     x[4 + 3] = cmul(x[4 + 3], mk2(S1, -s * C1)); x[8 + 3] = cmul(x[8 + 3], mk2(-H, -s * H));  x[12 + 3] = cmul(x[12 + 3], mk2(-C1, s * S1));
; #pragma unroll
;     for (int c = 0; c < 4; ++c) dft4<INV>(x[4 * c], x[4 * c + 1], x[4 * c + 2], x[4 * c + 3]);
; #pragma unroll
;     for (int c = 0; c < 4; ++c)
; #pragma unroll
;         for (int d = c + 1; d < 4; ++d) { const cf2 t = x[4 * c + d]; x[4 * c + d] = x[4 * d + c]; x[4 * d + c] = t; }
; }
; template <bool INV, int lS, class ZP> FFT_HD void fft_r16_pass(ZP z, int tid) {
;     ...
;         if (!INV) {
; #pragma unroll
;             for (int j = 1; j < 16; ++j) x[j] = cmul(x[j], tw[j]);
;         }
	v_mov_b32_e32 v112, v208
	v_mov_b32_e32 v113, v212
	v_mov_b32_e32 v212, v209
	v_mov_b32_e32 v203, v210
	v_mov_b32_e32 v210, v207
	v_add_f32_e64 v112, v112, -v212
	v_add_f32_e64 v113, v113, -v213
	v_add_f32 v202, v202, v210
	v_add_f32 v203, v203, v211
	s_mov_b32 s57, s24
	v_pk_mov_b32 v[204:205], v[112:113], v[202:203] op_sel:[1,0]
	v_mul_f32_e64 v206, v202, s56
	v_mul_f32_e64 v207, v203, s57
	v_pk_mov_b32 v[202:203], v[202:203], v[112:113] op_sel:[1,0]
	s_mov_b32 s28, s25
	s_mov_b32 s52, s27
	s_mov_b32 s53, s24
	s_mov_b32 s54, s24
	s_mov_b32 s55, s27
	v_mul_f32_e64 v202, v202, s28
	v_mul_f32_e64 v203, v203, s29
	v_mov_b32_e32 v99, v242
	v_mov_b32_e32 v115, v243
	v_fma_f32 v202, v204, s54, v202
	v_fma_f32 v203, v205, s55, v203
	v_fma_f32 v204, v112, s52, v206
	v_fma_f32 v205, v113, s53, v207
	v_add_f32_e64 v98, v98, -v114
	v_add_f32_e64 v99, v99, -v115
	v_mov_b32_e32 v190, v220
	v_add_f32 v206, v202, v98
	v_add_f32 v207, v203, v99
	v_add_f32 v208, v204, v190
	v_add_f32 v209, v205, v191
	v_mov_b32_e32 v42, v72
	v_add_f32 v112, v208, v206
	v_add_f32 v113, v209, v207
	v_pk_mov_b32 v[40:41], v[70:71], v[72:73] op_sel:[1,0]
	v_mul_f32 v73, v72, v112
	v_mul_f32 v72, v72, v113
	v_mov_b32_e32 v43, v71
	v_fma_f32 v210, v71, v112, -v72
	v_fma_f32 v211, v71, v113, -v73
	v_fma_f32 v70, v71, v112, v72
	v_fma_f32 v71, v71, v113, v73
	v_add_f32_e64 v72, v116, -v188
	v_add_f32_e64 v73, v117, -v189
	v_mov_b32_e32 v211, v71
	v_add_f32_e64 v70, v224, -v192
	v_add_f32_e64 v71, v225, -v193
	v_add_f32 v198, v224, v192
	v_add_f32 v199, v225, v193
	v_add_f32 v200, v116, v188
	v_add_f32 v201, v117, v189
	v_add_f32 v188, v70, v73
	v_add_f32 v189, v71, v72
	v_add_f32_e64 v192, v70, -v73
	v_add_f32_e64 v193, v71, -v72
	v_mov_b32_e32 v70, v188
	v_pk_mov_b32 v[72:73], v[192:193], v[188:189] op_sel:[1,0]
	v_mov_b32_e32 v71, v193
	v_pk_mov_b32 v[112:113], v[68:69], v[48:49] op_sel:[1,0]
	v_mul_f32 v68, v69, v72
	v_mul_f32 v69, v69, v73
	v_add_f32_e64 v116, v232, -v233
	v_add_f32_e64 v117, v232, -v233
	v_fma_f32 v212, v48, v188, -v68
	v_fma_f32 v213, v49, v189, -v69
	v_fma_f32 v68, v48, v70, v68
	v_fma_f32 v69, v48, v71, v69
	v_mul_f32 v70, v56, v112
	v_mul_f32 v71, v56, v113
	v_mov_b32_e32 v213, v69
	v_fma_f32 v68, v38, v50, v70
	v_fma_f32 v69, v38, v51, v71
	v_fma_f32 v72, v38, v50, -v70
	v_fma_f32 v73, v38, v51, -v71
	v_mov_b32_e32 v71, v73
	v_pk_mov_b32 v[72:73], v[72:73], v[68:69] op_sel:[1,0]
	v_add_f32_e64 v104, v106, -v104
	v_add_f32_e64 v105, v107, -v105
	v_pk_mov_b32 v[106:107], v[100:101], v[102:103] op_sel:[1,0]
	v_pk_mov_b32 v[100:101], v[102:103], v[100:101] op_sel:[1,0]
	v_mov_b32_e32 v70, v68
	v_add_f32 v114, v214, v215
	v_add_f32 v115, v214, v215
	v_mul_f32 v116, v72, v116
	v_mul_f32 v117, v73, v117
	v_add_f32_e64 v100, v106, -v100
	v_add_f32_e64 v101, v107, -v101
	v_mul_f32 v96, v46, v50
	v_mul_f32 v97, v47, v51
	v_fma_f32 v222, v68, v114, -v116
	v_fma_f32 v223, v69, v115, -v117
	v_fma_f32 v114, v70, v114, v116
	v_fma_f32 v115, v71, v115, v117
	v_add_f32 v102, v104, v100
	v_add_f32 v103, v105, v101
	v_add_f32_e64 v100, v104, -v100
	v_add_f32_e64 v101, v105, -v101
	v_mul_f32 v94, v44, v50
	v_mul_f32 v95, v45, v51
	v_mov_b32_e32 v223, v115
	v_add_f32 v114, v96, v97
	v_add_f32 v115, v96, v97
	v_pk_mov_b32 v[96:97], v[100:101], v[102:103] op_sel:[1,0]
	v_mov_b32_e32 v104, v102
	v_mov_b32_e32 v105, v101
	v_mul_f32 v96, v114, v96
	v_mul_f32 v97, v115, v97
	v_add_f32_e64 v116, v94, -v95
	v_add_f32_e64 v117, v94, -v95
	v_fma_f32 v224, v116, v102, -v96
	v_fma_f32 v225, v117, v103, -v97
	v_fma_f32 v94, v116, v104, v96
	v_fma_f32 v95, v117, v105, v97
	v_pk_mov_b32 v[96:97], v[98:99], v[220:221] op_sel:[1,0]
	v_mov_b32_e32 v225, v95
	v_pk_mov_b32 v[94:95], v[202:203], v[204:205] op_sel:[1,0]
	v_mov_b32_e32 v99, v191
	v_mov_b32_e32 v203, v205
	v_add_f32_e64 v94, v94, -v96
	v_add_f32_e64 v95, v95, -v97
	v_add_f32_e64 v96, v98, -v202
	v_add_f32_e64 v97, v99, -v203
	v_mul_f32 v92, v50, v42
	v_mul_f32 v93, v51, v43
	v_add_f32 v190, v96, v94
	v_add_f32 v191, v97, v95
	v_add_f32_e64 v202, v96, -v94
	v_add_f32_e64 v203, v97, -v95
	v_mul_f32 v84, v50, v40
	v_mul_f32 v85, v51, v41
	v_add_f32 v104, v92, v93
	v_add_f32 v105, v92, v93
	v_pk_mov_b32 v[92:93], v[202:203], v[190:191] op_sel:[1,0]
	v_mov_b32_e32 v94, v190
	v_mov_b32_e32 v95, v203
	v_mul_f32 v92, v104, v92
	v_mul_f32 v93, v105, v93
	v_add_f32_e64 v106, v84, -v85
	v_add_f32_e64 v107, v84, -v85
	v_fma_f32 v204, v106, v190, -v92
	v_fma_f32 v205, v107, v191, -v93
	v_fma_f32 v84, v106, v94, v92
	v_fma_f32 v85, v107, v95, v93
	v_mul_f32 v90, v38, v54
	v_mul_f32 v91, v39, v55
	v_mov_b32_e32 v205, v85
	v_add_f32_e64 v84, v198, -v200
	v_add_f32_e64 v85, v199, -v201
	v_add_f32 v110, v198, v200
	v_add_f32 v111, v199, v201
	v_mul_f32 v92, v76, v84
	v_mul_f32 v93, v76, v85
	v_fma_f32 v198, v75, v84, -v93
	v_fma_f32 v199, v75, v85, -v92
	v_fma_f32 v84, v75, v84, v93
	v_fma_f32 v85, v75, v85, v92
	v_add_f32_e64 v92, v216, -v226
	v_add_f32_e64 v93, v217, -v227
	v_mov_b32_e32 v199, v85
	v_add_f32_e64 v84, v90, -v91
	v_add_f32_e64 v85, v90, -v91
	v_pk_mov_b32 v[52:53], v[74:75], v[76:77] op_sel:[1,0]
	v_mul_f32 v90, v84, v92
	v_mul_f32 v91, v85, v93
	v_add_f32 v253, v87, v86
	v_add_f32 v87, v87, v86
	v_mov_b32_e32 v86, v253
	v_mul_f32 v88, v46, v52
	v_mul_f32 v89, v47, v53
	v_fma_f32 v200, v86, v92, -v91
	v_fma_f32 v201, v87, v93, -v90
	v_fma_f32 v253, v86, v92, v91
	v_fma_f32 v91, v87, v93, v90
	v_mov_b32_e32 v90, v253
	v_mul_f32 v82, v46, v54
	v_mul_f32 v83, v47, v55
	v_mov_b32_e32 v201, v91
	v_add_f32_e64 v90, v108, -v186
	v_add_f32_e64 v91, v109, -v187
	v_add_f32 v186, v88, v89
	v_add_f32 v187, v88, v89
	v_mul_f32 v88, v186, v90
; FFT_HD cf2 mk2(float x, float y) { return (cf2){x, y}; }
; FFT_HD cf2 cmul(cf2 a, cf2 b) { return mk2(a.x * b.x - a.y * b.y, a.x * b.y + a.y * b.x); }
; template <bool INV> FFT_HD void dft16(cf2 (&x)[16]) {
;     ...
;     x[4 + 1] = cmul(x[4 + 1], mk2(C1, -s * S1)); x[8 + 1] = cmul(x[8 + 1], mk2(H, -s * H));   x[12 + 1] = cmul(x[12 + 1], mk2(S1, -s * C1));
;     x[4 + 2] = cmul(x[4 + 2], mk2(H, -s * H));   x[8 + 2] = cmul(x[8 + 2], mk2(0.f, -s));     x[12 + 2] = cmul(x[12 + 2], mk2(-H, -s * H));
;     x[4 + 3] = cmul(x[4 + 3], mk2(S1, -s * C1)); x[8 + 3] = cmul(x[8 + 3], mk2(-H, -s * H));  x[12 + 3] = cmul(x[12 + 3], mk2(-C1, s * S1));
; #pragma unroll
;     for (int c = 0; c < 4; ++c) dft4<INV>(x[4 * c], x[4 * c + 1], x[4 * c + 2], x[4 * c + 3]);
; #pragma unroll
;     for (int c = 0; c < 4; ++c)
; #pragma unroll
;         for (int d = c + 1; d < 4; ++d) { const cf2 t = x[4 * c + d]; x[4 * c + d] = x[4 * d + c]; x[4 * d + c] = t; }
; }
; template <bool INV, int lS, class ZP> FFT_HD void fft_r16_pass(ZP z, int tid) {
;     ...
;         if (!INV) {
; #pragma unroll
;             for (int j = 1; j < 16; ++j) x[j] = cmul(x[j], tw[j]);
;         }
; #pragma unroll
;         for (int j = 0; j < 16; ++j) z[pb0 + j * STEP] = x[j];
	v_mul_f32 v89, v187, v91
	v_add_f32_e64 v216, v83, -v82
	v_add_f32_e64 v217, v83, -v82
	v_mul_f32 v80, v42, v52
	v_mul_f32 v81, v43, v53
	v_fma_f32 v220, v216, v90, -v89
	v_fma_f32 v221, v217, v91, -v88
	v_fma_f32 v82, v216, v90, v89
	v_fma_f32 v83, v217, v91, v88
	v_mul_f32 v78, v42, v54
	v_mul_f32 v79, v43, v55
	v_mov_b32_e32 v221, v83
	v_mov_b32_e32 v82, v206
	v_mov_b32_e32 v83, v209
	v_mov_b32_e32 v209, v207
	v_add_f32_e64 v82, v82, -v208
	v_add_f32_e64 v83, v83, -v209
	v_add_f32 v253, v80, v81
	v_add_f32 v81, v80, v81
	v_mov_b32_e32 v80, v253
	v_mul_f32 v88, v80, v82
	v_mul_f32 v89, v81, v83
	v_add_f32_e64 v253, v79, -v78
	v_add_f32_e64 v79, v79, -v78
	v_mov_b32_e32 v78, v253
	v_add_f32 v96, v232, v233
	v_add_f32 v97, v232, v233
	v_fma_f32 v206, v78, v82, -v89
	v_fma_f32 v207, v79, v83, -v88
	v_fma_f32 v82, v78, v82, v89
	v_fma_f32 v83, v79, v83, v88
	v_mul_f32 v88, v50, v76
	v_mul_f32 v89, v51, v76
	v_mov_b32_e32 v207, v83
	v_fma_f32 v82, v50, v75, -v89
	v_fma_f32 v83, v51, v75, -v88
	v_fma_f32 v90, v50, v75, v89
	v_fma_f32 v91, v51, v75, v88
	v_mov_b32_e32 v88, v82
	v_mov_b32_e32 v89, v91
	v_pk_mov_b32 v[90:91], v[90:91], v[82:83] op_sel:[1,0]
	v_add_f32_e64 v94, v214, -v215
	v_add_f32_e64 v95, v214, -v215
	v_mul_f32 v92, v90, v189
	v_mul_f32 v93, v91, v189
	v_ashrrev_i32_e32 v2, 2, v3
	v_fma_f32 v188, v82, v192, -v92
	v_fma_f32 v189, v83, v193, -v93
	v_fma_f32 v92, v88, v192, v92
	v_fma_f32 v93, v89, v192, v93
	v_add3_u32 v60, v4, v2, s71
	v_mov_b32_e32 v189, v93
	v_mul_f32 v92, v76, v70
	v_mul_f32 v93, v76, v71
	v_fma_f32 v76, v75, v70, -v93
	v_fma_f32 v77, v75, v71, -v92
	v_fma_f32 v253, v75, v70, v93
	v_fma_f32 v93, v75, v71, v92
	v_mov_b32_e32 v92, v253
	v_mov_b32_e32 v74, v76
	v_mov_b32_e32 v75, v93
	v_pk_mov_b32 v[92:93], v[92:93], v[76:77] op_sel:[1,0]
	v_add_u32_e32 v65, 0x800, v60
	v_mul_f32 v96, v92, v96
	v_mul_f32 v97, v93, v97
	v_add_u32_e32 v67, 0x1000, v60
	v_fma_f32 v192, v76, v94, -v96
	v_fma_f32 v193, v77, v95, -v97
	v_fma_f32 v94, v74, v94, v96
	v_fma_f32 v95, v75, v95, v97
	v_mul_f32 v96, v54, v116
	v_mul_f32 v97, v55, v117
	v_mov_b32_e32 v193, v95
	v_fma_f32 v94, -v54, v114, v97
	v_fma_f32 v95, -v55, v115, v96
	v_fma_f32 v98, v54, v114, v97
	v_fma_f32 v99, v55, v115, v96
	v_mov_b32_e32 v96, v94
	v_mov_b32_e32 v97, v99
	v_pk_mov_b32 v[98:99], v[98:99], v[94:95] op_sel:[1,0]
	v_add_u32_e32 v185, 0x1800, v60
	v_mul_f32 v102, v98, v103
	v_mul_f32 v103, v99, v103
	ds_read2_b64 v[2:5], v60 offset1:66
	ds_read2_b64 v[18:21], v60 offset0:132 offset1:198
	v_fma_f32 v208, v94, v100, -v102
	v_fma_f32 v209, v95, v101, -v103
	v_fma_f32 v101, v97, v100, v103
	v_fma_f32 v100, v96, v100, v102
	v_mul_f32 v102, v54, v106
	v_mul_f32 v103, v55, v107
	ds_read2_b64 v[6:9], v65 offset0:8 offset1:74
	ds_read2_b64 v[22:25], v65 offset0:140 offset1:206
	ds_read2_b64 v[10:13], v67 offset0:16 offset1:82
	ds_read2_b64 v[26:29], v67 offset0:148 offset1:214
	ds_read2_b64 v[14:17], v185 offset0:24 offset1:90
	ds_read2_b64 v[30:33], v185 offset0:156 offset1:222
	v_mov_b32_e32 v209, v101
	v_fma_f32 v100, -v54, v104, v103
	v_fma_f32 v101, -v55, v105, v102
	v_fma_f32 v108, v54, v104, v103
	v_fma_f32 v109, v55, v105, v102
	v_mov_b32_e32 v102, v100
	v_mov_b32_e32 v103, v109
	v_pk_mov_b32 v[108:109], v[108:109], v[100:101] op_sel:[1,0]
	v_cmp_ne_u64_e32 vcc, 0, v[34:35]
	v_mul_f32 v190, v108, v191
	v_mul_f32 v191, v109, v191
	s_nop 0
	v_fma_f32 v214, v100, v202, -v190
	v_fma_f32 v215, v101, v203, -v191
	v_fma_f32 v190, v102, v202, v190
	v_fma_f32 v191, v103, v202, v191
	s_waitcnt lgkmcnt(1)
	v_add_f32 v202, v6, v14
	v_add_f32 v203, v7, v15
	v_mov_b32_e32 v215, v191
	ds_write2_b64 v238, v[110:111], v[230:231] offset1:66
	ds_write2_b64 v238, v[218:219], v[210:211] offset0:132 offset1:198
	ds_write2_b64 v239, v[212:213], v[222:223] offset0:8 offset1:74
	ds_write2_b64 v239, v[224:225], v[204:205] offset0:140 offset1:206
	ds_write2_b64 v240, v[198:199], v[200:201] offset0:16 offset1:82
	ds_write2_b64 v240, v[220:221], v[206:207] offset0:148 offset1:214
	ds_write2_b64 v241, v[188:189], v[192:193] offset0:24 offset1:90
	ds_write2_b64 v241, v[208:209], v[214:215] offset0:156 offset1:222
	v_pk_mov_b32 v[110:111], v[4:5], v[8:9] op_sel:[1,0]
	v_pk_mov_b32 v[188:189], v[12:13], v[16:17] op_sel:[1,0]
	v_mov_b32_e32 v190, v12
	v_add_f32_e64 v110, v110, -v188
	v_add_f32_e64 v111, v111, -v189
	v_mov_b32_e32 v188, v4
	v_mov_b32_e32 v189, v9
	v_mov_b32_e32 v191, v17
	v_add_f32_e64 v188, v188, -v190
	v_add_f32_e64 v189, v189, -v191
	v_pk_mov_b32 v[190:191], v[18:19], v[22:23] op_sel:[1,0]
	s_waitcnt lgkmcnt(8)
; FFT_HD cf2 mk2(float x, float y) { return (cf2){x, y}; }
; FFT_HD cf2 cmul(cf2 a, cf2 b) { return mk2(a.x * b.x - a.y * b.y, a.x * b.y + a.y * b.x); }
; FFT_HD cf2 cadd(cf2 a, cf2 b) { return mk2(a.x + b.x, a.y + b.y); }
; FFT_HD cf2 csub(cf2 a, cf2 b) { return mk2(a.x - b.x, a.y - b.y); }
; template <bool INV> FFT_HD void dft4(cf2& a, cf2& b, cf2& c, cf2& d) {
;     const cf2 s0 = cadd(a, c), s1 = csub(a, c), s2 = cadd(b, d), s3 = csub(b, d);
;     a = cadd(s0, s2); c = csub(s0, s2);
;     const cf2 r = INV ? mk2(-s3.y, s3.x) : mk2(s3.y, -s3.x);
;     b = cadd(s1, r); d = csub(s1, r);
; }
; template <bool INV> FFT_HD void dft16(cf2 (&x)[16]) {
;     const float C1 = 0.9238795325112867f, S1 = 0.3826834323650898f, H = 0.7071067811865476f;
; #pragma unroll
;     for (int b = 0; b < 4; ++b) dft4<INV>(x[b], x[4 + b], x[8 + b], x[12 + b]);
;     const float s = INV ? -1.f : 1.f;
;     x[4 + 1] = cmul(x[4 + 1], mk2(C1, -s * S1)); x[8 + 1] = cmul(x[8 + 1], mk2(H, -s * H));   x[12 + 1] = cmul(x[12 + 1], mk2(S1, -s * C1));
;     x[4 + 2] = cmul(x[4 + 2], mk2(H, -s * H));   x[8 + 2] = cmul(x[8 + 2], mk2(0.f, -s));     x[12 + 2] = cmul(x[12 + 2], mk2(-H, -s * H));
;     x[4 + 3] = cmul(x[4 + 3], mk2(S1, -s * C1)); x[8 + 3] = cmul(x[8 + 3], mk2(-H, -s * H));  x[12 + 3] = cmul(x[12 + 3], mk2(-C1, s * S1));
; #pragma unroll
;     for (int c = 0; c < 4; ++c) dft4<INV>(x[4 * c], x[4 * c + 1], x[4 * c + 2], x[4 * c + 3]);
; #pragma unroll
;     for (int c = 0; c < 4; ++c)
; #pragma unroll
;         for (int d = c + 1; d < 4; ++d) { const cf2 t = x[4 * c + d]; x[4 * c + d] = x[4 * d + c]; x[4 * d + c] = t; }
; }
	v_pk_mov_b32 v[192:193], v[26:27], v[30:31] op_sel:[1,0]
	v_pk_mov_b32 v[206:207], v[20:21], v[4:5] op_sel:[1,0]
	v_pk_mov_b32 v[208:209], v[28:29], v[12:13] op_sel:[1,0]
	v_add_f32_e64 v190, v190, -v192
	v_add_f32_e64 v191, v191, -v193
	v_mov_b32_e32 v192, v18
	v_mov_b32_e32 v193, v23
	v_mov_b32_e32 v198, v26
	v_mov_b32_e32 v199, v31
	v_add_f32 v206, v206, v208
	v_add_f32 v207, v207, v209
	v_mov_b32_e32 v208, v4
	v_mov_b32_e32 v209, v20
	v_mov_b32_e32 v210, v12
	v_mov_b32_e32 v211, v28
	v_add_f32_e64 v192, v192, -v198
	v_add_f32_e64 v193, v193, -v199
	v_add_f32 v208, v208, v210
	v_add_f32 v209, v209, v211
	v_pk_mov_b32 v[210:211], v[24:25], v[8:9] op_sel:[1,0]
	v_pk_mov_b32 v[212:213], v[32:33], v[16:17] op_sel:[1,0]
	v_add_f32_e32 v39, v192, v193
	v_sub_f32_e32 v218, v190, v191
	v_sub_f32_e32 v219, v192, v193
	v_add_f32_e32 v200, v190, v191
	v_pk_mov_b32 v[190:191], v[20:21], v[24:25] op_sel:[1,0]
	v_pk_mov_b32 v[192:193], v[28:29], v[32:33] op_sel:[1,0]
	v_add_f32 v210, v210, v212
	v_add_f32 v211, v211, v213
	v_mov_b32_e32 v212, v8
	v_mov_b32_e32 v213, v24
	v_mov_b32_e32 v214, v16
	v_mov_b32_e32 v215, v32
	v_mov_b32_e32 v4, v20
	v_mov_b32_e32 v12, v28
	v_mov_b32_e32 v8, v24
	v_mov_b32_e32 v16, v32
	v_add_f32_e64 v190, v190, -v192
	v_add_f32_e64 v191, v191, -v193
	v_mov_b32_e32 v192, v20
	v_mov_b32_e32 v198, v28
	v_add_f32 v212, v212, v214
	v_add_f32 v213, v213, v215
	v_add_f32 v214, v4, v12
	v_add_f32 v215, v5, v13
	v_mov_b32_e32 v20, v5
	v_mov_b32_e32 v28, v13
	v_add_f32 v12, v8, v16
	v_add_f32 v13, v9, v17
	v_mov_b32_e32 v24, v9
	v_mov_b32_e32 v32, v17
	v_add_f32 v16, v18, v26
	v_add_f32 v17, v19, v27
	v_add_f32 v18, v22, v30
	v_add_f32 v19, v23, v31
	v_add_f32 v4, v20, v28
	v_add_f32 v5, v21, v29
	v_add_f32 v8, v24, v32
	v_add_f32 v9, v25, v33
	v_add_f32_e64 v20, v16, -v18
	v_add_f32_e64 v21, v17, -v19
	v_mov_b32_e32 v193, v25
	v_add_f32_e64 v24, v4, -v8
	v_add_f32_e64 v25, v5, -v9
	v_add_f32_e64 v26, v206, -v210
	v_add_f32_e64 v27, v207, -v211
	v_fma_f32 v28, v20, 0, v21
	v_fma_f32 v29, v21, 0, v20
	v_fma_f32 v253, v20, 0, -v21
	v_fma_f32 v21, v21, 0, -v20
	v_mov_b32_e32 v20, v253
	v_mov_b32_e32 v199, v33
	v_add_f32_e64 v12, v214, -v12
	v_add_f32_e64 v13, v215, -v13
	v_mov_b32_e32 v29, v21
	v_mul_f32_e64 v20, v24, s50
	v_mul_f32_e64 v21, v25, s51
	v_mul_f32_e64 v24, v26, s24
	v_mul_f32_e64 v25, v27, s25
	v_add_f32_e64 v192, v192, -v198
	v_add_f32_e64 v193, v193, -v199
	v_mul_f32_e32 v199, 0xbf3504f3, v200
	v_add_f32 v200, v2, v10
	v_add_f32 v201, v3, v11
	v_add_f32_e64 v22, v208, -v212
	v_add_f32_e64 v23, v209, -v213
	v_fma_f32 v12, v12, s24, -v24
	v_fma_f32 v13, v13, s25, -v25
	v_mov_b32_e32 v24, v208
	v_mov_b32_e32 v25, v4
	v_mov_b32_e32 v26, v212
	v_mov_b32_e32 v27, v8
	v_mov_b32_e32 v4, v209
	v_mov_b32_e32 v8, v213
	v_fma_f32 v20, v22, s50, v20
	v_fma_f32 v21, v23, s51, v21
	v_add_f32 v22, v200, v202
	v_add_f32 v23, v201, v203
	v_add_f32 v24, v24, v26
	v_add_f32 v25, v25, v27
	v_add_f32 v16, v16, v18
	v_add_f32 v17, v17, v19
	v_add_f32 v4, v4, v8
	v_add_f32 v5, v5, v9
	v_add_f32_e64 v204, v200, -v202
	v_add_f32_e64 v205, v201, -v203
	v_add_f32 v8, v22, v16
	v_add_f32 v9, v23, v17
	v_add_f32 v18, v24, v4
	v_add_f32 v19, v25, v5
	v_pk_mov_b32 v[26:27], v[22:23], v[24:25] op_sel:[1,0]
	v_pk_mov_b32 v[30:31], v[16:17], v[4:5] op_sel:[1,0]
	v_mov_b32_e32 v23, v25
	v_mov_b32_e32 v17, v5
	v_add_f32_e64 v4, v22, -v16
	v_add_f32_e64 v5, v23, -v17
	v_add_f32 v16, v8, v18
	v_add_f32 v17, v9, v19
	v_add_f32_e64 v8, v8, -v18
	v_add_f32_e64 v9, v9, -v19
	v_add_f32 v18, v204, v28
	v_add_f32 v19, v205, v29
	v_add_f32 v22, v20, v12
	v_add_f32 v23, v21, v13
	v_add_f32_e64 v26, v26, -v30
	v_add_f32_e64 v27, v27, -v31
	v_add_f32 v24, v18, v22
	v_add_f32 v25, v19, v23
	v_add_f32_e64 v18, v18, -v22
	v_add_f32_e64 v19, v19, -v23
	v_mul_f32 v22, v46, v25
	v_mul_f32 v23, v47, v25
	v_add_f32_e64 v2, v2, -v10
	v_add_f32_e64 v3, v3, -v11
	v_fma_f32 v30, v44, v24, -v22
	v_fma_f32 v31, v45, v25, -v23
	v_fma_f32 v22, v44, v24, v22
	v_fma_f32 v23, v45, v24, v23
	v_add_f32_e64 v24, v26, -v27
	v_add_f32_e64 v25, v26, -v27
	v_mov_b32_e32 v31, v23
	v_add_f32 v22, v4, v5
	v_add_f32 v23, v4, v5
	v_mul_f32 v24, v112, v24
	v_mul_f32 v25, v113, v25
	v_add_f32_e64 v10, v188, -v189
	v_add_f32_e64 v11, v188, -v189
	v_fma_f32 v32, v48, v22, -v24
	v_fma_f32 v33, v49, v23, -v25
	v_fma_f32 v22, v50, v22, v24
	v_fma_f32 v23, v51, v23, v25
	v_pk_mov_b32 v[24:25], v[12:13], v[20:21] op_sel:[1,0]
	v_pk_mov_b32 v[12:13], v[20:21], v[12:13] op_sel:[1,0]
	v_mov_b32_e32 v33, v23
	v_add_f32_e64 v22, v204, -v28
	v_add_f32_e64 v23, v205, -v29
	v_add_f32_e64 v12, v24, -v12
	v_add_f32_e64 v13, v25, -v13
	v_add_f32_e64 v6, v6, -v14
	v_add_f32_e64 v7, v7, -v15
	v_add_f32 v20, v22, v12
	v_add_f32 v21, v23, v13
	v_add_f32_e64 v12, v22, -v12
	v_add_f32_e64 v13, v23, -v13
	v_mov_b32_e32 v22, v20
	v_pk_mov_b32 v[24:25], v[12:13], v[20:21] op_sel:[1,0]
	v_mov_b32_e32 v23, v13
	v_mul_f32 v24, v114, v24
	v_mul_f32 v25, v115, v25
	v_mul_f32_e64 v10, v10, s48
	v_mul_f32_e64 v11, v11, s49
	v_fma_f32 v28, v116, v20, -v24
	v_fma_f32 v29, v117, v21, -v25
	v_fma_f32 v22, v116, v22, v24
	v_fma_f32 v23, v117, v23, v25
	v_add_f32 v14, v110, v111
	v_add_f32 v15, v110, v111
	v_mov_b32_e32 v29, v23
	v_mul_f32 v22, v54, v9
	v_mul_f32 v23, v55, v9
	v_mul_f32_e32 v198, 0xbf3504f3, v219
	v_fma_f32 v24, v52, v8, -v22
	v_fma_f32 v25, v53, v9, -v23
	v_fma_f32 v9, v53, v8, v23
	v_fma_f32 v8, v52, v8, v22
	v_sub_f32_e32 v198, v198, v199
	v_mov_b32_e32 v25, v9
	v_mul_f32 v8, v186, v18
	v_mul_f32 v9, v187, v19
	v_fmac_f32_e32 v199, 0xbf3504f3, v219
	v_fma_f32 v22, v216, v18, -v9
	v_fma_f32 v23, v217, v19, -v8
; __device__ __forceinline__ unsigned cvt_pk_bf16(float lo, float hi) { unsigned r; asm volatile("v_cvt_pk_bf16_f32 %0, %1, %2" : "=v"(r) : "v"(lo), "v"(hi)); return r; }
; FFT_HD cf2 cmul(cf2 a, cf2 b) { return mk2(a.x * b.x - a.y * b.y, a.x * b.y + a.y * b.x); }
; template <int BANK, int WAITN> __device__ __forceinline__ void bg_finish1(BgState& b) {
;     if (WAITN == 32) asm volatile("s_waitcnt vmcnt(32)" ::: "memory"); else asm volatile("s_waitcnt vmcnt(0)" ::: "memory");
;     asm volatile("" : BG_TIE16(BANK * 32) :: "memory");
;     asm volatile("" : BG_TIE16(BANK * 32 + 16) :: "memory");
;     bf16_t* dst = b.dst[BANK];
;     if (dst != nullptr) {
; #pragma unroll
;         for (int c = 0; c < 4; ++c) { u32x4 w;
;             w.x = cvt_pk_bf16(b.r[(BANK * 8 + 0) * 4 + c], b.r[(BANK * 8 + 1) * 4 + c]); w.y = cvt_pk_bf16(b.r[(BANK * 8 + 2) * 4 + c], b.r[(BANK * 8 + 3) * 4 + c]);
;             w.z = cvt_pk_bf16(b.r[(BANK * 8 + 4) * 4 + c], b.r[(BANK * 8 + 5) * 4 + c]); w.w = cvt_pk_bf16(b.r[(BANK * 8 + 6) * 4 + c], b.r[(BANK * 8 + 7) * 4 + c]);
;             bf16_t* dp = dst + (c & 1) * 512 + (c >> 1) * b.o2[BANK];
;             asm volatile("global_store_dwordx4 %0, %1, off\n\ts_nop 1" :: "v"(dp), "v"(w) : "memory"); }
;     }
; }
; template <bool INV, int lS, class ZP> FFT_HD void fft_r16_pass(ZP z, int tid) {
;     ...
;         dft16<INV>(y);
;         if (!INV) {
; #pragma unroll
;             for (int j = 1; j < 16; ++j) y[j] = cmul(y[j], tw[j]);
;         }
; #pragma unroll
;         for (int j = 0; j < 16; ++j) z[pb1 + j * STEP] = y[j];
	v_fma_f32 v253, v216, v18, v9
	v_fma_f32 v9, v217, v19, v8
	v_mov_b32_e32 v8, v253
	v_fma_f32 v18, v14, s26, v10
	v_fma_f32 v19, v15, s27, v11
	v_fma_f32 v10, v14, s26, -v10
	v_fma_f32 v11, v15, s27, -v11
	v_add_f32 v14, v190, v191
	v_add_f32 v15, v190, v191
	v_mov_b32_e32 v23, v9
	v_add_f32_e64 v8, v2, -v7
	v_add_f32_e64 v9, v3, -v6
	v_add_f32 v2, v2, v7
	v_add_f32 v3, v3, v6
	v_mov_b32_e32 v19, v11
	v_add_f32_e64 v10, v192, -v193
	v_add_f32_e64 v11, v192, -v193
	v_mul_f32_e64 v14, v14, s48
	v_mul_f32_e64 v15, v15, s49
	v_mov_b32_e32 v6, v8
	v_mov_b32_e32 v7, v3
	v_fma_f32 v10, v10, s30, -v14
	v_fma_f32 v11, v11, s31, -v15
	v_add_f32 v14, v6, v198
	v_add_f32 v15, v7, v199
	v_add_f32 v44, v18, v10
	v_add_f32 v45, v19, v11
	v_add_f32_e64 v6, v6, -v198
	v_add_f32_e64 v7, v7, -v199
	v_add_f32 v46, v14, v44
	v_add_f32 v47, v15, v45
	v_add_f32_e64 v10, v18, -v10
	v_add_f32_e64 v11, v19, -v11
	v_mul_f32 v42, v42, v47
	v_mul_f32 v43, v43, v47
	v_add_f32_e64 v14, v14, -v44
	v_add_f32_e64 v15, v15, -v45
	v_fma_f32 v44, v40, v46, -v42
	v_fma_f32 v45, v41, v47, -v43
	v_fma_f32 v40, v40, v46, v42
	v_fma_f32 v41, v41, v46, v43
	v_add_f32 v18, v6, v11
	v_add_f32 v19, v7, v10
	v_add_f32_e64 v6, v6, -v11
	v_add_f32_e64 v7, v7, -v10
	v_mov_b32_e32 v45, v41
	v_pk_mov_b32 v[40:41], v[6:7], v[18:19] op_sel:[1,0]
	v_mov_b32_e32 v10, v18
	v_mov_b32_e32 v11, v7
	v_mul_f32 v40, v104, v40
	v_mul_f32 v41, v105, v41
	v_add_f32 v50, v192, v193
	v_add_f32 v51, v192, v193
	v_fma_f32 v42, v106, v18, -v40
	v_fma_f32 v43, v107, v19, -v41
	v_fma_f32 v10, v106, v10, v40
	v_fma_f32 v11, v107, v11, v41
	v_mul_f32_e32 v39, 0x3f3504f3, v39
	v_mov_b32_e32 v43, v11
	v_add_f32 v10, v188, v189
	v_add_f32 v11, v188, v189
	v_mul_f32_e64 v10, v10, s26
	v_mul_f32_e64 v11, v11, s27
	v_add_f32_e64 v40, v110, -v111
	v_add_f32_e64 v41, v110, -v111
	v_mul_f32_e64 v50, v50, s48
	v_mul_f32_e64 v51, v51, s49
	v_add_f32_e64 v52, v190, -v191
	v_add_f32_e64 v53, v190, -v191
	v_fma_f32 v46, v40, s48, v10
	v_fma_f32 v47, v41, s49, v11
	v_fma_f32 v10, v40, s48, -v10
	v_fma_f32 v11, v41, s49, -v11
	v_fma_f32 v48, v218, s25, -v39
	v_fma_f32 v54, v52, s26, v50
	v_fma_f32 v55, v53, s27, v51
	v_fma_f32 v50, v52, s26, -v50
	v_fma_f32 v51, v53, s27, -v51
	v_mov_b32_e32 v10, v46
	v_fmamk_f32 v40, v218, 0x3f3504f3, v39
	v_mov_b32_e32 v41, v48
	v_mov_b32_e32 v50, v54
	v_mov_b32_e32 v3, v9
	v_mov_b32_e32 v49, v48
	v_add_f32 v52, v10, v50
	v_add_f32 v53, v11, v51
	v_add_f32 v104, v2, v40
	v_add_f32 v105, v3, v41
	v_mov_b32_e32 v3, v11
	v_mov_b32_e32 v41, v51
	v_add_f32_e64 v2, v2, -v40
	v_add_f32_e64 v3, v3, -v41
	v_pk_mov_b32 v[8:9], v[8:9], v[46:47] op_sel:[1,0]
	v_pk_mov_b32 v[10:11], v[48:49], v[54:55] op_sel:[1,0]
	v_add_f32 v40, v104, v52
	v_add_f32 v41, v105, v53
	v_add_f32_e64 v8, v8, -v10
	v_add_f32_e64 v9, v9, -v11
	v_mul_f32 v46, v56, v40
	v_mul_f32 v47, v56, v41
	v_fma_f32 v48, v38, v40, v47
	v_fma_f32 v49, v39, v41, v46
	v_fma_f32 v39, v38, v41, -v46
	v_fma_f32 v38, v38, v40, -v47
	v_add_f32_e64 v40, v8, -v9
	v_add_f32_e64 v41, v8, -v9
	v_mov_b32_e32 v49, v39
	v_add_f32 v38, v2, v3
	v_add_f32 v39, v2, v3
	v_mul_f32 v40, v72, v40
	v_mul_f32 v41, v73, v41
	v_add_f32_e64 v10, v104, -v52
	v_add_f32_e64 v11, v105, -v53
	v_fma_f32 v46, v68, v38, -v40
	v_fma_f32 v47, v69, v39, -v41
	v_fma_f32 v38, v70, v38, v40
	v_fma_f32 v39, v71, v39, v41
	v_add_f32_e64 v253, v4, -v5
	v_add_f32_e64 v5, v4, -v5
	v_mov_b32_e32 v4, v253
	v_mov_b32_e32 v47, v39
	v_mul_f32 v38, v84, v10
	v_mul_f32 v39, v85, v11
	v_add_f32_e64 v253, v2, -v3
	v_add_f32_e64 v3, v2, -v3
	v_mov_b32_e32 v2, v253
	v_fma_f32 v40, v86, v10, -v39
	v_fma_f32 v41, v87, v11, -v38
	v_fma_f32 v10, v86, v10, v39
	v_fma_f32 v11, v87, v11, v38
	s_nop 0
	v_mov_b32_e32 v41, v11
	v_mul_f32 v10, v80, v14
	v_mul_f32 v11, v81, v15
	s_nop 0
	v_fma_f32 v38, v78, v14, -v11
	v_fma_f32 v39, v79, v15, -v10
	v_fma_f32 v253, v78, v14, v11
	v_fma_f32 v11, v79, v15, v10
	v_mov_b32_e32 v10, v253
	s_nop 0
	v_mov_b32_e32 v39, v11
	v_add_f32 v10, v26, v27
	v_add_f32 v11, v26, v27
	v_mul_f32 v10, v90, v10
	v_mul_f32 v11, v91, v11
	s_nop 0
	v_fma_f32 v14, v82, v4, -v10
	v_fma_f32 v15, v83, v5, -v11
	v_fma_f32 v4, v88, v4, v10
	v_fma_f32 v5, v89, v5, v11
	s_nop 0
	v_mov_b32_e32 v15, v5
	v_add_f32 v4, v8, v9
	v_add_f32 v5, v8, v9
	v_mul_f32 v4, v92, v4
	v_mul_f32 v5, v93, v5
	s_nop 0
	v_fma_f32 v8, v76, v2, -v4
	v_fma_f32 v9, v77, v3, -v5
	v_fma_f32 v2, v74, v2, v4
	v_fma_f32 v3, v75, v3, v5
	s_nop 0
	v_mov_b32_e32 v9, v3
	v_mul_f32 v2, v98, v21
	v_mul_f32 v3, v99, v21
	s_nop 0
	v_fma_f32 v4, v94, v12, -v2
	v_fma_f32 v5, v95, v13, -v3
	v_fma_f32 v2, v96, v12, v2
	v_fma_f32 v3, v97, v12, v3
	s_nop 0
	v_mov_b32_e32 v5, v3
	v_mul_f32 v2, v108, v19
	v_mul_f32 v3, v109, v19
	s_nop 0
	v_fma_f32 v10, v100, v6, -v2
	v_fma_f32 v11, v101, v7, -v3
	v_fma_f32 v2, v102, v6, v2
	v_fma_f32 v3, v103, v6, v3
	s_nop 0
	v_mov_b32_e32 v11, v3
	ds_write2_b64 v60, v[16:17], v[48:49] offset1:66
	ds_write2_b64 v60, v[30:31], v[44:45] offset0:132 offset1:198
	ds_write2_b64 v65, v[32:33], v[46:47] offset0:8 offset1:74
	ds_write2_b64 v65, v[28:29], v[42:43] offset0:140 offset1:206
	ds_write2_b64 v67, v[24:25], v[40:41] offset0:16 offset1:82
	ds_write2_b64 v67, v[22:23], v[38:39] offset0:148 offset1:214
	ds_write2_b64 v185, v[14:15], v[8:9] offset0:24 offset1:90
	ds_write2_b64 v185, v[4:5], v[10:11] offset0:156 offset1:222
	s_waitcnt lgkmcnt(0)
	s_barrier
	s_waitcnt vmcnt(32)
	s_and_saveexec_b64 s[48:49], vcc
	s_cbranch_execz .LBB0_661
	v_cvt_pk_bf16_f32 v2, v145, v147
	v_cvt_pk_bf16_f32 v3, v146, v149
	v_cvt_pk_bf16_f32 v4, v148, v151
	v_cvt_pk_bf16_f32 v5, v150, v152
	v_lshl_add_u64 v[6:7], v[34:35], 0, s[22:23]
	global_store_dwordx4 v[34:35], v[2:5], off nt
	s_nop 1
	v_cvt_pk_bf16_f32 v2, v137, v139
	v_cvt_pk_bf16_f32 v3, v138, v141
	v_cvt_pk_bf16_f32 v4, v140, v143
	v_cvt_pk_bf16_f32 v5, v142, v144
	s_lshl_b32 s12, s44, 1
	global_store_dwordx4 v[6:7], v[2:5], off nt
	s_nop 1
	v_cvt_pk_bf16_f32 v2, v129, v131
	v_cvt_pk_bf16_f32 v3, v130, v133
	v_cvt_pk_bf16_f32 v4, v132, v135
	v_cvt_pk_bf16_f32 v5, v134, v136
	v_lshl_add_u64 v[8:9], v[34:35], 0, s[12:13]
	global_store_dwordx4 v[8:9], v[2:5], off nt
	s_nop 1
	v_cvt_pk_bf16_f32 v2, v121, v123
	v_cvt_pk_bf16_f32 v3, v122, v125
	v_cvt_pk_bf16_f32 v4, v124, v127
	v_cvt_pk_bf16_f32 v5, v126, v128
	v_lshl_add_u64 v[6:7], v[6:7], 0, s[12:13]
	global_store_dwordx4 v[6:7], v[2:5], off nt
	s_nop 1

; __device__ __forceinline__ KP kparams() { KP q = (KP)__builtin_amdgcn_kernarg_segment_ptr(); asm volatile("" : "+s"(q)); return q; }
; FFT_HD cf2 mk2(float x, float y) { return (cf2){x, y}; }
; FFT_HD void fft_sincos(float frac, float& s, float& c) { s = __builtin_amdgcn_sinf(frac); c = __builtin_amdgcn_cosf(frac); }
; FFT_HD cf2 cmul(cf2 a, cf2 b) { return mk2(a.x * b.x - a.y * b.y, a.x * b.y + a.y * b.x); }
; template <int BANK> __device__ __forceinline__ void bg_issue1(BgState& b, int wg, int NW, int lane) {
;     KP kp = kparams();
;     const float* src; int ldS; bf16_t* dst; int o2;
;     bg_decode(b.st, wg, NW, lane, kp, src, ldS, dst, o2);
;     b.dst[BANK] = dst; b.o2[BANK] = o2;
;     asm volatile("s_nop 6" ::: "memory");
; #pragma unroll
;     for (int i = 0; i < 8; ++i) { const float* p = src + (size_t)i * ldS;
;         asm volatile("global_load_dword %0, %4, off\n\tglobal_load_dword %1, %4, off offset:256\n\tglobal_load_dword %2, %4, off offset:512\n\tglobal_load_dword %3, %4, off offset:768"
;                      : "=&v"(b.r[(BANK * 8 + i) * 4 + 0]), "=&v"(b.r[(BANK * 8 + i) * 4 + 1]), "=&v"(b.r[(BANK * 8 + i) * 4 + 2]), "=&v"(b.r[(BANK * 8 + i) * 4 + 3]) : "v"(p) : "memory"); }
;     b.st += 1;
; }
; FFT_HD void fft_gen_tw(float frac, cf2 (&tw)[16]) {
;     float sn, cs; fft_sincos(frac, sn, cs);
;     tw[1] = mk2(cs, -sn);
;     tw[2] = cmul(tw[1], tw[1]); tw[3] = cmul(tw[2], tw[1]); tw[4] = cmul(tw[2], tw[2]); tw[5] = cmul(tw[4], tw[1]); tw[6] = cmul(tw[4], tw[2]); tw[7] = cmul(tw[4], tw[3]);
;     tw[8] = cmul(tw[4], tw[4]);
; #pragma unroll
;     for (int j = 9; j < 16; ++j) tw[j] = cmul(tw[8], tw[j - 8]);
; }
.LBB0_671:
	s_nop 6
	s_lshl_b32 s12, s44, 2
	global_load_dword v145, v[2:3], off nt
	global_load_dword v137, v[2:3], off offset:256 nt
	global_load_dword v129, v[2:3], off offset:512 nt
	global_load_dword v121, v[2:3], off offset:768 nt
	v_lshl_add_u64 v[2:3], v[2:3], 0, s[12:13]
	v_and_b32_e32 v14, 3, v120
	global_load_dword v147, v[2:3], off nt
	global_load_dword v139, v[2:3], off offset:256 nt
	global_load_dword v131, v[2:3], off offset:512 nt
	global_load_dword v123, v[2:3], off offset:768 nt
	v_lshl_add_u64 v[2:3], v[2:3], 0, s[12:13]
	v_cvt_f32_ubyte0_e32 v4, v14
	global_load_dword v146, v[2:3], off nt
	global_load_dword v138, v[2:3], off offset:256 nt
	global_load_dword v130, v[2:3], off offset:512 nt
	global_load_dword v122, v[2:3], off offset:768 nt
	v_lshl_add_u64 v[2:3], v[2:3], 0, s[12:13]
	v_mul_f32_e32 v4, 0x3c800000, v4
	global_load_dword v149, v[2:3], off nt
	global_load_dword v141, v[2:3], off offset:256 nt
	global_load_dword v133, v[2:3], off offset:512 nt
	global_load_dword v125, v[2:3], off offset:768 nt
	v_lshl_add_u64 v[2:3], v[2:3], 0, s[12:13]
	v_sin_f32_e32 v39, v4
	v_cos_f32_e32 v38, v4
	global_load_dword v148, v[2:3], off nt
	global_load_dword v140, v[2:3], off offset:256 nt
	global_load_dword v132, v[2:3], off offset:512 nt
	global_load_dword v124, v[2:3], off offset:768 nt
	v_lshl_add_u64 v[2:3], v[2:3], 0, s[12:13]
	global_load_dword v150, v[2:3], off nt
	global_load_dword v142, v[2:3], off offset:256 nt
	global_load_dword v134, v[2:3], off offset:512 nt
	global_load_dword v126, v[2:3], off offset:768 nt
	v_lshl_add_u64 v[2:3], v[2:3], 0, s[12:13]
	global_load_dword v151, v[2:3], off nt
	global_load_dword v143, v[2:3], off offset:256 nt
	global_load_dword v135, v[2:3], off offset:512 nt
	global_load_dword v127, v[2:3], off offset:768 nt
	v_lshl_add_u64 v[2:3], v[2:3], 0, s[12:13]
	global_load_dword v152, v[2:3], off nt
	global_load_dword v144, v[2:3], off offset:256 nt
	global_load_dword v136, v[2:3], off offset:512 nt
	global_load_dword v128, v[2:3], off offset:768 nt
	v_mul_f32 v2, v38, v38
	v_mul_f32 v3, v39, v39
	v_mul_f32_e64 v4, v38, -v39
	v_mov_b32_e32 v5, v2
	v_mov_b32_e32 v2, v4
	v_add_f32 v192, v4, v2
	v_add_f32 v193, v5, v3
	v_add_f32_e64 v202, v4, -v2
	v_add_f32_e64 v203, v5, -v3
	v_mov_b32_e32 v46, v192
	v_mov_b32_e32 v47, v203
	v_mul_f32 v8, v46, v46
	v_mul_f32 v9, v47, v47
	v_mul_f32 v10, v203, v46
	v_mul_f32 v11, v202, v47
	v_mov_b32_e32 v2, v39
	v_mov_b32_e32 v3, v38
	v_pk_mov_b32 v[12:13], v[8:9], v[10:11] op_sel:[1,0]
	v_mov_b32_e32 v9, v10
	v_mul_f32 v4, v2, v46
	v_mul_f32 v5, v3, v47
	v_mul_f32 v6, v38, v46
	v_mul_f32 v7, v39, v47
	v_add_f32_e64 v48, v12, -v8
	v_add_f32_e64 v49, v13, -v9
	v_add_f32 v68, v12, v8
	v_add_f32 v69, v13, v9
	v_mov_b32_e32 v50, v48
	v_mov_b32_e32 v51, v69
	v_mov_b32_e32 v8, v6
	v_mov_b32_e32 v9, v5
	v_pk_mov_b32 v[4:5], v[6:7], v[4:5] op_sel:[1,0]
	v_mul_f32 v6, v50, v69
	v_mul_f32 v7, v51, v68
	v_add_f32_e64 v72, v8, -v4
	v_add_f32_e64 v73, v9, -v5
	v_add_f32 v70, v8, v4
	v_add_f32 v71, v9, v5
	v_mul_f32 v4, v50, v50
	v_mul_f32 v5, v51, v51
	s_mov_b32 s44, s27
	v_mov_b32_e32 v7, v4
	v_mov_b32_e32 v4, v6
	v_add_f32 v76, v6, v4
	v_add_f32 v77, v7, v5
	v_add_f32_e64 v74, v6, -v4
	v_add_f32_e64 v75, v7, -v5
	v_mov_b32_e32 v54, v76
	v_mov_b32_e32 v55, v75
	v_mul_f32 v84, v2, v54
	v_mul_f32 v85, v3, v55
	v_and_b32_e32 v2, 0xffffffc0, v184
	v_ashrrev_i32_e32 v3, 5, v184
	v_add_u32_e32 v4, 0x2000, v2
	v_lshlrev_b32_e32 v2, 3, v2
	v_lshlrev_b32_e32 v5, 3, v14
	v_lshlrev_b32_e32 v3, 3, v3
	v_add3_u32 v2, 0, v2, v5
	v_and_b32_e32 v3, -16, v3
	v_add_u32_e32 v65, v2, v3
	ds_read2_b64 v[98:101], v65 offset1:4
	ds_read2_b64 v[102:105], v65 offset0:8 offset1:12
	ds_read2_b64 v[106:109], v65 offset0:16 offset1:20
	ds_read2_b64 v[110:113], v65 offset0:24 offset1:28
	ds_read2_b64 v[114:117], v65 offset0:32 offset1:36
	ds_read2_b64 v[184:187], v65 offset0:40 offset1:44
	ds_read2_b64 v[188:191], v65 offset0:48 offset1:52
	ds_read2_b64 v[198:201], v65 offset0:56 offset1:60
	s_waitcnt lgkmcnt(5)
	v_pk_mov_b32 v[204:205], v[100:101], v[108:109] op_sel:[1,0]
	s_waitcnt lgkmcnt(3)
	v_mov_b32_e32 v208, v116
	s_waitcnt lgkmcnt(2)
	v_mov_b32_e32 v212, v184
	s_waitcnt lgkmcnt(1)
	v_pk_mov_b32 v[206:207], v[116:117], v[190:191] op_sel:[1,0]
	v_mov_b32_e32 v209, v191
	v_add_f32_e64 v204, v204, -v206
	v_add_f32_e64 v205, v205, -v207
	v_mov_b32_e32 v206, v100
	v_mov_b32_e32 v207, v109
	v_add_f32_e64 v206, v206, -v208
	v_add_f32_e64 v207, v207, -v209
	v_pk_mov_b32 v[208:209], v[102:103], v[110:111] op_sel:[1,0]
	s_waitcnt lgkmcnt(0)
; FFT_HD cf2 mk2(float x, float y) { return (cf2){x, y}; }
; FFT_HD cf2 cmul(cf2 a, cf2 b) { return mk2(a.x * b.x - a.y * b.y, a.x * b.y + a.y * b.x); }
; FFT_HD cf2 cadd(cf2 a, cf2 b) { return mk2(a.x + b.x, a.y + b.y); }
; FFT_HD cf2 csub(cf2 a, cf2 b) { return mk2(a.x - b.x, a.y - b.y); }
; template <bool INV> FFT_HD void dft4(cf2& a, cf2& b, cf2& c, cf2& d) {
;     const cf2 s0 = cadd(a, c), s1 = csub(a, c), s2 = cadd(b, d), s3 = csub(b, d);
;     a = cadd(s0, s2); c = csub(s0, s2);
;     const cf2 r = INV ? mk2(-s3.y, s3.x) : mk2(s3.y, -s3.x);
;     b = cadd(s1, r); d = csub(s1, r);
; }
; template <bool INV> FFT_HD void dft16(cf2 (&x)[16]) {
;     const float C1 = 0.9238795325112867f, S1 = 0.3826834323650898f, H = 0.7071067811865476f;
; #pragma unroll
;     for (int b = 0; b < 4; ++b) dft4<INV>(x[b], x[4 + b], x[8 + b], x[12 + b]);
;     const float s = INV ? -1.f : 1.f;
;     x[4 + 1] = cmul(x[4 + 1], mk2(C1, -s * S1)); x[8 + 1] = cmul(x[8 + 1], mk2(H, -s * H));   x[12 + 1] = cmul(x[12 + 1], mk2(S1, -s * C1));
;     x[4 + 2] = cmul(x[4 + 2], mk2(H, -s * H));   x[8 + 2] = cmul(x[8 + 2], mk2(0.f, -s));     x[12 + 2] = cmul(x[12 + 2], mk2(-H, -s * H));
;     x[4 + 3] = cmul(x[4 + 3], mk2(S1, -s * C1)); x[8 + 3] = cmul(x[8 + 3], mk2(-H, -s * H));  x[12 + 3] = cmul(x[12 + 3], mk2(-C1, s * S1));
; #pragma unroll
;     for (int c = 0; c < 4; ++c) dft4<INV>(x[4 * c], x[4 * c + 1], x[4 * c + 2], x[4 * c + 3]);
; #pragma unroll
;     for (int c = 0; c < 4; ++c)
; #pragma unroll
;         for (int d = c + 1; d < 4; ++d) { const cf2 t = x[4 * c + d]; x[4 * c + d] = x[4 * d + c]; x[4 * d + c] = t; }
; }
	v_pk_mov_b32 v[210:211], v[184:185], v[198:199] op_sel:[1,0]
	v_mov_b32_e32 v213, v199
	v_add_f32_e64 v208, v208, -v210
	v_add_f32_e64 v209, v209, -v211
	v_mov_b32_e32 v210, v102
	v_mov_b32_e32 v211, v111
	v_add_f32_e64 v210, v210, -v212
	v_add_f32_e64 v211, v211, -v213
	v_pk_mov_b32 v[212:213], v[104:105], v[112:113] op_sel:[1,0]
	v_pk_mov_b32 v[214:215], v[186:187], v[200:201] op_sel:[1,0]
	v_mov_b32_e32 v216, v186
	v_add_f32_e64 v212, v212, -v214
	v_add_f32_e64 v213, v213, -v215
	v_mov_b32_e32 v214, v104
	v_mov_b32_e32 v215, v113
	v_mov_b32_e32 v217, v201
	v_add_f32_e64 v214, v214, -v216
	v_add_f32_e64 v215, v215, -v217
	v_mov_b32_e32 v217, v212
	v_mov_b32_e32 v216, v214
	v_mov_b32_e32 v218, v215
	v_mov_b32_e32 v219, v213
	v_add_f32_e32 v56, v210, v211
	v_add_f32_e64 v220, v216, -v218
	v_add_f32_e64 v221, v217, -v219
	v_add_f32 v216, v216, v218
	v_add_f32 v217, v217, v219
	v_mul_f32_e32 v232, 0x3f3504f3, v56
	v_mov_b32_e32 v221, v217
	v_mul_f32_e32 v56, 0x3ec3ef15, v217
	v_add_f32 v226, v206, v207
	v_add_f32 v227, v206, v207
	s_mov_b32 s45, s26
	v_add_f32 v253, v214, v215
	v_add_f32 v215, v214, v215
	v_mov_b32_e32 v214, v253
	v_sub_f32_e32 v67, v208, v209
	v_fma_f32 v218, v220, s30, -v56
	v_fma_f32 v219, v221, s31, -v56
	v_mul_f32_e32 v236, 0x3ec3ef15, v220
	v_mul_f32_e32 v237, 0x3f6c835e, v217
	v_add_f32 v216, v98, v114
	v_add_f32 v217, v99, v115
	v_add_f32 v220, v106, v188
	v_add_f32 v221, v107, v189
	v_add_f32_e64 v98, v98, -v114
	v_add_f32_e64 v99, v99, -v115
	v_add_f32_e64 v106, v106, -v188
	v_add_f32_e64 v107, v107, -v189
	v_mul_f32_e64 v226, v226, s26
	v_mul_f32_e64 v227, v227, s27
	v_add_f32_e64 v228, v204, -v205
	v_add_f32_e64 v229, v204, -v205
	v_mul_f32_e64 v214, v214, s44
	v_mul_f32_e64 v215, v215, s45
	v_add_f32_e64 v253, v212, -v213
	v_add_f32_e64 v213, v212, -v213
	v_mov_b32_e32 v212, v253
	v_pk_mov_b32 v[114:115], v[106:107], v[106:107] op_sel:[1,0]
	v_add_f32 v188, v98, v107
	v_add_f32 v189, v99, v106
	v_add_f32_e64 v253, v98, -v107
	v_add_f32_e64 v107, v99, -v106
	v_mov_b32_e32 v106, v253
	v_fma_f32 v230, v228, s44, v226
	v_fma_f32 v231, v229, s45, v227
	v_fma_f32 v226, v228, s44, -v226
	v_fma_f32 v227, v229, s45, -v227
	v_fmamk_f32 v228, v67, 0x3f3504f3, v232
	v_fma_f32 v232, v67, s25, -v232
	v_fma_f32 v234, v212, s26, v214
	v_fma_f32 v235, v213, s27, v215
	v_fma_f32 v212, v212, s26, -v214
	v_fma_f32 v213, v213, s27, -v215
	v_mov_b32_e32 v224, v188
	v_mov_b32_e32 v225, v107
	v_mov_b32_e32 v226, v230
	v_mov_b32_e32 v233, v232
	v_mov_b32_e32 v229, v232
	v_mov_b32_e32 v212, v234
	v_add_f32 v214, v224, v228
	v_add_f32 v215, v225, v229
	v_add_f32 v224, v226, v212
	v_add_f32 v225, v227, v213
	v_pk_mov_b32 v[106:107], v[106:107], v[230:231] op_sel:[1,0]
	v_pk_mov_b32 v[230:231], v[232:233], v[234:235] op_sel:[1,0]
	v_mov_b32_e32 v226, v188
	v_add_f32_e64 v230, v106, -v230
	v_add_f32_e64 v231, v107, -v231
	v_mov_b32_e32 v229, v213
	v_add_f32 v106, v214, v224
	v_add_f32 v107, v215, v225
	v_mov_b32_e32 v56, v39
	v_add_f32_e64 v212, v226, -v228
	v_add_f32_e64 v213, v227, -v229
	v_mul_f32 v226, v56, v106
	v_mul_f32 v227, v56, v107
	v_add_f32 v100, v100, v116
	v_add_f32 v101, v101, v117
	v_add_f32 v108, v108, v190
	v_add_f32 v109, v109, v191
	v_add_f32 v102, v102, v184
	v_add_f32 v103, v103, v185
	v_add_f32 v184, v110, v198
	v_add_f32 v185, v111, v199
	v_add_f32 v104, v104, v186
	v_add_f32 v105, v105, v187
	v_add_f32 v112, v112, v200
	v_add_f32 v113, v113, v201
	v_fma_f32 v228, v38, v106, v227
	v_fma_f32 v229, v39, v107, v226
	v_fma_f32 v106, v38, v106, -v227
	v_fma_f32 v107, v38, v107, -v226
	v_add_f32 v222, v216, v220
	v_add_f32 v223, v217, v221
	v_add_f32 v190, v102, v184
	v_add_f32 v191, v103, v185
	v_mov_b32_e32 v229, v107
	v_add_f32_e64 v106, v216, -v220
	v_add_f32_e64 v107, v217, -v221
	v_add_f32_e64 v102, v102, -v184
	v_add_f32_e64 v103, v103, -v185
	v_mov_b32_e32 v184, v104
	v_mov_b32_e32 v185, v101
	v_mov_b32_e32 v216, v112
	v_mov_b32_e32 v217, v109
	v_add_f32_e64 v184, v184, -v216
	v_add_f32_e64 v185, v185, -v217
	v_mov_b32_e32 v216, v100
	v_mov_b32_e32 v217, v104
	v_mov_b32_e32 v220, v108
	v_mov_b32_e32 v221, v112
	v_add_f32 v116, v100, v108
	v_add_f32 v117, v101, v109
	v_add_f32 v186, v104, v112
	v_add_f32 v187, v105, v113
	v_add_f32_e64 v216, v216, -v220
	v_add_f32_e64 v217, v217, -v221
	v_mov_b32_e32 v220, v101
	v_mov_b32_e32 v221, v105
	v_mov_b32_e32 v226, v109
	v_mov_b32_e32 v227, v113
	v_pk_mov_b32 v[100:101], v[104:105], v[100:101] op_sel:[1,0]
	v_pk_mov_b32 v[104:105], v[112:113], v[108:109] op_sel:[1,0]
	v_add_f32_e64 v220, v220, -v226
	v_add_f32_e64 v221, v221, -v227
	v_add_f32_e64 v100, v100, -v104
	v_add_f32_e64 v101, v101, -v105
	v_fma_f32 v104, v102, 0, v103
	v_fma_f32 v105, v103, 0, v102
	v_fma_f32 v253, v102, 0, -v103
	v_fma_f32 v103, v103, 0, -v102
	v_mov_b32_e32 v102, v253
	s_mov_b32 s50, s25
	s_mov_b32 s51, s24
	v_mov_b32_e32 v105, v103
	v_mul_f32_e64 v102, v220, s50
	v_mul_f32_e64 v103, v221, s51
	v_mul_f32_e64 v100, v100, s24
	v_mul_f32_e64 v101, v101, s25
	v_fma_f32 v102, v216, s50, v102
	v_fma_f32 v103, v217, s51, v103
	v_fma_f32 v100, v184, s24, -v100
	v_fma_f32 v101, v185, s25, -v101
	v_add_f32 v108, v106, v104
	v_add_f32 v109, v107, v105
	v_add_f32 v184, v102, v100
	v_add_f32 v185, v103, v101
	v_pk_mov_b32 v[44:45], v[202:203], v[192:193] op_sel:[1,0]
	v_add_f32 v112, v108, v184
	v_add_f32 v113, v109, v185
	s_mov_b32 s56, s26
	v_mul_f32 v193, v192, v112
	v_mul_f32 v192, v192, v113
	v_fma_f32 v216, v203, v112, -v192
	v_fma_f32 v217, v203, v113, -v193
	v_fma_f32 v112, v203, v112, v192
	v_fma_f32 v113, v203, v113, v193
	v_mov_b32_e32 v192, v204
	v_mov_b32_e32 v217, v113
	v_mov_b32_e32 v112, v206
; FFT_HD cf2 mk2(float x, float y) { return (cf2){x, y}; }
; FFT_HD cf2 cmul(cf2 a, cf2 b) { return mk2(a.x * b.x - a.y * b.y, a.x * b.y + a.y * b.x); }
; template <bool INV> FFT_HD void dft16(cf2 (&x)[16]) {
;     const float C1 = 0.9238795325112867f, S1 = 0.3826834323650898f, H = 0.7071067811865476f;
; #pragma unroll
;     for (int b = 0; b < 4; ++b) dft4<INV>(x[b], x[4 + b], x[8 + b], x[12 + b]);
;     const float s = INV ? -1.f : 1.f;
;     x[4 + 1] = cmul(x[4 + 1], mk2(C1, -s * S1)); x[8 + 1] = cmul(x[8 + 1], mk2(H, -s * H));   x[12 + 1] = cmul(x[12 + 1], mk2(S1, -s * C1));
;     x[4 + 2] = cmul(x[4 + 2], mk2(H, -s * H));   x[8 + 2] = cmul(x[8 + 2], mk2(0.f, -s));     x[12 + 2] = cmul(x[12 + 2], mk2(-H, -s * H));
;     x[4 + 3] = cmul(x[4 + 3], mk2(S1, -s * C1)); x[8 + 3] = cmul(x[8 + 3], mk2(-H, -s * H));  x[12 + 3] = cmul(x[12 + 3], mk2(-C1, s * S1));
; #pragma unroll
;     for (int c = 0; c < 4; ++c) dft4<INV>(x[4 * c], x[4 * c + 1], x[4 * c + 2], x[4 * c + 3]);
; #pragma unroll
;     for (int c = 0; c < 4; ++c)
; #pragma unroll
;         for (int d = c + 1; d < 4; ++d) { const cf2 t = x[4 * c + d]; x[4 * c + d] = x[4 * d + c]; x[4 * d + c] = t; }
; }
; template <bool INV, int lS, class ZP> FFT_HD void fft_r16_pass(ZP z, int tid) {
;     ...
;         if (!INV) {
; #pragma unroll
;             for (int j = 1; j < 16; ++j) x[j] = cmul(x[j], tw[j]);
;         }
	v_mov_b32_e32 v113, v210
	v_mov_b32_e32 v210, v207
	v_mov_b32_e32 v193, v208
	v_mov_b32_e32 v208, v205
	v_add_f32_e64 v112, v112, -v210
	v_add_f32_e64 v113, v113, -v211
	v_add_f32 v192, v192, v208
	v_add_f32 v193, v193, v209
	s_mov_b32 s57, s24
	v_pk_mov_b32 v[202:203], v[112:113], v[192:193] op_sel:[1,0]
	v_mul_f32_e64 v204, v192, s56
	v_mul_f32_e64 v205, v193, s57
	v_pk_mov_b32 v[192:193], v[192:193], v[112:113] op_sel:[1,0]
	s_mov_b32 s28, s25
	s_mov_b32 s52, s27
	s_mov_b32 s53, s24
	s_mov_b32 s54, s24
	s_mov_b32 s55, s27
	v_mul_f32_e64 v192, v192, s28
	v_mul_f32_e64 v193, v193, s29
	v_mov_b32_e32 v99, v236
	v_mov_b32_e32 v115, v237
	v_fma_f32 v192, v202, s54, v192
	v_fma_f32 v193, v203, s55, v193
	v_fma_f32 v202, v112, s52, v204
	v_fma_f32 v203, v113, s53, v205
	v_add_f32_e64 v98, v98, -v114
	v_add_f32_e64 v99, v99, -v115
	v_mov_b32_e32 v188, v218
	v_add_f32 v204, v192, v98
	v_add_f32 v205, v193, v99
	v_add_f32 v206, v202, v188
	v_add_f32 v207, v203, v189
	v_mov_b32_e32 v42, v72
	v_add_f32 v112, v206, v204
	v_add_f32 v113, v207, v205
	v_pk_mov_b32 v[40:41], v[70:71], v[72:73] op_sel:[1,0]
	v_mul_f32 v73, v72, v112
	v_mul_f32 v72, v72, v113
	v_mov_b32_e32 v43, v71
	v_fma_f32 v208, v71, v112, -v72
	v_fma_f32 v209, v71, v113, -v73
	v_fma_f32 v70, v71, v112, v72
	v_fma_f32 v71, v71, v113, v73
	v_add_f32_e64 v72, v116, -v186
	v_add_f32_e64 v73, v117, -v187
	v_mov_b32_e32 v209, v71
	v_add_f32_e64 v70, v222, -v190
	v_add_f32_e64 v71, v223, -v191
	v_add_f32 v198, v222, v190
	v_add_f32 v199, v223, v191
	v_add_f32 v200, v116, v186
	v_add_f32 v201, v117, v187
	v_add_f32 v186, v70, v73
	v_add_f32 v187, v71, v72
	v_add_f32_e64 v190, v70, -v73
	v_add_f32_e64 v191, v71, -v72
	v_mov_b32_e32 v70, v186
	v_pk_mov_b32 v[72:73], v[190:191], v[186:187] op_sel:[1,0]
	v_mov_b32_e32 v71, v191
	v_pk_mov_b32 v[112:113], v[68:69], v[48:49] op_sel:[1,0]
	v_mul_f32 v68, v69, v72
	v_mul_f32 v69, v69, v73
	v_add_f32_e64 v116, v230, -v231
	v_add_f32_e64 v117, v230, -v231
	v_fma_f32 v210, v48, v186, -v68
	v_fma_f32 v211, v49, v187, -v69
	v_fma_f32 v68, v48, v70, v68
	v_fma_f32 v69, v48, v71, v69
	v_mul_f32 v70, v56, v112
	v_mul_f32 v71, v56, v113
	v_mov_b32_e32 v211, v69
	v_fma_f32 v68, v38, v50, v70
	v_fma_f32 v69, v38, v51, v71
	v_fma_f32 v72, v38, v50, -v70
	v_fma_f32 v73, v38, v51, -v71
	v_mov_b32_e32 v71, v73
	v_pk_mov_b32 v[72:73], v[72:73], v[68:69] op_sel:[1,0]
	v_add_f32_e64 v104, v106, -v104
	v_add_f32_e64 v105, v107, -v105
	v_pk_mov_b32 v[106:107], v[100:101], v[102:103] op_sel:[1,0]
	v_pk_mov_b32 v[100:101], v[102:103], v[100:101] op_sel:[1,0]
	v_mov_b32_e32 v70, v68
	v_add_f32 v114, v212, v213
	v_add_f32 v115, v212, v213
	v_mul_f32 v116, v72, v116
	v_mul_f32 v117, v73, v117
	v_add_f32_e64 v100, v106, -v100
	v_add_f32_e64 v101, v107, -v101
	v_mul_f32 v96, v46, v50
	v_mul_f32 v97, v47, v51
	v_fma_f32 v220, v68, v114, -v116
	v_fma_f32 v221, v69, v115, -v117
	v_fma_f32 v114, v70, v114, v116
	v_fma_f32 v115, v71, v115, v117
	v_add_f32 v102, v104, v100
	v_add_f32 v103, v105, v101
	v_add_f32_e64 v100, v104, -v100
	v_add_f32_e64 v101, v105, -v101
	v_mul_f32 v94, v44, v50
	v_mul_f32 v95, v45, v51
	v_mov_b32_e32 v221, v115
	v_add_f32 v114, v96, v97
	v_add_f32 v115, v96, v97
	v_pk_mov_b32 v[96:97], v[100:101], v[102:103] op_sel:[1,0]
	v_mov_b32_e32 v104, v102
	v_mov_b32_e32 v105, v101
	v_mul_f32 v96, v114, v96
	v_mul_f32 v97, v115, v97
	v_add_f32_e64 v116, v94, -v95
	v_add_f32_e64 v117, v94, -v95
	v_fma_f32 v222, v116, v102, -v96
	v_fma_f32 v223, v117, v103, -v97
	v_fma_f32 v94, v116, v104, v96
	v_fma_f32 v95, v117, v105, v97
	v_pk_mov_b32 v[96:97], v[98:99], v[218:219] op_sel:[1,0]
	v_mov_b32_e32 v223, v95
	v_pk_mov_b32 v[94:95], v[192:193], v[202:203] op_sel:[1,0]
	v_mov_b32_e32 v99, v189
	v_mov_b32_e32 v193, v203
	v_add_f32_e64 v94, v94, -v96
	v_add_f32_e64 v95, v95, -v97
	v_add_f32_e64 v96, v98, -v192
	v_add_f32_e64 v97, v99, -v193
	v_mul_f32 v92, v50, v42
	v_mul_f32 v93, v51, v43
	v_add_f32 v188, v96, v94
	v_add_f32 v189, v97, v95
	v_add_f32_e64 v192, v96, -v94
	v_add_f32_e64 v193, v97, -v95
	v_mul_f32 v82, v50, v40
	v_mul_f32 v83, v51, v41
	v_add_f32 v104, v92, v93
	v_add_f32 v105, v92, v93
	v_pk_mov_b32 v[92:93], v[192:193], v[188:189] op_sel:[1,0]
	v_mov_b32_e32 v94, v188
	v_mov_b32_e32 v95, v193
	v_mul_f32 v92, v104, v92
	v_mul_f32 v93, v105, v93
	v_add_f32_e64 v106, v82, -v83
	v_add_f32_e64 v107, v82, -v83
	v_fma_f32 v202, v106, v188, -v92
	v_fma_f32 v203, v107, v189, -v93
	v_fma_f32 v82, v106, v94, v92
	v_fma_f32 v83, v107, v95, v93
	v_mul_f32 v90, v38, v54
	v_mul_f32 v91, v39, v55
	v_mov_b32_e32 v203, v83
	v_add_f32_e64 v82, v198, -v200
	v_add_f32_e64 v83, v199, -v201
	v_add_f32 v110, v198, v200
	v_add_f32 v111, v199, v201
	v_mul_f32 v92, v76, v82
	v_mul_f32 v93, v76, v83
	v_fma_f32 v198, v75, v82, -v93
	v_fma_f32 v199, v75, v83, -v92
	v_fma_f32 v82, v75, v82, v93
	v_fma_f32 v83, v75, v83, v92
	v_add_f32_e64 v92, v214, -v224
	v_add_f32_e64 v93, v215, -v225
	v_mov_b32_e32 v199, v83
	v_add_f32_e64 v82, v90, -v91
	v_add_f32_e64 v83, v90, -v91
	v_pk_mov_b32 v[52:53], v[74:75], v[76:77] op_sel:[1,0]
	v_mul_f32 v90, v82, v92
	v_mul_f32 v91, v83, v93
	v_add_f32 v253, v85, v84
	v_add_f32 v85, v85, v84
	v_mov_b32_e32 v84, v253
	v_mul_f32 v88, v46, v52
	v_mul_f32 v89, v47, v53
	v_fma_f32 v200, v84, v92, -v91
	v_fma_f32 v201, v85, v93, -v90
	v_fma_f32 v253, v84, v92, v91
	v_fma_f32 v91, v85, v93, v90
	v_mov_b32_e32 v90, v253
	v_mul_f32 v86, v46, v54
	v_mul_f32 v87, v47, v55
	v_mov_b32_e32 v201, v91
	v_add_f32_e64 v90, v108, -v184
	v_add_f32_e64 v91, v109, -v185
	v_add_f32 v184, v88, v89
	v_add_f32 v185, v88, v89
	v_mul_f32 v88, v184, v90
	v_mul_f32 v89, v185, v91
; FFT_HD cf2 cmul(cf2 a, cf2 b) { return mk2(a.x * b.x - a.y * b.y, a.x * b.y + a.y * b.x); }
; template <bool INV, int lS, class ZP> FFT_HD void fft_r16_pass(ZP z, int tid) {
;     ...
;         if (!INV) {
; #pragma unroll
;             for (int j = 1; j < 16; ++j) x[j] = cmul(x[j], tw[j]);
;         }
; #pragma unroll
;         for (int j = 0; j < 16; ++j) z[pb0 + j * STEP] = x[j];
	v_add_f32_e64 v214, v87, -v86
	v_add_f32_e64 v215, v87, -v86
	v_mul_f32 v80, v42, v52
	v_mul_f32 v81, v43, v53
	v_fma_f32 v218, v214, v90, -v89
	v_fma_f32 v219, v215, v91, -v88
	v_fma_f32 v86, v214, v90, v89
	v_fma_f32 v87, v215, v91, v88
	v_mul_f32 v78, v42, v54
	v_mul_f32 v79, v43, v55
	v_mov_b32_e32 v219, v87
	v_mov_b32_e32 v86, v204
	v_mov_b32_e32 v87, v207
	v_mov_b32_e32 v207, v205
	v_add_f32_e64 v86, v86, -v206
	v_add_f32_e64 v87, v87, -v207
	v_add_f32 v253, v80, v81
	v_add_f32 v81, v80, v81
	v_mov_b32_e32 v80, v253
	v_mul_f32 v88, v80, v86
	v_mul_f32 v89, v81, v87
	v_add_f32_e64 v253, v79, -v78
	v_add_f32_e64 v79, v79, -v78
	v_mov_b32_e32 v78, v253
	v_add_f32 v96, v230, v231
	v_add_f32 v97, v230, v231
	v_fma_f32 v204, v78, v86, -v89
	v_fma_f32 v205, v79, v87, -v88
	v_fma_f32 v86, v78, v86, v89
	v_fma_f32 v87, v79, v87, v88
	v_mul_f32 v88, v50, v76
	v_mul_f32 v89, v51, v76
	v_mov_b32_e32 v205, v87
	v_fma_f32 v86, v50, v75, -v89
	v_fma_f32 v87, v51, v75, -v88
	v_fma_f32 v90, v50, v75, v89
	v_fma_f32 v91, v51, v75, v88
	v_mov_b32_e32 v88, v86
	v_mov_b32_e32 v89, v91
	v_pk_mov_b32 v[90:91], v[90:91], v[86:87] op_sel:[1,0]
	v_add_f32_e64 v94, v212, -v213
	v_add_f32_e64 v95, v212, -v213
	v_mul_f32 v92, v90, v187
	v_mul_f32 v93, v91, v187
	v_ashrrev_i32_e32 v3, 2, v4
	v_fma_f32 v186, v86, v190, -v92
	v_fma_f32 v187, v87, v191, -v93
	v_fma_f32 v92, v88, v190, v92
	v_fma_f32 v93, v89, v190, v93
	v_add3_u32 v60, v2, v3, s71
	v_mov_b32_e32 v187, v93
	v_mul_f32 v92, v76, v70
	v_mul_f32 v93, v76, v71
	v_fma_f32 v76, v75, v70, -v93
	v_fma_f32 v77, v75, v71, -v92
	v_fma_f32 v253, v75, v70, v93
	v_fma_f32 v93, v75, v71, v92
	v_mov_b32_e32 v92, v253
	v_mov_b32_e32 v74, v76
	v_mov_b32_e32 v75, v93
	v_pk_mov_b32 v[92:93], v[92:93], v[76:77] op_sel:[1,0]
	ds_read2_b64 v[2:5], v60 offset1:4
	ds_read2_b64 v[18:21], v60 offset0:8 offset1:12
	ds_read2_b64 v[6:9], v60 offset0:16 offset1:20
	ds_read2_b64 v[22:25], v60 offset0:24 offset1:28
	ds_read2_b64 v[10:13], v60 offset0:32 offset1:36
	ds_read2_b64 v[26:29], v60 offset0:40 offset1:44
	ds_read2_b64 v[14:17], v60 offset0:48 offset1:52
	ds_read2_b64 v[30:33], v60 offset0:56 offset1:60
	v_mul_f32 v96, v92, v96
	v_mul_f32 v97, v93, v97
	v_cmp_ne_u64_e32 vcc, 0, v[36:37]
	v_fma_f32 v190, v76, v94, -v96
	v_fma_f32 v191, v77, v95, -v97
	v_fma_f32 v94, v74, v94, v96
	v_fma_f32 v95, v75, v95, v97
	v_mul_f32 v96, v54, v116
	v_mul_f32 v97, v55, v117
	v_mov_b32_e32 v191, v95
	v_fma_f32 v94, -v54, v114, v97
	v_fma_f32 v95, -v55, v115, v96
	v_fma_f32 v98, v54, v114, v97
	v_fma_f32 v99, v55, v115, v96
	v_mov_b32_e32 v96, v94
	v_mov_b32_e32 v97, v99
	v_pk_mov_b32 v[98:99], v[98:99], v[94:95] op_sel:[1,0]
	s_nop 0
	v_mul_f32 v102, v98, v103
	v_mul_f32 v103, v99, v103
	s_nop 0
	v_fma_f32 v206, v94, v100, -v102
	v_fma_f32 v207, v95, v101, -v103
	v_fma_f32 v101, v97, v100, v103
	v_fma_f32 v100, v96, v100, v102
	v_mul_f32 v102, v54, v106
	v_mul_f32 v103, v55, v107
	v_mov_b32_e32 v207, v101
	v_fma_f32 v100, -v54, v104, v103
	v_fma_f32 v101, -v55, v105, v102
	v_fma_f32 v108, v54, v104, v103
	v_fma_f32 v109, v55, v105, v102
	v_mov_b32_e32 v102, v100
	v_mov_b32_e32 v103, v109
	v_pk_mov_b32 v[108:109], v[108:109], v[100:101] op_sel:[1,0]
	s_nop 0
	v_mul_f32 v188, v108, v189
	v_mul_f32 v189, v109, v189
	s_nop 0
	v_fma_f32 v212, v100, v192, -v188
	v_fma_f32 v213, v101, v193, -v189
	v_fma_f32 v188, v102, v192, v188
	v_fma_f32 v189, v103, v192, v189
	s_waitcnt lgkmcnt(2)
	v_mov_b32_e32 v192, v26
	v_mov_b32_e32 v213, v189
	ds_write2_b64 v65, v[110:111], v[228:229] offset1:4
	ds_write2_b64 v65, v[216:217], v[208:209] offset0:8 offset1:12
	ds_write2_b64 v65, v[210:211], v[220:221] offset0:16 offset1:20
	ds_write2_b64 v65, v[222:223], v[202:203] offset0:24 offset1:28
	ds_write2_b64 v65, v[198:199], v[200:201] offset0:32 offset1:36
	ds_write2_b64 v65, v[218:219], v[204:205] offset0:40 offset1:44
	ds_write2_b64 v65, v[186:187], v[190:191] offset0:48 offset1:52
	ds_write2_b64 v65, v[206:207], v[212:213] offset0:56 offset1:60
	v_pk_mov_b32 v[110:111], v[4:5], v[8:9] op_sel:[1,0]
	s_waitcnt lgkmcnt(9)
	v_pk_mov_b32 v[186:187], v[12:13], v[16:17] op_sel:[1,0]
	v_mov_b32_e32 v188, v12
	v_add_f32_e64 v110, v110, -v186
	v_add_f32_e64 v111, v111, -v187
	v_mov_b32_e32 v186, v4
	v_mov_b32_e32 v187, v9
	v_mov_b32_e32 v189, v17
	v_add_f32_e64 v186, v186, -v188
	v_add_f32_e64 v187, v187, -v189
	v_pk_mov_b32 v[188:189], v[18:19], v[22:23] op_sel:[1,0]
	s_waitcnt lgkmcnt(8)
; FFT_HD cf2 mk2(float x, float y) { return (cf2){x, y}; }
; FFT_HD cf2 cmul(cf2 a, cf2 b) { return mk2(a.x * b.x - a.y * b.y, a.x * b.y + a.y * b.x); }
; FFT_HD cf2 cadd(cf2 a, cf2 b) { return mk2(a.x + b.x, a.y + b.y); }
; FFT_HD cf2 csub(cf2 a, cf2 b) { return mk2(a.x - b.x, a.y - b.y); }
; template <bool INV> FFT_HD void dft4(cf2& a, cf2& b, cf2& c, cf2& d) {
;     const cf2 s0 = cadd(a, c), s1 = csub(a, c), s2 = cadd(b, d), s3 = csub(b, d);
;     a = cadd(s0, s2); c = csub(s0, s2);
;     const cf2 r = INV ? mk2(-s3.y, s3.x) : mk2(s3.y, -s3.x);
;     b = cadd(s1, r); d = csub(s1, r);
; }
; template <bool INV> FFT_HD void dft16(cf2 (&x)[16]) {
;     const float C1 = 0.9238795325112867f, S1 = 0.3826834323650898f, H = 0.7071067811865476f;
; #pragma unroll
;     for (int b = 0; b < 4; ++b) dft4<INV>(x[b], x[4 + b], x[8 + b], x[12 + b]);
;     const float s = INV ? -1.f : 1.f;
;     x[4 + 1] = cmul(x[4 + 1], mk2(C1, -s * S1)); x[8 + 1] = cmul(x[8 + 1], mk2(H, -s * H));   x[12 + 1] = cmul(x[12 + 1], mk2(S1, -s * C1));
;     x[4 + 2] = cmul(x[4 + 2], mk2(H, -s * H));   x[8 + 2] = cmul(x[8 + 2], mk2(0.f, -s));     x[12 + 2] = cmul(x[12 + 2], mk2(-H, -s * H));
;     x[4 + 3] = cmul(x[4 + 3], mk2(S1, -s * C1)); x[8 + 3] = cmul(x[8 + 3], mk2(-H, -s * H));  x[12 + 3] = cmul(x[12 + 3], mk2(-C1, s * S1));
; #pragma unroll
;     for (int c = 0; c < 4; ++c) dft4<INV>(x[4 * c], x[4 * c + 1], x[4 * c + 2], x[4 * c + 3]);
; #pragma unroll
;     for (int c = 0; c < 4; ++c)
; #pragma unroll
;         for (int d = c + 1; d < 4; ++d) { const cf2 t = x[4 * c + d]; x[4 * c + d] = x[4 * d + c]; x[4 * d + c] = t; }
; }
	v_pk_mov_b32 v[190:191], v[26:27], v[30:31] op_sel:[1,0]
	v_pk_mov_b32 v[204:205], v[20:21], v[4:5] op_sel:[1,0]
	v_pk_mov_b32 v[206:207], v[28:29], v[12:13] op_sel:[1,0]
	v_add_f32_e64 v188, v188, -v190
	v_add_f32_e64 v189, v189, -v191
	v_mov_b32_e32 v190, v18
	v_mov_b32_e32 v191, v23
	v_mov_b32_e32 v193, v31
	v_add_f32 v204, v204, v206
	v_add_f32 v205, v205, v207
	v_mov_b32_e32 v206, v4
	v_mov_b32_e32 v207, v20
	v_mov_b32_e32 v208, v12
	v_mov_b32_e32 v209, v28
	v_add_f32_e64 v190, v190, -v192
	v_add_f32_e64 v191, v191, -v193
	v_add_f32 v206, v206, v208
	v_add_f32 v207, v207, v209
	v_pk_mov_b32 v[208:209], v[24:25], v[8:9] op_sel:[1,0]
	v_pk_mov_b32 v[210:211], v[32:33], v[16:17] op_sel:[1,0]
	v_add_f32_e32 v39, v190, v191
	v_sub_f32_e32 v65, v188, v189
	v_sub_f32_e32 v67, v190, v191
	v_add_f32_e32 v198, v188, v189
	v_pk_mov_b32 v[188:189], v[20:21], v[24:25] op_sel:[1,0]
	v_pk_mov_b32 v[190:191], v[28:29], v[32:33] op_sel:[1,0]
	v_add_f32 v208, v208, v210
	v_add_f32 v209, v209, v211
	v_mov_b32_e32 v210, v8
	v_mov_b32_e32 v211, v24
	v_mov_b32_e32 v212, v16
	v_mov_b32_e32 v213, v32
	v_mov_b32_e32 v4, v20
	v_mov_b32_e32 v12, v28
	v_mov_b32_e32 v8, v24
	v_mov_b32_e32 v16, v32
	v_add_f32_e64 v188, v188, -v190
	v_add_f32_e64 v189, v189, -v191
	v_mov_b32_e32 v190, v20
	v_mov_b32_e32 v192, v28
	v_add_f32 v210, v210, v212
	v_add_f32 v211, v211, v213
	v_add_f32 v212, v4, v12
	v_add_f32 v213, v5, v13
	v_mov_b32_e32 v20, v5
	v_mov_b32_e32 v28, v13
	v_add_f32 v12, v8, v16
	v_add_f32 v13, v9, v17
	v_mov_b32_e32 v24, v9
	v_mov_b32_e32 v32, v17
	v_add_f32 v16, v18, v26
	v_add_f32 v17, v19, v27
	v_add_f32 v18, v22, v30
	v_add_f32 v19, v23, v31
	v_add_f32 v4, v20, v28
	v_add_f32 v5, v21, v29
	v_add_f32 v8, v24, v32
	v_add_f32 v9, v25, v33
	v_add_f32_e64 v20, v16, -v18
	v_add_f32_e64 v21, v17, -v19
	v_mov_b32_e32 v191, v25
	v_add_f32_e64 v24, v4, -v8
	v_add_f32_e64 v25, v5, -v9
	v_add_f32_e64 v26, v204, -v208
	v_add_f32_e64 v27, v205, -v209
	v_fma_f32 v28, v20, 0, v21
	v_fma_f32 v29, v21, 0, v20
	v_fma_f32 v253, v20, 0, -v21
	v_fma_f32 v21, v21, 0, -v20
	v_mov_b32_e32 v20, v253
	v_mov_b32_e32 v193, v33
	v_add_f32_e64 v12, v212, -v12
	v_add_f32_e64 v13, v213, -v13
	v_mov_b32_e32 v29, v21
	v_mul_f32_e64 v20, v24, s50
	v_mul_f32_e64 v21, v25, s51
	v_mul_f32_e64 v24, v26, s24
	v_mul_f32_e64 v25, v27, s25
	v_add_f32_e64 v190, v190, -v192
	v_add_f32_e64 v191, v191, -v193
	v_mul_f32_e32 v193, 0xbf3504f3, v198
	v_add_f32 v198, v2, v10
	v_add_f32 v199, v3, v11
	v_add_f32 v200, v6, v14
	v_add_f32 v201, v7, v15
	v_add_f32_e64 v22, v206, -v210
	v_add_f32_e64 v23, v207, -v211
	v_fma_f32 v12, v12, s24, -v24
	v_fma_f32 v13, v13, s25, -v25
	v_mov_b32_e32 v24, v206
	v_mov_b32_e32 v25, v4
	v_mov_b32_e32 v26, v210
	v_mov_b32_e32 v27, v8
	v_mov_b32_e32 v4, v207
	v_mov_b32_e32 v8, v211
	v_fma_f32 v20, v22, s50, v20
	v_fma_f32 v21, v23, s51, v21
	v_add_f32 v22, v198, v200
	v_add_f32 v23, v199, v201
	v_add_f32 v24, v24, v26
	v_add_f32 v25, v25, v27
	v_add_f32 v16, v16, v18
	v_add_f32 v17, v17, v19
	v_add_f32 v4, v4, v8
	v_add_f32 v5, v5, v9
	v_add_f32_e64 v202, v198, -v200
	v_add_f32_e64 v203, v199, -v201
	v_add_f32 v8, v22, v16
	v_add_f32 v9, v23, v17
	v_add_f32 v18, v24, v4
	v_add_f32 v19, v25, v5
	v_pk_mov_b32 v[26:27], v[22:23], v[24:25] op_sel:[1,0]
	v_pk_mov_b32 v[30:31], v[16:17], v[4:5] op_sel:[1,0]
	v_mov_b32_e32 v23, v25
	v_mov_b32_e32 v17, v5
	v_add_f32_e64 v4, v22, -v16
	v_add_f32_e64 v5, v23, -v17
	v_add_f32 v16, v8, v18
	v_add_f32 v17, v9, v19
	v_add_f32_e64 v8, v8, -v18
	v_add_f32_e64 v9, v9, -v19
	v_add_f32 v18, v202, v28
	v_add_f32 v19, v203, v29
	v_add_f32 v22, v20, v12
	v_add_f32 v23, v21, v13
	v_add_f32_e64 v26, v26, -v30
	v_add_f32_e64 v27, v27, -v31
	v_add_f32 v24, v18, v22
	v_add_f32 v25, v19, v23
	v_add_f32_e64 v18, v18, -v22
	v_add_f32_e64 v19, v19, -v23
	v_mul_f32 v22, v46, v25
	v_mul_f32 v23, v47, v25
	v_add_f32_e64 v2, v2, -v10
	v_add_f32_e64 v3, v3, -v11
	v_fma_f32 v30, v44, v24, -v22
	v_fma_f32 v31, v45, v25, -v23
	v_fma_f32 v22, v44, v24, v22
	v_fma_f32 v23, v45, v24, v23
	v_add_f32_e64 v24, v26, -v27
	v_add_f32_e64 v25, v26, -v27
	v_mov_b32_e32 v31, v23
	v_add_f32 v22, v4, v5
	v_add_f32 v23, v4, v5
	v_mul_f32 v24, v112, v24
	v_mul_f32 v25, v113, v25
	v_add_f32_e64 v10, v186, -v187
	v_add_f32_e64 v11, v186, -v187
	v_fma_f32 v32, v48, v22, -v24
	v_fma_f32 v33, v49, v23, -v25
	v_fma_f32 v22, v50, v22, v24
	v_fma_f32 v23, v51, v23, v25
	v_pk_mov_b32 v[24:25], v[12:13], v[20:21] op_sel:[1,0]
	v_pk_mov_b32 v[12:13], v[20:21], v[12:13] op_sel:[1,0]
	v_mov_b32_e32 v33, v23
	v_add_f32_e64 v22, v202, -v28
	v_add_f32_e64 v23, v203, -v29
	v_add_f32_e64 v12, v24, -v12
	v_add_f32_e64 v13, v25, -v13
	v_add_f32_e64 v6, v6, -v14
	v_add_f32_e64 v7, v7, -v15
	v_add_f32 v20, v22, v12
	v_add_f32 v21, v23, v13
	v_add_f32_e64 v12, v22, -v12
	v_add_f32_e64 v13, v23, -v13
	v_mov_b32_e32 v22, v20
	v_pk_mov_b32 v[24:25], v[12:13], v[20:21] op_sel:[1,0]
	v_mov_b32_e32 v23, v13
	v_mul_f32 v24, v114, v24
	v_mul_f32 v25, v115, v25
	v_mul_f32_e64 v10, v10, s44
	v_mul_f32_e64 v11, v11, s45
	v_fma_f32 v28, v116, v20, -v24
	v_fma_f32 v29, v117, v21, -v25
	v_fma_f32 v22, v116, v22, v24
	v_fma_f32 v23, v117, v23, v25
	v_add_f32 v14, v110, v111
	v_add_f32 v15, v110, v111
	v_mov_b32_e32 v29, v23
	v_mul_f32 v22, v54, v9
	v_mul_f32 v23, v55, v9
	v_mul_f32_e32 v192, 0xbf3504f3, v67
	v_fma_f32 v24, v52, v8, -v22
	v_fma_f32 v25, v53, v9, -v23
	v_fma_f32 v9, v53, v8, v23
	v_fma_f32 v8, v52, v8, v22
	v_sub_f32_e32 v192, v192, v193
	v_mov_b32_e32 v25, v9
	v_mul_f32 v8, v184, v18
	v_mul_f32 v9, v185, v19
	v_fmac_f32_e32 v193, 0xbf3504f3, v67
	v_fma_f32 v22, v214, v18, -v9
	v_fma_f32 v23, v215, v19, -v8
; __device__ __forceinline__ unsigned cvt_pk_bf16(float lo, float hi) { unsigned r; asm volatile("v_cvt_pk_bf16_f32 %0, %1, %2" : "=v"(r) : "v"(lo), "v"(hi)); return r; }
; FFT_HD cf2 cmul(cf2 a, cf2 b) { return mk2(a.x * b.x - a.y * b.y, a.x * b.y + a.y * b.x); }
; template <int BANK, int WAITN> __device__ __forceinline__ void bg_finish1(BgState& b) {
;     if (WAITN == 32) asm volatile("s_waitcnt vmcnt(32)" ::: "memory"); else asm volatile("s_waitcnt vmcnt(0)" ::: "memory");
;     asm volatile("" : BG_TIE16(BANK * 32) :: "memory");
;     asm volatile("" : BG_TIE16(BANK * 32 + 16) :: "memory");
;     bf16_t* dst = b.dst[BANK];
;     if (dst != nullptr) {
; #pragma unroll
;         for (int c = 0; c < 4; ++c) { u32x4 w;
;             w.x = cvt_pk_bf16(b.r[(BANK * 8 + 0) * 4 + c], b.r[(BANK * 8 + 1) * 4 + c]); w.y = cvt_pk_bf16(b.r[(BANK * 8 + 2) * 4 + c], b.r[(BANK * 8 + 3) * 4 + c]);
;             w.z = cvt_pk_bf16(b.r[(BANK * 8 + 4) * 4 + c], b.r[(BANK * 8 + 5) * 4 + c]); w.w = cvt_pk_bf16(b.r[(BANK * 8 + 6) * 4 + c], b.r[(BANK * 8 + 7) * 4 + c]);
;             bf16_t* dp = dst + (c & 1) * 512 + (c >> 1) * b.o2[BANK];
;             asm volatile("global_store_dwordx4 %0, %1, off\n\ts_nop 1" :: "v"(dp), "v"(w) : "memory"); }
;     }
; }
; template <bool INV, int lS, class ZP> FFT_HD void fft_r16_pass(ZP z, int tid) {
;     ...
;         dft16<INV>(y);
;         if (!INV) {
; #pragma unroll
;             for (int j = 1; j < 16; ++j) y[j] = cmul(y[j], tw[j]);
;         }
; #pragma unroll
;         for (int j = 0; j < 16; ++j) z[pb1 + j * STEP] = y[j];
	v_fma_f32 v253, v214, v18, v9
	v_fma_f32 v9, v215, v19, v8
	v_mov_b32_e32 v8, v253
	v_fma_f32 v18, v14, s26, v10
	v_fma_f32 v19, v15, s27, v11
	v_fma_f32 v10, v14, s26, -v10
	v_fma_f32 v11, v15, s27, -v11
	v_add_f32 v14, v188, v189
	v_add_f32 v15, v188, v189
	v_mov_b32_e32 v23, v9
	v_add_f32_e64 v8, v2, -v7
	v_add_f32_e64 v9, v3, -v6
	v_add_f32 v2, v2, v7
	v_add_f32 v3, v3, v6
	v_mov_b32_e32 v19, v11
	v_add_f32_e64 v10, v190, -v191
	v_add_f32_e64 v11, v190, -v191
	v_mul_f32_e64 v14, v14, s44
	v_mul_f32_e64 v15, v15, s45
	v_mov_b32_e32 v6, v8
	v_mov_b32_e32 v7, v3
	v_fma_f32 v10, v10, s30, -v14
	v_fma_f32 v11, v11, s31, -v15
	v_add_f32 v14, v6, v192
	v_add_f32 v15, v7, v193
	v_add_f32 v44, v18, v10
	v_add_f32 v45, v19, v11
	v_add_f32_e64 v6, v6, -v192
	v_add_f32_e64 v7, v7, -v193
	v_add_f32 v46, v14, v44
	v_add_f32 v47, v15, v45
	v_add_f32_e64 v10, v18, -v10
	v_add_f32_e64 v11, v19, -v11
	v_mul_f32 v42, v42, v47
	v_mul_f32 v43, v43, v47
	v_add_f32_e64 v14, v14, -v44
	v_add_f32_e64 v15, v15, -v45
	v_fma_f32 v44, v40, v46, -v42
	v_fma_f32 v45, v41, v47, -v43
	v_fma_f32 v40, v40, v46, v42
	v_fma_f32 v41, v41, v46, v43
	v_add_f32 v18, v6, v11
	v_add_f32 v19, v7, v10
	v_add_f32_e64 v6, v6, -v11
	v_add_f32_e64 v7, v7, -v10
	v_mov_b32_e32 v45, v41
	v_pk_mov_b32 v[40:41], v[6:7], v[18:19] op_sel:[1,0]
	v_mov_b32_e32 v10, v18
	v_mov_b32_e32 v11, v7
	v_mul_f32 v40, v104, v40
	v_mul_f32 v41, v105, v41
	v_add_f32 v50, v190, v191
	v_add_f32 v51, v190, v191
	v_fma_f32 v42, v106, v18, -v40
	v_fma_f32 v43, v107, v19, -v41
	v_fma_f32 v10, v106, v10, v40
	v_fma_f32 v11, v107, v11, v41
	v_mul_f32_e32 v39, 0x3f3504f3, v39
	v_mov_b32_e32 v43, v11
	v_add_f32 v10, v186, v187
	v_add_f32 v11, v186, v187
	v_mul_f32_e64 v10, v10, s26
	v_mul_f32_e64 v11, v11, s27
	v_add_f32_e64 v40, v110, -v111
	v_add_f32_e64 v41, v110, -v111
	v_mul_f32_e64 v50, v50, s44
	v_mul_f32_e64 v51, v51, s45
	v_add_f32_e64 v52, v188, -v189
	v_add_f32_e64 v53, v188, -v189
	v_fma_f32 v46, v40, s44, v10
	v_fma_f32 v47, v41, s45, v11
	v_fma_f32 v10, v40, s44, -v10
	v_fma_f32 v11, v41, s45, -v11
	v_fma_f32 v48, v65, s25, -v39
	v_fma_f32 v54, v52, s26, v50
	v_fma_f32 v55, v53, s27, v51
	v_fma_f32 v50, v52, s26, -v50
	v_fma_f32 v51, v53, s27, -v51
	v_mov_b32_e32 v10, v46
	v_fmamk_f32 v40, v65, 0x3f3504f3, v39
	v_mov_b32_e32 v41, v48
	v_mov_b32_e32 v50, v54
	v_mov_b32_e32 v3, v9
	v_mov_b32_e32 v49, v48
	v_add_f32 v52, v10, v50
	v_add_f32 v53, v11, v51
	v_add_f32 v104, v2, v40
	v_add_f32 v105, v3, v41
	v_mov_b32_e32 v3, v11
	v_mov_b32_e32 v41, v51
	v_add_f32_e64 v2, v2, -v40
	v_add_f32_e64 v3, v3, -v41
	v_pk_mov_b32 v[8:9], v[8:9], v[46:47] op_sel:[1,0]
	v_pk_mov_b32 v[10:11], v[48:49], v[54:55] op_sel:[1,0]
	v_add_f32 v40, v104, v52
	v_add_f32 v41, v105, v53
	v_add_f32_e64 v8, v8, -v10
	v_add_f32_e64 v9, v9, -v11
	v_mul_f32 v46, v56, v40
	v_mul_f32 v47, v56, v41
	v_fma_f32 v48, v38, v40, v47
	v_fma_f32 v49, v39, v41, v46
	v_fma_f32 v39, v38, v41, -v46
	v_fma_f32 v38, v38, v40, -v47
	v_add_f32_e64 v40, v8, -v9
	v_add_f32_e64 v41, v8, -v9
	v_mov_b32_e32 v49, v39
	v_add_f32 v38, v2, v3
	v_add_f32 v39, v2, v3
	v_mul_f32 v40, v72, v40
	v_mul_f32 v41, v73, v41
	v_add_f32_e64 v10, v104, -v52
	v_add_f32_e64 v11, v105, -v53
	v_fma_f32 v46, v68, v38, -v40
	v_fma_f32 v47, v69, v39, -v41
	v_fma_f32 v38, v70, v38, v40
	v_fma_f32 v39, v71, v39, v41
	v_add_f32_e64 v253, v4, -v5
	v_add_f32_e64 v5, v4, -v5
	v_mov_b32_e32 v4, v253
	v_mov_b32_e32 v47, v39
	v_mul_f32 v38, v82, v10
	v_mul_f32 v39, v83, v11
	v_add_f32_e64 v253, v2, -v3
	v_add_f32_e64 v3, v2, -v3
	v_mov_b32_e32 v2, v253
	v_fma_f32 v40, v84, v10, -v39
	v_fma_f32 v41, v85, v11, -v38
	v_fma_f32 v10, v84, v10, v39
	v_fma_f32 v11, v85, v11, v38
	s_nop 0
	v_mov_b32_e32 v41, v11
	v_mul_f32 v10, v80, v14
	v_mul_f32 v11, v81, v15
	s_nop 0
	v_fma_f32 v38, v78, v14, -v11
	v_fma_f32 v39, v79, v15, -v10
	v_fma_f32 v253, v78, v14, v11
	v_fma_f32 v11, v79, v15, v10
	v_mov_b32_e32 v10, v253
	s_nop 0
	v_mov_b32_e32 v39, v11
	v_add_f32 v10, v26, v27
	v_add_f32 v11, v26, v27
	v_mul_f32 v10, v90, v10
	v_mul_f32 v11, v91, v11
	s_nop 0
	v_fma_f32 v14, v86, v4, -v10
	v_fma_f32 v15, v87, v5, -v11
	v_fma_f32 v4, v88, v4, v10
	v_fma_f32 v5, v89, v5, v11
	s_nop 0
	v_mov_b32_e32 v15, v5
	v_add_f32 v4, v8, v9
	v_add_f32 v5, v8, v9
	v_mul_f32 v4, v92, v4
	v_mul_f32 v5, v93, v5
	s_nop 0
	v_fma_f32 v8, v76, v2, -v4
	v_fma_f32 v9, v77, v3, -v5
	v_fma_f32 v2, v74, v2, v4
	v_fma_f32 v3, v75, v3, v5
	s_nop 0
	v_mov_b32_e32 v9, v3
	v_mul_f32 v2, v98, v21
	v_mul_f32 v3, v99, v21
	s_nop 0
	v_fma_f32 v4, v94, v12, -v2
	v_fma_f32 v5, v95, v13, -v3
	v_fma_f32 v2, v96, v12, v2
	v_fma_f32 v3, v97, v12, v3
	s_nop 0
	v_mov_b32_e32 v5, v3
	v_mul_f32 v2, v108, v19
	v_mul_f32 v3, v109, v19
	s_nop 0
	v_fma_f32 v10, v100, v6, -v2
	v_fma_f32 v11, v101, v7, -v3
	v_fma_f32 v2, v102, v6, v2
	v_fma_f32 v3, v103, v6, v3
	s_nop 0
	v_mov_b32_e32 v11, v3
	ds_write2_b64 v60, v[16:17], v[48:49] offset1:4
	ds_write2_b64 v60, v[30:31], v[44:45] offset0:8 offset1:12
	ds_write2_b64 v60, v[32:33], v[46:47] offset0:16 offset1:20
	ds_write2_b64 v60, v[28:29], v[42:43] offset0:24 offset1:28
	ds_write2_b64 v60, v[24:25], v[40:41] offset0:32 offset1:36
	ds_write2_b64 v60, v[22:23], v[38:39] offset0:40 offset1:44
	ds_write2_b64 v60, v[14:15], v[8:9] offset0:48 offset1:52
	ds_write2_b64 v60, v[4:5], v[10:11] offset0:56 offset1:60
	s_waitcnt lgkmcnt(0)
	s_barrier
	s_waitcnt vmcnt(32)
	s_and_saveexec_b64 s[44:45], vcc
	s_cbranch_execz .LBB0_673
	v_cvt_pk_bf16_f32 v2, v176, v178
	v_cvt_pk_bf16_f32 v3, v177, v180
	v_cvt_pk_bf16_f32 v4, v179, v181
	v_cvt_pk_bf16_f32 v5, v182, v183
	v_lshl_add_u64 v[6:7], v[36:37], 0, s[22:23]
	global_store_dwordx4 v[36:37], v[2:5], off nt
	s_nop 1
	v_cvt_pk_bf16_f32 v2, v168, v170
	v_cvt_pk_bf16_f32 v3, v169, v172
	v_cvt_pk_bf16_f32 v4, v171, v173
	v_cvt_pk_bf16_f32 v5, v174, v175
	s_lshl_b32 s12, s46, 1
	global_store_dwordx4 v[6:7], v[2:5], off nt
	s_nop 1
	v_cvt_pk_bf16_f32 v2, v160, v162
	v_cvt_pk_bf16_f32 v3, v161, v164
	v_cvt_pk_bf16_f32 v4, v163, v165
	v_cvt_pk_bf16_f32 v5, v166, v167
	v_lshl_add_u64 v[8:9], v[36:37], 0, s[12:13]
	global_store_dwordx4 v[8:9], v[2:5], off nt
	s_nop 1
	v_cvt_pk_bf16_f32 v2, v57, v154
	v_cvt_pk_bf16_f32 v3, v153, v156
	v_cvt_pk_bf16_f32 v4, v155, v157
	v_cvt_pk_bf16_f32 v5, v158, v159
	v_lshl_add_u64 v[6:7], v[6:7], 0, s[12:13]
	global_store_dwordx4 v[6:7], v[2:5], off nt
	s_nop 1

; FFT_HD cf2 mk2(float x, float y) { return (cf2){x, y}; }
; FFT_HD cf2 cadd(cf2 a, cf2 b) { return mk2(a.x + b.x, a.y + b.y); }
; FFT_HD cf2 csub(cf2 a, cf2 b) { return mk2(a.x - b.x, a.y - b.y); }
; template <bool INV> FFT_HD void dft4(cf2& a, cf2& b, cf2& c, cf2& d) {
;     const cf2 s0 = cadd(a, c), s1 = csub(a, c), s2 = cadd(b, d), s3 = csub(b, d);
;     a = cadd(s0, s2); c = csub(s0, s2);
;     const cf2 r = INV ? mk2(-s3.y, s3.x) : mk2(s3.y, -s3.x);
;     b = cadd(s1, r); d = csub(s1, r);
; }
; template <bool INV, class ZP> FFT_HD void fft_r4_pass(ZP z, int tid, int nthr) {
;     for (int w = tid; w < FN / 4; w += nthr) {
;         const int base = PADI(4 * w);
;         cf2 a = z[base], b = z[base + 1], c = z[base + 2], d = z[base + 3];
;         dft4<INV>(a, b, c, d);
;         z[base] = a; z[base + 1] = b; z[base + 2] = c; z[base + 3] = d;
;     }
.LBB0_685:
	v_and_b32_e32 v5, -16, v120
	v_add_u32_e32 v6, 0x200, v120
	v_add_u32_e32 v5, v4, v5
	v_cmp_lt_i32_e32 vcc, s82, v120
	v_mov_b32_e32 v120, v6
	ds_read_b128 v[6:9], v5
	ds_read_b128 v[10:13], v5 offset:16
	v_add_u32_e32 v4, 0x4000, v4
	s_or_b64 s[50:51], vcc, s[50:51]
	s_waitcnt lgkmcnt(0)
	v_add_f32 v14, v6, v10
	v_add_f32 v15, v7, v11
	v_add_f32 v16, v8, v12
	v_add_f32 v17, v9, v13
	v_add_f32_e64 v18, v6, -v10
	v_add_f32_e64 v19, v7, -v11
	v_add_f32_e64 v8, v8, -v12
	v_add_f32_e64 v9, v9, -v13
	v_add_f32 v6, v14, v16
	v_add_f32 v7, v15, v17
	v_add_f32_e64 v10, v14, -v16
	v_add_f32_e64 v11, v15, -v17
	v_add_f32 v14, v18, v9
	v_add_f32 v15, v19, v8
	v_add_f32_e64 v12, v18, -v9
	v_add_f32_e64 v13, v19, -v8
	v_mov_b32_e32 v8, v14
	v_mov_b32_e32 v9, v13
	v_mov_b32_e32 v13, v15
	ds_write_b128 v5, v[6:9]
	ds_write_b128 v5, v[10:13] offset:16
	s_andn2_b64 exec, exec, s[50:51]
	s_cbranch_execnz .LBB0_685

; __device__ __forceinline__ KP kparams() { KP q = (KP)__builtin_amdgcn_kernarg_segment_ptr(); asm volatile("" : "+s"(q)); return q; }
; __device__ __forceinline__ float bf_lo(unsigned w) { return __uint_as_float(w << 16); }
; __device__ __forceinline__ float bf_hi(unsigned w) { return __uint_as_float(w & 0xffff0000u); }
; template <int BANK> __device__ __forceinline__ void bg_issue1(BgState& b, int wg, int NW, int lane) {
;     KP kp = kparams();
;     const float* src; int ldS; bf16_t* dst; int o2;
;     bg_decode(b.st, wg, NW, lane, kp, src, ldS, dst, o2);
;     b.dst[BANK] = dst; b.o2[BANK] = o2;
;     asm volatile("s_nop 6" ::: "memory");
; #pragma unroll
;     for (int i = 0; i < 8; ++i) { const float* p = src + (size_t)i * ldS;
;         asm volatile("global_load_dword %0, %4, off\n\tglobal_load_dword %1, %4, off offset:256\n\tglobal_load_dword %2, %4, off offset:512\n\tglobal_load_dword %3, %4, off offset:768"
;                      : "=&v"(b.r[(BANK * 8 + i) * 4 + 0]), "=&v"(b.r[(BANK * 8 + i) * 4 + 1]), "=&v"(b.r[(BANK * 8 + i) * 4 + 2]), "=&v"(b.r[(BANK * 8 + i) * 4 + 3]) : "v"(p) : "memory"); }
;     b.st += 1;
; }
; __device__ __forceinline__ void hy_fft_phase(LAS unsigned char* lds, int bid, int G, const bf16_t* vgT, bf16_t* zT, const float* a3, const float* wout, const float* skip, float* filt, float4* gspec) {
;     ...
;             {   u32x2 gq[16], gh;
; #pragma unroll
;                 for (int i = 0; i < 16; ++i) { const unsigned off = 8u * tid + 4096u * i; SEG_LD64(gq[i], off, GS); }
;                 { const unsigned off = 8u * (FN / 2); SEG_LD64(gh, off, GS); }
;                 BG_I(0);
;                 SEG_WAIT(); asm volatile("" : SEG_TIE8(gq, 0), SEG_TIE8(gq, 8), "+v"(gh) :: "memory");
; #pragma unroll
;                 for (int i = 0; i < 16; ++i) { const int k = tid + NTHR * i;
;                     const int p1 = PADI(fpos(k)), p2 = PADI(fpos((FN - k) & (FN - 1)));
;                     const cf2 zk = z[p1], zm = z[p2];
;                     const cf2 V1 = mk2(0.5f * (zk.x + zm.x), 0.5f * (zk.y - zm.y)), V2 = mk2(0.5f * (zk.y + zm.y), -0.5f * (zk.x - zm.x));
;                     const cf2 Y1 = cmul(V1, mk2(bf_lo(gq[i].x), bf_hi(gq[i].x))), Y2 = cmul(V2, mk2(bf_lo(gq[i].y), bf_hi(gq[i].y)));
;                     z[p1] = mk2(Y1.x - Y2.y, Y1.y + Y2.x); z[p2] = mk2(Y1.x + Y2.y, Y2.x - Y1.y); }
.LBB0_698:
	s_nop 6
	s_lshl_b32 s12, s48, 2
	global_load_dword v106, v[40:41], off nt
	global_load_dword v98, v[40:41], off offset:256 nt
	global_load_dword v82, v[40:41], off offset:512 nt
	global_load_dword v68, v[40:41], off offset:768 nt
	v_lshl_add_u64 v[70:71], v[40:41], 0, s[12:13]
	global_load_dword v108, v[70:71], off nt
	global_load_dword v100, v[70:71], off offset:256 nt
	global_load_dword v84, v[70:71], off offset:512 nt
	global_load_dword v41, v[70:71], off offset:768 nt
	v_lshl_add_u64 v[70:71], v[70:71], 0, s[12:13]
	v_lshlrev_b32_e32 v65, 2, v114
	global_load_dword v107, v[70:71], off nt
	global_load_dword v99, v[70:71], off offset:256 nt
	global_load_dword v83, v[70:71], off offset:512 nt
	global_load_dword v40, v[70:71], off offset:768 nt
	v_lshl_add_u64 v[72:73], v[70:71], 0, s[12:13]
	v_lshlrev_b32_e32 v60, 10, v114
	v_and_b32_e32 v65, 0x3c0, v65
	global_load_dword v110, v[72:73], off nt
	global_load_dword v102, v[72:73], off offset:256 nt
	global_load_dword v86, v[72:73], off offset:512 nt
	global_load_dword v70, v[72:73], off offset:768 nt
	v_lshl_add_u64 v[72:73], v[72:73], 0, s[12:13]
	v_and_or_b32 v60, v60, s79, v65
	v_lshrrev_b32_e32 v65, 6, v114
	global_load_dword v109, v[72:73], off nt
	global_load_dword v101, v[72:73], off offset:256 nt
	global_load_dword v85, v[72:73], off offset:512 nt
	global_load_dword v69, v[72:73], off offset:768 nt
	v_lshl_add_u64 v[116:117], v[72:73], 0, s[12:13]
	v_ashrrev_i32_e32 v67, 12, v114
	v_and_or_b32 v65, v65, 60, v60
	global_load_dword v112, v[116:117], off nt
	global_load_dword v104, v[116:117], off offset:256 nt
	global_load_dword v88, v[116:117], off offset:512 nt
	global_load_dword v72, v[116:117], off offset:768 nt
	v_lshl_add_u64 v[116:117], v[116:117], 0, s[12:13]
	v_add_u32_e32 v67, v65, v67
	global_load_dword v111, v[116:117], off nt
	global_load_dword v103, v[116:117], off offset:256 nt
	global_load_dword v87, v[116:117], off offset:512 nt
	global_load_dword v71, v[116:117], off offset:768 nt
	v_lshl_add_u64 v[116:117], v[116:117], 0, s[12:13]
	v_ashrrev_i32_e32 v115, 5, v67
	global_load_dword v113, v[116:117], off nt
	global_load_dword v105, v[116:117], off offset:256 nt
	global_load_dword v90, v[116:117], off offset:512 nt
	global_load_dword v73, v[116:117], off offset:768 nt
	v_sub_u32_e32 v116, 0, v114
	v_lshlrev_b32_e32 v115, 3, v115
	v_lshlrev_b32_e32 v121, 2, v116
	v_lshlrev_b32_e32 v67, 3, v67
	v_and_b32_e32 v115, -16, v115
	v_and_b32_e32 v117, 0x3000, v116
	v_lshlrev_b32_e32 v120, 10, v116
	v_and_b32_e32 v121, 0x3c0, v121
	v_add3_u32 v67, 0, v67, v115
	v_lshrrev_b32_e32 v115, 3, v116
	s_waitcnt vmcnt(32)
	s_nop 7
	v_and_or_b32 v120, v120, s79, v121
	v_and_b32_e32 v115, 0x1e0, v115
	v_lshrrev_b32_e32 v116, 9, v117
	v_add3_u32 v115, 0, v115, v116
	v_lshlrev_b32_e32 v116, 3, v120
	v_lshrrev_b32_e32 v117, 2, v120
	v_add3_u32 v115, v115, v116, v117
	ds_read_b64 v[116:117], v67
	ds_read_b64 v[120:121], v115
	v_cmp_eq_u32_e32 vcc, 0, v114
	s_waitcnt lgkmcnt(0)
	v_add_f32 v122, v116, v120
	v_add_f32 v123, v117, v121
	v_add_f32_e64 v116, v116, -v120
	v_add_f32_e64 v117, v117, -v121
	v_lshlrev_b32_e32 v121, 16, v39
	v_mul_f32_e64 v116, v116, s34
	v_mul_f32_e64 v117, v117, s35
	v_lshlrev_b32_e32 v120, 16, v38
	v_and_b32_e32 v39, 0xffff0000, v39
	v_and_b32_e32 v38, 0xffff0000, v38
	v_mul_f32_e64 v122, v122, 0.5
	v_mul_f32_e64 v123, v123, 0.5
	v_mul_f32 v124, v117, v38
	v_mul_f32 v125, v116, v39
	v_mul_f32 v253, v117, v120
	v_mul_f32 v117, v116, v121
	v_mov_b32_e32 v116, v253
	v_fma_f32 v124, v122, v120, -v124
	v_fma_f32 v125, v123, v121, -v125
	v_fma_f32 v38, v122, v38, v116
	v_fma_f32 v39, v123, v39, v117
	s_nop 0
	v_add_f32_e64 v116, v124, -v39
	v_add_f32_e64 v117, v125, -v38
	v_add_f32 v253, v124, v39
	v_add_f32 v39, v125, v38
	v_mov_b32_e32 v38, v253
	v_mov_b32_e32 v120, v116
	v_mov_b32_e32 v121, v39
	v_mov_b32_e32 v39, v117
	ds_write_b64 v67, v[120:121]
	ds_write_b64 v115, v[38:39]
	v_add_u32_e32 v38, 0x200, v114
	v_lshrrev_b32_e32 v39, 6, v38
	v_and_b32_e32 v39, 60, v39
	v_ashrrev_i32_e32 v38, 12, v38
	v_add3_u32 v38, v60, v38, v39
	v_ashrrev_i32_e32 v39, 5, v38
	v_sub_u32_e32 v67, 0xfffffe00, v114
	v_lshlrev_b32_e32 v39, 3, v39
	v_lshlrev_b32_e32 v117, 2, v67
	v_lshlrev_b32_e32 v38, 3, v38
	v_and_b32_e32 v39, -16, v39
	v_and_b32_e32 v115, 0x3000, v67
	v_lshlrev_b32_e32 v116, 10, v67
	v_and_b32_e32 v117, 0x3c0, v117
	v_add3_u32 v124, 0, v38, v39
	v_lshrrev_b32_e32 v38, 3, v67
	v_and_or_b32 v116, v116, s79, v117
	v_and_b32_e32 v38, 0x1e0, v38
	v_lshrrev_b32_e32 v39, 9, v115
	v_add3_u32 v38, 0, v38, v39
	v_lshlrev_b32_e32 v39, 3, v116
	v_lshrrev_b32_e32 v67, 2, v116
	v_add3_u32 v67, v38, v39, v67
	ds_read_b64 v[38:39], v124
	ds_read_b64 v[116:117], v67
	s_waitcnt lgkmcnt(0)
	v_add_f32 v120, v38, v116
	v_add_f32 v121, v39, v117
	v_add_f32_e64 v38, v38, -v116
	v_add_f32_e64 v39, v39, -v117
	v_lshlrev_b32_e32 v117, 16, v37
	v_mul_f32_e64 v38, v38, s34
	v_mul_f32_e64 v39, v39, s35
	v_lshlrev_b32_e32 v116, 16, v36
	v_and_b32_e32 v37, 0xffff0000, v37
	v_and_b32_e32 v36, 0xffff0000, v36
	v_mul_f32_e64 v120, v120, 0.5
	v_mul_f32_e64 v121, v121, 0.5
	v_mul_f32 v122, v39, v36
	v_mul_f32 v123, v38, v37
	v_mul_f32 v253, v39, v116
	v_mul_f32 v39, v38, v117
	v_mov_b32_e32 v38, v253
	v_fma_f32 v122, v120, v116, -v122
	v_fma_f32 v123, v121, v117, -v123
	v_fma_f32 v36, v120, v36, v38
	v_fma_f32 v37, v121, v37, v39
	s_nop 0
	v_add_f32_e64 v38, v122, -v37
	v_add_f32_e64 v39, v123, -v36
	v_add_f32 v253, v122, v37
	v_add_f32 v37, v123, v36
	v_mov_b32_e32 v36, v253
	v_mov_b32_e32 v116, v38
	v_mov_b32_e32 v117, v37
	v_mov_b32_e32 v37, v39
	ds_write_b64 v124, v[116:117]
	ds_write_b64 v67, v[36:37]
	v_add_u32_e32 v36, 0x400, v114
	v_lshrrev_b32_e32 v37, 6, v36
	v_and_b32_e32 v37, 60, v37
	v_ashrrev_i32_e32 v36, 12, v36
	v_add3_u32 v36, v60, v36, v37
	v_ashrrev_i32_e32 v37, 5, v36
	v_sub_u32_e32 v38, 0xfffffc00, v114
	v_lshlrev_b32_e32 v115, 2, v38
	v_lshlrev_b32_e32 v37, 3, v37
	v_lshlrev_b32_e32 v67, 10, v38
	v_and_b32_e32 v115, 0x3c0, v115
	v_lshlrev_b32_e32 v36, 3, v36
	v_and_b32_e32 v37, -16, v37
	v_and_b32_e32 v39, 0x3000, v38
	v_and_or_b32 v67, v67, s79, v115
	v_add3_u32 v115, 0, v36, v37
	v_lshrrev_b32_e32 v36, 3, v38
	v_and_b32_e32 v36, 0x1e0, v36
	v_lshrrev_b32_e32 v37, 9, v39
	v_add3_u32 v36, 0, v36, v37
	v_lshlrev_b32_e32 v37, 3, v67
	v_lshrrev_b32_e32 v38, 2, v67
	v_add3_u32 v67, v36, v37, v38
	ds_read_b64 v[36:37], v115
	ds_read_b64 v[38:39], v67
	s_waitcnt lgkmcnt(0)
; __device__ __forceinline__ float bf_lo(unsigned w) { return __uint_as_float(w << 16); }
; __device__ __forceinline__ float bf_hi(unsigned w) { return __uint_as_float(w & 0xffff0000u); }
; FFT_HD cf2 mk2(float x, float y) { return (cf2){x, y}; }
; FFT_HD cf2 cmul(cf2 a, cf2 b) { return mk2(a.x * b.x - a.y * b.y, a.x * b.y + a.y * b.x); }
; FFT_HD int fpos(int k) { return ((k & 15) << 10) + (((k >> 4) & 15) << 6) + (((k >> 8) & 15) << 2) + (k >> 12); }
; __device__ __forceinline__ void hy_fft_phase(LAS unsigned char* lds, int bid, int G, const bf16_t* vgT, bf16_t* zT, const float* a3, const float* wout, const float* skip, float* filt, float4* gspec) {
;     ...
;                 for (int i = 0; i < 16; ++i) { const int k = tid + NTHR * i;
;                     const int p1 = PADI(fpos(k)), p2 = PADI(fpos((FN - k) & (FN - 1)));
;                     const cf2 zk = z[p1], zm = z[p2];
;                     const cf2 V1 = mk2(0.5f * (zk.x + zm.x), 0.5f * (zk.y - zm.y)), V2 = mk2(0.5f * (zk.y + zm.y), -0.5f * (zk.x - zm.x));
;                     const cf2 Y1 = cmul(V1, mk2(bf_lo(gq[i].x), bf_hi(gq[i].x))), Y2 = cmul(V2, mk2(bf_lo(gq[i].y), bf_hi(gq[i].y)));
;                     z[p1] = mk2(Y1.x - Y2.y, Y1.y + Y2.x); z[p2] = mk2(Y1.x + Y2.y, Y2.x - Y1.y); }
	v_add_f32 v116, v36, v38
	v_add_f32 v117, v37, v39
	v_add_f32_e64 v36, v36, -v38
	v_add_f32_e64 v37, v37, -v39
	v_lshlrev_b32_e32 v39, 16, v35
	v_mul_f32_e64 v36, v36, s34
	v_mul_f32_e64 v37, v37, s35
	v_lshlrev_b32_e32 v38, 16, v34
	v_and_b32_e32 v35, 0xffff0000, v35
	v_and_b32_e32 v34, 0xffff0000, v34
	v_mul_f32_e64 v116, v116, 0.5
	v_mul_f32_e64 v117, v117, 0.5
	v_mul_f32 v120, v37, v34
	v_mul_f32 v121, v36, v35
	v_mul_f32 v253, v37, v38
	v_mul_f32 v37, v36, v39
	v_mov_b32_e32 v36, v253
	v_fma_f32 v120, v116, v38, -v120
	v_fma_f32 v121, v117, v39, -v121
	v_fma_f32 v34, v116, v34, v36
	v_fma_f32 v35, v117, v35, v37
	s_nop 0
	v_add_f32_e64 v36, v120, -v35
	v_add_f32_e64 v37, v121, -v34
	v_add_f32 v253, v120, v35
	v_add_f32 v35, v121, v34
	v_mov_b32_e32 v34, v253
	v_mov_b32_e32 v38, v36
	v_mov_b32_e32 v39, v35
	v_mov_b32_e32 v35, v37
	ds_write_b64 v115, v[38:39]
	ds_write_b64 v67, v[34:35]
	v_add_u32_e32 v34, 0x600, v114
	v_lshrrev_b32_e32 v35, 6, v34
	v_and_b32_e32 v35, 60, v35
	v_ashrrev_i32_e32 v34, 12, v34
	v_add3_u32 v34, v60, v34, v35
	v_ashrrev_i32_e32 v35, 5, v34
	v_sub_u32_e32 v36, 0xfffffa00, v114
	v_lshlrev_b32_e32 v35, 3, v35
	v_lshlrev_b32_e32 v39, 2, v36
	v_lshlrev_b32_e32 v34, 3, v34
	v_and_b32_e32 v35, -16, v35
	v_and_b32_e32 v37, 0x3000, v36
	v_lshlrev_b32_e32 v38, 10, v36
	v_and_b32_e32 v39, 0x3c0, v39
	v_add3_u32 v67, 0, v34, v35
	v_lshrrev_b32_e32 v34, 3, v36
	v_and_or_b32 v38, v38, s79, v39
	v_and_b32_e32 v34, 0x1e0, v34
	v_lshrrev_b32_e32 v35, 9, v37
	v_add3_u32 v34, 0, v34, v35
	v_lshlrev_b32_e32 v35, 3, v38
	v_lshrrev_b32_e32 v36, 2, v38
	v_add3_u32 v115, v34, v35, v36
	ds_read_b64 v[34:35], v67
	ds_read_b64 v[36:37], v115
	s_waitcnt lgkmcnt(0)
	v_add_f32 v38, v34, v36
	v_add_f32 v39, v35, v37
	v_add_f32_e64 v34, v34, -v36
	v_add_f32_e64 v35, v35, -v37
	v_lshlrev_b32_e32 v37, 16, v33
	v_mul_f32_e64 v34, v34, s34
	v_mul_f32_e64 v35, v35, s35
	v_lshlrev_b32_e32 v36, 16, v32
	v_and_b32_e32 v33, 0xffff0000, v33
	v_and_b32_e32 v32, 0xffff0000, v32
	v_mul_f32_e64 v38, v38, 0.5
	v_mul_f32_e64 v39, v39, 0.5
	v_mul_f32 v116, v35, v32
	v_mul_f32 v117, v34, v33
	v_mul_f32 v253, v35, v36
	v_mul_f32 v35, v34, v37
	v_mov_b32_e32 v34, v253
	v_fma_f32 v116, v38, v36, -v116
	v_fma_f32 v117, v39, v37, -v117
	v_fma_f32 v32, v38, v32, v34
	v_fma_f32 v33, v39, v33, v35
	s_nop 0
	v_add_f32_e64 v34, v116, -v33
	v_add_f32_e64 v35, v117, -v32
	v_add_f32 v253, v116, v33
	v_add_f32 v33, v117, v32
	v_mov_b32_e32 v32, v253
	v_mov_b32_e32 v36, v34
	v_mov_b32_e32 v37, v33
	v_mov_b32_e32 v33, v35
	ds_write_b64 v67, v[36:37]
	ds_write_b64 v115, v[32:33]
	v_add_u32_e32 v32, 0x800, v114
	v_lshrrev_b32_e32 v33, 6, v32
	v_and_b32_e32 v33, 60, v33
	v_ashrrev_i32_e32 v32, 12, v32
	v_add3_u32 v32, v60, v32, v33
	v_ashrrev_i32_e32 v33, 5, v32
	v_sub_u32_e32 v34, 0xfffff800, v114
	v_lshlrev_b32_e32 v33, 3, v33
	v_lshlrev_b32_e32 v37, 2, v34
	v_lshlrev_b32_e32 v32, 3, v32
	v_and_b32_e32 v33, -16, v33
	v_and_b32_e32 v35, 0x3000, v34
	v_lshlrev_b32_e32 v36, 10, v34
	v_and_b32_e32 v37, 0x3c0, v37
	v_add3_u32 v67, 0, v32, v33
	v_lshrrev_b32_e32 v32, 3, v34
	v_and_or_b32 v36, v36, s79, v37
	v_and_b32_e32 v32, 0x1e0, v32
	v_lshrrev_b32_e32 v33, 9, v35
	v_add3_u32 v32, 0, v32, v33
	v_lshlrev_b32_e32 v33, 3, v36
	v_lshrrev_b32_e32 v34, 2, v36
	v_add3_u32 v115, v32, v33, v34
	ds_read_b64 v[32:33], v67
	ds_read_b64 v[34:35], v115
	s_waitcnt lgkmcnt(0)
	v_add_f32 v36, v32, v34
	v_add_f32 v37, v33, v35
	v_add_f32_e64 v32, v32, -v34
	v_add_f32_e64 v33, v33, -v35
	v_lshlrev_b32_e32 v35, 16, v31
	v_mul_f32_e64 v32, v32, s34
	v_mul_f32_e64 v33, v33, s35
	v_lshlrev_b32_e32 v34, 16, v30
	v_and_b32_e32 v31, 0xffff0000, v31
	v_and_b32_e32 v30, 0xffff0000, v30
	v_mul_f32_e64 v36, v36, 0.5
	v_mul_f32_e64 v37, v37, 0.5
	v_mul_f32 v38, v33, v30
	v_mul_f32 v39, v32, v31
	v_mul_f32 v253, v33, v34
	v_mul_f32 v33, v32, v35
	v_mov_b32_e32 v32, v253
	v_fma_f32 v38, v36, v34, -v38
	v_fma_f32 v39, v37, v35, -v39
	v_fma_f32 v30, v36, v30, v32
	v_fma_f32 v31, v37, v31, v33
	s_nop 0
	v_add_f32_e64 v32, v38, -v31
	v_add_f32_e64 v33, v39, -v30
	v_add_f32 v253, v38, v31
	v_add_f32 v31, v39, v30
	v_mov_b32_e32 v30, v253
	v_mov_b32_e32 v34, v32
	v_mov_b32_e32 v35, v31
	v_mov_b32_e32 v31, v33
	ds_write_b64 v67, v[34:35]
	ds_write_b64 v115, v[30:31]
	v_add_u32_e32 v30, 0xa00, v114
	v_lshrrev_b32_e32 v31, 6, v30
	v_and_b32_e32 v31, 60, v31
	v_ashrrev_i32_e32 v30, 12, v30
	v_add3_u32 v30, v60, v30, v31
	v_ashrrev_i32_e32 v31, 5, v30
	v_sub_u32_e32 v32, 0xfffff600, v114
	v_lshlrev_b32_e32 v31, 3, v31
	v_lshlrev_b32_e32 v35, 2, v32
	v_lshlrev_b32_e32 v30, 3, v30
	v_and_b32_e32 v31, -16, v31
	v_and_b32_e32 v33, 0x3000, v32
	v_lshlrev_b32_e32 v34, 10, v32
	v_and_b32_e32 v35, 0x3c0, v35
	v_add3_u32 v38, 0, v30, v31
	v_lshrrev_b32_e32 v30, 3, v32
	v_and_or_b32 v34, v34, s79, v35
	v_and_b32_e32 v30, 0x1e0, v30
	v_lshrrev_b32_e32 v31, 9, v33
	v_add3_u32 v30, 0, v30, v31
	v_lshlrev_b32_e32 v31, 3, v34
	v_lshrrev_b32_e32 v32, 2, v34
	v_add3_u32 v39, v30, v31, v32
	ds_read_b64 v[30:31], v38
	ds_read_b64 v[32:33], v39
	s_waitcnt lgkmcnt(0)
; __device__ __forceinline__ float bf_lo(unsigned w) { return __uint_as_float(w << 16); }
; __device__ __forceinline__ float bf_hi(unsigned w) { return __uint_as_float(w & 0xffff0000u); }
; FFT_HD cf2 mk2(float x, float y) { return (cf2){x, y}; }
; FFT_HD cf2 cmul(cf2 a, cf2 b) { return mk2(a.x * b.x - a.y * b.y, a.x * b.y + a.y * b.x); }
; FFT_HD int fpos(int k) { return ((k & 15) << 10) + (((k >> 4) & 15) << 6) + (((k >> 8) & 15) << 2) + (k >> 12); }
; __device__ __forceinline__ void hy_fft_phase(LAS unsigned char* lds, int bid, int G, const bf16_t* vgT, bf16_t* zT, const float* a3, const float* wout, const float* skip, float* filt, float4* gspec) {
;     ...
;                 for (int i = 0; i < 16; ++i) { const int k = tid + NTHR * i;
;                     const int p1 = PADI(fpos(k)), p2 = PADI(fpos((FN - k) & (FN - 1)));
;                     const cf2 zk = z[p1], zm = z[p2];
;                     const cf2 V1 = mk2(0.5f * (zk.x + zm.x), 0.5f * (zk.y - zm.y)), V2 = mk2(0.5f * (zk.y + zm.y), -0.5f * (zk.x - zm.x));
;                     const cf2 Y1 = cmul(V1, mk2(bf_lo(gq[i].x), bf_hi(gq[i].x))), Y2 = cmul(V2, mk2(bf_lo(gq[i].y), bf_hi(gq[i].y)));
;                     z[p1] = mk2(Y1.x - Y2.y, Y1.y + Y2.x); z[p2] = mk2(Y1.x + Y2.y, Y2.x - Y1.y); }
	v_add_f32 v34, v30, v32
	v_add_f32 v35, v31, v33
	v_add_f32_e64 v30, v30, -v32
	v_add_f32_e64 v31, v31, -v33
	v_lshlrev_b32_e32 v33, 16, v29
	v_mul_f32_e64 v30, v30, s34
	v_mul_f32_e64 v31, v31, s35
	v_lshlrev_b32_e32 v32, 16, v28
	v_and_b32_e32 v29, 0xffff0000, v29
	v_and_b32_e32 v28, 0xffff0000, v28
	v_mul_f32_e64 v34, v34, 0.5
	v_mul_f32_e64 v35, v35, 0.5
	v_mul_f32 v36, v31, v28
	v_mul_f32 v37, v30, v29
	v_mul_f32 v253, v31, v32
	v_mul_f32 v31, v30, v33
	v_mov_b32_e32 v30, v253
	v_fma_f32 v36, v34, v32, -v36
	v_fma_f32 v37, v35, v33, -v37
	v_fma_f32 v28, v34, v28, v30
	v_fma_f32 v29, v35, v29, v31
	s_nop 0
	v_add_f32_e64 v30, v36, -v29
	v_add_f32_e64 v31, v37, -v28
	v_add_f32 v253, v36, v29
	v_add_f32 v29, v37, v28
	v_mov_b32_e32 v28, v253
	v_mov_b32_e32 v32, v30
	v_mov_b32_e32 v33, v29
	v_mov_b32_e32 v29, v31
	ds_write_b64 v38, v[32:33]
	ds_write_b64 v39, v[28:29]
	v_add_u32_e32 v28, 0xc00, v114
	v_lshrrev_b32_e32 v29, 6, v28
	v_and_b32_e32 v29, 60, v29
	v_ashrrev_i32_e32 v28, 12, v28
	v_add3_u32 v28, v60, v28, v29
	v_ashrrev_i32_e32 v29, 5, v28
	v_sub_u32_e32 v30, 0xfffff400, v114
	v_lshlrev_b32_e32 v29, 3, v29
	v_lshlrev_b32_e32 v33, 2, v30
	v_lshlrev_b32_e32 v28, 3, v28
	v_and_b32_e32 v29, -16, v29
	v_and_b32_e32 v31, 0x3000, v30
	v_lshlrev_b32_e32 v32, 10, v30
	v_and_b32_e32 v33, 0x3c0, v33
	v_add3_u32 v36, 0, v28, v29
	v_lshrrev_b32_e32 v28, 3, v30
	v_and_or_b32 v32, v32, s79, v33
	v_and_b32_e32 v28, 0x1e0, v28
	v_lshrrev_b32_e32 v29, 9, v31
	v_add3_u32 v28, 0, v28, v29
	v_lshlrev_b32_e32 v29, 3, v32
	v_lshrrev_b32_e32 v30, 2, v32
	v_add3_u32 v37, v28, v29, v30
	ds_read_b64 v[28:29], v36
	ds_read_b64 v[30:31], v37
	s_waitcnt lgkmcnt(0)
	v_add_f32 v32, v28, v30
	v_add_f32 v33, v29, v31
	v_add_f32_e64 v28, v28, -v30
	v_add_f32_e64 v29, v29, -v31
	v_lshlrev_b32_e32 v31, 16, v27
	v_mul_f32_e64 v28, v28, s34
	v_mul_f32_e64 v29, v29, s35
	v_lshlrev_b32_e32 v30, 16, v26
	v_and_b32_e32 v27, 0xffff0000, v27
	v_and_b32_e32 v26, 0xffff0000, v26
	v_mul_f32_e64 v32, v32, 0.5
	v_mul_f32_e64 v33, v33, 0.5
	v_mul_f32 v34, v29, v26
	v_mul_f32 v35, v28, v27
	v_mul_f32 v253, v29, v30
	v_mul_f32 v29, v28, v31
	v_mov_b32_e32 v28, v253
	v_fma_f32 v34, v32, v30, -v34
	v_fma_f32 v35, v33, v31, -v35
	v_fma_f32 v26, v32, v26, v28
	v_fma_f32 v27, v33, v27, v29
	s_nop 0
	v_add_f32_e64 v28, v34, -v27
	v_add_f32_e64 v29, v35, -v26
	v_add_f32 v253, v34, v27
	v_add_f32 v27, v35, v26
	v_mov_b32_e32 v26, v253
	v_mov_b32_e32 v30, v28
	v_mov_b32_e32 v31, v27
	v_mov_b32_e32 v27, v29
	ds_write_b64 v36, v[30:31]
	ds_write_b64 v37, v[26:27]
	v_add_u32_e32 v26, 0xe00, v114
	v_lshrrev_b32_e32 v27, 6, v26
	v_and_b32_e32 v27, 60, v27
	v_ashrrev_i32_e32 v26, 12, v26
	v_add3_u32 v26, v60, v26, v27
	v_ashrrev_i32_e32 v27, 5, v26
	v_sub_u32_e32 v28, 0xfffff200, v114
	v_lshlrev_b32_e32 v27, 3, v27
	v_lshlrev_b32_e32 v31, 2, v28
	v_lshlrev_b32_e32 v26, 3, v26
	v_and_b32_e32 v27, -16, v27
	v_and_b32_e32 v29, 0x3000, v28
	v_lshlrev_b32_e32 v30, 10, v28
	v_and_b32_e32 v31, 0x3c0, v31
	v_add3_u32 v34, 0, v26, v27
	v_lshrrev_b32_e32 v26, 3, v28
	v_and_or_b32 v30, v30, s79, v31
	v_and_b32_e32 v26, 0x1e0, v26
	v_lshrrev_b32_e32 v27, 9, v29
	v_add3_u32 v26, 0, v26, v27
	v_lshlrev_b32_e32 v27, 3, v30
	v_lshrrev_b32_e32 v28, 2, v30
	v_add3_u32 v35, v26, v27, v28
	ds_read_b64 v[26:27], v34
	ds_read_b64 v[28:29], v35
	s_waitcnt lgkmcnt(0)
	v_add_f32 v30, v26, v28
	v_add_f32 v31, v27, v29
	v_add_f32_e64 v26, v26, -v28
	v_add_f32_e64 v27, v27, -v29
	v_lshlrev_b32_e32 v29, 16, v25
	v_mul_f32_e64 v26, v26, s34
	v_mul_f32_e64 v27, v27, s35
	v_lshlrev_b32_e32 v28, 16, v24
	v_and_b32_e32 v25, 0xffff0000, v25
	v_and_b32_e32 v24, 0xffff0000, v24
	v_mul_f32_e64 v30, v30, 0.5
	v_mul_f32_e64 v31, v31, 0.5
	v_mul_f32 v32, v27, v24
	v_mul_f32 v33, v26, v25
	v_mul_f32 v253, v27, v28
	v_mul_f32 v27, v26, v29
	v_mov_b32_e32 v26, v253
	v_fma_f32 v32, v30, v28, -v32
	v_fma_f32 v33, v31, v29, -v33
	v_fma_f32 v24, v30, v24, v26
	v_fma_f32 v25, v31, v25, v27
	s_nop 0
	v_add_f32_e64 v26, v32, -v25
	v_add_f32_e64 v27, v33, -v24
	v_add_f32 v253, v32, v25
	v_add_f32 v25, v33, v24
	v_mov_b32_e32 v24, v253
	v_mov_b32_e32 v28, v26
	v_mov_b32_e32 v29, v25
	v_mov_b32_e32 v25, v27
	ds_write_b64 v34, v[28:29]
	ds_write_b64 v35, v[24:25]
	v_add_u32_e32 v24, 0x1000, v114
	v_ashrrev_i32_e32 v24, 12, v24
	v_add_u32_e32 v24, v65, v24
	v_ashrrev_i32_e32 v25, 5, v24
	v_sub_u32_e32 v26, 0xfffff000, v114
	v_lshlrev_b32_e32 v25, 3, v25
	v_lshlrev_b32_e32 v29, 2, v26
	v_lshlrev_b32_e32 v24, 3, v24
	v_and_b32_e32 v25, -16, v25
	v_and_b32_e32 v27, 0x3000, v26
	v_lshlrev_b32_e32 v28, 10, v26
	v_and_b32_e32 v29, 0x3c0, v29
	v_add3_u32 v32, 0, v24, v25
	v_lshrrev_b32_e32 v24, 3, v26
	v_and_or_b32 v28, v28, s79, v29
	v_and_b32_e32 v24, 0x1e0, v24
	v_lshrrev_b32_e32 v25, 9, v27
	v_add3_u32 v24, 0, v24, v25
	v_lshlrev_b32_e32 v25, 3, v28
	v_lshrrev_b32_e32 v26, 2, v28
	v_add3_u32 v33, v24, v25, v26
	ds_read_b64 v[24:25], v32
	ds_read_b64 v[26:27], v33
	s_waitcnt lgkmcnt(0)
; __device__ __forceinline__ float bf_lo(unsigned w) { return __uint_as_float(w << 16); }
; __device__ __forceinline__ float bf_hi(unsigned w) { return __uint_as_float(w & 0xffff0000u); }
; FFT_HD cf2 mk2(float x, float y) { return (cf2){x, y}; }
; FFT_HD cf2 cmul(cf2 a, cf2 b) { return mk2(a.x * b.x - a.y * b.y, a.x * b.y + a.y * b.x); }
; FFT_HD int fpos(int k) { return ((k & 15) << 10) + (((k >> 4) & 15) << 6) + (((k >> 8) & 15) << 2) + (k >> 12); }
; __device__ __forceinline__ void hy_fft_phase(LAS unsigned char* lds, int bid, int G, const bf16_t* vgT, bf16_t* zT, const float* a3, const float* wout, const float* skip, float* filt, float4* gspec) {
;     ...
;                 for (int i = 0; i < 16; ++i) { const int k = tid + NTHR * i;
;                     const int p1 = PADI(fpos(k)), p2 = PADI(fpos((FN - k) & (FN - 1)));
;                     const cf2 zk = z[p1], zm = z[p2];
;                     const cf2 V1 = mk2(0.5f * (zk.x + zm.x), 0.5f * (zk.y - zm.y)), V2 = mk2(0.5f * (zk.y + zm.y), -0.5f * (zk.x - zm.x));
;                     const cf2 Y1 = cmul(V1, mk2(bf_lo(gq[i].x), bf_hi(gq[i].x))), Y2 = cmul(V2, mk2(bf_lo(gq[i].y), bf_hi(gq[i].y)));
;                     z[p1] = mk2(Y1.x - Y2.y, Y1.y + Y2.x); z[p2] = mk2(Y1.x + Y2.y, Y2.x - Y1.y); }
	v_add_f32 v28, v24, v26
	v_add_f32 v29, v25, v27
	v_add_f32_e64 v24, v24, -v26
	v_add_f32_e64 v25, v25, -v27
	v_lshlrev_b32_e32 v27, 16, v23
	v_mul_f32_e64 v24, v24, s34
	v_mul_f32_e64 v25, v25, s35
	v_lshlrev_b32_e32 v26, 16, v22
	v_and_b32_e32 v23, 0xffff0000, v23
	v_and_b32_e32 v22, 0xffff0000, v22
	v_mul_f32_e64 v28, v28, 0.5
	v_mul_f32_e64 v29, v29, 0.5
	v_mul_f32 v30, v25, v22
	v_mul_f32 v31, v24, v23
	v_mul_f32 v253, v25, v26
	v_mul_f32 v25, v24, v27
	v_mov_b32_e32 v24, v253
	v_fma_f32 v30, v28, v26, -v30
	v_fma_f32 v31, v29, v27, -v31
	v_fma_f32 v22, v28, v22, v24
	v_fma_f32 v23, v29, v23, v25
	s_nop 0
	v_add_f32_e64 v24, v30, -v23
	v_add_f32_e64 v25, v31, -v22
	v_add_f32 v253, v30, v23
	v_add_f32 v23, v31, v22
	v_mov_b32_e32 v22, v253
	v_mov_b32_e32 v26, v24
	v_mov_b32_e32 v27, v23
	v_mov_b32_e32 v23, v25
	ds_write_b64 v32, v[26:27]
	ds_write_b64 v33, v[22:23]
	v_add_u32_e32 v22, 0x1200, v114
	v_lshrrev_b32_e32 v23, 6, v22
	v_and_b32_e32 v23, 60, v23
	v_ashrrev_i32_e32 v22, 12, v22
	v_add3_u32 v22, v60, v22, v23
	v_ashrrev_i32_e32 v23, 5, v22
	v_sub_u32_e32 v24, 0xffffee00, v114
	v_lshlrev_b32_e32 v23, 3, v23
	v_lshlrev_b32_e32 v27, 2, v24
	v_lshlrev_b32_e32 v22, 3, v22
	v_and_b32_e32 v23, -16, v23
	v_and_b32_e32 v25, 0x3000, v24
	v_lshlrev_b32_e32 v26, 10, v24
	v_and_b32_e32 v27, 0x3c0, v27
	v_add3_u32 v30, 0, v22, v23
	v_lshrrev_b32_e32 v22, 3, v24
	v_and_or_b32 v26, v26, s79, v27
	v_and_b32_e32 v22, 0x1e0, v22
	v_lshrrev_b32_e32 v23, 9, v25
	v_add3_u32 v22, 0, v22, v23
	v_lshlrev_b32_e32 v23, 3, v26
	v_lshrrev_b32_e32 v24, 2, v26
	v_add3_u32 v31, v22, v23, v24
	ds_read_b64 v[22:23], v30
	ds_read_b64 v[24:25], v31
	s_waitcnt lgkmcnt(0)
	v_add_f32 v26, v22, v24
	v_add_f32 v27, v23, v25
	v_add_f32_e64 v22, v22, -v24
	v_add_f32_e64 v23, v23, -v25
	v_lshlrev_b32_e32 v25, 16, v21
	v_mul_f32_e64 v22, v22, s34
	v_mul_f32_e64 v23, v23, s35
	v_lshlrev_b32_e32 v24, 16, v20
	v_and_b32_e32 v21, 0xffff0000, v21
	v_and_b32_e32 v20, 0xffff0000, v20
	v_mul_f32_e64 v26, v26, 0.5
	v_mul_f32_e64 v27, v27, 0.5
	v_mul_f32 v28, v23, v20
	v_mul_f32 v29, v22, v21
	v_mul_f32 v253, v23, v24
	v_mul_f32 v23, v22, v25
	v_mov_b32_e32 v22, v253
	v_fma_f32 v28, v26, v24, -v28
	v_fma_f32 v29, v27, v25, -v29
	v_fma_f32 v20, v26, v20, v22
	v_fma_f32 v21, v27, v21, v23
	s_nop 0
	v_add_f32_e64 v22, v28, -v21
	v_add_f32_e64 v23, v29, -v20
	v_add_f32 v253, v28, v21
	v_add_f32 v21, v29, v20
	v_mov_b32_e32 v20, v253
	v_mov_b32_e32 v24, v22
	v_mov_b32_e32 v25, v21
	v_mov_b32_e32 v21, v23
	ds_write_b64 v30, v[24:25]
	ds_write_b64 v31, v[20:21]
	v_add_u32_e32 v20, 0x1400, v114
	v_lshrrev_b32_e32 v21, 6, v20
	v_and_b32_e32 v21, 60, v21
	v_ashrrev_i32_e32 v20, 12, v20
	v_add3_u32 v20, v60, v20, v21
	v_ashrrev_i32_e32 v21, 5, v20
	v_sub_u32_e32 v22, 0xffffec00, v114
	v_lshlrev_b32_e32 v21, 3, v21
	v_lshlrev_b32_e32 v25, 2, v22
	v_lshlrev_b32_e32 v20, 3, v20
	v_and_b32_e32 v21, -16, v21
	v_and_b32_e32 v23, 0x3000, v22
	v_lshlrev_b32_e32 v24, 10, v22
	v_and_b32_e32 v25, 0x3c0, v25
	v_add3_u32 v28, 0, v20, v21
	v_lshrrev_b32_e32 v20, 3, v22
	v_and_or_b32 v24, v24, s79, v25
	v_and_b32_e32 v20, 0x1e0, v20
	v_lshrrev_b32_e32 v21, 9, v23
	v_add3_u32 v20, 0, v20, v21
	v_lshlrev_b32_e32 v21, 3, v24
	v_lshrrev_b32_e32 v22, 2, v24
	v_add3_u32 v29, v20, v21, v22
	ds_read_b64 v[20:21], v28
	ds_read_b64 v[22:23], v29
	s_waitcnt lgkmcnt(0)
	v_add_f32 v24, v20, v22
	v_add_f32 v25, v21, v23
	v_add_f32_e64 v20, v20, -v22
	v_add_f32_e64 v21, v21, -v23
	v_lshlrev_b32_e32 v23, 16, v19
	v_mul_f32_e64 v20, v20, s34
	v_mul_f32_e64 v21, v21, s35
	v_lshlrev_b32_e32 v22, 16, v18
	v_and_b32_e32 v19, 0xffff0000, v19
	v_and_b32_e32 v18, 0xffff0000, v18
	v_mul_f32_e64 v24, v24, 0.5
	v_mul_f32_e64 v25, v25, 0.5
	v_mul_f32 v26, v21, v18
	v_mul_f32 v27, v20, v19
	v_mul_f32 v253, v21, v22
	v_mul_f32 v21, v20, v23
	v_mov_b32_e32 v20, v253
	v_fma_f32 v26, v24, v22, -v26
	v_fma_f32 v27, v25, v23, -v27
	v_fma_f32 v18, v24, v18, v20
	v_fma_f32 v19, v25, v19, v21
	s_nop 0
	v_add_f32_e64 v20, v26, -v19
	v_add_f32_e64 v21, v27, -v18
	v_add_f32 v253, v26, v19
	v_add_f32 v19, v27, v18
	v_mov_b32_e32 v18, v253
	v_mov_b32_e32 v22, v20
	v_mov_b32_e32 v23, v19
	v_mov_b32_e32 v19, v21
	ds_write_b64 v28, v[22:23]
	ds_write_b64 v29, v[18:19]
	v_add_u32_e32 v18, 0x1600, v114
	v_lshrrev_b32_e32 v19, 6, v18
	v_and_b32_e32 v19, 60, v19
	v_ashrrev_i32_e32 v18, 12, v18
	v_add3_u32 v18, v60, v18, v19
	v_ashrrev_i32_e32 v19, 5, v18
	v_sub_u32_e32 v20, 0xffffea00, v114
	v_lshlrev_b32_e32 v19, 3, v19
	v_lshlrev_b32_e32 v23, 2, v20
	v_lshlrev_b32_e32 v18, 3, v18
	v_and_b32_e32 v19, -16, v19
	v_and_b32_e32 v21, 0x3000, v20
	v_lshlrev_b32_e32 v22, 10, v20
	v_and_b32_e32 v23, 0x3c0, v23
	v_add3_u32 v26, 0, v18, v19
	v_lshrrev_b32_e32 v18, 3, v20
	v_and_or_b32 v22, v22, s79, v23
	v_and_b32_e32 v18, 0x1e0, v18
	v_lshrrev_b32_e32 v19, 9, v21
	v_add3_u32 v18, 0, v18, v19
	v_lshlrev_b32_e32 v19, 3, v22
	v_lshrrev_b32_e32 v20, 2, v22
	v_add3_u32 v27, v18, v19, v20
	ds_read_b64 v[18:19], v26
	ds_read_b64 v[20:21], v27
	s_waitcnt lgkmcnt(0)
; __device__ __forceinline__ float bf_lo(unsigned w) { return __uint_as_float(w << 16); }
; __device__ __forceinline__ float bf_hi(unsigned w) { return __uint_as_float(w & 0xffff0000u); }
; FFT_HD cf2 mk2(float x, float y) { return (cf2){x, y}; }
; FFT_HD cf2 cmul(cf2 a, cf2 b) { return mk2(a.x * b.x - a.y * b.y, a.x * b.y + a.y * b.x); }
; FFT_HD int fpos(int k) { return ((k & 15) << 10) + (((k >> 4) & 15) << 6) + (((k >> 8) & 15) << 2) + (k >> 12); }
; __device__ __forceinline__ void hy_fft_phase(LAS unsigned char* lds, int bid, int G, const bf16_t* vgT, bf16_t* zT, const float* a3, const float* wout, const float* skip, float* filt, float4* gspec) {
;     ...
;                 for (int i = 0; i < 16; ++i) { const int k = tid + NTHR * i;
;                     const int p1 = PADI(fpos(k)), p2 = PADI(fpos((FN - k) & (FN - 1)));
;                     const cf2 zk = z[p1], zm = z[p2];
;                     const cf2 V1 = mk2(0.5f * (zk.x + zm.x), 0.5f * (zk.y - zm.y)), V2 = mk2(0.5f * (zk.y + zm.y), -0.5f * (zk.x - zm.x));
;                     const cf2 Y1 = cmul(V1, mk2(bf_lo(gq[i].x), bf_hi(gq[i].x))), Y2 = cmul(V2, mk2(bf_lo(gq[i].y), bf_hi(gq[i].y)));
;                     z[p1] = mk2(Y1.x - Y2.y, Y1.y + Y2.x); z[p2] = mk2(Y1.x + Y2.y, Y2.x - Y1.y); }
	v_add_f32 v22, v18, v20
	v_add_f32 v23, v19, v21
	v_add_f32_e64 v18, v18, -v20
	v_add_f32_e64 v19, v19, -v21
	v_lshlrev_b32_e32 v21, 16, v17
	v_mul_f32_e64 v18, v18, s34
	v_mul_f32_e64 v19, v19, s35
	v_lshlrev_b32_e32 v20, 16, v16
	v_and_b32_e32 v17, 0xffff0000, v17
	v_and_b32_e32 v16, 0xffff0000, v16
	v_mul_f32_e64 v22, v22, 0.5
	v_mul_f32_e64 v23, v23, 0.5
	v_mul_f32 v24, v19, v16
	v_mul_f32 v25, v18, v17
	v_mul_f32 v253, v19, v20
	v_mul_f32 v19, v18, v21
	v_mov_b32_e32 v18, v253
	v_fma_f32 v24, v22, v20, -v24
	v_fma_f32 v25, v23, v21, -v25
	v_fma_f32 v16, v22, v16, v18
	v_fma_f32 v17, v23, v17, v19
	s_nop 0
	v_add_f32_e64 v18, v24, -v17
	v_add_f32_e64 v19, v25, -v16
	v_add_f32 v253, v24, v17
	v_add_f32 v17, v25, v16
	v_mov_b32_e32 v16, v253
	v_mov_b32_e32 v20, v18
	v_mov_b32_e32 v21, v17
	v_mov_b32_e32 v17, v19
	ds_write_b64 v26, v[20:21]
	ds_write_b64 v27, v[16:17]
	v_add_u32_e32 v16, 0x1800, v114
	v_lshrrev_b32_e32 v17, 6, v16
	v_and_b32_e32 v17, 60, v17
	v_ashrrev_i32_e32 v16, 12, v16
	v_add3_u32 v16, v60, v16, v17
	v_ashrrev_i32_e32 v17, 5, v16
	v_sub_u32_e32 v18, 0xffffe800, v114
	v_lshlrev_b32_e32 v17, 3, v17
	v_lshlrev_b32_e32 v21, 2, v18
	v_lshlrev_b32_e32 v16, 3, v16
	v_and_b32_e32 v17, -16, v17
	v_and_b32_e32 v19, 0x3000, v18
	v_lshlrev_b32_e32 v20, 10, v18
	v_and_b32_e32 v21, 0x3c0, v21
	v_add3_u32 v24, 0, v16, v17
	v_lshrrev_b32_e32 v16, 3, v18
	v_and_or_b32 v20, v20, s79, v21
	v_and_b32_e32 v16, 0x1e0, v16
	v_lshrrev_b32_e32 v17, 9, v19
	v_add3_u32 v16, 0, v16, v17
	v_lshlrev_b32_e32 v17, 3, v20
	v_lshrrev_b32_e32 v18, 2, v20
	v_add3_u32 v25, v16, v17, v18
	ds_read_b64 v[16:17], v24
	ds_read_b64 v[18:19], v25
	s_waitcnt lgkmcnt(0)
	v_add_f32 v20, v16, v18
	v_add_f32 v21, v17, v19
	v_add_f32_e64 v16, v16, -v18
	v_add_f32_e64 v17, v17, -v19
	v_lshlrev_b32_e32 v19, 16, v15
	v_mul_f32_e64 v16, v16, s34
	v_mul_f32_e64 v17, v17, s35
	v_lshlrev_b32_e32 v18, 16, v14
	v_and_b32_e32 v15, 0xffff0000, v15
	v_and_b32_e32 v14, 0xffff0000, v14
	v_mul_f32_e64 v20, v20, 0.5
	v_mul_f32_e64 v21, v21, 0.5
	v_mul_f32 v22, v17, v14
	v_mul_f32 v23, v16, v15
	v_mul_f32 v253, v17, v18
	v_mul_f32 v17, v16, v19
	v_mov_b32_e32 v16, v253
	v_fma_f32 v22, v20, v18, -v22
	v_fma_f32 v23, v21, v19, -v23
	v_fma_f32 v14, v20, v14, v16
	v_fma_f32 v15, v21, v15, v17
	s_nop 0
	v_add_f32_e64 v16, v22, -v15
	v_add_f32_e64 v17, v23, -v14
	v_add_f32 v253, v22, v15
	v_add_f32 v15, v23, v14
	v_mov_b32_e32 v14, v253
	v_mov_b32_e32 v18, v16
	v_mov_b32_e32 v19, v15
	v_mov_b32_e32 v15, v17
	ds_write_b64 v24, v[18:19]
	ds_write_b64 v25, v[14:15]
	v_add_u32_e32 v14, 0x1a00, v114
	v_lshrrev_b32_e32 v15, 6, v14
	v_and_b32_e32 v15, 60, v15
	v_ashrrev_i32_e32 v14, 12, v14
	v_add3_u32 v14, v60, v14, v15
	v_ashrrev_i32_e32 v15, 5, v14
	v_sub_u32_e32 v16, 0xffffe600, v114
	v_lshlrev_b32_e32 v15, 3, v15
	v_lshlrev_b32_e32 v19, 2, v16
	v_lshlrev_b32_e32 v14, 3, v14
	v_and_b32_e32 v15, -16, v15
	v_and_b32_e32 v17, 0x3000, v16
	v_lshlrev_b32_e32 v18, 10, v16
	v_and_b32_e32 v19, 0x3c0, v19
	v_add3_u32 v22, 0, v14, v15
	v_lshrrev_b32_e32 v14, 3, v16
	v_and_or_b32 v18, v18, s79, v19
	v_and_b32_e32 v14, 0x1e0, v14
	v_lshrrev_b32_e32 v15, 9, v17
	v_add3_u32 v14, 0, v14, v15
	v_lshlrev_b32_e32 v15, 3, v18
	v_lshrrev_b32_e32 v16, 2, v18
	v_add3_u32 v23, v14, v15, v16
	ds_read_b64 v[14:15], v22
	ds_read_b64 v[16:17], v23
	s_waitcnt lgkmcnt(0)
; __device__ __forceinline__ float bf_lo(unsigned w) { return __uint_as_float(w << 16); }
; __device__ __forceinline__ float bf_hi(unsigned w) { return __uint_as_float(w & 0xffff0000u); }
; FFT_HD cf2 mk2(float x, float y) { return (cf2){x, y}; }
; FFT_HD cf2 cmul(cf2 a, cf2 b) { return mk2(a.x * b.x - a.y * b.y, a.x * b.y + a.y * b.x); }
; FFT_HD int fpos(int k) { return ((k & 15) << 10) + (((k >> 4) & 15) << 6) + (((k >> 8) & 15) << 2) + (k >> 12); }
; __device__ __forceinline__ void hy_fft_phase(LAS unsigned char* lds, int bid, int G, const bf16_t* vgT, bf16_t* zT, const float* a3, const float* wout, const float* skip, float* filt, float4* gspec) {
;     ...
;                 for (int i = 0; i < 16; ++i) { const int k = tid + NTHR * i;
;                     const int p1 = PADI(fpos(k)), p2 = PADI(fpos((FN - k) & (FN - 1)));
;                     const cf2 zk = z[p1], zm = z[p2];
;                     const cf2 V1 = mk2(0.5f * (zk.x + zm.x), 0.5f * (zk.y - zm.y)), V2 = mk2(0.5f * (zk.y + zm.y), -0.5f * (zk.x - zm.x));
;                     const cf2 Y1 = cmul(V1, mk2(bf_lo(gq[i].x), bf_hi(gq[i].x))), Y2 = cmul(V2, mk2(bf_lo(gq[i].y), bf_hi(gq[i].y)));
;                     z[p1] = mk2(Y1.x - Y2.y, Y1.y + Y2.x); z[p2] = mk2(Y1.x + Y2.y, Y2.x - Y1.y); }
;                 if (tid == 0) { const int k = FN / 2, p1 = PADI(fpos(k)); const cf2 zk = z[p1]; const float4 g1 = make_float4(bf_lo(gh.x), bf_hi(gh.x), bf_lo(gh.y), bf_hi(gh.y));
;                     z[p1] = mk2(zk.x * g1.x, zk.y * g1.z); }
	v_add_f32 v18, v14, v16
	v_add_f32 v19, v15, v17
	v_add_f32_e64 v14, v14, -v16
	v_add_f32_e64 v15, v15, -v17
	v_lshlrev_b32_e32 v17, 16, v13
	v_mul_f32_e64 v14, v14, s34
	v_mul_f32_e64 v15, v15, s35
	v_lshlrev_b32_e32 v16, 16, v12
	v_and_b32_e32 v13, 0xffff0000, v13
	v_and_b32_e32 v12, 0xffff0000, v12
	v_mul_f32_e64 v18, v18, 0.5
	v_mul_f32_e64 v19, v19, 0.5
	v_mul_f32 v20, v15, v12
	v_mul_f32 v21, v14, v13
	v_mul_f32 v253, v15, v16
	v_mul_f32 v15, v14, v17
	v_mov_b32_e32 v14, v253
	v_fma_f32 v20, v18, v16, -v20
	v_fma_f32 v21, v19, v17, -v21
	v_fma_f32 v12, v18, v12, v14
	v_fma_f32 v13, v19, v13, v15
	s_nop 0
	v_add_f32_e64 v14, v20, -v13
	v_add_f32_e64 v15, v21, -v12
	v_add_f32 v253, v20, v13
	v_add_f32 v13, v21, v12
	v_mov_b32_e32 v12, v253
	v_mov_b32_e32 v16, v14
	v_mov_b32_e32 v17, v13
	v_mov_b32_e32 v13, v15
	ds_write_b64 v22, v[16:17]
	ds_write_b64 v23, v[12:13]
	v_add_u32_e32 v12, 0x1c00, v114
	v_lshrrev_b32_e32 v13, 6, v12
	v_and_b32_e32 v13, 60, v13
	v_ashrrev_i32_e32 v12, 12, v12
	v_add3_u32 v12, v60, v12, v13
	v_ashrrev_i32_e32 v13, 5, v12
	v_sub_u32_e32 v14, 0xffffe400, v114
	v_lshlrev_b32_e32 v13, 3, v13
	v_lshlrev_b32_e32 v17, 2, v14
	v_lshlrev_b32_e32 v12, 3, v12
	v_and_b32_e32 v13, -16, v13
	v_and_b32_e32 v15, 0x3000, v14
	v_lshlrev_b32_e32 v16, 10, v14
	v_and_b32_e32 v17, 0x3c0, v17
	v_add3_u32 v20, 0, v12, v13
	v_lshrrev_b32_e32 v12, 3, v14
	v_and_or_b32 v16, v16, s79, v17
	v_and_b32_e32 v12, 0x1e0, v12
	v_lshrrev_b32_e32 v13, 9, v15
	v_add3_u32 v12, 0, v12, v13
	v_lshlrev_b32_e32 v13, 3, v16
	v_lshrrev_b32_e32 v14, 2, v16
	v_add3_u32 v21, v12, v13, v14
	ds_read_b64 v[12:13], v20
	ds_read_b64 v[14:15], v21
	s_waitcnt lgkmcnt(0)
	v_add_f32 v16, v12, v14
	v_add_f32 v17, v13, v15
	v_add_f32_e64 v12, v12, -v14
	v_add_f32_e64 v13, v13, -v15
	v_lshlrev_b32_e32 v15, 16, v11
	v_mul_f32_e64 v12, v12, s34
	v_mul_f32_e64 v13, v13, s35
	v_lshlrev_b32_e32 v14, 16, v10
	v_and_b32_e32 v11, 0xffff0000, v11
	v_and_b32_e32 v10, 0xffff0000, v10
	v_mul_f32_e64 v16, v16, 0.5
	v_mul_f32_e64 v17, v17, 0.5
	v_mul_f32 v18, v13, v10
	v_mul_f32 v19, v12, v11
	v_mul_f32 v253, v13, v14
	v_mul_f32 v13, v12, v15
	v_mov_b32_e32 v12, v253
	v_fma_f32 v18, v16, v14, -v18
	v_fma_f32 v19, v17, v15, -v19
	v_fma_f32 v10, v16, v10, v12
	v_fma_f32 v11, v17, v11, v13
	s_nop 0
	v_add_f32_e64 v12, v18, -v11
	v_add_f32_e64 v13, v19, -v10
	v_add_f32 v253, v18, v11
	v_add_f32 v11, v19, v10
	v_mov_b32_e32 v10, v253
	v_mov_b32_e32 v14, v12
	v_mov_b32_e32 v15, v11
	v_mov_b32_e32 v11, v13
	ds_write_b64 v20, v[14:15]
	ds_write_b64 v21, v[10:11]
	v_add_u32_e32 v10, 0x1e00, v114
	v_lshrrev_b32_e32 v11, 6, v10
	v_and_b32_e32 v11, 60, v11
	v_ashrrev_i32_e32 v10, 12, v10
	v_add3_u32 v10, v60, v10, v11
	v_ashrrev_i32_e32 v11, 5, v10
	v_sub_u32_e32 v12, 0xffffe200, v114
	v_lshlrev_b32_e32 v11, 3, v11
	v_lshlrev_b32_e32 v15, 2, v12
	v_lshlrev_b32_e32 v10, 3, v10
	v_and_b32_e32 v11, -16, v11
	v_and_b32_e32 v13, 0x3000, v12
	v_lshlrev_b32_e32 v14, 10, v12
	v_and_b32_e32 v15, 0x3c0, v15
	v_add3_u32 v18, 0, v10, v11
	v_lshrrev_b32_e32 v10, 3, v12
	v_and_or_b32 v14, v14, s79, v15
	v_and_b32_e32 v10, 0x1e0, v10
	v_lshrrev_b32_e32 v11, 9, v13
	v_add3_u32 v10, 0, v10, v11
	v_lshlrev_b32_e32 v11, 3, v14
	v_lshrrev_b32_e32 v12, 2, v14
	v_add3_u32 v19, v10, v11, v12
	ds_read_b64 v[10:11], v18
	ds_read_b64 v[12:13], v19
	s_waitcnt lgkmcnt(0)
	v_add_f32 v14, v10, v12
	v_add_f32 v15, v11, v13
	v_add_f32_e64 v10, v10, -v12
	v_add_f32_e64 v11, v11, -v13
	v_lshlrev_b32_e32 v13, 16, v9
	v_mul_f32_e64 v10, v10, s34
	v_mul_f32_e64 v11, v11, s35
	v_lshlrev_b32_e32 v12, 16, v8
	v_and_b32_e32 v9, 0xffff0000, v9
	v_and_b32_e32 v8, 0xffff0000, v8
	v_mul_f32_e64 v14, v14, 0.5
	v_mul_f32_e64 v15, v15, 0.5
	v_mul_f32 v16, v11, v8
	v_mul_f32 v17, v10, v9
	v_mul_f32 v253, v11, v12
	v_mul_f32 v11, v10, v13
	v_mov_b32_e32 v10, v253
	v_fma_f32 v16, v14, v12, -v16
	v_fma_f32 v17, v15, v13, -v17
	v_fma_f32 v8, v14, v8, v10
	v_fma_f32 v9, v15, v9, v11
	s_nop 0
	v_add_f32_e64 v10, v16, -v9
	v_add_f32_e64 v11, v17, -v8
	v_add_f32 v253, v16, v9
	v_add_f32 v9, v17, v8
	v_mov_b32_e32 v8, v253
	v_mov_b32_e32 v12, v10
	v_mov_b32_e32 v13, v9
	v_mov_b32_e32 v9, v11
	ds_write_b64 v18, v[12:13]
	ds_write_b64 v19, v[8:9]
	s_and_saveexec_b64 s[48:49], vcc
	s_cbranch_execz .LBB0_700
	ds_read_b64 v[8:9], v61 offset:16
	v_lshlrev_b32_e32 v7, 16, v7
	v_lshlrev_b32_e32 v6, 16, v6
	s_waitcnt lgkmcnt(0)
	v_mul_f32 v6, v8, v6
	v_mul_f32 v7, v9, v7
	ds_write_b64 v61, v[6:7] offset:16

; FFT_HD cf2 mk2(float x, float y) { return (cf2){x, y}; }
; FFT_HD cf2 cadd(cf2 a, cf2 b) { return mk2(a.x + b.x, a.y + b.y); }
; FFT_HD cf2 csub(cf2 a, cf2 b) { return mk2(a.x - b.x, a.y - b.y); }
; template <bool INV> FFT_HD void dft4(cf2& a, cf2& b, cf2& c, cf2& d) {
;     const cf2 s0 = cadd(a, c), s1 = csub(a, c), s2 = cadd(b, d), s3 = csub(b, d);
;     a = cadd(s0, s2); c = csub(s0, s2);
;     const cf2 r = INV ? mk2(-s3.y, s3.x) : mk2(s3.y, -s3.x);
;     b = cadd(s1, r); d = csub(s1, r);
; }
; template <bool INV, class ZP> FFT_HD void fft_r4_pass(ZP z, int tid, int nthr) {
;     for (int w = tid; w < FN / 4; w += nthr) {
;         const int base = PADI(4 * w);
;         cf2 a = z[base], b = z[base + 1], c = z[base + 2], d = z[base + 3];
;         dft4<INV>(a, b, c, d);
;         z[base] = a; z[base + 1] = b; z[base + 2] = c; z[base + 3] = d;
;     }
; }
.LBB0_714:
	v_and_b32_e32 v6, -16, v3
	v_add_u32_e32 v7, 0x200, v3
	v_add_u32_e32 v20, v2, v6
	v_cmp_lt_i32_e32 vcc, s82, v3
	v_mov_b32_e32 v3, v7
	ds_read_b128 v[6:9], v20
	ds_read_b128 v[10:13], v20 offset:16
	v_add_u32_e32 v2, 0x4000, v2
	s_or_b64 s[50:51], vcc, s[50:51]
	s_waitcnt lgkmcnt(0)
	v_add_f32 v14, v6, v10
	v_add_f32 v15, v7, v11
	v_add_f32 v16, v8, v12
	v_add_f32 v17, v9, v13
	v_add_f32_e64 v18, v6, -v10
	v_add_f32_e64 v19, v7, -v11
	v_add_f32_e64 v8, v8, -v12
	v_add_f32_e64 v9, v9, -v13
	v_add_f32 v6, v14, v16
	v_add_f32 v7, v15, v17
	v_add_f32_e64 v10, v14, -v16
	v_add_f32_e64 v11, v15, -v17
	v_add_f32_e64 v14, v18, -v9
	v_add_f32_e64 v15, v19, -v8
	v_add_f32 v12, v18, v9
	v_add_f32 v13, v19, v8
	v_mov_b32_e32 v8, v14
	v_mov_b32_e32 v9, v13
	v_mov_b32_e32 v13, v15
	ds_write_b128 v20, v[6:9]
	ds_write_b128 v20, v[10:13] offset:16
	s_andn2_b64 exec, exec, s[50:51]
	s_cbranch_execnz .LBB0_714

; __device__ __forceinline__ KP kparams() { KP q = (KP)__builtin_amdgcn_kernarg_segment_ptr(); asm volatile("" : "+s"(q)); return q; }
; FFT_HD cf2 mk2(float x, float y) { return (cf2){x, y}; }
; FFT_HD void fft_sincos(float frac, float& s, float& c) { s = __builtin_amdgcn_sinf(frac); c = __builtin_amdgcn_cosf(frac); }
; FFT_HD cf2 cmul(cf2 a, cf2 b) { return mk2(a.x * b.x - a.y * b.y, a.x * b.y + a.y * b.x); }
; template <int BANK> __device__ __forceinline__ void bg_issue1(BgState& b, int wg, int NW, int lane) {
;     KP kp = kparams();
;     const float* src; int ldS; bf16_t* dst; int o2;
;     bg_decode(b.st, wg, NW, lane, kp, src, ldS, dst, o2);
;     b.dst[BANK] = dst; b.o2[BANK] = o2;
;     asm volatile("s_nop 6" ::: "memory");
; #pragma unroll
;     for (int i = 0; i < 8; ++i) { const float* p = src + (size_t)i * ldS;
;         asm volatile("global_load_dword %0, %4, off\n\tglobal_load_dword %1, %4, off offset:256\n\tglobal_load_dword %2, %4, off offset:512\n\tglobal_load_dword %3, %4, off offset:768"
;                      : "=&v"(b.r[(BANK * 8 + i) * 4 + 0]), "=&v"(b.r[(BANK * 8 + i) * 4 + 1]), "=&v"(b.r[(BANK * 8 + i) * 4 + 2]), "=&v"(b.r[(BANK * 8 + i) * 4 + 3]) : "v"(p) : "memory"); }
;     b.st += 1;
; }
; FFT_HD void fft_gen_tw(float frac, cf2 (&tw)[16]) {
;     float sn, cs; fft_sincos(frac, sn, cs);
;     tw[1] = mk2(cs, -sn);
;     tw[2] = cmul(tw[1], tw[1]); tw[3] = cmul(tw[2], tw[1]); tw[4] = cmul(tw[2], tw[2]); tw[5] = cmul(tw[4], tw[1]); tw[6] = cmul(tw[4], tw[2]); tw[7] = cmul(tw[4], tw[3]);
;     tw[8] = cmul(tw[4], tw[4]);
; #pragma unroll
;     for (int j = 9; j < 16; ++j) tw[j] = cmul(tw[8], tw[j - 8]);
; }
.LBB0_727:
	s_nop 6
	s_lshl_b32 s12, s46, 2
	v_and_b32_e32 v24, 3, v128
	global_load_dword v161, v[2:3], off nt
	global_load_dword v120, v[2:3], off offset:256 nt
	global_load_dword v110, v[2:3], off offset:512 nt
	global_load_dword v102, v[2:3], off offset:768 nt
	v_lshl_add_u64 v[2:3], v[2:3], 0, s[12:13]
	v_cvt_f32_ubyte0_e32 v4, v24
	global_load_dword v163, v[2:3], off nt
	global_load_dword v122, v[2:3], off offset:256 nt
	global_load_dword v112, v[2:3], off offset:512 nt
	global_load_dword v104, v[2:3], off offset:768 nt
	v_lshl_add_u64 v[2:3], v[2:3], 0, s[12:13]
	v_mul_f32_e32 v4, 0x3c800000, v4
	global_load_dword v162, v[2:3], off nt
	global_load_dword v121, v[2:3], off offset:256 nt
	global_load_dword v111, v[2:3], off offset:512 nt
	global_load_dword v103, v[2:3], off offset:768 nt
	v_lshl_add_u64 v[2:3], v[2:3], 0, s[12:13]
	v_sin_f32_e32 v94, v4
	global_load_dword v165, v[2:3], off nt
	global_load_dword v124, v[2:3], off offset:256 nt
	global_load_dword v114, v[2:3], off offset:512 nt
	global_load_dword v106, v[2:3], off offset:768 nt
	v_lshl_add_u64 v[2:3], v[2:3], 0, s[12:13]
	v_cos_f32_e32 v96, v4
	global_load_dword v164, v[2:3], off nt
	global_load_dword v123, v[2:3], off offset:256 nt
	global_load_dword v113, v[2:3], off offset:512 nt
	global_load_dword v105, v[2:3], off offset:768 nt
	v_lshl_add_u64 v[2:3], v[2:3], 0, s[12:13]
	global_load_dword v167, v[2:3], off nt
	global_load_dword v126, v[2:3], off offset:256 nt
	global_load_dword v116, v[2:3], off offset:512 nt
	global_load_dword v108, v[2:3], off offset:768 nt
	v_lshl_add_u64 v[2:3], v[2:3], 0, s[12:13]
	global_load_dword v166, v[2:3], off nt
	global_load_dword v125, v[2:3], off offset:256 nt
	global_load_dword v115, v[2:3], off offset:512 nt
	global_load_dword v107, v[2:3], off offset:768 nt
	v_lshl_add_u64 v[2:3], v[2:3], 0, s[12:13]
	v_xor_b32_e32 v97, 0x80000000, v94
	global_load_dword v168, v[2:3], off nt
	global_load_dword v127, v[2:3], off offset:256 nt
	global_load_dword v117, v[2:3], off offset:512 nt
	global_load_dword v109, v[2:3], off offset:768 nt
	v_mov_b32_e32 v95, v96
	v_mov_b32_e32 v2, v94
	v_mov_b32_e32 v3, v97
	v_mul_f32 v2, v94, v2
	v_mul_f32 v3, v95, v3
	v_lshlrev_b32_e32 v169, 4, v128
	v_fma_f32 v38, v96, v96, -v2
	v_fma_f32 v39, v96, v97, -v3
	v_fma_f32 v40, v96, v96, v2
	v_fma_f32 v41, v96, v97, v3
	v_pk_mov_b32 v[4:5], v[40:41], v[38:39] op_sel:[1,0]
	v_mov_b32_e32 v2, v38
	v_mov_b32_e32 v3, v41
	v_mul_f32 v10, v41, v4
	v_mul_f32 v11, v41, v5
	v_mov_b32_e32 v97, v94
	v_fma_f32 v56, v38, v2, -v10
	v_fma_f32 v57, v38, v3, -v11
	v_fma_f32 v186, v38, v2, v10
	v_fma_f32 v187, v38, v3, v11
	v_mov_b32_e32 v68, v56
	v_mov_b32_e32 v69, v187
	v_mul_f32 v18, v68, v68
	v_mul_f32 v19, v69, v69
	v_mul_f32 v20, v68, v187
	v_mul_f32 v21, v69, v186
	v_mov_b32_e32 v22, v18
	v_mov_b32_e32 v23, v20
	v_pk_mov_b32 v[18:19], v[18:19], v[20:21] op_sel:[1,0]
	v_mul_f32 v6, v96, v2
	v_mul_f32 v7, v97, v3
	v_add_f32_e64 v48, v22, -v18
	v_add_f32_e64 v49, v23, -v19
	v_add_f32 v52, v22, v18
	v_add_f32 v53, v23, v19
	v_mul_f32 v8, v94, v2
	v_mul_f32 v9, v95, v3
	v_mov_b32_e32 v188, v48
	v_mov_b32_e32 v189, v53
	v_mul_f32 v14, v2, v68
	v_mul_f32 v15, v3, v69
	v_mul_f32 v16, v4, v68
	v_mul_f32 v17, v5, v69
	v_mul_f32 v190, v2, v188
	v_mul_f32 v191, v3, v189
	v_mul_f32 v192, v4, v188
	v_mul_f32 v193, v5, v189
	v_mov_b32_e32 v2, v6
	v_mov_b32_e32 v3, v9
	v_pk_mov_b32 v[4:5], v[6:7], v[8:9] op_sel:[1,0]
	v_mul_f32 v10, v96, v68
	v_mul_f32 v11, v97, v69
	v_add_f32 v72, v2, v4
	v_add_f32 v73, v3, v5
	v_add_f32_e64 v54, v2, -v4
	v_add_f32_e64 v55, v3, -v5
	v_mul_f32 v12, v94, v68
	v_mul_f32 v13, v95, v69
	v_mov_b32_e32 v2, v72
	v_mov_b32_e32 v3, v55
	v_pk_mov_b32 v[4:5], v[54:55], v[72:73] op_sel:[1,0]
	v_mul_f32 v6, v68, v2
	v_mul_f32 v7, v69, v3
	v_mul_f32 v8, v68, v4
	v_mul_f32 v9, v69, v5
	v_mul_f32 v100, v2, v188
	v_mul_f32 v101, v3, v189
	v_mul_f32 v98, v4, v188
	v_mul_f32 v99, v5, v189
	v_mov_b32_e32 v2, v10
	v_mov_b32_e32 v3, v13
	v_pk_mov_b32 v[4:5], v[10:11], v[12:13] op_sel:[1,0]
	v_pk_mov_b32 v[70:71], v[186:187], v[56:57] op_sel:[1,0]
	v_add_f32 v202, v2, v4
	v_add_f32 v203, v3, v5
	v_add_f32_e64 v204, v2, -v4
	v_add_f32_e64 v205, v3, -v5
	v_mov_b32_e32 v2, v14
	v_mov_b32_e32 v3, v16
	v_mov_b32_e32 v16, v15
	v_add_f32_e64 v46, v2, -v16
	v_add_f32_e64 v47, v3, -v17
	v_add_f32 v50, v2, v16
	v_add_f32 v51, v3, v17
	v_mov_b32_e32 v2, v46
	v_mov_b32_e32 v3, v51
	v_mul_f32 v210, v188, v2
	v_mul_f32 v211, v189, v3
	v_pk_mov_b32 v[2:3], v[50:51], v[46:47] op_sel:[1,0]
	v_lshlrev_b32_e32 v5, 3, v24
	v_mul_f32 v212, v188, v2
	v_mul_f32 v213, v189, v3
	v_mov_b32_e32 v2, v6
	v_mov_b32_e32 v3, v8
	v_mov_b32_e32 v8, v7
	v_add_f32_e64 v78, v2, -v8
	v_add_f32_e64 v79, v3, -v9
	v_add_f32 v80, v2, v8
	v_add_f32 v81, v3, v9
	v_mov_b32_e32 v2, v78
	v_mov_b32_e32 v3, v81
	v_mul_f32 v214, v188, v2
	v_mul_f32 v215, v189, v3
	v_pk_mov_b32 v[2:3], v[80:81], v[78:79] op_sel:[1,0]
	v_mov_b32_e32 v42, v202
	v_mul_f32 v216, v188, v2
	v_mul_f32 v217, v189, v3
	v_and_b32_e32 v2, 0xffffffc0, v169
	v_bfe_i32 v3, v128, 1, 27
	v_add_u32_e32 v4, 0x2000, v2
	v_lshlrev_b32_e32 v2, 3, v2
	v_lshlrev_b32_e32 v3, 3, v3
	v_add3_u32 v2, 0, v2, v5
	v_and_b32_e32 v3, -16, v3
	v_add_u32_e32 v65, v2, v3
	ds_read2_b64 v[170:173], v65 offset1:4
	ds_read2_b64 v[74:77], v65 offset0:8 offset1:12
	ds_read2_b64 v[82:85], v65 offset0:16 offset1:20
	ds_read2_b64 v[86:89], v65 offset0:24 offset1:28
	ds_read2_b64 v[90:93], v65 offset0:32 offset1:36
	ds_read2_b64 v[174:177], v65 offset0:40 offset1:44
	ds_read2_b64 v[178:181], v65 offset0:48 offset1:52
	ds_read2_b64 v[182:185], v65 offset0:56 offset1:60
	s_waitcnt lgkmcnt(6)
; FFT_HD cf2 mk2(float x, float y) { return (cf2){x, y}; }
; FFT_HD cf2 cmul(cf2 a, cf2 b) { return mk2(a.x * b.x - a.y * b.y, a.x * b.y + a.y * b.x); }
; FFT_HD cf2 cmulc(cf2 a, cf2 b) { return mk2(a.x * b.x + a.y * b.y, a.y * b.x - a.x * b.y); }
; template <bool INV> FFT_HD void dft16(cf2 (&x)[16]) {
;     const float C1 = 0.9238795325112867f, S1 = 0.3826834323650898f, H = 0.7071067811865476f;
; #pragma unroll
;     for (int b = 0; b < 4; ++b) dft4<INV>(x[b], x[4 + b], x[8 + b], x[12 + b]);
;     const float s = INV ? -1.f : 1.f;
;     x[4 + 1] = cmul(x[4 + 1], mk2(C1, -s * S1)); x[8 + 1] = cmul(x[8 + 1], mk2(H, -s * H));   x[12 + 1] = cmul(x[12 + 1], mk2(S1, -s * C1));
;     x[4 + 2] = cmul(x[4 + 2], mk2(H, -s * H));   x[8 + 2] = cmul(x[8 + 2], mk2(0.f, -s));     x[12 + 2] = cmul(x[12 + 2], mk2(-H, -s * H));
;     x[4 + 3] = cmul(x[4 + 3], mk2(S1, -s * C1)); x[8 + 3] = cmul(x[8 + 3], mk2(-H, -s * H));  x[12 + 3] = cmul(x[12 + 3], mk2(-C1, s * S1));
; template <bool INV, int lS, class ZP> FFT_HD void fft_r16_pass(ZP z, int tid) {
;     ...
;         if (INV) {
; #pragma unroll
;             for (int j = 1; j < 16; ++j) x[j] = cmulc(x[j], tw[j]);
;         }
;         dft16<INV>(x);
;         if (!INV) {
; #pragma unroll
;             for (int j = 1; j < 16; ++j) x[j] = cmul(x[j], tw[j]);
;         }
; #pragma unroll
;         for (int j = 0; j < 16; ++j) z[pb0 + j * STEP] = x[j];
;         if (INV) {
; #pragma unroll
;             for (int j = 1; j < 16; ++j) y[j] = cmulc(y[j], tw[j]);
;         }
;         dft16<INV>(y);
	v_mul_f32 v218, v41, v75
	v_mul_f32 v219, v41, v74
	v_mov_b32_e32 v43, v205
	v_fma_f32 v220, v38, v74, v218
	v_fma_f32 v221, v38, v75, v219
	v_fma_f32 v218, v38, v74, -v218
	v_fma_f32 v219, v38, v75, -v219
	v_mul_f32 v74, v55, v77
	v_mul_f32 v75, v55, v76
	v_pk_mov_b32 v[44:45], v[204:205], v[202:203] op_sel:[1,0]
	v_fma_f32 v222, v72, v76, v74
	v_fma_f32 v223, v72, v77, v75
	v_fma_f32 v224, v72, v76, -v74
	v_fma_f32 v225, v72, v77, -v75
	s_waitcnt lgkmcnt(5)
	v_mul_f32 v74, v187, v83
	v_mul_f32 v75, v187, v82
	v_mul_f32_e32 v54, v94, v53
	v_fma_f32 v186, v56, v82, v74
	v_fma_f32 v187, v57, v83, v75
	v_fma_f32 v74, v56, v82, -v74
	v_fma_f32 v75, v56, v83, -v75
	v_mov_b32_e32 v187, v75
	v_mul_f32 v74, v205, v85
	v_mul_f32 v75, v205, v84
	s_waitcnt lgkmcnt(3)
	v_mov_b32_e32 v82, v92
	v_fma_f32 v204, v202, v84, v74
	v_fma_f32 v205, v202, v85, v75
	v_fma_f32 v203, v202, v85, -v75
	v_fma_f32 v202, v202, v84, -v74
	v_mul_f32 v74, v51, v87
	v_mul_f32 v75, v51, v86
	v_pk_mov_b32 v[84:85], v[92:93], v[172:173] op_sel:[1,0]
	v_fma_f32 v226, v46, v86, v74
	v_fma_f32 v227, v46, v87, v75
	v_fma_f32 v228, v46, v86, -v74
	v_fma_f32 v229, v46, v87, -v75
	v_mul_f32 v74, v81, v89
	v_mul_f32 v75, v81, v88
	v_mov_b32_e32 v83, v173
	v_fma_f32 v230, v78, v88, v74
	v_fma_f32 v231, v78, v89, v75
	v_fma_f32 v232, v78, v88, -v74
	v_fma_f32 v233, v78, v89, -v75
	v_mul_f32 v74, v53, v91
	v_mul_f32 v75, v53, v90
	v_mul_f32 v200, v70, v188
	v_mul_f32 v201, v71, v189
	v_fma_f32 v234, v48, v90, v74
	v_fma_f32 v235, v49, v91, v75
	v_fma_f32 v74, v48, v90, -v74
	v_fma_f32 v75, v48, v91, -v75
	v_mov_b32_e32 v235, v75
	v_fma_f32 v74, v96, v188, v54
	v_fma_f32 v75, v97, v189, v54
	v_mul_f32_e32 v54, v96, v53
	v_fma_f32 v76, -v94, v188, v54
	v_fma_f32 v77, -v95, v189, v54
	v_mov_b32_e32 v75, v96
	v_mov_b32_e32 v77, v94
	v_mul_f32 v86, v76, v84
	v_mul_f32 v87, v77, v85
	v_add_f32 v88, v192, v193
	v_add_f32 v89, v192, v193
	v_fma_f32 v172, v74, v82, v86
	v_fma_f32 v173, v75, v83, v87
	v_mul_f32 v82, v76, v82
	v_mul_f32 v83, v77, v83
	v_mul_f32 v198, v68, v188
	v_mul_f32 v199, v69, v189
	v_mul_f32 v206, v188, v42
	v_mul_f32 v207, v189, v43
	v_mul_f32 v208, v188, v44
	v_mul_f32 v209, v189, v45
	v_fma_f32 v188, v74, v84, -v82
	v_fma_f32 v189, v75, v85, -v83
	v_add_f32_e64 v86, v190, -v191
	v_add_f32_e64 v87, v190, -v191
	s_waitcnt lgkmcnt(2)
	v_mul_f32 v82, v88, v174
	v_mul_f32 v83, v89, v175
	v_add_f32 v94, v200, v201
	v_add_f32 v95, v200, v201
	v_fma_f32 v190, v86, v174, v83
	v_fma_f32 v191, v87, v175, v82
	v_fma_f32 v174, v86, v174, -v83
	v_fma_f32 v175, v87, v175, -v82
	v_add_f32_e64 v96, v198, -v199
	v_add_f32_e64 v97, v198, -v199
	s_waitcnt lgkmcnt(1)
	v_mul_f32 v82, v94, v178
	v_mul_f32 v83, v95, v179
	v_add_f32_e64 v84, v206, -v207
	v_add_f32_e64 v85, v206, -v207
	v_fma_f32 v192, v96, v178, v83
	v_fma_f32 v193, v97, v179, v82
	v_fma_f32 v253, v96, v178, -v83
	v_fma_f32 v83, v97, v179, -v82
	v_mov_b32_e32 v82, v253
	v_add_f32 v92, v212, v213
	v_add_f32 v93, v212, v213
	v_mov_b32_e32 v193, v83
	v_add_f32 v82, v208, v209
	v_add_f32 v83, v208, v209
	v_mul_f32 v90, v82, v180
	v_mul_f32 v91, v83, v181
	s_waitcnt lgkmcnt(0)
	v_mul_f32 v198, v92, v182
	v_mul_f32 v199, v93, v183
	v_fma_f32 v178, v84, v180, v91
	v_fma_f32 v179, v85, v181, v90
	v_fma_f32 v180, v84, v180, -v91
	v_fma_f32 v181, v85, v181, -v90
	v_add_f32_e64 v90, v210, -v211
	v_add_f32_e64 v91, v210, -v211
	v_mov_b32_e32 v202, v204
	v_mov_b32_e32 v179, v181
	v_fma_f32 v200, v90, v182, v199
	v_fma_f32 v201, v91, v183, v198
	v_fma_f32 v182, v90, v182, -v199
	v_fma_f32 v183, v91, v183, -v198
	v_mov_b32_e32 v221, v219
	v_mov_b32_e32 v228, v226
	v_mov_b32_e32 v191, v175
	v_mov_b32_e32 v182, v200
	v_add_f32 v210, v189, v172
	v_add_f32 v211, v188, v173
	v_add_f32 v212, v202, v178
	v_add_f32 v213, v203, v179
	v_pk_mov_b32 v[204:205], v[172:173], v[204:205] op_sel:[1,0]
	v_mov_b32_e32 v202, v189
	v_mov_b32_e32 v173, v181
	v_mov_b32_e32 v236, v188
	v_add_f32_e64 v172, v202, -v172
	v_add_f32_e64 v173, v203, -v173
	v_add_f32 v188, v220, v190
	v_add_f32 v189, v221, v191
	v_add_f32 v202, v228, v182
	v_add_f32 v203, v229, v183
	v_mov_b32_e32 v221, v229
	v_mov_b32_e32 v191, v183
	v_mov_b32_e32 v237, v178
	v_add_f32_e64 v182, v220, -v190
	v_add_f32_e64 v183, v221, -v191
	v_add_f32 v190, v188, v202
	v_add_f32 v191, v189, v203
	v_add_f32_e64 v188, v188, -v202
	v_add_f32_e64 v189, v189, -v203
	v_add_f32 v198, v170, v234
	v_add_f32 v199, v171, v235
	v_add_f32 v206, v186, v192
	v_add_f32 v207, v187, v193
	v_add_f32_e64 v178, v204, -v236
	v_add_f32_e64 v179, v205, -v237
	v_pk_mov_b32 v[204:205], v[218:219], v[226:227] op_sel:[1,0]
	v_pk_mov_b32 v[174:175], v[174:175], v[200:201] op_sel:[1,0]
	v_fma_f32 v202, v188, 0, -v189
	v_fma_f32 v203, v189, 0, -v188
	v_fma_f32 v253, v188, 0, v189
	v_fma_f32 v189, v189, 0, v188
	v_mov_b32_e32 v188, v253
	v_add_f32 v208, v198, v206
	v_add_f32 v209, v199, v207
	v_add_f32_e64 v174, v204, -v174
	v_add_f32_e64 v175, v205, -v175
	v_add_f32_e64 v198, v198, -v206
	v_add_f32_e64 v199, v199, -v207
	v_mov_b32_e32 v203, v189
	v_mov_b32_e32 v223, v225
	v_sub_f32_e32 v54, v182, v183
	v_pk_mov_b32 v[200:201], v[224:225], v[230:231] op_sel:[1,0]
	v_add_f32_e64 v186, v186, -v192
	v_add_f32_e64 v187, v187, -v193
	v_add_f32_e64 v224, v172, -v173
	v_add_f32_e64 v225, v172, -v173
	v_add_f32 v226, v178, v179
	v_add_f32 v227, v178, v179
	v_add_f32 v188, v198, v202
	v_add_f32 v189, v199, v203
	v_add_f32_e64 v198, v198, -v202
	v_add_f32_e64 v199, v199, -v203
	v_mov_b32_e32 v202, v182
	v_mov_b32_e32 v203, v172
	v_mov_b32_e32 v172, v183
	v_mov_b32_e32 v182, v174
	v_mov_b32_e32 v183, v178
	v_mov_b32_e32 v178, v175
; FFT_HD cf2 mk2(float x, float y) { return (cf2){x, y}; }
; FFT_HD cf2 cmul(cf2 a, cf2 b) { return mk2(a.x * b.x - a.y * b.y, a.x * b.y + a.y * b.x); }
; template <bool INV> FFT_HD void dft16(cf2 (&x)[16]) {
;     const float C1 = 0.9238795325112867f, S1 = 0.3826834323650898f, H = 0.7071067811865476f;
; #pragma unroll
;     for (int b = 0; b < 4; ++b) dft4<INV>(x[b], x[4 + b], x[8 + b], x[12 + b]);
;     const float s = INV ? -1.f : 1.f;
;     x[4 + 1] = cmul(x[4 + 1], mk2(C1, -s * S1)); x[8 + 1] = cmul(x[8 + 1], mk2(H, -s * H));   x[12 + 1] = cmul(x[12 + 1], mk2(S1, -s * C1));
;     x[4 + 2] = cmul(x[4 + 2], mk2(H, -s * H));   x[8 + 2] = cmul(x[8 + 2], mk2(0.f, -s));     x[12 + 2] = cmul(x[12 + 2], mk2(-H, -s * H));
;     x[4 + 3] = cmul(x[4 + 3], mk2(S1, -s * C1)); x[8 + 3] = cmul(x[8 + 3], mk2(-H, -s * H));  x[12 + 3] = cmul(x[12 + 3], mk2(-C1, s * S1));
; #pragma unroll
;     for (int c = 0; c < 4; ++c) dft4<INV>(x[4 * c], x[4 * c + 1], x[4 * c + 2], x[4 * c + 3]);
; #pragma unroll
;     for (int c = 0; c < 4; ++c)
; #pragma unroll
;         for (int d = c + 1; d < 4; ++d) { const cf2 t = x[4 * c + d]; x[4 * c + d] = x[4 * d + c]; x[4 * d + c] = t; }
; }
	v_add_f32_e32 v67, v174, v175
	v_add_f32_e64 v170, v170, -v234
	v_add_f32_e64 v171, v171, -v235
	v_pk_mov_b32 v[192:193], v[186:187], v[186:187] op_sel:[1,0]
	v_add_f32 v172, v202, v172
	v_add_f32 v173, v203, v173
	v_add_f32_e64 v174, v182, -v178
	v_add_f32_e64 v175, v183, -v179
	v_add_f32 v220, v208, v190
	v_add_f32 v221, v209, v191
	v_add_f32_e64 v190, v208, -v190
	v_add_f32_e64 v191, v209, -v191
	v_add_f32_e64 v208, v170, -v187
	v_add_f32_e64 v209, v171, -v186
	v_add_f32 v253, v170, v187
	v_add_f32 v187, v171, v186
	v_mov_b32_e32 v186, v253
	v_mul_f32_e32 v170, 0x3ec3ef15, v173
	v_mul_f32_e32 v192, 0x3f6c835e, v175
	v_ashrrev_i32_e32 v3, 2, v4
	v_add_f32_e64 v170, v170, -v192
	v_add_f32_e64 v171, v171, -v193
	v_mov_b32_e32 v192, v214
	v_mov_b32_e32 v193, v100
	v_mov_b32_e32 v100, v215
	v_add3_u32 v60, v2, v3, s71
	v_add_f32_e64 v100, v192, -v100
	v_add_f32_e64 v101, v193, -v101
	v_mov_b32_e32 v192, v216
	v_mov_b32_e32 v193, v98
	v_mov_b32_e32 v98, v217
	ds_read2_b64 v[2:5], v60 offset1:4
	ds_read2_b64 v[30:33], v60 offset0:8 offset1:12
	ds_read2_b64 v[14:17], v60 offset0:16 offset1:20
	ds_read2_b64 v[26:29], v60 offset0:24 offset1:28
	ds_read2_b64 v[10:13], v60 offset0:32 offset1:36
	ds_read2_b64 v[22:25], v60 offset0:40 offset1:44
	ds_read2_b64 v[6:9], v60 offset0:48 offset1:52
	ds_read2_b64 v[18:21], v60 offset0:56 offset1:60
	v_add_f32 v98, v192, v98
	v_add_f32 v99, v193, v99
	s_waitcnt lgkmcnt(5)
	v_mul_f32 v70, v70, v14
	v_mul_f32 v71, v71, v14
	v_mul_f32_e32 v73, 0x3f3504f3, v54
	v_mul_f32_e32 v219, 0x3f3504f3, v67
	v_mul_f32 v192, v99, v177
	v_mul_f32 v193, v99, v176
	v_fma_f32 v56, v56, v15, -v70
	v_fma_f32 v57, v57, v15, -v71
	v_fma_f32 v14, v68, v15, v70
	v_fma_f32 v15, v69, v15, v71
	v_mov_b32_e32 v80, v55
	v_mov_b32_e32 v68, v33
	s_waitcnt lgkmcnt(4)
	v_mov_b32_e32 v69, v29
	v_sub_f32_e32 v218, v73, v219
	v_fma_f32 v202, v101, v176, v192
	v_fma_f32 v203, v101, v177, v193
	v_fma_f32 v176, v101, v176, -v192
	v_fma_f32 v177, v101, v177, -v193
	v_mul_f32 v192, v98, v185
	v_mul_f32 v193, v98, v184
	v_mov_b32_e32 v57, v15
	v_mov_b32_e32 v73, v78
	v_mov_b32_e32 v14, v32
	v_mov_b32_e32 v15, v28
	v_mul_f32 v68, v80, v68
	v_mul_f32 v69, v81, v69
	v_mov_b32_e32 v203, v177
	v_fma_f32 v206, v100, v184, v192
	v_fma_f32 v207, v100, v185, v193
	v_fma_f32 v184, v100, v184, -v192
	v_fma_f32 v185, v100, v185, -v193
	v_fma_f32 v14, v72, v14, v68
	v_fma_f32 v15, v73, v15, v69
	v_mov_b32_e32 v68, v29
	v_mov_b32_e32 v69, v33
	v_mov_b32_e32 v29, v32
	s_waitcnt lgkmcnt(3)
	v_mul_f32 v32, v53, v11
	v_mul_f32 v33, v53, v10
	v_mov_b32_e32 v232, v230
	v_mov_b32_e32 v204, v222
	v_mov_b32_e32 v205, v233
	v_mov_b32_e32 v184, v206
	v_add_f32 v192, v222, v202
	v_add_f32 v193, v223, v203
	v_pk_mov_b32 v[176:177], v[176:177], v[206:207] op_sel:[1,0]
	v_mov_b32_e32 v203, v185
	v_fma_f32 v52, v48, v10, v32
	v_fma_f32 v53, v49, v11, v33
	v_fma_f32 v10, v48, v10, -v32
	v_fma_f32 v11, v48, v11, -v33
	v_add_f32 v214, v232, v184
	v_add_f32 v215, v233, v185
	v_add_f32_e64 v176, v200, -v176
	v_add_f32_e64 v177, v201, -v177
	v_add_f32_e64 v184, v204, -v202
	v_add_f32_e64 v185, v205, -v203
	v_mov_b32_e32 v53, v11
	s_waitcnt lgkmcnt(1)
	v_mul_f32 v10, v96, v6
	v_mul_f32 v11, v97, v7
	v_mov_b32_e32 v202, v184
	v_mov_b32_e32 v203, v176
	v_mov_b32_e32 v204, v185
	v_mov_b32_e32 v205, v177
	v_fma_f32 v32, -v94, v6, v11
	v_fma_f32 v33, -v95, v7, v10
	v_fma_f32 v6, v94, v6, v11
	v_fma_f32 v7, v95, v7, v10
	v_add_f32 v206, v202, v204
	v_add_f32 v207, v203, v205
	v_add_f32_e64 v202, v202, -v204
	v_add_f32_e64 v203, v203, -v205
	v_mov_b32_e32 v33, v7
	v_mov_b32_e32 v7, v24
	s_waitcnt lgkmcnt(0)
	v_mov_b32_e32 v24, v21
	s_mov_b32 s46, s27
	s_mov_b32 s47, s26
	v_fmac_f32_e32 v219, 0x3f3504f3, v54
	v_mov_b32_e32 v207, v203
	v_mul_f32_e32 v54, 0x3f6c835e, v203
	v_mov_b32_e32 v6, v20
	v_mul_f32 v10, v98, v24
	v_mul_f32 v11, v99, v25
	v_add_f32 v180, v210, v212
	v_add_f32 v181, v211, v213
	v_mul_f32_e64 v226, v226, s46
	v_mul_f32_e64 v227, v227, s47
	v_add_f32 v200, v192, v214
	v_add_f32 v201, v193, v215
	v_fma_f32 v204, v206, s14, -v54
	v_fma_f32 v205, v207, s15, -v54
	v_add_f32 v253, v176, v177
	v_add_f32 v177, v176, v177
	v_mov_b32_e32 v176, v253
	v_mov_b32_e32 v54, v81
	v_fma_f32 v10, v100, v6, v10
	v_fma_f32 v11, v101, v7, v11
	v_mul_f32 v6, v98, v6
	v_mul_f32 v7, v99, v7
	v_mov_b32_e32 v209, v187
	v_fma_f32 v228, v224, s26, -v226
	v_fma_f32 v229, v225, s27, -v227
	v_fma_f32 v224, v224, s26, v226
	v_fma_f32 v225, v225, s27, v227
	v_add_f32 v216, v180, v200
	v_add_f32 v217, v181, v201
	v_add_f32_e64 v253, v184, -v185
	v_add_f32_e64 v185, v184, -v185
	v_mov_b32_e32 v184, v253
	v_mul_f32_e64 v176, v176, s26
	v_mul_f32_e64 v177, v177, s27
	v_mov_b32_e32 v79, v72
	v_mul_f32 v28, v54, v28
	v_mul_f32 v29, v55, v29
	v_fma_f32 v6, v100, v24, -v6
	v_fma_f32 v7, v101, v25, -v7
	v_add_f32_e64 v20, v2, -v52
	v_add_f32_e64 v21, v3, -v53
	v_add_f32_e64 v24, v56, -v32
	v_add_f32_e64 v25, v57, -v33
	v_mov_b32_e32 v229, v225
	v_add_f32 v224, v208, v218
	v_add_f32 v225, v209, v219
	v_add_f32_e64 v208, v208, -v218
	v_add_f32_e64 v209, v209, -v219
	v_add_f32 v218, v220, v216
	v_add_f32 v219, v221, v217
	v_add_f32_e64 v216, v220, -v216
	v_add_f32_e64 v217, v221, -v217
	v_fma_f32 v220, v184, s46, -v176
	v_fma_f32 v221, v185, s47, -v177
	v_fma_f32 v176, v184, s46, v176
	v_fma_f32 v177, v185, s47, v177
	v_fma_f32 v28, v78, v68, -v28
	v_fma_f32 v29, v79, v69, -v29
	v_add_f32 v48, v20, v24
	v_add_f32 v49, v21, v25
	v_add_f32_e64 v54, v20, -v24
	v_add_f32_e64 v55, v21, -v25
	v_mov_b32_e32 v221, v177
	v_mov_b32_e32 v49, v55
	v_add_f32_e64 v54, v14, -v11
	v_add_f32_e64 v55, v15, -v10
	v_add_f32_e64 v68, v28, -v6
; FFT_HD cf2 mk2(float x, float y) { return (cf2){x, y}; }
; FFT_HD cf2 cmul(cf2 a, cf2 b) { return mk2(a.x * b.x - a.y * b.y, a.x * b.y + a.y * b.x); }
; FFT_HD cf2 cmulc(cf2 a, cf2 b) { return mk2(a.x * b.x + a.y * b.y, a.y * b.x - a.x * b.y); }
; template <bool INV> FFT_HD void dft16(cf2 (&x)[16]) {
;     const float C1 = 0.9238795325112867f, S1 = 0.3826834323650898f, H = 0.7071067811865476f;
; #pragma unroll
;     for (int b = 0; b < 4; ++b) dft4<INV>(x[b], x[4 + b], x[8 + b], x[12 + b]);
;     const float s = INV ? -1.f : 1.f;
;     x[4 + 1] = cmul(x[4 + 1], mk2(C1, -s * S1)); x[8 + 1] = cmul(x[8 + 1], mk2(H, -s * H));   x[12 + 1] = cmul(x[12 + 1], mk2(S1, -s * C1));
;     x[4 + 2] = cmul(x[4 + 2], mk2(H, -s * H));   x[8 + 2] = cmul(x[8 + 2], mk2(0.f, -s));     x[12 + 2] = cmul(x[12 + 2], mk2(-H, -s * H));
;     x[4 + 3] = cmul(x[4 + 3], mk2(S1, -s * C1)); x[8 + 3] = cmul(x[8 + 3], mk2(-H, -s * H));  x[12 + 3] = cmul(x[12 + 3], mk2(-C1, s * S1));
; #pragma unroll
;     for (int c = 0; c < 4; ++c) dft4<INV>(x[4 * c], x[4 * c + 1], x[4 * c + 2], x[4 * c + 3]);
; #pragma unroll
;     for (int c = 0; c < 4; ++c)
; #pragma unroll
;         for (int d = c + 1; d < 4; ++d) { const cf2 t = x[4 * c + d]; x[4 * c + d] = x[4 * d + c]; x[4 * d + c] = t; }
; }
; template <bool INV, int lS, class ZP> FFT_HD void fft_r16_pass(ZP z, int tid) {
;     ...
;         if (INV) {
; #pragma unroll
;             for (int j = 1; j < 16; ++j) y[j] = cmulc(y[j], tw[j]);
;         }
;         dft16<INV>(y);
	v_add_f32_e64 v69, v29, -v7
	v_add_f32 v176, v228, v220
	v_add_f32 v177, v229, v221
	v_add_f32 v70, v68, v54
	v_add_f32 v71, v69, v55
	v_add_f32_e64 v72, v68, -v54
	v_add_f32_e64 v73, v69, -v55
	v_mul_f32 v40, v41, v30
	v_mul_f32 v41, v41, v31
	v_add_f32 v184, v224, v176
	v_add_f32 v185, v225, v177
	v_add_f32_e64 v176, v224, -v176
	v_add_f32_e64 v177, v225, -v177
	v_mov_b32_e32 v225, v192
	v_mov_b32_e32 v227, v214
	v_mov_b32_e32 v192, v211
	v_mov_b32_e32 v214, v213
	v_mov_b32_e32 v78, v70
	v_mov_b32_e32 v79, v73
	v_pk_mov_b32 v[70:71], v[72:73], v[70:71] op_sel:[1,0]
	v_fma_f32 v72, v38, v30, v41
	v_fma_f32 v73, v38, v31, v40
	v_fma_f32 v30, v38, v30, -v41
	v_fma_f32 v31, v38, v31, -v40
	v_mul_f32 v38, v51, v27
	v_mul_f32 v39, v51, v26
	s_mov_b32 s52, s25
	s_mov_b32 s53, s27
	v_mov_b32_e32 v224, v210
	v_mov_b32_e32 v226, v212
	v_add_f32_e64 v192, v192, -v214
	v_add_f32_e64 v193, v193, -v215
	s_mov_b32 s12, s25
	v_fma_f32 v40, v46, v26, v38
	v_fma_f32 v41, v46, v27, v39
	v_fma_f32 v26, v46, v26, -v38
	v_fma_f32 v27, v46, v27, -v39
	v_mul_f32 v38, v88, v22
	v_mul_f32 v39, v89, v23
	v_mul_f32_e64 v178, v174, s52
	v_mul_f32_e64 v179, v175, s53
	v_add_f32_e64 v224, v224, -v226
	v_add_f32_e64 v225, v225, -v227
	s_mov_b32 s53, s24
	v_mul_f32_e64 v192, v192, s12
	v_mul_f32_e64 v193, v193, s12
	v_fma_f32 v46, v86, v22, v39
	v_fma_f32 v47, v87, v23, v38
	v_fma_f32 v22, v86, v22, -v39
	v_fma_f32 v23, v87, v23, -v38
	v_mul_f32 v38, v92, v18
	v_mul_f32 v39, v93, v19
	v_fma_f32 v210, v224, s52, -v192
	v_fma_f32 v211, v225, s53, -v193
	v_fma_f32 v212, v224, s52, v192
	v_fma_f32 v213, v225, s53, v193
	v_fma_f32 v192, v224, s12, -v192
	v_fma_f32 v193, v225, s12, -v193
	s_mov_b32 s12, s29
	v_fma_f32 v50, v90, v18, v39
	v_fma_f32 v51, v91, v19, v38
	v_fma_f32 v18, v90, v18, -v39
	v_fma_f32 v19, v91, v19, -v38
	v_mul_f32_e64 v70, v70, s12
	v_mul_f32_e64 v71, v71, s12
	v_mov_b32_e32 v73, v31
	v_mov_b32_e32 v26, v40
	v_mov_b32_e32 v47, v23
	v_mov_b32_e32 v18, v50
	v_fma_f32 v70, v78, s38, v70
	v_fma_f32 v71, v79, s39, v71
	v_add_f32 v38, v72, v46
	v_add_f32 v39, v73, v47
	v_add_f32 v78, v26, v18
	v_add_f32 v79, v27, v19
	v_pk_mov_b32 v[30:31], v[30:31], v[40:41] op_sel:[1,0]
	v_pk_mov_b32 v[22:23], v[22:23], v[50:51] op_sel:[1,0]
	v_mov_b32_e32 v73, v27
	v_add_f32_e64 v22, v30, -v22
	v_add_f32_e64 v23, v31, -v23
	v_mov_b32_e32 v47, v19
	v_add_f32_e64 v26, v38, -v78
	v_add_f32_e64 v27, v39, -v79
	v_add_f32_e64 v18, v72, -v46
	v_add_f32_e64 v19, v73, -v47
	v_sub_f32_e32 v40, v22, v23
	v_fma_f32 v30, v26, 0, -v27
	v_fma_f32 v31, v27, 0, -v26
	v_fma_f32 v253, v26, 0, v27
	v_fma_f32 v27, v27, 0, v26
	v_mov_b32_e32 v26, v253
	v_add_f32 v46, v18, v19
	v_add_f32 v47, v18, v19
	v_mul_f32_e32 v26, 0x3f3504f3, v40
	v_mul_f32 v44, v44, v16
	v_mul_f32 v45, v45, v16
	v_mov_b32_e32 v31, v27
	v_fma_f32 v27, v47, s25, -v26
	v_fma_f32 v26, v46, s24, -v26
	v_fma_f32 v46, v42, v17, -v44
	v_fma_f32 v47, v43, v17, -v45
	v_fma_f32 v16, v42, v17, v44
	v_fma_f32 v17, v43, v17, v45
	v_mov_b32_e32 v43, v5
	v_pk_mov_b32 v[4:5], v[12:13], v[4:5] op_sel:[1,0]
	v_mov_b32_e32 v42, v12
	v_mul_f32 v12, v76, v4
	v_mul_f32 v13, v77, v5
	v_mov_b32_e32 v16, v46
	v_fma_f32 v12, v74, v42, v12
	v_fma_f32 v13, v75, v43, v13
	v_mul_f32 v42, v76, v42
	v_mul_f32 v43, v77, v43
	v_add_f32 v2, v2, v52
	v_add_f32 v3, v3, v53
	v_fma_f32 v4, v74, v4, -v42
	v_fma_f32 v5, v75, v5, -v43
	v_mul_f32 v42, v84, v8
	v_mul_f32 v43, v85, v9
	v_add_f32 v32, v56, v32
	v_add_f32 v33, v57, v33
	v_fma_f32 v44, -v82, v8, v43
	v_fma_f32 v45, -v83, v9, v42
	v_fma_f32 v8, v82, v8, v43
	v_fma_f32 v9, v83, v9, v42
	v_add_f32 v42, v13, v4
	v_add_f32 v43, v12, v5
	v_mov_b32_e32 v45, v9
	v_add_f32 v50, v16, v44
	v_add_f32 v51, v17, v45
	v_mov_b32_e32 v16, v13
	v_mov_b32_e32 v8, v4
	v_pk_mov_b32 v[4:5], v[4:5], v[46:47] op_sel:[1,0]
	v_mov_b32_e32 v13, v44
	v_add_f32_e64 v8, v16, -v8
	v_add_f32_e64 v9, v17, -v9
	v_add_f32_e64 v4, v4, -v12
	v_add_f32_e64 v5, v5, -v13
	v_add_f32 v12, v42, v50
	v_add_f32 v13, v43, v51
	v_add_f32_e64 v16, v42, -v50
	v_add_f32_e64 v17, v43, -v51
	v_sub_f32_e32 v42, v4, v5
	v_add_f32_e32 v44, v8, v9
	v_mul_f32_e32 v43, 0x3f6c835e, v42
	v_mul_f32_e32 v45, 0x3ec3ef15, v44
	v_mul_f32_e32 v46, 0x3ec3ef15, v42
	v_mul_f32_e32 v50, 0x3f6c835e, v44
	v_mul_f32_e32 v42, 0x3f3504f3, v17
	v_mul_f32_e32 v44, 0x3f3504f3, v16
	v_pk_mov_b32 v[52:53], v[28:29], v[14:15] op_sel:[1,0]
	v_mov_b32_e32 v56, v7
	v_mov_b32_e32 v57, v11
	v_mov_b32_e32 v29, v15
	v_mov_b32_e32 v7, v10
	v_add_f32_e64 v253, v8, -v9
	v_add_f32_e64 v9, v8, -v9
	v_mov_b32_e32 v8, v253
	v_add_f32 v52, v52, v56
	v_add_f32 v53, v53, v57
	v_add_f32 v6, v28, v6
	v_add_f32 v7, v29, v7
	v_add_f32 v253, v4, v5
	v_add_f32 v5, v4, v5
	v_mov_b32_e32 v4, v253
	v_mul_f32_e64 v8, v8, s46
	v_mul_f32_e64 v9, v9, s47
	v_add_f32_e32 v16, v42, v44
	v_fma_f32 v17, v17, s25, -v44
	v_mov_b32_e32 v44, v24
	v_mov_b32_e32 v51, v25
	v_mov_b32_e32 v24, v54
	v_mov_b32_e32 v25, v18
	v_mov_b32_e32 v18, v68
	s_mov_b32 s50, s24
	s_mov_b32 s51, s26
	v_add_f32 v10, v52, v6
	v_add_f32 v11, v53, v7
	v_add_f32_e64 v6, v52, -v6
	v_add_f32_e64 v7, v53, -v7
	v_fma_f32 v14, v4, s26, v8
	v_fma_f32 v15, v5, s27, v9
	v_fma_f32 v4, v4, s26, -v8
	v_fma_f32 v5, v5, s27, -v9
	v_add_f32_e64 v18, v24, -v18
	v_add_f32_e64 v19, v25, -v19
	v_pk_mov_b32 v[24:25], v[68:69], v[22:23] op_sel:[1,0]
	v_mov_b32_e32 v22, v55
	v_fma_f32 v182, v172, s50, -v178
	v_fma_f32 v183, v173, s51, -v179
	v_fma_f32 v178, v172, s50, v178
	v_fma_f32 v179, v173, s51, v179
	s_mov_b32 s50, s27
	s_mov_b32 s51, s25
	v_add_f32_e64 v40, v2, -v33
	v_add_f32_e64 v41, v3, -v32
	v_mul_f32_e32 v4, 0x3f3504f3, v6
	v_add_f32 v28, v38, v78
; FFT_HD cf2 mk2(float x, float y) { return (cf2){x, y}; }
; FFT_HD cf2 cmul(cf2 a, cf2 b) { return mk2(a.x * b.x - a.y * b.y, a.x * b.y + a.y * b.x); }
; FFT_HD cf2 cmulc(cf2 a, cf2 b) { return mk2(a.x * b.x + a.y * b.y, a.y * b.x - a.x * b.y); }
; template <bool INV> FFT_HD void dft16(cf2 (&x)[16]) {
;     const float C1 = 0.9238795325112867f, S1 = 0.3826834323650898f, H = 0.7071067811865476f;
; #pragma unroll
;     for (int b = 0; b < 4; ++b) dft4<INV>(x[b], x[4 + b], x[8 + b], x[12 + b]);
;     const float s = INV ? -1.f : 1.f;
;     x[4 + 1] = cmul(x[4 + 1], mk2(C1, -s * S1)); x[8 + 1] = cmul(x[8 + 1], mk2(H, -s * H));   x[12 + 1] = cmul(x[12 + 1], mk2(S1, -s * C1));
;     x[4 + 2] = cmul(x[4 + 2], mk2(H, -s * H));   x[8 + 2] = cmul(x[8 + 2], mk2(0.f, -s));     x[12 + 2] = cmul(x[12 + 2], mk2(-H, -s * H));
;     x[4 + 3] = cmul(x[4 + 3], mk2(S1, -s * C1)); x[8 + 3] = cmul(x[8 + 3], mk2(-H, -s * H));  x[12 + 3] = cmul(x[12 + 3], mk2(-C1, s * S1));
; #pragma unroll
;     for (int c = 0; c < 4; ++c) dft4<INV>(x[4 * c], x[4 * c + 1], x[4 * c + 2], x[4 * c + 3]);
; #pragma unroll
;     for (int c = 0; c < 4; ++c)
; #pragma unroll
;         for (int d = c + 1; d < 4; ++d) { const cf2 t = x[4 * c + d]; x[4 * c + d] = x[4 * d + c]; x[4 * d + c] = t; }
; }
; template <bool INV, int lS, class ZP> FFT_HD void fft_r16_pass(ZP z, int tid) {
;     ...
;         for (int j = 0; j < 16; ++j) z[pb0 + j * STEP] = x[j];
;         if (INV) {
; #pragma unroll
;             for (int j = 1; j < 16; ++j) y[j] = cmulc(y[j], tw[j]);
;         }
;         dft16<INV>(y);
;         if (!INV) {
; #pragma unroll
;             for (int j = 1; j < 16; ++j) y[j] = cmul(y[j], tw[j]);
;         }
; #pragma unroll
;         for (int j = 0; j < 16; ++j) z[pb1 + j * STEP] = y[j];
	v_add_f32 v29, v39, v79
	v_add_f32 v2, v2, v33
	v_add_f32 v3, v3, v32
	v_add_f32 v22, v24, v22
	v_add_f32 v23, v25, v23
	v_mov_b32_e32 v15, v5
	v_add_f32_e64 v8, v12, -v10
	v_add_f32_e64 v9, v13, -v11
	v_fma_f32 v5, v7, s53, -v4
	v_fma_f32 v4, v7, s52, -v4
	v_add_f32_e64 v6, v2, -v28
	v_add_f32_e64 v7, v3, -v29
	v_add_f32 v10, v12, v10
	v_add_f32 v11, v13, v11
	v_add_f32 v2, v2, v28
	v_add_f32 v3, v3, v29
	v_mul_f32_e64 v24, v22, s50
	v_mul_f32_e64 v25, v23, s51
	v_mul_f32_e64 v22, v22, s36
	v_mul_f32_e64 v23, v23, s37
	v_add_f32 v12, v2, v11
	v_add_f32 v13, v3, v10
	v_add_f32_e64 v2, v2, -v11
	v_add_f32_e64 v3, v3, -v10
	v_add_f32_e64 v10, v6, -v8
	v_add_f32_e64 v11, v7, -v9
	v_add_f32 v6, v6, v8
	v_add_f32 v7, v7, v9
	v_mov_b32_e32 v42, v20
	v_mov_b32_e32 v47, v21
	v_fma_f32 v22, v18, s50, -v22
	v_fma_f32 v23, v19, s51, -v23
	v_mov_b32_e32 v207, v174
	v_mov_b32_e32 v8, v10
	v_mov_b32_e32 v9, v7
	v_mov_b32_e32 v7, v11
	v_add_f32_e64 v10, v42, -v44
	v_add_f32_e64 v11, v43, -v45
	v_add_f32 v20, v46, v50
	v_add_f32 v21, v47, v51
	v_pk_mov_b32 v[28:29], v[22:23], v[22:23] op_sel:[1,0]
	v_fma_f32 v18, v18, s36, v24
	v_fma_f32 v19, v19, s37, v25
	v_mul_f32_e64 v174, v206, s36
	v_mul_f32_e64 v175, v207, s37
	v_pk_mov_b32 v[172:173], v[202:203], v[172:173] op_sel:[1,0]
	v_add_f32_e64 v253, v10, -v23
	v_add_f32_e64 v23, v11, -v22
	v_mov_b32_e32 v22, v253
	v_add_f32_e64 v24, v20, -v18
	v_add_f32_e64 v25, v21, -v19
	v_pk_mov_b32 v[32:33], v[10:11], v[20:21] op_sel:[1,0]
	v_pk_mov_b32 v[38:39], v[28:29], v[18:19] op_sel:[1,0]
	v_mov_b32_e32 v11, v21
	v_mov_b32_e32 v29, v19
	v_mov_b32_e32 v183, v179
	v_fma_f32 v172, v172, s50, -v174
	v_fma_f32 v173, v173, s51, -v175
	v_mov_b32_e32 v174, v186
	v_mov_b32_e32 v175, v204
	v_add_f32 v10, v10, v28
	v_add_f32 v11, v11, v29
	v_add_f32_e64 v20, v22, -v24
	v_add_f32_e64 v21, v23, -v25
	v_add_f32 v28, v24, v22
	v_add_f32 v29, v25, v23
	v_add_f32_e64 v22, v24, -v22
	v_add_f32_e64 v23, v25, -v23
	v_mov_b32_e32 v187, v171
	v_pk_mov_b32 v[178:179], v[178:179], v[170:171] op_sel:[1,0]
	v_pk_mov_b32 v[214:215], v[210:211], v[212:213] op_sel:[1,0]
	v_mov_b32_e32 v213, v192
	v_mov_b32_e32 v210, v193
	v_add_f32 v170, v170, v172
	v_add_f32 v171, v171, v173
	v_add_f32 v174, v182, v174
	v_add_f32 v175, v183, v175
	v_mov_b32_e32 v183, v173
	v_mov_b32_e32 v205, v172
	v_mov_b32_e32 v21, v29
	v_mov_b32_e32 v29, v23
	v_add_f32_e64 v22, v40, -v30
	v_add_f32_e64 v23, v41, -v31
	v_add_f32_e64 v24, v16, -v4
	v_add_f32_e64 v25, v17, -v5
	v_add_f32 v30, v40, v30
	v_add_f32 v31, v41, v31
	v_add_f32 v4, v16, v4
	v_add_f32 v5, v17, v5
	v_add_f32_e64 v180, v180, -v200
	v_add_f32_e64 v181, v181, -v201
	v_add_f32_e64 v220, v228, -v220
	v_add_f32_e64 v221, v229, -v221
	v_add_f32 v214, v192, v214
	v_add_f32 v215, v193, v215
	v_add_f32_e64 v192, v212, -v210
	v_add_f32_e64 v193, v213, -v211
	v_add_f32 v202, v170, v174
	v_add_f32 v203, v171, v175
	v_mov_b32_e32 v206, v174
	v_mov_b32_e32 v207, v171
	v_mov_b32_e32 v171, v175
	v_add_f32_e64 v174, v186, -v182
	v_add_f32_e64 v175, v187, -v183
	v_add_f32_e64 v172, v178, -v204
	v_add_f32_e64 v173, v179, -v205
	v_add_f32 v32, v32, v38
	v_add_f32 v33, v33, v39
	v_add_f32 v16, v30, v5
	v_add_f32 v17, v31, v4
	v_add_f32_e64 v253, v30, -v5
	v_add_f32_e64 v5, v31, -v4
	v_mov_b32_e32 v4, v253
	v_add_f32_e64 v30, v22, -v24
	v_add_f32_e64 v31, v23, -v25
	v_add_f32 v22, v22, v24
	v_add_f32 v23, v23, v25
	v_add_f32_e64 v200, v190, -v181
	v_add_f32_e64 v201, v191, -v180
	v_add_f32 v253, v190, v181
	v_add_f32 v181, v191, v180
	v_mov_b32_e32 v180, v253
	v_add_f32_e64 v222, v208, -v221
	v_add_f32_e64 v223, v209, -v220
	v_add_f32 v208, v208, v221
	v_add_f32 v209, v209, v220
	v_add_f32_e64 v210, v198, -v192
	v_add_f32_e64 v211, v199, -v193
	v_add_f32 v192, v198, v192
	v_add_f32 v193, v199, v193
	v_add_f32_e64 v178, v174, -v172
	v_add_f32_e64 v179, v175, -v173
	v_add_f32 v172, v174, v172
	v_add_f32 v173, v175, v173
	v_add_f32 v18, v10, v32
	v_add_f32 v19, v11, v33
	v_add_f32_e64 v10, v10, -v32
	v_add_f32_e64 v11, v11, -v33
	v_mov_b32_e32 v24, v30
	v_mov_b32_e32 v25, v23
	v_mov_b32_e32 v23, v31
	v_add_f32_e64 v30, v48, -v26
	v_add_f32_e64 v31, v49, -v27
	v_add_f32_e64 v32, v14, -v70
	v_add_f32_e64 v33, v15, -v71
	v_add_f32 v26, v48, v26
	v_add_f32 v27, v49, v27
	v_add_f32 v14, v14, v70
	v_add_f32 v15, v15, v71
	v_mov_b32_e32 v191, v181
	v_mov_b32_e32 v221, v209
	v_mov_b32_e32 v199, v193
	v_mov_b32_e32 v175, v173
	v_mov_b32_e32 v181, v201
	v_mov_b32_e32 v209, v223
	v_mov_b32_e32 v193, v211
	v_mov_b32_e32 v173, v179
	v_add_f32 v38, v26, v15
	v_add_f32 v39, v27, v14
	v_add_f32_e64 v253, v26, -v15
	v_add_f32_e64 v15, v27, -v14
	v_mov_b32_e32 v14, v253
	v_add_f32_e64 v26, v30, -v32
	v_add_f32_e64 v27, v31, -v33
	v_add_f32 v30, v30, v32
	v_add_f32 v31, v31, v33
	v_mov_b32_e32 v190, v200
	v_mov_b32_e32 v220, v222
	v_add_f32 v224, v188, v214
	v_add_f32 v225, v189, v215
	v_add_f32_e64 v188, v188, -v214
	v_add_f32_e64 v189, v189, -v215
	v_mov_b32_e32 v198, v210
	v_add_f32_e64 v170, v206, -v170
	v_add_f32_e64 v171, v207, -v171
	v_mov_b32_e32 v174, v178
	ds_write2_b64 v65, v[218:219], v[184:185] offset1:4
	ds_write2_b64 v65, v[224:225], v[202:203] offset0:8 offset1:12
	ds_write2_b64 v65, v[190:191], v[220:221] offset0:16 offset1:20
	ds_write2_b64 v65, v[198:199], v[174:175] offset0:24 offset1:28
	ds_write2_b64 v65, v[216:217], v[176:177] offset0:32 offset1:36
	ds_write2_b64 v65, v[188:189], v[170:171] offset0:40 offset1:44
	ds_write2_b64 v65, v[180:181], v[208:209] offset0:48 offset1:52
	ds_write2_b64 v65, v[192:193], v[172:173] offset0:56 offset1:60
	v_mov_b32_e32 v32, v26
	v_mov_b32_e32 v33, v31
	v_mov_b32_e32 v31, v27
	ds_write2_b64 v60, v[12:13], v[18:19] offset1:4
	ds_write2_b64 v60, v[16:17], v[38:39] offset0:8 offset1:12
	ds_write2_b64 v60, v[8:9], v[20:21] offset0:16 offset1:20
	ds_write2_b64 v60, v[24:25], v[32:33] offset0:24 offset1:28
	ds_write2_b64 v60, v[2:3], v[10:11] offset0:32 offset1:36
	ds_write2_b64 v60, v[4:5], v[14:15] offset0:40 offset1:44
	ds_write2_b64 v60, v[6:7], v[28:29] offset0:48 offset1:52
	ds_write2_b64 v60, v[22:23], v[30:31] offset0:56 offset1:60
	s_waitcnt lgkmcnt(0)
	s_barrier
; __device__ __forceinline__ unsigned cvt_pk_bf16(float lo, float hi) { unsigned r; asm volatile("v_cvt_pk_bf16_f32 %0, %1, %2" : "=v"(r) : "v"(lo), "v"(hi)); return r; }
; template <int BANK, int WAITN> __device__ __forceinline__ void bg_finish1(BgState& b) {
;     if (WAITN == 32) asm volatile("s_waitcnt vmcnt(32)" ::: "memory"); else asm volatile("s_waitcnt vmcnt(0)" ::: "memory");
;     asm volatile("" : BG_TIE16(BANK * 32) :: "memory");
;     asm volatile("" : BG_TIE16(BANK * 32 + 16) :: "memory");
;     bf16_t* dst = b.dst[BANK];
;     if (dst != nullptr) {
; #pragma unroll
;         for (int c = 0; c < 4; ++c) { u32x4 w;
;             w.x = cvt_pk_bf16(b.r[(BANK * 8 + 0) * 4 + c], b.r[(BANK * 8 + 1) * 4 + c]); w.y = cvt_pk_bf16(b.r[(BANK * 8 + 2) * 4 + c], b.r[(BANK * 8 + 3) * 4 + c]);
;             w.z = cvt_pk_bf16(b.r[(BANK * 8 + 4) * 4 + c], b.r[(BANK * 8 + 5) * 4 + c]); w.w = cvt_pk_bf16(b.r[(BANK * 8 + 6) * 4 + c], b.r[(BANK * 8 + 7) * 4 + c]);
;             bf16_t* dp = dst + (c & 1) * 512 + (c >> 1) * b.o2[BANK];
;             asm volatile("global_store_dwordx4 %0, %1, off\n\ts_nop 1" :: "v"(dp), "v"(w) : "memory"); }
;     }
; }
	s_waitcnt vmcnt(32)
	v_cmp_ne_u64_e32 vcc, 0, v[34:35]
	s_and_saveexec_b64 s[46:47], vcc
	s_cbranch_execz .LBB0_729
	v_cvt_pk_bf16_f32 v2, v153, v155
	v_cvt_pk_bf16_f32 v3, v154, v157
	v_cvt_pk_bf16_f32 v4, v156, v159
	v_cvt_pk_bf16_f32 v5, v158, v160
	v_lshl_add_u64 v[6:7], v[34:35], 0, s[22:23]
	global_store_dwordx4 v[34:35], v[2:5], off nt
	s_nop 1
	v_cvt_pk_bf16_f32 v2, v145, v147
	v_cvt_pk_bf16_f32 v3, v146, v149
	v_cvt_pk_bf16_f32 v4, v148, v151
	v_cvt_pk_bf16_f32 v5, v150, v152
	s_lshl_b32 s12, s48, 1
	global_store_dwordx4 v[6:7], v[2:5], off nt
	s_nop 1
	v_cvt_pk_bf16_f32 v2, v137, v139
	v_cvt_pk_bf16_f32 v3, v138, v141
	v_cvt_pk_bf16_f32 v4, v140, v143
	v_cvt_pk_bf16_f32 v5, v142, v144
	v_lshl_add_u64 v[8:9], v[34:35], 0, s[12:13]
	global_store_dwordx4 v[8:9], v[2:5], off nt
	s_nop 1
	v_cvt_pk_bf16_f32 v2, v129, v131
	v_cvt_pk_bf16_f32 v3, v130, v133
	v_cvt_pk_bf16_f32 v4, v132, v135
	v_cvt_pk_bf16_f32 v5, v134, v136
	v_lshl_add_u64 v[6:7], v[6:7], 0, s[12:13]
	global_store_dwordx4 v[6:7], v[2:5], off nt
	s_nop 1

; __device__ __forceinline__ KP kparams() { KP q = (KP)__builtin_amdgcn_kernarg_segment_ptr(); asm volatile("" : "+s"(q)); return q; }
; FFT_HD cf2 mk2(float x, float y) { return (cf2){x, y}; }
; FFT_HD void fft_sincos(float frac, float& s, float& c) { s = __builtin_amdgcn_sinf(frac); c = __builtin_amdgcn_cosf(frac); }
; FFT_HD cf2 cmul(cf2 a, cf2 b) { return mk2(a.x * b.x - a.y * b.y, a.x * b.y + a.y * b.x); }
; template <int BANK> __device__ __forceinline__ void bg_issue1(BgState& b, int wg, int NW, int lane) {
;     KP kp = kparams();
;     const float* src; int ldS; bf16_t* dst; int o2;
;     bg_decode(b.st, wg, NW, lane, kp, src, ldS, dst, o2);
;     b.dst[BANK] = dst; b.o2[BANK] = o2;
;     asm volatile("s_nop 6" ::: "memory");
; #pragma unroll
;     for (int i = 0; i < 8; ++i) { const float* p = src + (size_t)i * ldS;
;         asm volatile("global_load_dword %0, %4, off\n\tglobal_load_dword %1, %4, off offset:256\n\tglobal_load_dword %2, %4, off offset:512\n\tglobal_load_dword %3, %4, off offset:768"
;                      : "=&v"(b.r[(BANK * 8 + i) * 4 + 0]), "=&v"(b.r[(BANK * 8 + i) * 4 + 1]), "=&v"(b.r[(BANK * 8 + i) * 4 + 2]), "=&v"(b.r[(BANK * 8 + i) * 4 + 3]) : "v"(p) : "memory"); }
;     b.st += 1;
; }
; FFT_HD void fft_gen_tw(float frac, cf2 (&tw)[16]) {
;     float sn, cs; fft_sincos(frac, sn, cs);
;     tw[1] = mk2(cs, -sn);
;     tw[2] = cmul(tw[1], tw[1]); tw[3] = cmul(tw[2], tw[1]); tw[4] = cmul(tw[2], tw[2]); tw[5] = cmul(tw[4], tw[1]); tw[6] = cmul(tw[4], tw[2]); tw[7] = cmul(tw[4], tw[3]);
;     tw[8] = cmul(tw[4], tw[4]);
; #pragma unroll
;     for (int j = 9; j < 16; ++j) tw[j] = cmul(tw[8], tw[j - 8]);
; }
.LBB0_739:
	s_nop 6
	s_lshl_b32 s12, s48, 2
	v_and_b32_e32 v24, 63, v128
	global_load_dword v153, v[2:3], off nt
	global_load_dword v145, v[2:3], off offset:256 nt
	global_load_dword v137, v[2:3], off offset:512 nt
	global_load_dword v129, v[2:3], off offset:768 nt
	v_lshl_add_u64 v[2:3], v[2:3], 0, s[12:13]
	v_cvt_f32_ubyte0_e32 v4, v24
	global_load_dword v155, v[2:3], off nt
	global_load_dword v147, v[2:3], off offset:256 nt
	global_load_dword v139, v[2:3], off offset:512 nt
	global_load_dword v131, v[2:3], off offset:768 nt
	v_lshl_add_u64 v[2:3], v[2:3], 0, s[12:13]
	v_mul_f32_e32 v4, 0x3a800000, v4
	global_load_dword v154, v[2:3], off nt
	global_load_dword v146, v[2:3], off offset:256 nt
	global_load_dword v138, v[2:3], off offset:512 nt
	global_load_dword v130, v[2:3], off offset:768 nt
	v_lshl_add_u64 v[2:3], v[2:3], 0, s[12:13]
	v_sin_f32_e32 v186, v4
	global_load_dword v157, v[2:3], off nt
	global_load_dword v149, v[2:3], off offset:256 nt
	global_load_dword v141, v[2:3], off offset:512 nt
	global_load_dword v133, v[2:3], off offset:768 nt
	v_lshl_add_u64 v[2:3], v[2:3], 0, s[12:13]
	v_cos_f32_e32 v78, v4
	global_load_dword v156, v[2:3], off nt
	global_load_dword v148, v[2:3], off offset:256 nt
	global_load_dword v140, v[2:3], off offset:512 nt
	global_load_dword v132, v[2:3], off offset:768 nt
	v_lshl_add_u64 v[2:3], v[2:3], 0, s[12:13]
	global_load_dword v159, v[2:3], off nt
	global_load_dword v151, v[2:3], off offset:256 nt
	global_load_dword v143, v[2:3], off offset:512 nt
	global_load_dword v135, v[2:3], off offset:768 nt
	v_lshl_add_u64 v[2:3], v[2:3], 0, s[12:13]
	global_load_dword v158, v[2:3], off nt
	global_load_dword v150, v[2:3], off offset:256 nt
	global_load_dword v142, v[2:3], off offset:512 nt
	global_load_dword v134, v[2:3], off offset:768 nt
	v_lshl_add_u64 v[2:3], v[2:3], 0, s[12:13]
	v_xor_b32_e32 v79, 0x80000000, v186
	global_load_dword v160, v[2:3], off nt
	global_load_dword v152, v[2:3], off offset:256 nt
	global_load_dword v144, v[2:3], off offset:512 nt
	global_load_dword v136, v[2:3], off offset:768 nt
	v_mov_b32_e32 v187, v78
	v_mov_b32_e32 v2, v186
	v_mov_b32_e32 v3, v79
	v_mul_f32 v2, v186, v2
	v_mul_f32 v3, v187, v3
	s_mov_b32 s48, s27
	v_fma_f32 v38, v78, v78, -v2
	v_fma_f32 v39, v78, v79, -v3
	v_fma_f32 v40, v78, v78, v2
	v_fma_f32 v41, v78, v79, v3
	v_pk_mov_b32 v[4:5], v[40:41], v[38:39] op_sel:[1,0]
	v_mov_b32_e32 v2, v38
	v_mov_b32_e32 v3, v41
	v_mul_f32 v10, v41, v4
	v_mul_f32 v11, v41, v5
	v_mov_b32_e32 v79, v186
	v_fma_f32 v56, v38, v2, -v10
	v_fma_f32 v57, v38, v3, -v11
	v_fma_f32 v74, v38, v2, v10
	v_fma_f32 v75, v38, v3, v11
	v_mov_b32_e32 v68, v56
	v_mov_b32_e32 v69, v75
	v_mul_f32 v18, v68, v68
	v_mul_f32 v19, v69, v69
	v_mul_f32 v20, v68, v75
	v_mul_f32 v21, v69, v74
	v_mov_b32_e32 v22, v18
	v_mov_b32_e32 v23, v20
	v_pk_mov_b32 v[18:19], v[18:19], v[20:21] op_sel:[1,0]
	v_mul_f32 v6, v78, v2
	v_mul_f32 v7, v79, v3
	v_add_f32_e64 v48, v22, -v18
	v_add_f32_e64 v49, v23, -v19
	v_add_f32 v52, v22, v18
	v_add_f32 v53, v23, v19
	v_mul_f32 v8, v186, v2
	v_mul_f32 v9, v187, v3
	v_mov_b32_e32 v188, v48
	v_mov_b32_e32 v189, v53
	v_mul_f32 v14, v2, v68
	v_mul_f32 v15, v3, v69
	v_mul_f32 v16, v4, v68
	v_mul_f32 v17, v5, v69
	v_mul_f32 v190, v2, v188
	v_mul_f32 v191, v3, v189
	v_mul_f32 v192, v4, v188
	v_mul_f32 v193, v5, v189
	v_mov_b32_e32 v2, v6
	v_mov_b32_e32 v3, v9
	v_pk_mov_b32 v[4:5], v[6:7], v[8:9] op_sel:[1,0]
	v_mul_f32 v10, v78, v68
	v_mul_f32 v11, v79, v69
	v_add_f32 v72, v2, v4
	v_add_f32 v73, v3, v5
	v_add_f32_e64 v54, v2, -v4
	v_add_f32_e64 v55, v3, -v5
	v_mul_f32 v12, v186, v68
	v_mul_f32 v13, v187, v69
	v_mov_b32_e32 v2, v72
	v_mov_b32_e32 v3, v55
	v_pk_mov_b32 v[4:5], v[54:55], v[72:73] op_sel:[1,0]
	v_mul_f32 v6, v68, v2
	v_mul_f32 v7, v69, v3
	v_mul_f32 v8, v68, v4
	v_mul_f32 v9, v69, v5
	v_mul_f32 v100, v2, v188
	v_mul_f32 v101, v3, v189
	v_mul_f32 v98, v4, v188
	v_mul_f32 v99, v5, v189
	v_mov_b32_e32 v2, v10
	v_mov_b32_e32 v3, v13
	v_pk_mov_b32 v[4:5], v[10:11], v[12:13] op_sel:[1,0]
	v_pk_mov_b32 v[70:71], v[74:75], v[56:57] op_sel:[1,0]
	v_add_f32 v202, v2, v4
	v_add_f32 v203, v3, v5
	v_add_f32_e64 v204, v2, -v4
	v_add_f32_e64 v205, v3, -v5
	v_mov_b32_e32 v2, v14
	v_mov_b32_e32 v3, v16
	v_mov_b32_e32 v16, v15
	v_add_f32_e64 v46, v2, -v16
	v_add_f32_e64 v47, v3, -v17
	v_add_f32 v50, v2, v16
	v_add_f32 v51, v3, v17
	v_mov_b32_e32 v2, v46
	v_mov_b32_e32 v3, v51
	v_mul_f32 v210, v188, v2
	v_mul_f32 v211, v189, v3
	v_pk_mov_b32 v[2:3], v[50:51], v[46:47] op_sel:[1,0]
	v_lshlrev_b32_e32 v5, 3, v24
	v_mul_f32 v212, v188, v2
	v_mul_f32 v213, v189, v3
	v_mov_b32_e32 v2, v6
	v_mov_b32_e32 v3, v8
	v_mov_b32_e32 v8, v7
	v_add_f32_e64 v76, v2, -v8
	v_add_f32_e64 v77, v3, -v9
	v_add_f32 v80, v2, v8
	v_add_f32 v81, v3, v9
	v_mov_b32_e32 v2, v76
	v_mov_b32_e32 v3, v81
	v_mul_f32 v214, v188, v2
	v_mul_f32 v215, v189, v3
	v_pk_mov_b32 v[2:3], v[80:81], v[76:77] op_sel:[1,0]
	v_mov_b32_e32 v42, v202
	v_mul_f32 v216, v188, v2
	v_mul_f32 v217, v189, v3
	v_and_b32_e32 v2, 0xfffffc00, v169
	v_lshlrev_b32_e32 v4, 3, v2
	v_add_u32_e32 v3, 0x2000, v2
	v_add3_u32 v4, 0, v4, v5
	v_ashrrev_i32_e32 v2, 2, v2
	v_add_u32_e32 v238, v4, v2
	v_add_u32_e32 v239, 0x800, v238
	ds_read2_b64 v[170:173], v238 offset1:66
	ds_read2_b64 v[82:85], v238 offset0:132 offset1:198
	ds_read2_b64 v[86:89], v239 offset0:8 offset1:74
	ds_read2_b64 v[90:93], v239 offset0:140 offset1:206
	v_add_u32_e32 v240, 0x1000, v238
	ds_read2_b64 v[94:97], v240 offset0:16 offset1:82
	ds_read2_b64 v[174:177], v240 offset0:148 offset1:214
	v_mov_b32_e32 v43, v205
	s_waitcnt lgkmcnt(3)
; FFT_HD cf2 mk2(float x, float y) { return (cf2){x, y}; }
; FFT_HD cf2 cmul(cf2 a, cf2 b) { return mk2(a.x * b.x - a.y * b.y, a.x * b.y + a.y * b.x); }
; FFT_HD cf2 cmulc(cf2 a, cf2 b) { return mk2(a.x * b.x + a.y * b.y, a.y * b.x - a.x * b.y); }
; template <bool INV> FFT_HD void dft16(cf2 (&x)[16]) {
;     const float C1 = 0.9238795325112867f, S1 = 0.3826834323650898f, H = 0.7071067811865476f;
; #pragma unroll
;     for (int b = 0; b < 4; ++b) dft4<INV>(x[b], x[4 + b], x[8 + b], x[12 + b]);
;     const float s = INV ? -1.f : 1.f;
;     x[4 + 1] = cmul(x[4 + 1], mk2(C1, -s * S1)); x[8 + 1] = cmul(x[8 + 1], mk2(H, -s * H));   x[12 + 1] = cmul(x[12 + 1], mk2(S1, -s * C1));
;     x[4 + 2] = cmul(x[4 + 2], mk2(H, -s * H));   x[8 + 2] = cmul(x[8 + 2], mk2(0.f, -s));     x[12 + 2] = cmul(x[12 + 2], mk2(-H, -s * H));
;     x[4 + 3] = cmul(x[4 + 3], mk2(S1, -s * C1)); x[8 + 3] = cmul(x[8 + 3], mk2(-H, -s * H));  x[12 + 3] = cmul(x[12 + 3], mk2(-C1, s * S1));
; template <bool INV, int lS, class ZP> FFT_HD void fft_r16_pass(ZP z, int tid) {
;     ...
;         if (INV) {
; #pragma unroll
;             for (int j = 1; j < 16; ++j) x[j] = cmulc(x[j], tw[j]);
;         }
;         dft16<INV>(x);
;         if (!INV) {
; #pragma unroll
;             for (int j = 1; j < 16; ++j) x[j] = cmul(x[j], tw[j]);
;         }
; #pragma unroll
;         for (int j = 0; j < 16; ++j) z[pb0 + j * STEP] = x[j];
;         if (INV) {
; #pragma unroll
;             for (int j = 1; j < 16; ++j) y[j] = cmulc(y[j], tw[j]);
;         }
;         dft16<INV>(y);
	v_mul_f32 v74, v75, v87
	v_mul_f32 v75, v75, v86
	v_pk_mov_b32 v[44:45], v[204:205], v[202:203] op_sel:[1,0]
	v_fma_f32 v226, v56, v86, v74
	v_fma_f32 v227, v57, v87, v75
	v_fma_f32 v74, v56, v86, -v74
	v_fma_f32 v75, v56, v87, -v75
	v_mov_b32_e32 v227, v75
	v_mul_f32 v74, v205, v89
	v_mul_f32 v75, v205, v88
	v_mul_f32 v218, v41, v83
	v_mul_f32 v219, v41, v82
	v_fma_f32 v204, v202, v88, v74
	v_fma_f32 v205, v202, v89, v75
	v_fma_f32 v203, v202, v89, -v75
	v_fma_f32 v202, v202, v88, -v74
	s_waitcnt lgkmcnt(2)
	v_mul_f32 v74, v51, v91
	v_mul_f32 v75, v51, v90
	v_fma_f32 v220, v38, v82, v218
	v_fma_f32 v221, v38, v83, v219
	v_fma_f32 v228, v46, v90, v74
	v_fma_f32 v229, v46, v91, v75
	v_fma_f32 v230, v46, v90, -v74
	v_fma_f32 v231, v46, v91, -v75
	v_mul_f32 v74, v81, v93
	v_mul_f32 v75, v81, v92
	v_fma_f32 v218, v38, v82, -v218
	v_fma_f32 v219, v38, v83, -v219
	v_fma_f32 v232, v76, v92, v74
	v_fma_f32 v233, v76, v93, v75
	v_fma_f32 v234, v76, v92, -v74
	v_fma_f32 v235, v76, v93, -v75
	s_waitcnt lgkmcnt(1)
	v_mul_f32 v74, v53, v95
	v_mul_f32 v75, v53, v94
	v_mul_f32 v82, v55, v85
	v_mul_f32 v83, v55, v84
	v_fma_f32 v236, v48, v94, v74
	v_fma_f32 v237, v49, v95, v75
	v_fma_f32 v74, v48, v94, -v74
	v_fma_f32 v75, v48, v95, -v75
	v_mul_f32_e32 v54, v186, v53
	v_mov_b32_e32 v237, v75
	v_fma_f32 v74, v78, v188, v54
	v_fma_f32 v75, v79, v189, v54
	v_mul_f32_e32 v54, v78, v53
	v_add_u32_e32 v241, 0x1800, v238
	v_mov_b32_e32 v75, v78
	v_fma_f32 v78, -v186, v188, v54
	v_fma_f32 v79, -v187, v189, v54
	ds_read2_b64 v[178:181], v241 offset0:24 offset1:90
	ds_read2_b64 v[182:185], v241 offset0:156 offset1:222
	v_fma_f32 v222, v72, v84, v82
	v_fma_f32 v223, v72, v85, v83
	v_fma_f32 v224, v72, v84, -v82
	v_fma_f32 v225, v72, v85, -v83
	v_mov_b32_e32 v79, v186
	v_pk_mov_b32 v[84:85], v[96:97], v[172:173] op_sel:[1,0]
	v_mov_b32_e32 v82, v96
	v_mov_b32_e32 v83, v173
	v_mul_f32 v86, v78, v84
	v_mul_f32 v87, v79, v85
	v_mul_f32 v200, v70, v188
	v_mul_f32 v201, v71, v189
	v_fma_f32 v172, v74, v82, v86
	v_fma_f32 v173, v75, v83, v87
	v_mul_f32 v82, v78, v82
	v_mul_f32 v83, v79, v83
	v_add_f32 v88, v192, v193
	v_add_f32 v89, v192, v193
	v_mul_f32 v198, v68, v188
	v_mul_f32 v199, v69, v189
	v_fma_f32 v186, v74, v84, -v82
	v_fma_f32 v187, v75, v85, -v83
	v_add_f32_e64 v86, v190, -v191
	v_add_f32_e64 v87, v190, -v191
	s_waitcnt lgkmcnt(2)
	v_mul_f32 v82, v88, v174
	v_mul_f32 v83, v89, v175
	v_add_f32 v94, v200, v201
	v_add_f32 v95, v200, v201
	v_mul_f32 v206, v188, v42
	v_mul_f32 v207, v189, v43
	v_mul_f32 v208, v188, v44
	v_mul_f32 v209, v189, v45
	v_fma_f32 v188, v86, v174, v83
	v_fma_f32 v189, v87, v175, v82
	v_fma_f32 v174, v86, v174, -v83
	v_fma_f32 v175, v87, v175, -v82
	v_add_f32_e64 v96, v198, -v199
	v_add_f32_e64 v97, v198, -v199
	s_waitcnt lgkmcnt(1)
	v_mul_f32 v82, v94, v178
	v_mul_f32 v83, v95, v179
	v_add_f32_e64 v84, v206, -v207
	v_add_f32_e64 v85, v206, -v207
	v_fma_f32 v190, v96, v178, v83
	v_fma_f32 v191, v97, v179, v82
	v_fma_f32 v253, v96, v178, -v83
	v_fma_f32 v83, v97, v179, -v82
	v_mov_b32_e32 v82, v253
	v_add_f32 v92, v212, v213
	v_add_f32 v93, v212, v213
	v_mov_b32_e32 v191, v83
	v_add_f32 v82, v208, v209
	v_add_f32 v83, v208, v209
	v_mul_f32 v90, v82, v180
	v_mul_f32 v91, v83, v181
	s_waitcnt lgkmcnt(0)
	v_mul_f32 v192, v92, v182
	v_mul_f32 v193, v93, v183
	v_fma_f32 v178, v84, v180, v91
	v_fma_f32 v179, v85, v181, v90
	v_fma_f32 v180, v84, v180, -v91
	v_fma_f32 v181, v85, v181, -v90
	v_add_f32_e64 v90, v210, -v211
	v_add_f32_e64 v91, v210, -v211
	v_mov_b32_e32 v202, v204
	v_mov_b32_e32 v179, v181
	v_fma_f32 v198, v90, v182, v193
	v_fma_f32 v199, v91, v183, v192
	v_fma_f32 v182, v90, v182, -v193
	v_fma_f32 v183, v91, v183, -v192
	v_mov_b32_e32 v221, v219
	v_mov_b32_e32 v230, v228
	v_mov_b32_e32 v189, v175
	v_mov_b32_e32 v182, v198
	v_add_f32 v208, v187, v172
	v_add_f32 v209, v186, v173
	v_add_f32 v210, v202, v178
	v_add_f32 v211, v203, v179
	v_pk_mov_b32 v[204:205], v[172:173], v[204:205] op_sel:[1,0]
	v_mov_b32_e32 v202, v187
	v_mov_b32_e32 v173, v181
	v_ashrrev_i32_e32 v2, 2, v3
	v_mov_b32_e32 v212, v186
	v_add_f32_e64 v172, v202, -v172
	v_add_f32_e64 v173, v203, -v173
	v_add_f32 v186, v220, v188
	v_add_f32 v187, v221, v189
	v_add_f32 v202, v230, v182
	v_add_f32 v203, v231, v183
	v_mov_b32_e32 v221, v231
	v_mov_b32_e32 v189, v183
	v_add3_u32 v60, v4, v2, s71
	v_add_f32 v192, v170, v236
	v_add_f32 v193, v171, v237
	v_add_f32 v200, v226, v190
	v_add_f32 v201, v227, v191
	v_add_f32_e64 v182, v220, -v188
	v_add_f32_e64 v183, v221, -v189
	v_add_f32 v188, v186, v202
	v_add_f32 v189, v187, v203
	v_add_f32_e64 v186, v186, -v202
	v_add_f32_e64 v187, v187, -v203
	v_add_u32_e32 v65, 0x800, v60
	v_add_f32 v206, v192, v200
	v_add_f32 v207, v193, v201
	v_add_f32_e64 v192, v192, -v200
	v_add_f32_e64 v193, v193, -v201
	v_fma_f32 v200, v186, 0, -v187
	v_fma_f32 v201, v187, 0, -v186
	v_fma_f32 v253, v186, 0, v187
	v_fma_f32 v187, v187, 0, v186
	v_mov_b32_e32 v186, v253
	ds_read2_b64 v[2:5], v60 offset1:66
	ds_read2_b64 v[30:33], v60 offset0:132 offset1:198
	ds_read2_b64 v[14:17], v65 offset0:8 offset1:74
	ds_read2_b64 v[22:25], v65 offset0:140 offset1:206
	v_mov_b32_e32 v201, v187
	v_mov_b32_e32 v223, v225
	v_mov_b32_e32 v213, v178
	v_pk_mov_b32 v[174:175], v[174:175], v[198:199] op_sel:[1,0]
	v_pk_mov_b32 v[198:199], v[224:225], v[232:233] op_sel:[1,0]
	v_add_f32_e64 v224, v172, -v173
	v_add_f32_e64 v225, v172, -v173
	v_add_f32 v186, v192, v200
	v_add_f32 v187, v193, v201
	v_add_f32_e64 v192, v192, -v200
	v_add_f32_e64 v193, v193, -v201
	v_mov_b32_e32 v200, v182
	v_mov_b32_e32 v201, v172
	v_mov_b32_e32 v172, v183
	v_add_u32_e32 v67, 0x1000, v60
	v_add_f32_e64 v178, v204, -v212
	v_add_f32_e64 v179, v205, -v213
	v_pk_mov_b32 v[204:205], v[218:219], v[228:229] op_sel:[1,0]
	v_add_f32 v172, v200, v172
	v_add_f32 v173, v201, v173
	v_mov_b32_e32 v200, v214
	v_mov_b32_e32 v201, v100
	v_mov_b32_e32 v100, v215
	ds_read2_b64 v[10:13], v67 offset0:16 offset1:82
	ds_read2_b64 v[26:29], v67 offset0:148 offset1:214
	v_add_f32_e64 v174, v204, -v174
	v_add_f32_e64 v175, v205, -v175
	v_add_f32_e64 v100, v200, -v100
	v_add_f32_e64 v101, v201, -v101
	v_mov_b32_e32 v200, v216
	v_mov_b32_e32 v201, v98
	v_mov_b32_e32 v98, v217
	v_add_u32_e32 v169, 0x1800, v60
	v_sub_f32_e32 v54, v182, v183
	v_add_f32_e64 v190, v226, -v190
	v_add_f32_e64 v191, v227, -v191
	v_add_f32 v226, v178, v179
	v_add_f32 v227, v178, v179
	v_mov_b32_e32 v182, v174
	v_mov_b32_e32 v183, v178
	v_mov_b32_e32 v178, v175
	v_add_f32 v98, v200, v98
	v_add_f32 v99, v201, v99
	s_waitcnt lgkmcnt(3)
; FFT_HD cf2 mk2(float x, float y) { return (cf2){x, y}; }
; FFT_HD cf2 cmul(cf2 a, cf2 b) { return mk2(a.x * b.x - a.y * b.y, a.x * b.y + a.y * b.x); }
; template <bool INV> FFT_HD void dft16(cf2 (&x)[16]) {
;     const float C1 = 0.9238795325112867f, S1 = 0.3826834323650898f, H = 0.7071067811865476f;
; #pragma unroll
;     for (int b = 0; b < 4; ++b) dft4<INV>(x[b], x[4 + b], x[8 + b], x[12 + b]);
;     const float s = INV ? -1.f : 1.f;
;     x[4 + 1] = cmul(x[4 + 1], mk2(C1, -s * S1)); x[8 + 1] = cmul(x[8 + 1], mk2(H, -s * H));   x[12 + 1] = cmul(x[12 + 1], mk2(S1, -s * C1));
;     x[4 + 2] = cmul(x[4 + 2], mk2(H, -s * H));   x[8 + 2] = cmul(x[8 + 2], mk2(0.f, -s));     x[12 + 2] = cmul(x[12 + 2], mk2(-H, -s * H));
;     x[4 + 3] = cmul(x[4 + 3], mk2(S1, -s * C1)); x[8 + 3] = cmul(x[8 + 3], mk2(-H, -s * H));  x[12 + 3] = cmul(x[12 + 3], mk2(-C1, s * S1));
; #pragma unroll
;     for (int c = 0; c < 4; ++c) dft4<INV>(x[4 * c], x[4 * c + 1], x[4 * c + 2], x[4 * c + 3]);
; #pragma unroll
;     for (int c = 0; c < 4; ++c)
; #pragma unroll
;         for (int d = c + 1; d < 4; ++d) { const cf2 t = x[4 * c + d]; x[4 * c + d] = x[4 * d + c]; x[4 * d + c] = t; }
; }
	v_mul_f32 v70, v70, v14
	v_mul_f32 v71, v71, v14
	ds_read2_b64 v[6:9], v169 offset0:24 offset1:90
	ds_read2_b64 v[18:21], v169 offset0:156 offset1:222
	v_add_f32_e32 v73, v174, v175
	v_add_f32 v218, v206, v188
	v_add_f32 v219, v207, v189
	v_add_f32_e64 v188, v206, -v188
	v_add_f32_e64 v189, v207, -v189
	v_add_f32_e64 v170, v170, -v236
	v_add_f32_e64 v171, v171, -v237
	v_pk_mov_b32 v[206:207], v[190:191], v[190:191] op_sel:[1,0]
	v_add_f32_e64 v174, v182, -v178
	v_add_f32_e64 v175, v183, -v179
	v_mul_f32 v200, v99, v177
	v_mul_f32 v201, v99, v176
	v_fma_f32 v56, v56, v15, -v70
	v_fma_f32 v57, v57, v15, -v71
	v_fma_f32 v14, v68, v15, v70
	v_fma_f32 v15, v69, v15, v71
	v_mov_b32_e32 v80, v55
	v_mov_b32_e32 v68, v33
	s_waitcnt lgkmcnt(4)
	v_mov_b32_e32 v69, v25
	v_mul_f32_e32 v213, 0x3f3504f3, v73
	v_add_f32_e64 v220, v170, -v191
	v_add_f32_e64 v221, v171, -v190
	v_add_f32 v253, v170, v191
	v_add_f32 v191, v171, v190
	v_mov_b32_e32 v190, v253
	v_mul_f32_e32 v170, 0x3ec3ef15, v173
	v_mul_f32_e32 v206, 0x3f6c835e, v175
	v_fma_f32 v202, v101, v176, v200
	v_fma_f32 v203, v101, v177, v201
	v_fma_f32 v176, v101, v176, -v200
	v_fma_f32 v177, v101, v177, -v201
	v_mul_f32 v200, v98, v185
	v_mul_f32 v201, v98, v184
	v_mov_b32_e32 v57, v15
	v_mov_b32_e32 v73, v76
	v_mov_b32_e32 v14, v32
	v_mov_b32_e32 v15, v24
	v_mul_f32 v68, v80, v68
	v_mul_f32 v69, v81, v69
	v_add_f32_e64 v170, v170, -v206
	v_add_f32_e64 v171, v171, -v207
	v_mov_b32_e32 v203, v177
	v_fma_f32 v206, v100, v184, v200
	v_fma_f32 v207, v100, v185, v201
	v_fma_f32 v184, v100, v184, -v200
	v_fma_f32 v185, v100, v185, -v201
	v_fma_f32 v14, v72, v14, v68
	v_fma_f32 v15, v73, v15, v69
	v_mov_b32_e32 v68, v25
	v_mov_b32_e32 v69, v33
	v_mov_b32_e32 v25, v32
	s_waitcnt lgkmcnt(3)
	v_mul_f32 v32, v53, v11
	v_mul_f32 v33, v53, v10
	v_mov_b32_e32 v234, v232
	v_mov_b32_e32 v204, v222
	v_mov_b32_e32 v205, v235
	v_mov_b32_e32 v184, v206
	v_add_f32 v200, v222, v202
	v_add_f32 v201, v223, v203
	v_pk_mov_b32 v[176:177], v[176:177], v[206:207] op_sel:[1,0]
	v_mov_b32_e32 v203, v185
	v_fma_f32 v52, v48, v10, v32
	v_fma_f32 v53, v49, v11, v33
	v_fma_f32 v10, v48, v10, -v32
	v_fma_f32 v11, v48, v11, -v33
	v_add_f32 v214, v234, v184
	v_add_f32 v215, v235, v185
	v_add_f32_e64 v176, v198, -v176
	v_add_f32_e64 v177, v199, -v177
	v_add_f32_e64 v184, v204, -v202
	v_add_f32_e64 v185, v205, -v203
	v_mov_b32_e32 v53, v11
	s_waitcnt lgkmcnt(1)
	v_mul_f32 v10, v96, v6
	v_mul_f32 v11, v97, v7
	v_mov_b32_e32 v202, v184
	v_mov_b32_e32 v203, v176
	v_mov_b32_e32 v204, v185
	v_mov_b32_e32 v205, v177
	v_fma_f32 v32, -v94, v6, v11
	v_fma_f32 v33, -v95, v7, v10
	v_fma_f32 v6, v94, v6, v11
	v_fma_f32 v7, v95, v7, v10
	v_mul_f32_e32 v77, 0x3f3504f3, v54
	v_add_f32 v206, v202, v204
	v_add_f32 v207, v203, v205
	v_add_f32_e64 v202, v202, -v204
	v_add_f32_e64 v203, v203, -v205
	v_mov_b32_e32 v33, v7
	v_mov_b32_e32 v7, v28
	s_waitcnt lgkmcnt(0)
	v_mov_b32_e32 v28, v21
	s_mov_b32 s49, s26
	v_sub_f32_e32 v212, v77, v213
	v_fmac_f32_e32 v213, 0x3f3504f3, v54
	v_mov_b32_e32 v207, v203
	v_mul_f32_e32 v54, 0x3f6c835e, v203
	v_mov_b32_e32 v6, v20
	v_mul_f32 v10, v98, v28
	v_mul_f32 v11, v99, v29
	v_add_f32 v180, v208, v210
	v_add_f32 v181, v209, v211
	v_mul_f32_e64 v226, v226, s48
	v_mul_f32_e64 v227, v227, s49
	v_add_f32 v198, v200, v214
	v_add_f32 v199, v201, v215
	v_fma_f32 v204, v206, s14, -v54
	v_fma_f32 v205, v207, s15, -v54
	v_add_f32 v253, v176, v177
	v_add_f32 v177, v176, v177
	v_mov_b32_e32 v176, v253
	v_mov_b32_e32 v54, v81
	v_fma_f32 v10, v100, v6, v10
	v_fma_f32 v11, v101, v7, v11
	v_mul_f32 v6, v98, v6
	v_mul_f32 v7, v99, v7
	v_mov_b32_e32 v221, v191
	v_fma_f32 v228, v224, s26, -v226
	v_fma_f32 v229, v225, s27, -v227
	v_fma_f32 v224, v224, s26, v226
	v_fma_f32 v225, v225, s27, v227
	v_add_f32 v216, v180, v198
	v_add_f32 v217, v181, v199
	v_add_f32_e64 v253, v184, -v185
	v_add_f32_e64 v185, v184, -v185
	v_mov_b32_e32 v184, v253
	v_mul_f32_e64 v176, v176, s26
	v_mul_f32_e64 v177, v177, s27
	v_mov_b32_e32 v77, v72
	v_mul_f32 v24, v54, v24
	v_mul_f32 v25, v55, v25
	v_fma_f32 v6, v100, v28, -v6
	v_fma_f32 v7, v101, v29, -v7
	v_add_f32_e64 v20, v2, -v52
	v_add_f32_e64 v21, v3, -v53
	v_add_f32_e64 v28, v56, -v32
	v_add_f32_e64 v29, v57, -v33
	v_mov_b32_e32 v229, v225
	v_add_f32 v224, v220, v212
	v_add_f32 v225, v221, v213
	v_add_f32_e64 v212, v220, -v212
	v_add_f32_e64 v213, v221, -v213
	v_add_f32 v220, v218, v216
	v_add_f32 v221, v219, v217
	v_add_f32_e64 v216, v218, -v216
	v_add_f32_e64 v217, v219, -v217
	v_fma_f32 v218, v184, s48, -v176
	v_fma_f32 v219, v185, s49, -v177
	v_fma_f32 v176, v184, s48, v176
	v_fma_f32 v177, v185, s49, v177
	v_fma_f32 v24, v76, v68, -v24
	v_fma_f32 v25, v77, v69, -v25
	v_add_f32 v48, v20, v28
	v_add_f32 v49, v21, v29
	v_add_f32_e64 v54, v20, -v28
	v_add_f32_e64 v55, v21, -v29
	v_mov_b32_e32 v219, v177
	v_mov_b32_e32 v49, v55
	v_add_f32_e64 v54, v14, -v11
	v_add_f32_e64 v55, v15, -v10
	v_add_f32_e64 v68, v24, -v6
	v_add_f32_e64 v69, v25, -v7
	v_add_f32 v176, v228, v218
	v_add_f32 v177, v229, v219
	v_add_f32 v70, v68, v54
	v_add_f32 v71, v69, v55
	v_add_f32_e64 v72, v68, -v54
	v_add_f32_e64 v73, v69, -v55
	v_mul_f32 v40, v41, v30
	v_mul_f32 v41, v41, v31
	v_add_f32 v184, v224, v176
	v_add_f32 v185, v225, v177
	v_add_f32_e64 v176, v224, -v176
	v_add_f32_e64 v177, v225, -v177
	v_mov_b32_e32 v225, v200
	v_mov_b32_e32 v227, v214
	v_mov_b32_e32 v200, v209
	v_mov_b32_e32 v214, v211
	v_mov_b32_e32 v76, v70
	v_mov_b32_e32 v77, v73
	v_pk_mov_b32 v[70:71], v[72:73], v[70:71] op_sel:[1,0]
	v_fma_f32 v72, v38, v30, v41
	v_fma_f32 v73, v38, v31, v40
	v_fma_f32 v30, v38, v30, -v41
	v_fma_f32 v31, v38, v31, -v40
; FFT_HD cf2 mk2(float x, float y) { return (cf2){x, y}; }
; FFT_HD cf2 cmul(cf2 a, cf2 b) { return mk2(a.x * b.x - a.y * b.y, a.x * b.y + a.y * b.x); }
; template <bool INV> FFT_HD void dft16(cf2 (&x)[16]) {
;     const float C1 = 0.9238795325112867f, S1 = 0.3826834323650898f, H = 0.7071067811865476f;
; #pragma unroll
;     for (int b = 0; b < 4; ++b) dft4<INV>(x[b], x[4 + b], x[8 + b], x[12 + b]);
;     const float s = INV ? -1.f : 1.f;
;     x[4 + 1] = cmul(x[4 + 1], mk2(C1, -s * S1)); x[8 + 1] = cmul(x[8 + 1], mk2(H, -s * H));   x[12 + 1] = cmul(x[12 + 1], mk2(S1, -s * C1));
;     x[4 + 2] = cmul(x[4 + 2], mk2(H, -s * H));   x[8 + 2] = cmul(x[8 + 2], mk2(0.f, -s));     x[12 + 2] = cmul(x[12 + 2], mk2(-H, -s * H));
;     x[4 + 3] = cmul(x[4 + 3], mk2(S1, -s * C1)); x[8 + 3] = cmul(x[8 + 3], mk2(-H, -s * H));  x[12 + 3] = cmul(x[12 + 3], mk2(-C1, s * S1));
; #pragma unroll
;     for (int c = 0; c < 4; ++c) dft4<INV>(x[4 * c], x[4 * c + 1], x[4 * c + 2], x[4 * c + 3]);
; #pragma unroll
;     for (int c = 0; c < 4; ++c)
; #pragma unroll
;         for (int d = c + 1; d < 4; ++d) { const cf2 t = x[4 * c + d]; x[4 * c + d] = x[4 * d + c]; x[4 * d + c] = t; }
; }
	v_mul_f32 v38, v51, v23
	v_mul_f32 v39, v51, v22
	s_mov_b32 s52, s25
	s_mov_b32 s53, s27
	v_mov_b32_e32 v224, v208
	v_mov_b32_e32 v226, v210
	v_add_f32_e64 v200, v200, -v214
	v_add_f32_e64 v201, v201, -v215
	s_mov_b32 s12, s25
	v_fma_f32 v40, v46, v22, v38
	v_fma_f32 v41, v46, v23, v39
	v_fma_f32 v22, v46, v22, -v38
	v_fma_f32 v23, v46, v23, -v39
	v_mul_f32 v38, v88, v26
	v_mul_f32 v39, v89, v27
	v_mul_f32_e64 v178, v174, s52
	v_mul_f32_e64 v179, v175, s53
	v_add_f32_e64 v224, v224, -v226
	v_add_f32_e64 v225, v225, -v227
	s_mov_b32 s53, s24
	v_mul_f32_e64 v200, v200, s12
	v_mul_f32_e64 v201, v201, s12
	v_fma_f32 v46, v86, v26, v39
	v_fma_f32 v47, v87, v27, v38
	v_fma_f32 v26, v86, v26, -v39
	v_fma_f32 v27, v87, v27, -v38
	v_mul_f32 v38, v92, v18
	v_mul_f32 v39, v93, v19
	v_fma_f32 v208, v224, s52, -v200
	v_fma_f32 v209, v225, s53, -v201
	v_fma_f32 v210, v224, s52, v200
	v_fma_f32 v211, v225, s53, v201
	v_fma_f32 v200, v224, s12, -v200
	v_fma_f32 v201, v225, s12, -v201
	s_mov_b32 s12, s29
	v_fma_f32 v50, v90, v18, v39
	v_fma_f32 v51, v91, v19, v38
	v_fma_f32 v18, v90, v18, -v39
	v_fma_f32 v19, v91, v19, -v38
	v_mul_f32_e64 v70, v70, s12
	v_mul_f32_e64 v71, v71, s12
	v_mov_b32_e32 v73, v31
	v_mov_b32_e32 v22, v40
	v_mov_b32_e32 v47, v27
	v_mov_b32_e32 v18, v50
	v_fma_f32 v70, v76, s38, v70
	v_fma_f32 v71, v77, s39, v71
	v_add_f32 v38, v72, v46
	v_add_f32 v39, v73, v47
	v_add_f32 v76, v22, v18
	v_add_f32 v77, v23, v19
	v_pk_mov_b32 v[30:31], v[30:31], v[40:41] op_sel:[1,0]
	v_pk_mov_b32 v[26:27], v[26:27], v[50:51] op_sel:[1,0]
	v_mov_b32_e32 v73, v23
	v_add_f32_e64 v26, v30, -v26
	v_add_f32_e64 v27, v31, -v27
	v_mov_b32_e32 v47, v19
	v_add_f32_e64 v22, v38, -v76
	v_add_f32_e64 v23, v39, -v77
	v_add_f32_e64 v18, v72, -v46
	v_add_f32_e64 v19, v73, -v47
	v_sub_f32_e32 v40, v26, v27
	v_fma_f32 v30, v22, 0, -v23
	v_fma_f32 v31, v23, 0, -v22
	v_fma_f32 v253, v22, 0, v23
	v_fma_f32 v23, v23, 0, v22
	v_mov_b32_e32 v22, v253
	v_add_f32 v46, v18, v19
	v_add_f32 v47, v18, v19
	v_mul_f32_e32 v22, 0x3f3504f3, v40
	v_mul_f32 v44, v44, v16
	v_mul_f32 v45, v45, v16
	v_mov_b32_e32 v31, v23
	v_fma_f32 v23, v47, s25, -v22
	v_fma_f32 v22, v46, s24, -v22
	v_fma_f32 v46, v42, v17, -v44
	v_fma_f32 v47, v43, v17, -v45
	v_fma_f32 v16, v42, v17, v44
	v_fma_f32 v17, v43, v17, v45
	v_mov_b32_e32 v43, v5
	v_pk_mov_b32 v[4:5], v[12:13], v[4:5] op_sel:[1,0]
	v_mov_b32_e32 v42, v12
	v_mul_f32 v12, v78, v4
	v_mul_f32 v13, v79, v5
	v_mov_b32_e32 v16, v46
	v_fma_f32 v12, v74, v42, v12
	v_fma_f32 v13, v75, v43, v13
	v_mul_f32 v42, v78, v42
	v_mul_f32 v43, v79, v43
	v_add_f32 v2, v2, v52
	v_add_f32 v3, v3, v53
	v_fma_f32 v4, v74, v4, -v42
	v_fma_f32 v5, v75, v5, -v43
	v_mul_f32 v42, v84, v8
	v_mul_f32 v43, v85, v9
	v_add_f32 v32, v56, v32
	v_add_f32 v33, v57, v33
	v_fma_f32 v44, -v82, v8, v43
	v_fma_f32 v45, -v83, v9, v42
	v_fma_f32 v8, v82, v8, v43
	v_fma_f32 v9, v83, v9, v42
	v_add_f32 v42, v13, v4
	v_add_f32 v43, v12, v5
	v_mov_b32_e32 v45, v9
	v_add_f32 v50, v16, v44
	v_add_f32 v51, v17, v45
	v_mov_b32_e32 v16, v13
	v_mov_b32_e32 v8, v4
	v_add_f32_e64 v8, v16, -v8
	v_add_f32_e64 v9, v17, -v9
	v_pk_mov_b32 v[4:5], v[4:5], v[46:47] op_sel:[1,0]
	v_mov_b32_e32 v13, v44
	v_add_f32_e64 v4, v4, -v12
	v_add_f32_e64 v5, v5, -v13
	v_add_f32_e32 v44, v8, v9
	v_pk_mov_b32 v[52:53], v[24:25], v[14:15] op_sel:[1,0]
	v_mov_b32_e32 v56, v7
	v_mov_b32_e32 v57, v11
	v_mov_b32_e32 v25, v15
	v_mov_b32_e32 v7, v10
	v_add_f32_e64 v253, v8, -v9
	v_add_f32_e64 v9, v8, -v9
	v_mov_b32_e32 v8, v253
	v_add_f32 v12, v42, v50
	v_add_f32 v13, v43, v51
	v_add_f32_e64 v16, v42, -v50
	v_add_f32_e64 v17, v43, -v51
	v_sub_f32_e32 v42, v4, v5
	v_add_f32 v52, v52, v56
	v_add_f32 v53, v53, v57
	v_add_f32 v6, v24, v6
	v_add_f32 v7, v25, v7
	v_add_f32 v253, v4, v5
	v_add_f32 v5, v4, v5
	v_mov_b32_e32 v4, v253
	v_mul_f32_e64 v8, v8, s48
	v_mul_f32_e64 v9, v9, s49
	v_add_f32 v10, v52, v6
	v_add_f32 v11, v53, v7
	v_add_f32_e64 v6, v52, -v6
	v_add_f32_e64 v7, v53, -v7
	v_fma_f32 v14, v4, s26, v8
	v_fma_f32 v15, v5, s27, v9
	v_fma_f32 v4, v4, s26, -v8
	v_fma_f32 v5, v5, s27, -v9
	v_add_f32_e64 v40, v2, -v33
	v_add_f32_e64 v41, v3, -v32
	v_mul_f32_e32 v4, 0x3f3504f3, v6
	v_add_f32 v24, v38, v76
	v_add_f32 v25, v39, v77
	v_add_f32 v2, v2, v33
	v_add_f32 v3, v3, v32
	v_mov_b32_e32 v15, v5
	v_fma_f32 v5, v7, s53, -v4
	v_fma_f32 v4, v7, s52, -v4
	v_add_f32_e64 v6, v2, -v24
	v_add_f32_e64 v7, v3, -v25
	v_add_f32 v2, v2, v24
	v_add_f32 v3, v3, v25
	v_mov_b32_e32 v24, v54
	v_mov_b32_e32 v25, v18
	v_mov_b32_e32 v18, v68
	s_mov_b32 s50, s24
	s_mov_b32 s51, s26
	v_add_f32_e64 v18, v24, -v18
	v_add_f32_e64 v19, v25, -v19
	v_pk_mov_b32 v[24:25], v[68:69], v[26:27] op_sel:[1,0]
	v_mov_b32_e32 v26, v55
	v_fma_f32 v182, v172, s50, -v178
	v_fma_f32 v183, v173, s51, -v179
	v_fma_f32 v178, v172, s50, v178
	v_fma_f32 v179, v173, s51, v179
	s_mov_b32 s50, s27
	s_mov_b32 s51, s25
	v_add_f32 v24, v24, v26
	v_add_f32 v25, v25, v27
	v_mul_f32_e32 v43, 0x3f6c835e, v42
	v_mul_f32_e32 v45, 0x3ec3ef15, v44
	v_mul_f32_e32 v46, 0x3ec3ef15, v42
	v_mul_f32_e32 v50, 0x3f6c835e, v44
	v_mul_f32_e32 v42, 0x3f3504f3, v17
	v_mul_f32_e32 v44, 0x3f3504f3, v16
	v_add_f32_e64 v8, v12, -v10
	v_add_f32_e64 v9, v13, -v11
	v_add_f32 v10, v12, v10
	v_add_f32 v11, v13, v11
	v_mul_f32_e64 v26, v24, s50
	v_mul_f32_e64 v27, v25, s51
	v_mul_f32_e64 v24, v24, s36
	v_mul_f32_e64 v25, v25, s37
	v_add_f32_e32 v16, v42, v44
	v_fma_f32 v17, v17, s25, -v44
	v_add_f32 v12, v2, v11
	v_add_f32 v13, v3, v10
	v_add_f32_e64 v2, v2, -v11
	v_add_f32_e64 v3, v3, -v10
	v_add_f32_e64 v10, v6, -v8
	v_add_f32_e64 v11, v7, -v9
	v_add_f32 v6, v6, v8
	v_add_f32 v7, v7, v9
	v_mov_b32_e32 v42, v20
; __device__ __forceinline__ unsigned cvt_pk_bf16(float lo, float hi) { unsigned r; asm volatile("v_cvt_pk_bf16_f32 %0, %1, %2" : "=v"(r) : "v"(lo), "v"(hi)); return r; }
; FFT_HD cf2 mk2(float x, float y) { return (cf2){x, y}; }
; FFT_HD cf2 cmul(cf2 a, cf2 b) { return mk2(a.x * b.x - a.y * b.y, a.x * b.y + a.y * b.x); }
; template <int BANK, int WAITN> __device__ __forceinline__ void bg_finish1(BgState& b) {
;     if (WAITN == 32) asm volatile("s_waitcnt vmcnt(32)" ::: "memory"); else asm volatile("s_waitcnt vmcnt(0)" ::: "memory");
;     asm volatile("" : BG_TIE16(BANK * 32) :: "memory");
;     asm volatile("" : BG_TIE16(BANK * 32 + 16) :: "memory");
;     bf16_t* dst = b.dst[BANK];
;     if (dst != nullptr) {
; #pragma unroll
;         for (int c = 0; c < 4; ++c) { u32x4 w;
;             w.x = cvt_pk_bf16(b.r[(BANK * 8 + 0) * 4 + c], b.r[(BANK * 8 + 1) * 4 + c]); w.y = cvt_pk_bf16(b.r[(BANK * 8 + 2) * 4 + c], b.r[(BANK * 8 + 3) * 4 + c]);
;             w.z = cvt_pk_bf16(b.r[(BANK * 8 + 4) * 4 + c], b.r[(BANK * 8 + 5) * 4 + c]); w.w = cvt_pk_bf16(b.r[(BANK * 8 + 6) * 4 + c], b.r[(BANK * 8 + 7) * 4 + c]);
;             bf16_t* dp = dst + (c & 1) * 512 + (c >> 1) * b.o2[BANK];
;             asm volatile("global_store_dwordx4 %0, %1, off\n\ts_nop 1" :: "v"(dp), "v"(w) : "memory"); }
;     }
; }
; template <bool INV> FFT_HD void dft16(cf2 (&x)[16]) {
;     const float C1 = 0.9238795325112867f, S1 = 0.3826834323650898f, H = 0.7071067811865476f;
; #pragma unroll
;     for (int b = 0; b < 4; ++b) dft4<INV>(x[b], x[4 + b], x[8 + b], x[12 + b]);
;     const float s = INV ? -1.f : 1.f;
;     x[4 + 1] = cmul(x[4 + 1], mk2(C1, -s * S1)); x[8 + 1] = cmul(x[8 + 1], mk2(H, -s * H));   x[12 + 1] = cmul(x[12 + 1], mk2(S1, -s * C1));
;     x[4 + 2] = cmul(x[4 + 2], mk2(H, -s * H));   x[8 + 2] = cmul(x[8 + 2], mk2(0.f, -s));     x[12 + 2] = cmul(x[12 + 2], mk2(-H, -s * H));
;     x[4 + 3] = cmul(x[4 + 3], mk2(S1, -s * C1)); x[8 + 3] = cmul(x[8 + 3], mk2(-H, -s * H));  x[12 + 3] = cmul(x[12 + 3], mk2(-C1, s * S1));
; #pragma unroll
;     for (int c = 0; c < 4; ++c) dft4<INV>(x[4 * c], x[4 * c + 1], x[4 * c + 2], x[4 * c + 3]);
; #pragma unroll
;     for (int c = 0; c < 4; ++c)
; #pragma unroll
;         for (int d = c + 1; d < 4; ++d) { const cf2 t = x[4 * c + d]; x[4 * c + d] = x[4 * d + c]; x[4 * d + c] = t; }
; }
	v_mov_b32_e32 v44, v28
	v_mov_b32_e32 v47, v21
	v_mov_b32_e32 v51, v29
	v_fma_f32 v24, v18, s50, -v24
	v_fma_f32 v25, v19, s51, -v25
	v_mov_b32_e32 v207, v174
	v_mov_b32_e32 v8, v10
	v_mov_b32_e32 v9, v7
	v_mov_b32_e32 v7, v11
	v_add_f32_e64 v10, v42, -v44
	v_add_f32_e64 v11, v43, -v45
	v_add_f32 v20, v46, v50
	v_add_f32 v21, v47, v51
	v_pk_mov_b32 v[28:29], v[24:25], v[24:25] op_sel:[1,0]
	v_fma_f32 v18, v18, s36, v26
	v_fma_f32 v19, v19, s37, v27
	v_mul_f32_e64 v174, v206, s36
	v_mul_f32_e64 v175, v207, s37
	v_pk_mov_b32 v[172:173], v[202:203], v[172:173] op_sel:[1,0]
	v_add_f32_e64 v253, v10, -v25
	v_add_f32_e64 v25, v11, -v24
	v_mov_b32_e32 v24, v253
	v_add_f32_e64 v26, v20, -v18
	v_add_f32_e64 v27, v21, -v19
	v_pk_mov_b32 v[32:33], v[10:11], v[20:21] op_sel:[1,0]
	v_pk_mov_b32 v[38:39], v[28:29], v[18:19] op_sel:[1,0]
	v_mov_b32_e32 v11, v21
	v_mov_b32_e32 v29, v19
	v_mov_b32_e32 v183, v179
	v_fma_f32 v172, v172, s50, -v174
	v_fma_f32 v173, v173, s51, -v175
	v_mov_b32_e32 v174, v190
	v_mov_b32_e32 v175, v204
	v_add_f32 v10, v10, v28
	v_add_f32 v11, v11, v29
	v_add_f32_e64 v20, v24, -v26
	v_add_f32_e64 v21, v25, -v27
	v_add_f32 v28, v26, v24
	v_add_f32 v29, v27, v25
	v_add_f32_e64 v24, v26, -v24
	v_add_f32_e64 v25, v27, -v25
	v_mov_b32_e32 v191, v171
	v_pk_mov_b32 v[178:179], v[178:179], v[170:171] op_sel:[1,0]
	v_pk_mov_b32 v[214:215], v[208:209], v[210:211] op_sel:[1,0]
	v_mov_b32_e32 v211, v200
	v_mov_b32_e32 v208, v201
	v_add_f32 v170, v170, v172
	v_add_f32 v171, v171, v173
	v_add_f32 v174, v182, v174
	v_add_f32 v175, v183, v175
	v_mov_b32_e32 v183, v173
	v_mov_b32_e32 v205, v172
	v_mov_b32_e32 v21, v29
	v_mov_b32_e32 v29, v25
	v_add_f32_e64 v24, v40, -v30
	v_add_f32_e64 v25, v41, -v31
	v_add_f32_e64 v26, v16, -v4
	v_add_f32_e64 v27, v17, -v5
	v_add_f32 v30, v40, v30
	v_add_f32 v31, v41, v31
	v_add_f32 v4, v16, v4
	v_add_f32 v5, v17, v5
	v_add_f32_e64 v180, v180, -v198
	v_add_f32_e64 v181, v181, -v199
	v_add_f32_e64 v218, v228, -v218
	v_add_f32_e64 v219, v229, -v219
	v_add_f32 v214, v200, v214
	v_add_f32 v215, v201, v215
	v_add_f32_e64 v200, v210, -v208
	v_add_f32_e64 v201, v211, -v209
	v_add_f32 v202, v170, v174
	v_add_f32 v203, v171, v175
	v_mov_b32_e32 v206, v174
	v_mov_b32_e32 v207, v171
	v_mov_b32_e32 v171, v175
	v_add_f32_e64 v174, v190, -v182
	v_add_f32_e64 v175, v191, -v183
	v_add_f32_e64 v172, v178, -v204
	v_add_f32_e64 v173, v179, -v205
	v_add_f32 v32, v32, v38
	v_add_f32 v33, v33, v39
	v_add_f32 v16, v30, v5
	v_add_f32 v17, v31, v4
	v_add_f32_e64 v253, v30, -v5
	v_add_f32_e64 v5, v31, -v4
	v_mov_b32_e32 v4, v253
	v_add_f32_e64 v30, v24, -v26
	v_add_f32_e64 v31, v25, -v27
	v_add_f32 v24, v24, v26
	v_add_f32 v25, v25, v27
	v_add_f32_e64 v198, v188, -v181
	v_add_f32_e64 v199, v189, -v180
	v_add_f32 v253, v188, v181
	v_add_f32 v181, v189, v180
	v_mov_b32_e32 v180, v253
	v_add_f32_e64 v222, v212, -v219
	v_add_f32_e64 v223, v213, -v218
	v_add_f32 v212, v212, v219
	v_add_f32 v213, v213, v218
	v_add_f32_e64 v208, v192, -v200
	v_add_f32_e64 v209, v193, -v201
	v_add_f32 v192, v192, v200
	v_add_f32 v193, v193, v201
	v_add_f32_e64 v178, v174, -v172
	v_add_f32_e64 v179, v175, -v173
	v_add_f32 v172, v174, v172
	v_add_f32 v173, v175, v173
	v_add_f32 v18, v10, v32
	v_add_f32 v19, v11, v33
	v_add_f32_e64 v10, v10, -v32
	v_add_f32_e64 v11, v11, -v33
	v_mov_b32_e32 v26, v30
	v_mov_b32_e32 v27, v25
	v_mov_b32_e32 v25, v31
	v_add_f32_e64 v30, v48, -v22
	v_add_f32_e64 v31, v49, -v23
	v_add_f32_e64 v32, v14, -v70
	v_add_f32_e64 v33, v15, -v71
	v_add_f32 v22, v48, v22
	v_add_f32 v23, v49, v23
	v_add_f32 v14, v14, v70
	v_add_f32 v15, v15, v71
	v_mov_b32_e32 v189, v181
	v_mov_b32_e32 v219, v213
	v_mov_b32_e32 v201, v193
	v_mov_b32_e32 v175, v173
	v_mov_b32_e32 v181, v199
	v_mov_b32_e32 v213, v223
	v_mov_b32_e32 v193, v209
	v_mov_b32_e32 v173, v179
	v_add_f32 v38, v22, v15
	v_add_f32 v39, v23, v14
	v_add_f32_e64 v253, v22, -v15
	v_add_f32_e64 v15, v23, -v14
	v_mov_b32_e32 v14, v253
	v_add_f32_e64 v22, v30, -v32
	v_add_f32_e64 v23, v31, -v33
	v_add_f32 v30, v30, v32
	v_add_f32 v31, v31, v33
	v_mov_b32_e32 v188, v198
	v_mov_b32_e32 v218, v222
	v_add_f32 v224, v186, v214
	v_add_f32 v225, v187, v215
	v_add_f32_e64 v186, v186, -v214
	v_add_f32_e64 v187, v187, -v215
	v_mov_b32_e32 v200, v208
	v_add_f32_e64 v170, v206, -v170
	v_add_f32_e64 v171, v207, -v171
	v_mov_b32_e32 v174, v178
	ds_write2_b64 v238, v[220:221], v[184:185] offset1:66
	ds_write2_b64 v238, v[224:225], v[202:203] offset0:132 offset1:198
	ds_write2_b64 v239, v[188:189], v[218:219] offset0:8 offset1:74
	ds_write2_b64 v239, v[200:201], v[174:175] offset0:140 offset1:206
	ds_write2_b64 v240, v[216:217], v[176:177] offset0:16 offset1:82
	ds_write2_b64 v240, v[186:187], v[170:171] offset0:148 offset1:214
	ds_write2_b64 v241, v[180:181], v[212:213] offset0:24 offset1:90
	ds_write2_b64 v241, v[192:193], v[172:173] offset0:156 offset1:222
	v_mov_b32_e32 v32, v22
	v_mov_b32_e32 v33, v31
	v_mov_b32_e32 v31, v23
	ds_write2_b64 v60, v[12:13], v[18:19] offset1:66
	ds_write2_b64 v60, v[16:17], v[38:39] offset0:132 offset1:198
	ds_write2_b64 v65, v[8:9], v[20:21] offset0:8 offset1:74
	ds_write2_b64 v65, v[26:27], v[32:33] offset0:140 offset1:206
	ds_write2_b64 v67, v[2:3], v[10:11] offset0:16 offset1:82
	ds_write2_b64 v67, v[4:5], v[14:15] offset0:148 offset1:214
	ds_write2_b64 v169, v[6:7], v[28:29] offset0:24 offset1:90
	ds_write2_b64 v169, v[24:25], v[30:31] offset0:156 offset1:222
	s_waitcnt lgkmcnt(0)
	s_barrier
	s_waitcnt vmcnt(32)
	v_cmp_ne_u64_e32 vcc, 0, v[36:37]
	s_and_saveexec_b64 s[48:49], vcc
	s_cbranch_execz .LBB0_741
	v_cvt_pk_bf16_f32 v2, v161, v163
	v_cvt_pk_bf16_f32 v3, v162, v165
	v_cvt_pk_bf16_f32 v4, v164, v167
	v_cvt_pk_bf16_f32 v5, v166, v168
	v_lshl_add_u64 v[6:7], v[36:37], 0, s[22:23]
	global_store_dwordx4 v[36:37], v[2:5], off nt
	s_nop 1
	v_cvt_pk_bf16_f32 v2, v120, v122
	v_cvt_pk_bf16_f32 v3, v121, v124
	v_cvt_pk_bf16_f32 v4, v123, v126
	v_cvt_pk_bf16_f32 v5, v125, v127
	s_lshl_b32 s12, s44, 1
	global_store_dwordx4 v[6:7], v[2:5], off nt
	s_nop 1
	v_cvt_pk_bf16_f32 v2, v110, v112
	v_cvt_pk_bf16_f32 v3, v111, v114
	v_cvt_pk_bf16_f32 v4, v113, v116
	v_cvt_pk_bf16_f32 v5, v115, v117
	v_lshl_add_u64 v[8:9], v[36:37], 0, s[12:13]
	global_store_dwordx4 v[8:9], v[2:5], off nt
	s_nop 1
	v_cvt_pk_bf16_f32 v2, v102, v104
	v_cvt_pk_bf16_f32 v3, v103, v106
	v_cvt_pk_bf16_f32 v4, v105, v108
	v_cvt_pk_bf16_f32 v5, v107, v109
	v_lshl_add_u64 v[6:7], v[6:7], 0, s[12:13]
	global_store_dwordx4 v[6:7], v[2:5], off nt
	s_nop 1

; FFT_HD cf2 mk2(float x, float y) { return (cf2){x, y}; }
; FFT_HD void fft_sincos(float frac, float& s, float& c) { s = __builtin_amdgcn_sinf(frac); c = __builtin_amdgcn_cosf(frac); }
; FFT_HD cf2 cmul(cf2 a, cf2 b) { return mk2(a.x * b.x - a.y * b.y, a.x * b.y + a.y * b.x); }
; FFT_HD cf2 cmulc(cf2 a, cf2 b) { return mk2(a.x * b.x + a.y * b.y, a.y * b.x - a.x * b.y); }
; FFT_HD void fft_gen_tw(float frac, cf2 (&tw)[16]) {
;     float sn, cs; fft_sincos(frac, sn, cs);
;     tw[1] = mk2(cs, -sn);
;     tw[2] = cmul(tw[1], tw[1]); tw[3] = cmul(tw[2], tw[1]); tw[4] = cmul(tw[2], tw[2]); tw[5] = cmul(tw[4], tw[1]); tw[6] = cmul(tw[4], tw[2]); tw[7] = cmul(tw[4], tw[3]);
;     tw[8] = cmul(tw[4], tw[4]);
; #pragma unroll
;     for (int j = 9; j < 16; ++j) tw[j] = cmul(tw[8], tw[j - 8]);
; }
; template <bool INV, int lS, class ZP> FFT_HD void fft_r16_pass(ZP z, int tid) {
;     ...
;         for (int it = 0; it < 2; ++it) {
;             const int w = tid + 512 * it;
;             const int blk = w >> lS, p = w & (S - 1), pb = PADI((blk << (lS + 4)) + p);
;             fft_gen_tw((float)p * inv, tw);
;             cf2 x[16];
; #pragma unroll
;             for (int j = 0; j < 16; ++j) x[j] = z[pb + j * STEP];
;             if (INV) {
; #pragma unroll
;                 for (int j = 1; j < 16; ++j) x[j] = cmulc(x[j], tw[j]);
;             }
.LBB0_752:
	v_add_u32_e32 v2, s12, v128
	v_and_b32_e32 v3, 0x3ff, v2
	v_lshlrev_b32_e32 v2, 4, v2
	v_and_or_b32 v60, v2, s81, v3
	v_cvt_f32_u32_e32 v2, v3
	v_ashrrev_i32_e32 v65, 5, v60
	v_lshlrev_b32_e32 v65, 3, v65
	v_and_b32_e32 v65, 0xfffff0f0, v65
	v_mul_f32_e32 v3, 0x38800000, v2
	v_sin_f32_e32 v2, v3
	v_cos_f32_e32 v4, v3
	v_lshlrev_b32_e32 v60, 3, v60
	v_add3_u32 v60, 0, v65, v60
	v_xor_b32_e32 v5, 0x80000000, v2
	v_mov_b32_e32 v3, v4
	v_mov_b32_e32 v6, v2
	v_mov_b32_e32 v7, v5
	v_mul_f32 v6, v2, v6
	v_mul_f32 v7, v3, v7
	ds_read_b64 v[82:83], v60
	ds_read_b64 v[80:81], v60 offset:8448
	ds_read_b64 v[84:85], v60 offset:16896
	ds_read_b64 v[86:87], v60 offset:25344
	ds_read_b64 v[88:89], v60 offset:33792
	ds_read_b64 v[90:91], v60 offset:42240
	ds_read_b64 v[92:93], v60 offset:50688
	ds_read_b64 v[162:163], v60 offset:59136
	v_fma_f32 v8, v4, v4, -v6
	v_fma_f32 v9, v4, v5, -v7
	v_fma_f32 v6, v4, v4, v6
	v_fma_f32 v7, v4, v5, v7
	v_mov_b32_e32 v10, v8
	v_mov_b32_e32 v11, v7
	v_pk_mov_b32 v[12:13], v[6:7], v[8:9] op_sel:[1,0]
	v_mov_b32_e32 v5, v2
	v_mul_f32 v14, v4, v10
	v_mul_f32 v15, v5, v11
	v_mul_f32 v16, v2, v10
	v_mul_f32 v17, v3, v11
	v_mul_f32 v18, v7, v12
	v_mul_f32 v19, v7, v13
	v_mov_b32_e32 v42, v14
	v_fma_f32 v20, v8, v10, -v18
	v_fma_f32 v21, v8, v11, -v19
	v_fma_f32 v18, v8, v10, v18
	v_fma_f32 v19, v8, v11, v19
	v_mov_b32_e32 v43, v17
	v_pk_mov_b32 v[14:15], v[14:15], v[16:17] op_sel:[1,0]
	v_mov_b32_e32 v22, v20
	v_mov_b32_e32 v23, v19
	v_add_f32 v16, v42, v14
	v_add_f32 v17, v43, v15
	v_add_f32_e64 v14, v42, -v14
	v_add_f32_e64 v15, v43, -v15
	s_waitcnt lgkmcnt(5)
	v_mul_f32 v6, v85, v7
	v_mul_f32 v7, v84, v7
	v_mul_f32 v26, v4, v22
	v_mul_f32 v27, v5, v23
	v_mul_f32 v28, v2, v22
	v_mul_f32 v29, v3, v23
	v_mul_f32 v30, v10, v22
	v_mul_f32 v31, v11, v23
	v_mul_f32 v32, v12, v22
	v_mul_f32 v33, v13, v23
	v_mul_f32 v36, v22, v22
	v_mul_f32 v37, v23, v23
	v_mul_f32 v38, v22, v19
	v_mul_f32 v39, v23, v18
	v_add_u32_e32 v65, 0x10800, v60
	v_fma_f32 v180, v84, v8, v6
	v_fma_f32 v181, v85, v8, v7
	v_fma_f32 v6, v84, v8, -v6
	v_fma_f32 v7, v85, v8, -v7
	s_waitcnt lgkmcnt(4)
	v_mul_f32 v8, v87, v15
	v_mul_f32 v9, v86, v15
	v_mov_b32_e32 v40, v36
	v_mov_b32_e32 v41, v38
	v_pk_mov_b32 v[36:37], v[36:37], v[38:39] op_sel:[1,0]
	v_mov_b32_e32 v42, v16
	v_mov_b32_e32 v43, v15
	v_pk_mov_b32 v[44:45], v[14:15], v[16:17] op_sel:[1,0]
	v_mov_b32_e32 v50, v26
	v_mov_b32_e32 v51, v29
	v_pk_mov_b32 v[26:27], v[26:27], v[28:29] op_sel:[1,0]
	v_mov_b32_e32 v54, v30
	v_mov_b32_e32 v55, v32
	v_mov_b32_e32 v32, v31
	ds_read_b64 v[164:165], v65
	v_add_u32_e32 v67, 0x12900, v60
	v_fma_f32 v14, v86, v16, v8
	v_fma_f32 v15, v87, v16, v9
	v_fma_f32 v8, v86, v16, -v8
	v_fma_f32 v9, v87, v16, -v9
	s_waitcnt lgkmcnt(4)
	v_mul_f32 v16, v89, v19
	v_mul_f32 v17, v88, v19
	v_pk_mov_b32 v[24:25], v[18:19], v[20:21] op_sel:[1,0]
	v_add_f32_e64 v38, v40, -v36
	v_add_f32_e64 v39, v41, -v37
	v_add_f32 v36, v40, v36
	v_add_f32 v37, v41, v37
	v_mul_f32 v46, v22, v42
	v_mul_f32 v47, v23, v43
	v_mul_f32 v48, v22, v44
	v_mul_f32 v49, v23, v45
	v_add_f32 v28, v50, v26
	v_add_f32 v29, v51, v27
	v_add_f32_e64 v26, v50, -v26
	v_add_f32_e64 v27, v51, -v27
	v_add_f32_e64 v30, v54, -v32
	v_add_f32_e64 v31, v55, -v33
	v_add_f32 v32, v54, v32
	v_add_f32 v33, v55, v33
	ds_read_b64 v[166:167], v67
	v_add_u32_e32 v76, 0x18c00, v60
	v_fma_f32 v18, v88, v20, v16
	v_fma_f32 v19, v89, v21, v17
	v_fma_f32 v16, v88, v20, -v16
	v_fma_f32 v17, v89, v20, -v17
	v_mov_b32_e32 v40, v38
	v_mov_b32_e32 v41, v37
	v_mov_b32_e32 v51, v27
	v_pk_mov_b32 v[52:53], v[26:27], v[28:29] op_sel:[1,0]
	v_pk_mov_b32 v[56:57], v[32:33], v[30:31] op_sel:[1,0]
	v_mov_b32_e32 v70, v46
	v_mov_b32_e32 v71, v48
	v_mov_b32_e32 v48, v47
	v_add_u32_e32 v74, 0x14a00, v60
	ds_read_b64 v[172:173], v76
	v_mov_b32_e32 v19, v17
	s_waitcnt lgkmcnt(5)
	v_mul_f32 v16, v91, v27
	v_mul_f32 v17, v90, v27
	s_waitcnt lgkmcnt(4)
	v_mul_f32 v26, v93, v33
	v_mul_f32 v27, v92, v33
	v_mul_f32_e32 v32, v2, v37
	v_mov_b32_e32 v55, v33
	v_add_f32_e64 v46, v70, -v48
	v_add_f32_e64 v47, v71, -v49
	v_add_f32 v48, v70, v48
	v_add_f32 v49, v71, v49
	ds_read_b64 v[168:169], v74
	v_add_u32_e32 v75, 0x16b00, v60
	v_add_u32_e32 v77, 0x1ad00, v60
	v_fma_f32 v33, v5, v41, v32
	v_fma_f32 v32, v4, v40, v32
	v_mov_b32_e32 v50, v28
	v_mov_b32_e32 v54, v30
	ds_read_b64 v[170:171], v75
	ds_read_b64 v[174:175], v77
	v_add_u32_e32 v78, 0x1ce00, v60
	v_fma_f32 v20, v90, v28, v16
	v_fma_f32 v21, v91, v28, v17
	v_fma_f32 v16, v90, v28, -v16
	v_fma_f32 v17, v91, v28, -v17
	v_fma_f32 v28, v92, v30, v26
	v_fma_f32 v29, v93, v30, v27
	v_fma_f32 v31, v93, v30, -v27
	v_fma_f32 v30, v92, v30, -v26
	s_waitcnt lgkmcnt(6)
	v_mul_f32 v26, v163, v49
	v_mul_f32 v27, v162, v49
	v_mov_b32_e32 v33, v4
	v_mul_f32_e32 v4, v4, v37
	v_mul_f32 v24, v24, v40
	v_mul_f32 v25, v25, v41
	ds_read_b64 v[176:177], v78
	v_fma_f32 v84, v162, v46, v26
	v_fma_f32 v85, v163, v46, v27
	v_fma_f32 v86, v162, v46, -v26
	v_fma_f32 v87, v163, v46, -v27
	s_waitcnt lgkmcnt(6)
	v_mul_f32 v26, v165, v37
	v_mul_f32 v27, v164, v37
	v_fma_f32 v5, -v3, v41, v4
	v_fma_f32 v4, -v2, v40, v4
	v_mul_f32 v12, v12, v40
	v_mul_f32 v13, v13, v41
	v_mul_f32 v22, v22, v40
	v_mul_f32 v23, v23, v41
	v_add_u32_e32 v79, 0x1ef00, v60
	v_fma_f32 v88, v164, v38, v26
	v_fma_f32 v89, v165, v39, v27
	v_fma_f32 v26, v164, v38, -v26
	v_fma_f32 v27, v165, v38, -v27
	s_waitcnt lgkmcnt(5)
; FFT_HD cf2 mk2(float x, float y) { return (cf2){x, y}; }
; FFT_HD cf2 cmul(cf2 a, cf2 b) { return mk2(a.x * b.x - a.y * b.y, a.x * b.y + a.y * b.x); }
; FFT_HD cf2 cmulc(cf2 a, cf2 b) { return mk2(a.x * b.x + a.y * b.y, a.y * b.x - a.x * b.y); }
; FFT_HD cf2 cadd(cf2 a, cf2 b) { return mk2(a.x + b.x, a.y + b.y); }
; FFT_HD cf2 csub(cf2 a, cf2 b) { return mk2(a.x - b.x, a.y - b.y); }
; template <bool INV> FFT_HD void dft4(cf2& a, cf2& b, cf2& c, cf2& d) {
;     const cf2 s0 = cadd(a, c), s1 = csub(a, c), s2 = cadd(b, d), s3 = csub(b, d);
;     a = cadd(s0, s2); c = csub(s0, s2);
;     const cf2 r = INV ? mk2(-s3.y, s3.x) : mk2(s3.y, -s3.x);
;     b = cadd(s1, r); d = csub(s1, r);
; }
; template <bool INV> FFT_HD void dft16(cf2 (&x)[16]) {
;     const float C1 = 0.9238795325112867f, S1 = 0.3826834323650898f, H = 0.7071067811865476f;
; #pragma unroll
;     for (int b = 0; b < 4; ++b) dft4<INV>(x[b], x[4 + b], x[8 + b], x[12 + b]);
;     const float s = INV ? -1.f : 1.f;
;     x[4 + 1] = cmul(x[4 + 1], mk2(C1, -s * S1)); x[8 + 1] = cmul(x[8 + 1], mk2(H, -s * H));   x[12 + 1] = cmul(x[12 + 1], mk2(S1, -s * C1));
;     x[4 + 2] = cmul(x[4 + 2], mk2(H, -s * H));   x[8 + 2] = cmul(x[8 + 2], mk2(0.f, -s));     x[12 + 2] = cmul(x[12 + 2], mk2(-H, -s * H));
;     x[4 + 3] = cmul(x[4 + 3], mk2(S1, -s * C1)); x[8 + 3] = cmul(x[8 + 3], mk2(-H, -s * H));  x[12 + 3] = cmul(x[12 + 3], mk2(-C1, s * S1));
; #pragma unroll
;     for (int c = 0; c < 4; ++c) dft4<INV>(x[4 * c], x[4 * c + 1], x[4 * c + 2], x[4 * c + 3]);
; #pragma unroll
;     for (int c = 0; c < 4; ++c)
; #pragma unroll
;         for (int d = c + 1; d < 4; ++d) { const cf2 t = x[4 * c + d]; x[4 * c + d] = x[4 * d + c]; x[4 * d + c] = t; }
; }
; template <bool INV, int lS, class ZP> FFT_HD void fft_r16_pass(ZP z, int tid) {
;     ...
;             fft_gen_tw((float)p * inv, tw);
;             cf2 x[16];
; #pragma unroll
;             for (int j = 0; j < 16; ++j) x[j] = z[pb + j * STEP];
;             if (INV) {
; #pragma unroll
;                 for (int j = 1; j < 16; ++j) x[j] = cmulc(x[j], tw[j]);
;             }
;             dft16<INV>(x);
;             if (!INV) {
; #pragma unroll
;                 for (int j = 1; j < 16; ++j) x[j] = cmul(x[j], tw[j]);
;             }
; #pragma unroll
;             for (int j = 0; j < 16; ++j) z[pb + j * STEP] = x[j];
	v_pk_mov_b32 v[38:39], v[166:167], v[80:81] op_sel:[1,0]
	v_mov_b32_e32 v5, v2
	v_add_f32 v253, v24, v25
	v_add_f32 v25, v24, v25
	v_mov_b32_e32 v24, v253
	v_mul_f32 v10, v10, v40
	v_mul_f32 v11, v11, v41
	v_mul_f32 v44, v44, v40
	v_mul_f32 v45, v45, v41
	v_mul_f32 v52, v40, v52
	v_mul_f32 v53, v41, v53
	ds_read_b64 v[178:179], v79
	v_mov_b32_e32 v89, v27
	v_mov_b32_e32 v26, v166
	v_mov_b32_e32 v27, v81
	v_mul_f32 v2, v38, v4
	v_mul_f32 v3, v39, v5
	v_add_f32 v253, v12, v13
	v_add_f32 v13, v12, v13
	v_mov_b32_e32 v12, v253
	v_add_f32_e64 v253, v22, -v23
	v_add_f32_e64 v23, v22, -v23
	v_mov_b32_e32 v22, v253
	s_waitcnt lgkmcnt(5)
	v_mul_f32 v24, v24, v173
	v_mul_f32 v25, v25, v172
	v_mul_f32 v42, v42, v40
	v_mul_f32 v43, v43, v41
	v_mul_f32 v50, v40, v50
	v_mul_f32 v51, v41, v51
	v_mul_f32 v56, v40, v56
	v_mul_f32 v57, v41, v57
	v_fma_f32 v2, v26, v32, v2
	v_fma_f32 v3, v27, v33, v3
	v_mul_f32 v4, v26, v4
	v_mul_f32 v5, v27, v5
	v_add_f32_e64 v253, v10, -v11
	v_add_f32_e64 v11, v10, -v11
	v_mov_b32_e32 v10, v253
	s_waitcnt lgkmcnt(4)
	v_mul_f32 v12, v169, v12
	v_mul_f32 v13, v168, v13
	v_add_f32 v26, v44, v45
	v_add_f32 v27, v44, v45
	v_fma_f32 v92, v22, v172, v24
	v_fma_f32 v93, v23, v173, v25
	v_fma_f32 v22, v22, v172, -v24
	v_fma_f32 v23, v23, v173, -v25
	v_add_f32 v24, v52, v53
	v_add_f32 v25, v52, v53
	v_mul_f32 v54, v40, v54
	v_mul_f32 v55, v41, v55
	v_mov_b32_e32 v70, v46
	v_pk_mov_b32 v[72:73], v[48:49], v[46:47] op_sel:[1,0]
	v_fma_f32 v4, v38, v32, -v4
	v_fma_f32 v5, v39, v33, -v5
	v_fma_f32 v46, v168, v10, v12
	v_fma_f32 v47, v169, v11, v13
	v_fma_f32 v10, v168, v10, -v12
	v_fma_f32 v11, v169, v11, -v13
	v_add_f32_e64 v12, v42, -v43
	v_add_f32_e64 v13, v42, -v43
	s_waitcnt lgkmcnt(3)
	v_mul_f32 v26, v171, v26
	v_mul_f32 v27, v170, v27
	v_mov_b32_e32 v93, v23
	v_add_f32_e64 v22, v50, -v51
	v_add_f32_e64 v23, v50, -v51
	s_waitcnt lgkmcnt(2)
	v_mul_f32 v24, v24, v175
	v_mul_f32 v25, v25, v174
	v_add_f32 v32, v56, v57
	v_add_f32 v33, v56, v57
	v_mov_b32_e32 v71, v49
	v_mul_f32 v72, v40, v72
	v_mul_f32 v73, v41, v73
	v_fma_f32 v90, v170, v12, v26
	v_fma_f32 v91, v171, v13, v27
	v_fma_f32 v12, v170, v12, -v26
	v_fma_f32 v13, v171, v13, -v27
	v_fma_f32 v26, v22, v174, v24
	v_fma_f32 v27, v23, v175, v25
	v_fma_f32 v22, v22, v174, -v24
	v_fma_f32 v23, v23, v175, -v25
	v_add_f32_e64 v24, v54, -v55
	v_add_f32_e64 v25, v54, -v55
	s_waitcnt lgkmcnt(1)
	v_mul_f32 v32, v32, v177
	v_mul_f32 v33, v33, v176
	v_mul_f32 v70, v40, v70
	v_mul_f32 v71, v41, v71
	v_fma_f32 v48, v24, v176, v32
	v_fma_f32 v49, v25, v177, v33
	v_fma_f32 v50, v24, v176, -v32
	v_fma_f32 v51, v25, v177, -v33
	v_add_f32 v32, v72, v73
	v_add_f32 v33, v72, v73
	v_mov_b32_e32 v16, v20
	v_mov_b32_e32 v27, v23
	v_add_f32_e64 v24, v70, -v71
	v_add_f32_e64 v25, v70, -v71
	s_waitcnt lgkmcnt(0)
	v_mul_f32 v32, v32, v179
	v_mul_f32 v33, v33, v178
	v_mov_b32_e32 v181, v7
	v_mov_b32_e32 v47, v11
	v_fma_f32 v52, v24, v178, v32
	v_fma_f32 v53, v25, v179, v33
	v_fma_f32 v54, v24, v178, -v32
	v_fma_f32 v55, v25, v179, -v33
	v_add_f32 v32, v5, v2
	v_add_f32 v33, v4, v3
	v_add_f32 v36, v16, v26
	v_add_f32 v37, v17, v27
	v_mov_b32_e32 v24, v4
	v_mov_b32_e32 v16, v5
	v_pk_mov_b32 v[4:5], v[6:7], v[28:29] op_sel:[1,0]
	v_pk_mov_b32 v[6:7], v[10:11], v[48:49] op_sel:[1,0]
	v_mov_b32_e32 v15, v9
	v_mov_b32_e32 v30, v28
	v_mov_b32_e32 v86, v84
	v_mov_b32_e32 v91, v13
	v_mov_b32_e32 v50, v48
	v_mov_b32_e32 v54, v52
	v_pk_mov_b32 v[20:21], v[2:3], v[20:21] op_sel:[1,0]
	v_mov_b32_e32 v25, v26
	v_add_f32 v42, v180, v46
	v_add_f32 v43, v181, v47
	v_add_f32_e64 v28, v4, -v6
	v_add_f32_e64 v29, v5, -v7
	v_mov_b32_e32 v181, v31
	v_mov_b32_e32 v47, v51
	v_pk_mov_b32 v[6:7], v[8:9], v[84:85] op_sel:[1,0]
	v_pk_mov_b32 v[8:9], v[12:13], v[52:53] op_sel:[1,0]
	v_add_f32 v38, v82, v88
	v_add_f32 v39, v83, v89
	v_add_f32 v40, v18, v92
	v_add_f32 v41, v19, v93
	v_add_f32_e64 v24, v20, -v24
	v_add_f32_e64 v25, v21, -v25
	v_mov_b32_e32 v3, v23
	v_add_f32 v44, v30, v50
	v_add_f32 v45, v31, v51
	v_add_f32_e64 v30, v180, -v46
	v_add_f32_e64 v31, v181, -v47
	v_add_f32 v46, v14, v90
	v_add_f32 v47, v15, v91
	v_add_f32 v48, v86, v54
	v_add_f32 v49, v87, v55
	v_add_f32_e64 v52, v6, -v8
	v_add_f32_e64 v53, v7, -v9
	v_mov_b32_e32 v15, v87
	v_mov_b32_e32 v91, v55
	v_add_f32 v56, v38, v40
	v_add_f32 v57, v39, v41
	v_add_f32_e64 v26, v16, -v2
	v_add_f32_e64 v27, v17, -v3
	v_add_f32 v4, v42, v44
	v_add_f32 v5, v43, v45
	v_add_f32_e64 v54, v14, -v90
	v_add_f32_e64 v55, v15, -v91
	v_add_f32 v12, v46, v48
	v_add_f32 v13, v47, v49
	v_mov_b32_e32 v7, v52
	v_mov_b32_e32 v9, v53
	v_add_f32 v72, v24, v25
	v_add_f32 v73, v24, v25
	s_mov_b32 s50, s27
	s_mov_b32 s51, s26
	v_add_f32 v253, v52, v53
	v_add_f32 v53, v52, v53
	v_mov_b32_e32 v52, v253
	v_add_f32_e64 v38, v38, -v40
	v_add_f32_e64 v39, v39, -v41
	v_add_f32_e64 v40, v42, -v44
	v_add_f32_e64 v41, v43, -v45
	v_mov_b32_e32 v43, v46
	v_mov_b32_e32 v45, v48
	v_mov_b32_e32 v46, v33
	v_mov_b32_e32 v48, v37
	v_add_f32 v2, v32, v36
	v_add_f32 v3, v33, v37
	v_mov_b32_e32 v6, v54
	v_mov_b32_e32 v8, v55
	v_add_f32_e64 v70, v26, -v27
	v_add_f32_e64 v71, v26, -v27
	v_mul_f32_e64 v72, v72, s50
	v_mul_f32_e64 v73, v73, s51
	v_add_f32_e64 v253, v54, -v55
	v_add_f32_e64 v55, v54, -v55
	v_mov_b32_e32 v54, v253
	v_mul_f32_e64 v52, v52, s26
	v_mul_f32_e64 v53, v53, s27
	v_mov_b32_e32 v42, v32
	v_mov_b32_e32 v44, v36
	v_add_f32_e64 v32, v46, -v48
	v_add_f32_e64 v33, v47, -v49
	s_mov_b32 s12, s25
	v_add_f32_e64 v16, v82, -v88
	v_add_f32_e64 v17, v83, -v89
	v_fma_f32 v82, v70, s26, -v72
	v_fma_f32 v83, v71, s27, -v73
	v_fma_f32 v70, v70, s26, v72
	v_fma_f32 v71, v71, s27, v73
	v_fma_f32 v72, v54, s50, -v52
; FFT_HD cf2 mk2(float x, float y) { return (cf2){x, y}; }
; template <int BANK, int WAITN> __device__ __forceinline__ void bg_finish1(BgState& b) {
;     if (WAITN == 32) asm volatile("s_waitcnt vmcnt(32)" ::: "memory"); else asm volatile("s_waitcnt vmcnt(0)" ::: "memory");
;     asm volatile("" : BG_TIE16(BANK * 32) :: "memory");
;     asm volatile("" : BG_TIE16(BANK * 32 + 16) :: "memory");
;     bf16_t* dst = b.dst[BANK];
;     if (dst != nullptr) {
; #pragma unroll
;         for (int c = 0; c < 4; ++c) { u32x4 w;
;             w.x = cvt_pk_bf16(b.r[(BANK * 8 + 0) * 4 + c], b.r[(BANK * 8 + 1) * 4 + c]); w.y = cvt_pk_bf16(b.r[(BANK * 8 + 2) * 4 + c], b.r[(BANK * 8 + 3) * 4 + c]);
;             w.z = cvt_pk_bf16(b.r[(BANK * 8 + 4) * 4 + c], b.r[(BANK * 8 + 5) * 4 + c]); w.w = cvt_pk_bf16(b.r[(BANK * 8 + 6) * 4 + c], b.r[(BANK * 8 + 7) * 4 + c]);
;             bf16_t* dp = dst + (c & 1) * 512 + (c >> 1) * b.o2[BANK];
;             asm volatile("global_store_dwordx4 %0, %1, off\n\ts_nop 1" :: "v"(dp), "v"(w) : "memory"); }
;     }
; }
; template <bool INV> FFT_HD void dft4(cf2& a, cf2& b, cf2& c, cf2& d) {
;     const cf2 s0 = cadd(a, c), s1 = csub(a, c), s2 = cadd(b, d), s3 = csub(b, d);
;     a = cadd(s0, s2); c = csub(s0, s2);
;     const cf2 r = INV ? mk2(-s3.y, s3.x) : mk2(s3.y, -s3.x);
;     b = cadd(s1, r); d = csub(s1, r);
; }
; template <bool INV> FFT_HD void dft16(cf2 (&x)[16]) {
;     const float C1 = 0.9238795325112867f, S1 = 0.3826834323650898f, H = 0.7071067811865476f;
; #pragma unroll
;     for (int b = 0; b < 4; ++b) dft4<INV>(x[b], x[4 + b], x[8 + b], x[12 + b]);
;     const float s = INV ? -1.f : 1.f;
;     x[4 + 1] = cmul(x[4 + 1], mk2(C1, -s * S1)); x[8 + 1] = cmul(x[8 + 1], mk2(H, -s * H));   x[12 + 1] = cmul(x[12 + 1], mk2(S1, -s * C1));
;     x[4 + 2] = cmul(x[4 + 2], mk2(H, -s * H));   x[8 + 2] = cmul(x[8 + 2], mk2(0.f, -s));     x[12 + 2] = cmul(x[12 + 2], mk2(-H, -s * H));
;     x[4 + 3] = cmul(x[4 + 3], mk2(S1, -s * C1)); x[8 + 3] = cmul(x[8 + 3], mk2(-H, -s * H));  x[12 + 3] = cmul(x[12 + 3], mk2(-C1, s * S1));
; #pragma unroll
;     for (int c = 0; c < 4; ++c) dft4<INV>(x[4 * c], x[4 * c + 1], x[4 * c + 2], x[4 * c + 3]);
; #pragma unroll
;     for (int c = 0; c < 4; ++c)
; #pragma unroll
;         for (int d = c + 1; d < 4; ++d) { const cf2 t = x[4 * c + d]; x[4 * c + d] = x[4 * d + c]; x[4 * d + c] = t; }
; }
	v_fma_f32 v73, v55, s51, -v53
	v_fma_f32 v52, v54, s50, v52
	v_fma_f32 v53, v55, s51, v53
	v_add_f32_e64 v42, v42, -v44
	v_add_f32_e64 v43, v43, -v45
	v_fma_f32 v36, v40, 0, -v41
	v_fma_f32 v37, v41, 0, -v40
	v_fma_f32 v253, v40, 0, v41
	v_fma_f32 v41, v41, 0, v40
	v_mov_b32_e32 v40, v253
	s_mov_b32 s50, s25
	s_mov_b32 s51, s24
	v_mul_f32_e64 v32, v32, s12
	v_mul_f32_e64 v33, v33, s12
	v_add_f32 v22, v6, v8
	v_add_f32 v23, v7, v9
	v_add_f32_e64 v20, v6, -v8
	v_add_f32_e64 v21, v7, -v9
	v_mov_b32_e32 v37, v41
	v_fma_f32 v40, v42, s50, -v32
	v_fma_f32 v41, v43, s51, -v33
	v_fma_f32 v44, v42, s50, v32
	v_fma_f32 v45, v43, s51, v33
	v_fma_f32 v32, v42, s12, -v32
	v_fma_f32 v33, v43, s12, -v33
	v_add_f32_e32 v10, v28, v29
	v_mov_b32_e32 v23, v21
	v_mul_f32_e32 v6, 0x3f6c835e, v21
	v_pk_mov_b32 v[46:47], v[40:41], v[44:45] op_sel:[1,0]
	v_mov_b32_e32 v45, v32
	v_mov_b32_e32 v40, v33
	v_sub_f32_e32 v80, v30, v31
	v_mul_f32_e32 v51, 0x3f3504f3, v10
	v_fma_f32 v10, v22, s14, -v6
	v_fma_f32 v11, v23, s15, -v6
	v_add_f32 v6, v56, v4
	v_add_f32 v7, v57, v5
	v_add_f32 v14, v2, v12
	v_add_f32 v15, v3, v13
	v_add_f32 v46, v32, v46
	v_add_f32 v47, v33, v47
	v_add_f32_e64 v32, v44, -v40
	v_add_f32_e64 v33, v45, -v41
	v_mov_b32_e32 v40, v30
	v_mov_b32_e32 v41, v26
	v_mov_b32_e32 v26, v31
	v_mov_b32_e32 v30, v28
	v_mov_b32_e32 v31, v24
	v_mov_b32_e32 v24, v29
	v_add_f32 v8, v6, v14
	v_add_f32 v9, v7, v15
	v_add_f32_e64 v6, v6, -v14
	v_add_f32_e64 v7, v7, -v15
	v_add_f32_e64 v14, v18, -v92
	v_add_f32_e64 v15, v19, -v93
	v_add_f32_e64 v24, v30, -v24
	v_add_f32_e64 v25, v31, -v25
	s_mov_b32 s52, s25
	s_mov_b32 s53, s27
	v_pk_mov_b32 v[18:19], v[14:15], v[14:15] op_sel:[1,0]
	v_add_f32 v26, v40, v26
	v_add_f32 v27, v41, v27
	s_mov_b32 s50, s24
	s_mov_b32 s51, s26
	v_mul_f32_e64 v28, v24, s52
	v_mul_f32_e64 v29, v25, s53
	v_mov_b32_e32 v23, v24
	v_mul_f32_e32 v50, 0x3f3504f3, v80
	v_add_f32_e64 v4, v56, -v4
	v_add_f32_e64 v5, v57, -v5
	v_add_f32_e64 v56, v16, -v15
	v_add_f32_e64 v57, v17, -v14
	v_add_f32 v253, v16, v15
	v_add_f32 v15, v17, v14
	v_mov_b32_e32 v14, v253
	v_mul_f32_e32 v16, 0x3ec3ef15, v27
	v_mul_f32_e32 v18, 0x3f6c835e, v25
	v_mul_f32_e64 v22, v22, s40
	v_mul_f32_e64 v23, v23, s41
	v_fma_f32 v24, v26, s50, -v28
	v_fma_f32 v25, v27, s51, -v29
	v_fma_f32 v28, v26, s50, v28
	v_fma_f32 v29, v27, s51, v29
	v_pk_mov_b32 v[20:21], v[20:21], v[26:27] op_sel:[1,0]
	s_mov_b32 s50, s27
	s_mov_b32 s51, s25
	v_mov_b32_e32 v57, v15
	v_mov_b32_e32 v83, v71
	v_sub_f32_e32 v50, v50, v51
	v_fmac_f32_e32 v51, 0x3f3504f3, v80
	v_mov_b32_e32 v73, v53
	v_mov_b32_e32 v25, v29
	v_fma_f32 v20, v20, s50, v22
	v_fma_f32 v21, v21, s51, v23
	v_add_f32_e64 v16, v16, -v18
	v_add_f32_e64 v17, v17, -v19
	v_mov_b32_e32 v15, v10
	v_add_f32 v52, v56, v50
	v_add_f32 v53, v57, v51
	v_add_f32 v54, v82, v72
	v_add_f32 v55, v83, v73
	v_add_f32 v18, v16, v20
	v_add_f32 v19, v17, v21
	v_add_f32 v22, v24, v14
	v_add_f32 v23, v25, v15
	v_mov_b32_e32 v15, v17
	v_mov_b32_e32 v25, v21
	v_pk_mov_b32 v[16:17], v[28:29], v[16:17] op_sel:[1,0]
	v_mov_b32_e32 v11, v20
	v_add_f32_e64 v12, v2, -v12
	v_add_f32_e64 v13, v3, -v13
	v_add_f32 v70, v52, v54
	v_add_f32 v71, v53, v55
	v_add_f32_e64 v54, v52, -v54
	v_add_f32_e64 v55, v53, -v55
	v_add_f32_e64 v52, v56, -v50
	v_add_f32_e64 v53, v57, -v51
	v_add_f32_e64 v56, v82, -v72
	v_add_f32_e64 v57, v83, -v73
	v_add_f32 v42, v38, v36
	v_add_f32 v43, v39, v37
	v_add_f32_e64 v36, v38, -v36
	v_add_f32_e64 v37, v39, -v37
	v_add_f32_e64 v14, v14, -v24
	v_add_f32_e64 v15, v15, -v25
	v_add_f32_e64 v10, v16, -v10
	v_add_f32_e64 v11, v17, -v11
	v_add_f32_e64 v2, v4, -v13
	v_add_f32_e64 v3, v5, -v12
	v_add_f32 v4, v4, v13
	v_add_f32 v5, v5, v12
	v_add_f32_e64 v50, v52, -v57
	v_add_f32_e64 v51, v53, -v56
	v_add_f32 v52, v52, v57
	v_add_f32 v53, v53, v56
	v_add_f32_e64 v38, v36, -v32
	v_add_f32_e64 v39, v37, -v33
	v_add_f32 v32, v36, v32
	v_add_f32 v33, v37, v33
	v_add_f32_e64 v16, v14, -v10
	v_add_f32_e64 v17, v15, -v11
	v_add_f32 v10, v14, v10
	v_add_f32 v11, v15, v11
	v_mov_b32_e32 v13, v5
	v_mov_b32_e32 v57, v53
	v_mov_b32_e32 v37, v33
	v_add_f32 v26, v18, v22
	v_add_f32 v27, v19, v23
	v_mov_b32_e32 v30, v22
	v_mov_b32_e32 v31, v19
	v_mov_b32_e32 v19, v23
	v_mov_b32_e32 v15, v11
	v_mov_b32_e32 v5, v3
	v_mov_b32_e32 v53, v51
	v_mov_b32_e32 v33, v39
	v_mov_b32_e32 v11, v17
	s_movk_i32 s12, 0x200
	s_and_b64 vcc, exec, s[48:49]
	s_mov_b64 s[48:49], 0
	v_mov_b32_e32 v12, v2
	v_mov_b32_e32 v56, v50
	v_add_f32 v48, v42, v46
	v_add_f32 v49, v43, v47
	v_add_f32_e64 v42, v42, -v46
	v_add_f32_e64 v43, v43, -v47
	v_mov_b32_e32 v36, v38
	v_add_f32_e64 v18, v30, -v18
	v_add_f32_e64 v19, v31, -v19
	v_mov_b32_e32 v14, v16
	ds_write_b64 v60, v[8:9]
	ds_write_b64 v60, v[70:71] offset:8448
	ds_write_b64 v60, v[48:49] offset:16896
	ds_write_b64 v60, v[26:27] offset:25344
	ds_write_b64 v60, v[12:13] offset:33792
	ds_write_b64 v60, v[56:57] offset:42240
	ds_write_b64 v60, v[36:37] offset:50688
	ds_write_b64 v60, v[14:15] offset:59136
	ds_write_b64 v65, v[6:7]
	ds_write_b64 v67, v[54:55]
	ds_write_b64 v74, v[42:43]
	ds_write_b64 v75, v[18:19]
	ds_write_b64 v76, v[4:5]
	ds_write_b64 v77, v[52:53]
	ds_write_b64 v78, v[32:33]
	ds_write_b64 v79, v[10:11]
	s_cbranch_vccnz .LBB0_752
	s_waitcnt lgkmcnt(0)
	s_barrier
	s_waitcnt vmcnt(32)
	v_cmp_ne_u64_e32 vcc, 0, v[34:35]
	s_and_saveexec_b64 s[48:49], vcc
	s_cbranch_execz .LBB0_755
	v_cvt_pk_bf16_f32 v2, v153, v155
	v_cvt_pk_bf16_f32 v3, v154, v157
	v_cvt_pk_bf16_f32 v4, v156, v159
	v_cvt_pk_bf16_f32 v5, v158, v160
	v_lshl_add_u64 v[6:7], v[34:35], 0, s[22:23]
	global_store_dwordx4 v[34:35], v[2:5], off nt
	s_nop 1
	v_cvt_pk_bf16_f32 v2, v145, v147
	v_cvt_pk_bf16_f32 v3, v146, v149
	v_cvt_pk_bf16_f32 v4, v148, v151
	v_cvt_pk_bf16_f32 v5, v150, v152
	s_lshl_b32 s12, s46, 1
	global_store_dwordx4 v[6:7], v[2:5], off nt
	s_nop 1
	v_cvt_pk_bf16_f32 v2, v137, v139
	v_cvt_pk_bf16_f32 v3, v138, v141
	v_cvt_pk_bf16_f32 v4, v140, v143
	v_cvt_pk_bf16_f32 v5, v142, v144
	v_lshl_add_u64 v[8:9], v[34:35], 0, s[12:13]
	global_store_dwordx4 v[8:9], v[2:5], off nt
	s_nop 1
	v_cvt_pk_bf16_f32 v2, v129, v131
	v_cvt_pk_bf16_f32 v3, v130, v133
	v_cvt_pk_bf16_f32 v4, v132, v135
	v_cvt_pk_bf16_f32 v5, v134, v136
	v_lshl_add_u64 v[6:7], v[6:7], 0, s[12:13]
	global_store_dwordx4 v[6:7], v[2:5], off nt
	s_nop 1
